# previous stack + P5 dispatch tail: four cursor atomics issued back-to-back, one wait
# speedup vs baseline: 1.0073x; 1.0020x over previous
; #define GAS __attribute__((address_space(1)))
; __device__ __forceinline__ f32x4 bf4(unsigned a, unsigned b) { return (f32x4){bflo(a), bfhi(a), bflo(b), bfhi(b)}; }
; __device__ __forceinline__ int affine_item(int item_, int G) { if (G != 256) return item_; const int c = item_ & 255, i = item_ >> 8; return 64 * (c & 7) + (c >> 3) + 32 * i; }
; template <int l>
; __device__ __forceinline__ void layer_phases(Frame& F, const XcdBarrier& bar, const int lo, const int hi) {
;     ...
;             for (int item_ = blockIdx.x; item_ < T / 32; item_ += F.G) {
;                 const int item = affine_item(item_, F.G);
;                 const int m0 = item * 32 + 4 * F.wave;
;                 int lq = F.lane; asm volatile("" : "+v"(lq));
;                 const int r32 = lq & 31, hi5 = lq >> 5;
;                 const float* mrow = (const float*)(ws + WS_MOD) + ((size_t)l * 8 + (m0 >> 11)) * 12288;
; #pragma unroll
;                 for (int rp = 0; rp < 2; ++rp) {
;                 f32x4 vv[2][8];
; #pragma unroll
;                 for (int rr = 0; rr < 2; ++rr)
; #pragma unroll
;                     for (int j = 0; j < 8; ++j) { const size_t off = (size_t)(m0 + 2 * rp + rr) * D + 4 * lq + 256 * j;
;                         f32x4 xv; if (l == 0) xv = __builtin_nontemporal_load((const GAS f32x4*)(xin + off)); else { const v2u xw_ = __builtin_nontemporal_load((const GAS v2u*)(xinb + off)); xv = bf4(xw_.x, xw_.y); } const v2u mw = __builtin_nontemporal_load((const GAS v2u*)(mixb + off)); const f32x4 gv = *(const GAS f32x4*)(mrow + 4096 + 4 * lq + 256 * j);
;                         vv[rr][j] = xv * ALPHA + gv * (f32x4){bflo(mw.x), bfhi(mw.x), bflo(mw.y), bfhi(mw.y)}; }
.LBB0_612:
	s_lshl_b32 s0, s0, 5
	s_add_i32 s42, s0, s54
	s_ashr_i32 s0, s42, 11
	v_mov_b32_e32 v227, v72
	s_mul_hi_i32 s1, s0, 0xc000
	s_mul_i32 s0, s0, 0xc000
	v_readlane_b32 s14, v248, 19
	s_add_u32 s0, s14, s0
	v_readlane_b32 s14, v248, 20
	v_lshlrev_b32_e32 v86, 2, v227
	s_addc_u32 s1, s14, s1
	v_ashrrev_i32_e32 v87, 31, v86
	s_ashr_i32 s43, s42, 31
	s_lshl_b64 s[18:19], s[42:43], 11
	v_lshlrev_b64 v[32:33], 2, v[86:87]
	v_lshl_add_u64 v[20:21], s[18:19], 0, v[86:87]
	v_lshl_add_u64 v[88:89], s[0:1], 0, v[32:33]
	s_movk_i32 s22, 0x5000
	v_lshl_add_u64 v[28:29], v[20:21], 1, s[26:27]
	v_add_co_u32_e32 v64, vcc, s22, v88
	s_mov_b64 s[0:1], 0x4000
	global_load_dwordx2 v[62:63], v[28:29], off nt
	global_load_dwordx2 v[68:69], v[28:29], off offset:512 nt
	global_load_dwordx2 v[70:71], v[28:29], off offset:1024 nt
	global_load_dwordx2 v[82:83], v[28:29], off offset:1536 nt
	global_load_dwordx2 v[84:85], v[28:29], off offset:2048 nt
	v_addc_co_u32_e32 v65, vcc, 0, v89, vcc
	global_load_dwordx2 v[106:107], v[28:29], off offset:2560 nt
	global_load_dwordx4 v[0:3], v[64:65], off offset:-4096
	v_lshl_add_u64 v[66:67], v[88:89], 0, s[0:1]
	global_load_dwordx4 v[16:19], v[66:67], off offset:1024
	global_load_dwordx4 v[12:15], v[66:67], off offset:2048
	global_load_dwordx4 v[8:11], v[66:67], off offset:3072
	global_load_dwordx4 v[4:7], v[64:65], off
	v_lshl_add_u64 v[20:21], v[20:21], 2, s[20:21]
	global_load_dwordx4 v[34:37], v[20:21], off nt
	global_load_dwordx4 v[38:41], v[20:21], off offset:1024 nt
	global_load_dwordx4 v[42:45], v[20:21], off offset:2048 nt
	global_load_dwordx4 v[46:49], v[20:21], off offset:3072 nt
	v_add_co_u32_e32 v90, vcc, s87, v20
	v_readlane_b32 s0, v248, 13
	s_nop 0
	v_addc_co_u32_e32 v91, vcc, 0, v21, vcc
	global_load_dwordx4 v[50:53], v[90:91], off nt
	global_load_dwordx4 v[20:23], v[64:65], off offset:1024
	global_load_dwordx4 v[54:57], v[90:91], off offset:1024 nt
	global_load_dwordx2 v[112:113], v[28:29], off offset:3072 nt
	global_load_dwordx4 v[24:27], v[64:65], off offset:2048
	global_load_dwordx4 v[58:61], v[90:91], off offset:2048 nt
	global_load_dwordx2 v[114:115], v[28:29], off offset:3584 nt
	s_nop 0
	global_load_dwordx4 v[28:31], v[64:65], off offset:3072
	global_load_dwordx4 v[92:95], v[90:91], off offset:3072 nt
	v_readlane_b32 s1, v248, 14
	s_or_b32 s44, s42, 1
	s_ashr_i32 s45, s44, 31
	s_lshl_b64 s[16:17], s[44:45], 11
	s_mov_b32 s23, 0x9000
	s_movk_i32 s28, 0x7000
	v_mov_b32_e32 v158, 0
	v_mov_b32_e32 v174, 0
	v_mov_b32_e32 v246, 0
	s_waitcnt vmcnt(23)
	v_lshlrev_b32_e32 v90, 16, v62
	v_and_b32_e32 v91, 0xffff0000, v62
	v_lshlrev_b32_e32 v62, 16, v63
	v_and_b32_e32 v63, 0xffff0000, v63
	s_waitcnt vmcnt(19)
	v_lshlrev_b32_e32 v102, 16, v84
	v_and_b32_e32 v103, 0xffff0000, v84
	v_lshlrev_b32_e32 v84, 16, v85
	v_and_b32_e32 v85, 0xffff0000, v85
	s_waitcnt vmcnt(17)
	v_pk_mul_f32 v[90:91], v[0:1], v[90:91]
	v_lshlrev_b32_e32 v96, 16, v68
	v_and_b32_e32 v97, 0xffff0000, v68
	v_lshlrev_b32_e32 v100, 16, v82
	v_and_b32_e32 v101, 0xffff0000, v82
	v_lshlrev_b32_e32 v82, 16, v83
	v_and_b32_e32 v83, 0xffff0000, v83
	v_lshlrev_b32_e32 v116, 16, v106
	v_pk_mul_f32 v[62:63], v[2:3], v[62:63]
	s_waitcnt vmcnt(13)
	v_pk_mul_f32 v[122:123], v[6:7], v[84:85]
	s_waitcnt vmcnt(12)
	v_pk_fma_f32 v[84:85], v[34:35], s[40:41], v[90:91] op_sel_hi:[1,0,1]
	v_and_b32_e32 v117, 0xffff0000, v106
	v_lshlrev_b32_e32 v34, 16, v107
	v_and_b32_e32 v35, 0xffff0000, v107
	v_lshlrev_b32_e32 v98, 16, v70
	v_and_b32_e32 v99, 0xffff0000, v70
	v_pk_mul_f32 v[104:105], v[16:17], v[96:97]
	v_pk_mul_f32 v[110:111], v[10:11], v[82:83]
	v_pk_mul_f32 v[118:119], v[8:9], v[100:101]
	v_pk_fma_f32 v[82:83], v[36:37], s[40:41], v[62:63] op_sel_hi:[1,0,1]
	s_waitcnt vmcnt(7)
	v_pk_mul_f32 v[36:37], v[20:21], v[116:117]
	v_pk_mul_f32 v[34:35], v[22:23], v[34:35]
	v_pk_mul_f32 v[108:109], v[12:13], v[98:99]
	v_pk_fma_f32 v[98:99], v[38:39], s[40:41], v[104:105] op_sel_hi:[1,0,1]
	v_pk_fma_f32 v[104:105], v[46:47], s[40:41], v[118:119] op_sel_hi:[1,0,1]
	s_waitcnt vmcnt(6)
	v_pk_fma_f32 v[116:117], v[56:57], s[40:41], v[34:35] op_sel_hi:[1,0,1]
	v_pk_fma_f32 v[118:119], v[54:55], s[40:41], v[36:37] op_sel_hi:[1,0,1]
	s_waitcnt vmcnt(5)
	v_lshlrev_b32_e32 v34, 16, v112
	v_and_b32_e32 v35, 0xffff0000, v112
	v_lshlrev_b32_e32 v36, 16, v113
	v_and_b32_e32 v37, 0xffff0000, v113
	s_waitcnt vmcnt(4)
	v_pk_mul_f32 v[34:35], v[24:25], v[34:35]
	v_pk_mul_f32 v[36:37], v[26:27], v[36:37]
	v_lshlrev_b32_e32 v68, 16, v69
	v_and_b32_e32 v69, 0xffff0000, v69
	v_lshlrev_b32_e32 v70, 16, v71
	v_and_b32_e32 v71, 0xffff0000, v71
	s_waitcnt vmcnt(3)
	v_pk_fma_f32 v[124:125], v[60:61], s[40:41], v[36:37] op_sel_hi:[1,0,1]
	v_pk_fma_f32 v[126:127], v[58:59], s[40:41], v[34:35] op_sel_hi:[1,0,1]
	s_waitcnt vmcnt(2)
	v_lshlrev_b32_e32 v34, 16, v114
	v_and_b32_e32 v35, 0xffff0000, v114
	v_lshlrev_b32_e32 v36, 16, v115
	v_and_b32_e32 v37, 0xffff0000, v115
	v_pk_mul_f32 v[68:69], v[18:19], v[68:69]
	v_pk_mul_f32 v[70:71], v[14:15], v[70:71]
	s_waitcnt vmcnt(1)
	v_pk_mul_f32 v[34:35], v[28:29], v[34:35]
	v_pk_mul_f32 v[36:37], v[30:31], v[36:37]
	v_pk_fma_f32 v[96:97], v[40:41], s[40:41], v[68:69] op_sel_hi:[1,0,1]
	v_pk_fma_f32 v[100:101], v[44:45], s[40:41], v[70:71] op_sel_hi:[1,0,1]
	s_waitcnt vmcnt(0)
; template <int l>
; __device__ __forceinline__ void layer_phases(Frame& F, const XcdBarrier& bar, const int lo, const int hi) {
;     ...
; #pragma unroll
;                 for (int rq = 0; rq < 2; ++rq) { const int rr = 2 * rp + rq, m = m0 + rr, rloc = 4 * F.wave + rr;
;                     f32x4 (&v)[8] = vv[rq]; float s = 0.f;
; #pragma unroll
;                     for (int j = 0; j < 8; ++j) s += (v[j].x + v[j].y) + (v[j].z + v[j].w);
;                     const float mean = wave_sum(s) * (1.f / D); float s2 = 0.f;
; #pragma unroll
;                     for (int j = 0; j < 8; ++j) { v[j] = v[j] - mean; s2 += (v[j].x * v[j].x + v[j].y * v[j].y) + (v[j].z * v[j].z + v[j].w * v[j].w); }
;                     const float rstd = 1.f / sqrtf(wave_sum(s2) * (1.f / D) + LN_EPS);
	v_pk_fma_f32 v[68:69], v[94:95], s[40:41], v[36:37] op_sel_hi:[1,0,1]
	v_pk_fma_f32 v[70:71], v[92:93], s[40:41], v[34:35] op_sel_hi:[1,0,1]
	v_mov_b32_e32 v34, v84
	v_mov_b32_e32 v35, v98
	v_mov_b32_e32 v36, v85
	v_mov_b32_e32 v37, v99
	v_pk_add_f32 v[34:35], v[34:35], v[36:37]
	v_mov_b32_e32 v36, v82
	v_mov_b32_e32 v37, v96
	v_mov_b32_e32 v38, v83
	v_mov_b32_e32 v39, v97
	v_pk_mul_f32 v[120:121], v[4:5], v[102:103]
	v_pk_fma_f32 v[102:103], v[42:43], s[40:41], v[108:109] op_sel_hi:[1,0,1]
	v_pk_add_f32 v[36:37], v[36:37], v[38:39]
	v_mov_b32_e32 v38, v102
	v_pk_add_f32 v[34:35], v[34:35], v[36:37]
	v_pk_mov_b32 v[36:37], v[102:103], v[100:101] op_sel:[1,0]
	v_mov_b32_e32 v39, v101
	v_pk_add_f32 v[36:37], v[36:37], v[38:39]
	v_pk_fma_f32 v[90:91], v[48:49], s[40:41], v[110:111] op_sel_hi:[1,0,1]
	v_pk_fma_f32 v[108:109], v[52:53], s[40:41], v[122:123] op_sel_hi:[1,0,1]
	v_pk_fma_f32 v[110:111], v[50:51], s[40:41], v[120:121] op_sel_hi:[1,0,1]
	v_add_f32_e32 v34, 0, v34
	v_pk_add_f32 v[36:37], v[36:37], v[36:37] op_sel:[0,1] op_sel_hi:[1,0]
	v_add_f32_e32 v34, v34, v35
	v_add_f32_e32 v38, v104, v105
	v_add_f32_e32 v40, v90, v91
	v_mov_b32_e32 v35, v110
	v_mov_b32_e32 v37, v111
	v_mov_b32_e32 v39, v108
	v_mov_b32_e32 v41, v109
	v_pk_add_f32 v[34:35], v[34:35], v[36:37]
	v_pk_add_f32 v[36:37], v[38:39], v[40:41]
	v_mov_b32_e32 v38, v118
	v_pk_add_f32 v[34:35], v[34:35], v[36:37]
	v_pk_mov_b32 v[36:37], v[118:119], v[116:117] op_sel:[1,0]
	v_mov_b32_e32 v39, v117
	v_pk_add_f32 v[36:37], v[36:37], v[38:39]
	v_pk_add_f32 v[34:35], v[34:35], v[34:35] op_sel:[0,1] op_sel_hi:[1,0]
	v_pk_add_f32 v[36:37], v[36:37], v[36:37] op_sel:[0,1] op_sel_hi:[1,0]
	v_add_f32_e32 v38, v126, v127
	v_add_f32_e32 v40, v124, v125
	v_mov_b32_e32 v35, v70
	v_mov_b32_e32 v37, v71
	v_mov_b32_e32 v39, v68
	v_mov_b32_e32 v41, v69
	v_pk_add_f32 v[34:35], v[34:35], v[36:37]
	v_pk_add_f32 v[36:37], v[38:39], v[40:41]
	v_lshl_add_u64 v[112:113], s[0:1], 0, v[32:33]
	v_pk_add_f32 v[34:35], v[34:35], v[36:37]
	v_lshl_add_u64 v[114:115], s[24:25], 0, v[32:33]
	v_add_f32_e32 v34, v34, v35
	ds_bpermute_b32 v35, v73, v34
	global_load_dwordx4 v[92:95], v[112:113], off
	global_load_dwordx4 v[120:123], v[114:115], off
	s_waitcnt lgkmcnt(0)
	v_add_f32_e32 v34, v34, v35
	ds_bpermute_b32 v35, v217, v34
	s_waitcnt lgkmcnt(0)
	v_add_f32_e32 v34, v34, v35
	ds_bpermute_b32 v35, v218, v34
	s_waitcnt lgkmcnt(0)
	v_add_f32_e32 v34, v34, v35
	ds_bpermute_b32 v35, v219, v34
	s_waitcnt lgkmcnt(0)
	v_add_f32_e32 v34, v34, v35
	ds_bpermute_b32 v35, v220, v34
	s_waitcnt lgkmcnt(0)
	v_add_f32_e32 v34, v34, v35
	ds_bpermute_b32 v35, v221, v34
	s_waitcnt lgkmcnt(0)
	v_add_f32_e32 v42, v34, v35
	v_fmamk_f32 v85, v42, 0xba000000, v85
	v_fmamk_f32 v99, v42, 0xba000000, v99
	v_fmamk_f32 v83, v42, 0xba000000, v83
	v_fmac_f32_e32 v84, 0xba000000, v42
	v_fmamk_f32 v97, v42, 0xba000000, v97
	v_fmac_f32_e32 v98, 0xba000000, v42
	v_mov_b32_e32 v36, v85
	v_mov_b32_e32 v37, v99
	v_fmac_f32_e32 v82, 0xba000000, v42
	v_fmac_f32_e32 v96, 0xba000000, v42
	v_mov_b32_e32 v34, v84
	v_mov_b32_e32 v35, v98
	v_pk_mul_f32 v[36:37], v[36:37], v[36:37]
	v_mov_b32_e32 v38, v83
	v_mov_b32_e32 v39, v97
	v_pk_fma_f32 v[34:35], v[34:35], v[34:35], v[36:37]
	v_mov_b32_e32 v36, v82
	v_mov_b32_e32 v37, v96
	v_pk_mul_f32 v[38:39], v[38:39], v[38:39]
	v_fmamk_f32 v103, v42, 0xba000000, v103
	v_pk_fma_f32 v[36:37], v[36:37], v[36:37], v[38:39]
	v_fmac_f32_e32 v102, 0xba000000, v42
	v_pk_add_f32 v[34:35], v[34:35], v[36:37]
	v_fmamk_f32 v101, v42, 0xba000000, v101
	v_fmac_f32_e32 v100, 0xba000000, v42
	v_pk_add_f32 v[34:35], v[34:35], v[34:35] op_sel_hi:[0,1]
	v_pk_mul_f32 v[36:37], v[100:101], v[100:101]
	v_pk_mul_f32 v[38:39], v[102:103], v[102:103]
	v_fmac_f32_e32 v104, 0xba000000, v42
	v_pk_mov_b32 v[40:41], v[38:39], v[36:37] op_sel:[1,0]
	v_mov_b32_e32 v39, v37
	v_fmamk_f32 v105, v42, 0xba000000, v105
	v_fmac_f32_e32 v90, 0xba000000, v42
	v_mul_f32_e32 v34, v104, v104
	v_pk_add_f32 v[36:37], v[40:41], v[38:39]
	v_fmamk_f32 v91, v42, 0xba000000, v91
	v_pk_fma_f32 v[38:39], v[104:105], v[104:105], v[34:35] op_sel_hi:[1,1,0]
	v_mul_f32_e32 v34, v90, v90
	v_pk_add_f32 v[36:37], v[36:37], v[36:37] op_sel_hi:[0,1]
	v_pk_fma_f32 v[40:41], v[90:91], v[90:91], v[34:35] op_sel_hi:[1,1,0]
	v_fmamk_f32 v109, v42, 0xba000000, v109
	v_fmac_f32_e32 v108, 0xba000000, v42
	v_fmamk_f32 v111, v42, 0xba000000, v111
	v_fmac_f32_e32 v110, 0xba000000, v42
	v_mul_f32_e32 v38, v110, v110
	v_mul_f32_e32 v40, v111, v111
	v_mul_f32_e32 v36, v108, v108
	v_mul_f32_e32 v34, v109, v109
	v_pk_add_f32 v[38:39], v[38:39], v[40:41]
	v_pk_add_f32 v[34:35], v[36:37], v[34:35]
	v_fmamk_f32 v119, v42, 0xba000000, v119
	v_pk_add_f32 v[34:35], v[38:39], v[34:35]
	v_fmac_f32_e32 v118, 0xba000000, v42
	v_fmamk_f32 v117, v42, 0xba000000, v117
	v_fmac_f32_e32 v116, 0xba000000, v42
	v_pk_add_f32 v[34:35], v[34:35], v[34:35] op_sel_hi:[0,1]
	v_pk_mul_f32 v[36:37], v[116:117], v[116:117]
	v_pk_mul_f32 v[38:39], v[118:119], v[118:119]
	v_fmac_f32_e32 v126, 0xba000000, v42
	v_pk_mov_b32 v[40:41], v[38:39], v[36:37] op_sel:[1,0]
	v_mov_b32_e32 v39, v37
	v_fmamk_f32 v127, v42, 0xba000000, v127
	v_fmac_f32_e32 v124, 0xba000000, v42
	v_mul_f32_e32 v34, v126, v126
	v_pk_add_f32 v[36:37], v[40:41], v[38:39]
	v_fmamk_f32 v125, v42, 0xba000000, v125
	v_pk_fma_f32 v[38:39], v[126:127], v[126:127], v[34:35] op_sel_hi:[1,1,0]
	v_mul_f32_e32 v34, v124, v124
	v_pk_add_f32 v[36:37], v[36:37], v[36:37] op_sel_hi:[0,1]
	v_pk_fma_f32 v[40:41], v[124:125], v[124:125], v[34:35] op_sel_hi:[1,1,0]
	v_fmamk_f32 v69, v42, 0xba000000, v69
	v_fmac_f32_e32 v68, 0xba000000, v42
	v_fmamk_f32 v71, v42, 0xba000000, v71
	v_fmac_f32_e32 v70, 0xba000000, v42
	v_mul_f32_e32 v38, v70, v70
	v_mul_f32_e32 v40, v71, v71
	v_mul_f32_e32 v36, v68, v68
	v_mul_f32_e32 v34, v69, v69
	v_pk_add_f32 v[38:39], v[38:39], v[40:41]
	v_pk_add_f32 v[34:35], v[36:37], v[34:35]
	s_nop 0
	v_pk_add_f32 v[34:35], v[38:39], v[34:35]
	s_nop 0
	v_add_f32_e32 v34, v34, v35
	ds_bpermute_b32 v35, v73, v34
	s_waitcnt lgkmcnt(0)
; #define GAS __attribute__((address_space(1)))
; __device__ __forceinline__ unsigned pk2(float lo, float hi) { return f2bf(lo) | (f2bf(hi) << 16); }
; __device__ __forceinline__ unsigned pk4_fp8(float a, float b, float c, float d) { int r = __builtin_amdgcn_cvt_pk_fp8_f32(a, b, 0, false); r = __builtin_amdgcn_cvt_pk_fp8_f32(c, d, r, true); return (unsigned)r; }
; __device__ __forceinline__ f32x4 bf4(unsigned a, unsigned b) { return (f32x4){bflo(a), bfhi(a), bflo(b), bfhi(b)}; }
; template <int l>
; __device__ __forceinline__ void layer_phases(Frame& F, const XcdBarrier& bar, const int lo, const int hi) {
;     ...
;                         f32x4 xv; if (l == 0) xv = __builtin_nontemporal_load((const GAS f32x4*)(xin + off)); else { const v2u xw_ = __builtin_nontemporal_load((const GAS v2u*)(xinb + off)); xv = bf4(xw_.x, xw_.y); } const v2u mw = __builtin_nontemporal_load((const GAS v2u*)(mixb + off)); const f32x4 gv = *(const GAS f32x4*)(mrow + 4096 + 4 * lq + 256 * j);
;                         vv[rr][j] = xv * ALPHA + gv * (f32x4){bflo(mw.x), bfhi(mw.x), bflo(mw.y), bfhi(mw.y)}; }
; #pragma unroll
;                 for (int rq = 0; rq < 2; ++rq) { const int rr = 2 * rp + rq, m = m0 + rr, rloc = 4 * F.wave + rr;
;                     f32x4 (&v)[8] = vv[rq]; float s = 0.f;
; #pragma unroll
;                     for (int j = 0; j < 8; ++j) s += (v[j].x + v[j].y) + (v[j].z + v[j].w);
;                     const float mean = wave_sum(s) * (1.f / D); float s2 = 0.f;
; #pragma unroll
;                     for (int j = 0; j < 8; ++j) { v[j] = v[j] - mean; s2 += (v[j].x * v[j].x + v[j].y * v[j].y) + (v[j].z * v[j].z + v[j].w * v[j].w); }
;                     const float rstd = 1.f / sqrtf(wave_sum(s2) * (1.f / D) + LN_EPS);
; #pragma unroll
;                     for (int j = 0; j < 8; ++j) { const int k = 4 * lq + 256 * j;
;                         const f32x4 xv = v[j] * rstd * *(const GAS f32x4*)(g1 + k) + *(const GAS f32x4*)(b1 + k);
;                         { v2u xo; xo.x = pk2(xv.x, xv.y); xo.y = pk2(xv.z, xv.w); *(GAS v2u*)(x1 + (size_t)m * D + k) = xo; }
;                         const f32x4 hv = xv * (*(const GAS f32x4*)(mrow + 8192 + k) + 1.0f) + *(const GAS f32x4*)(mrow + 6144 + k);
;                         v2u o; o.x = pk2(hv.x, hv.y); o.y = pk2(hv.z, hv.w);
;                         *(GAS unsigned*)(h2q + (size_t)m * D + k) = pk4_fp8(hv.x, hv.y, hv.z, hv.w);
	v_add_f32_e32 v32, v34, v35
	ds_bpermute_b32 v33, v217, v32
	s_waitcnt lgkmcnt(0)
	v_add_f32_e32 v36, v32, v33
	ds_bpermute_b32 v37, v218, v36
	v_lshl_add_u64 v[32:33], s[16:17], 0, v[86:87]
	v_lshl_add_u64 v[34:35], v[32:33], 2, s[20:21]
	v_lshl_add_u64 v[106:107], v[32:33], 1, s[26:27]
	global_load_dwordx4 v[60:63], v[34:35], off nt
	global_load_dwordx4 v[56:59], v[34:35], off offset:1024 nt
	global_load_dwordx4 v[48:51], v[34:35], off offset:2048 nt
	global_load_dwordx4 v[40:43], v[34:35], off offset:3072 nt
	s_waitcnt lgkmcnt(0)
	v_add_f32_e32 v32, v36, v37
	ds_bpermute_b32 v33, v219, v32
	global_load_dwordx2 v[140:141], v[106:107], off nt
	global_load_dwordx2 v[138:139], v[106:107], off offset:512 nt
	global_load_dwordx2 v[136:137], v[106:107], off offset:1024 nt
	global_load_dwordx2 v[132:133], v[106:107], off offset:1536 nt
	s_waitcnt lgkmcnt(0)
	v_add_f32_e32 v32, v32, v33
	ds_bpermute_b32 v33, v220, v32
	s_waitcnt lgkmcnt(0)
	v_add_f32_e32 v36, v32, v33
	ds_bpermute_b32 v37, v221, v36
	v_add_co_u32_e32 v32, vcc, s87, v34
	s_waitcnt lgkmcnt(0)
	v_add_f32_e32 v34, v36, v37
	v_addc_co_u32_e32 v33, vcc, 0, v35, vcc
	v_fmamk_f32 v34, v34, 0x3a000000, v223
	v_mul_f32_e32 v35, 0x4f800000, v34
	v_cmp_gt_f32_e32 vcc, s89, v34
	s_waitcnt vmcnt(3)
	v_and_b32_e32 v159, 0xffff0000, v140
	v_cndmask_b32_e32 v80, v34, v35, vcc
	v_sqrt_f32_e32 v128, v80
	global_load_dwordx4 v[52:55], v[32:33], off nt
	global_load_dwordx4 v[44:47], v[32:33], off offset:1024 nt
	global_load_dwordx4 v[36:39], v[32:33], off offset:2048 nt
	s_nop 0
	global_load_dwordx4 v[32:35], v[32:33], off offset:3072 nt
	s_nop 0
	global_load_dwordx2 v[148:149], v[106:107], off offset:2048 nt
	global_load_dwordx2 v[146:147], v[106:107], off offset:2560 nt
	global_load_dwordx2 v[144:145], v[106:107], off offset:3072 nt
	global_load_dwordx2 v[142:143], v[106:107], off offset:3584 nt
	s_waitcnt vmcnt(10)
	v_lshlrev_b32_e32 v160, 16, v138
	v_add_u32_e32 v129, -1, v128
	v_fma_f32 v130, -v129, v128, v80
	v_cmp_ge_f32_e64 s[14:15], 0, v130
	v_add_u32_e32 v130, 1, v128
	v_and_b32_e32 v161, 0xffff0000, v138
	v_cndmask_b32_e64 v129, v128, v129, s[14:15]
	v_fma_f32 v128, -v130, v128, v80
	v_cmp_lt_f32_e64 s[14:15], 0, v128
	v_lshlrev_b32_e32 v138, 16, v139
	v_and_b32_e32 v139, 0xffff0000, v139
	v_cndmask_b32_e64 v128, v129, v130, s[14:15]
	v_mul_f32_e32 v129, 0x37800000, v128
	v_cndmask_b32_e32 v128, v128, v129, vcc
	v_cmp_class_f32_e32 vcc, v80, v224
	s_waitcnt vmcnt(9)
	v_lshlrev_b32_e32 v162, 16, v136
	v_and_b32_e32 v163, 0xffff0000, v136
	v_cndmask_b32_e32 v80, v128, v80, vcc
	v_div_scale_f32 v128, s[0:1], v80, v80, 1.0
	v_rcp_f32_e32 v129, v128
	s_lshl_b64 s[0:1], s[42:43], 12
	s_add_u32 s0, s3, s0
	s_addc_u32 s1, s41, s1
	v_fma_f32 v106, -v128, v129, 1.0
	v_fmac_f32_e32 v129, v106, v129
	v_div_scale_f32 v106, vcc, 1.0, v80, 1.0
	v_mul_f32_e32 v107, v106, v129
	v_fma_f32 v130, -v128, v107, v106
	v_fmac_f32_e32 v107, v130, v129
	v_fma_f32 v106, -v128, v107, v106
	v_div_fmas_f32 v106, v106, v129, v107
	v_div_fixup_f32 v80, v106, v80, 1.0
	v_pk_mul_f32 v[84:85], v[84:85], v[80:81] op_sel_hi:[1,0]
	v_pk_mul_f32 v[82:83], v[82:83], v[80:81] op_sel_hi:[1,0]
	v_pk_fma_f32 v[134:135], v[92:93], v[84:85], v[120:121]
	v_pk_fma_f32 v[106:107], v[94:95], v[82:83], v[122:123]
	v_bfe_u32 v82, v134, 16, 1
	v_add3_u32 v82, v134, v82, s90
	v_bfe_u32 v83, v135, 16, 1
	v_lshrrev_b32_e32 v82, 16, v82
	v_add3_u32 v83, v135, v83, s90
	v_and_or_b32 v82, v83, s86, v82
	v_bfe_u32 v83, v106, 16, 1
	v_add3_u32 v83, v106, v83, s90
	v_bfe_u32 v84, v107, 16, 1
	v_lshrrev_b32_e32 v83, 16, v83
	v_add3_u32 v84, v107, v84, s90
	v_lshlrev_b64 v[128:129], 1, v[86:87]
	v_and_or_b32 v83, v84, s86, v83
	v_lshl_add_u64 v[130:131], s[0:1], 0, v[128:129]
	global_store_dwordx2 v[130:131], v[82:83], off
	v_add_co_u32_e32 v82, vcc, s23, v88
	s_add_u32 s0, s50, s18
	s_nop 0
	v_addc_co_u32_e32 v83, vcc, 0, v89, vcc
	v_add_co_u32_e32 v84, vcc, s28, v88
	s_addc_u32 s1, s51, s19
	s_nop 0
	v_addc_co_u32_e32 v85, vcc, 0, v89, vcc
	global_load_dwordx4 v[92:95], v[82:83], off offset:-4096
	global_load_dwordx4 v[120:123], v[84:85], off offset:-4096
	v_pk_mul_f32 v[96:97], v[96:97], v[80:81] op_sel_hi:[1,0]
	v_pk_mul_f32 v[100:101], v[100:101], v[80:81] op_sel_hi:[1,0]
	v_pk_mul_f32 v[90:91], v[90:91], v[80:81] op_sel_hi:[1,0]
	v_pk_mul_f32 v[110:111], v[110:111], v[80:81] op_sel_hi:[1,0]
	v_pk_mul_f32 v[108:109], v[108:109], v[80:81] op_sel_hi:[1,0]
	v_pk_mul_f32 v[118:119], v[118:119], v[80:81] op_sel_hi:[1,0]
	v_pk_mul_f32 v[116:117], v[116:117], v[80:81] op_sel_hi:[1,0]
	v_pk_mul_f32 v[126:127], v[126:127], v[80:81] op_sel_hi:[1,0]
	v_pk_mul_f32 v[124:125], v[124:125], v[80:81] op_sel_hi:[1,0]
	v_lshlrev_b32_e32 v136, 16, v137
	v_and_b32_e32 v137, 0xffff0000, v137
	s_waitcnt vmcnt(11)
	v_lshlrev_b32_e32 v164, 16, v132
	v_and_b32_e32 v165, 0xffff0000, v132
	v_lshlrev_b32_e32 v132, 16, v133
	v_and_b32_e32 v133, 0xffff0000, v133
	s_waitcnt vmcnt(3)
; #define GAS __attribute__((address_space(1)))
; #define LAS __attribute__((address_space(3)))
; __device__ __forceinline__ unsigned pk2(float lo, float hi) { return f2bf(lo) | (f2bf(hi) << 16); }
; __device__ __forceinline__ unsigned pk4_fp8(float a, float b, float c, float d) { int r = __builtin_amdgcn_cvt_pk_fp8_f32(a, b, 0, false); r = __builtin_amdgcn_cvt_pk_fp8_f32(c, d, r, true); return (unsigned)r; }
; template <int l>
; __device__ __forceinline__ void layer_phases(Frame& F, const XcdBarrier& bar, const int lo, const int hi) {
;     ...
; #pragma unroll
;                     for (int j = 0; j < 8; ++j) { const int k = 4 * lq + 256 * j;
;                         const f32x4 xv = v[j] * rstd * *(const GAS f32x4*)(g1 + k) + *(const GAS f32x4*)(b1 + k);
;                         { v2u xo; xo.x = pk2(xv.x, xv.y); xo.y = pk2(xv.z, xv.w); *(GAS v2u*)(x1 + (size_t)m * D + k) = xo; }
;                         const f32x4 hv = xv * (*(const GAS f32x4*)(mrow + 8192 + k) + 1.0f) + *(const GAS f32x4*)(mrow + 6144 + k);
;                         v2u o; o.x = pk2(hv.x, hv.y); o.y = pk2(hv.z, hv.w);
;                         *(GAS unsigned*)(h2q + (size_t)m * D + k) = pk4_fp8(hv.x, hv.y, hv.z, hv.w);
;                         const int chunk = (lq >> 1) + 32 * j;
;                         *(LAS v2u*)(h2s + rloc * 4096 + ((chunk ^ (rloc & 15)) << 4) + (lq & 1) * 8) = o; }
	v_lshlrev_b32_e32 v172, 16, v142
	v_and_b32_e32 v173, 0xffff0000, v142
	v_lshlrev_b32_e32 v142, 16, v143
	v_and_b32_e32 v143, 0xffff0000, v143
	v_pk_mul_f32 v[142:143], v[30:31], v[142:143]
	v_lshlrev_b32_e32 v168, 16, v146
	v_and_b32_e32 v169, 0xffff0000, v146
	v_lshlrev_b32_e32 v146, 16, v147
	v_and_b32_e32 v147, 0xffff0000, v147
	v_lshlrev_b32_e32 v170, 16, v144
	v_and_b32_e32 v171, 0xffff0000, v144
	v_lshlrev_b32_e32 v144, 16, v145
	v_and_b32_e32 v145, 0xffff0000, v145
	v_pk_mul_f32 v[18:19], v[18:19], v[138:139]
	v_pk_mul_f32 v[16:17], v[16:17], v[160:161]
	v_pk_mul_f32 v[14:15], v[14:15], v[136:137]
	v_pk_mul_f32 v[10:11], v[10:11], v[132:133]
	v_pk_mul_f32 v[8:9], v[8:9], v[164:165]
	v_pk_mul_f32 v[132:133], v[20:21], v[168:169]
	v_pk_mul_f32 v[136:137], v[22:23], v[146:147]
	v_pk_mul_f32 v[138:139], v[24:25], v[170:171]
	v_pk_fma_f32 v[24:25], v[58:59], s[40:41], v[18:19] op_sel_hi:[1,0,1]
	v_pk_fma_f32 v[18:19], v[40:41], s[40:41], v[8:9] op_sel_hi:[1,0,1]
	v_pk_fma_f32 v[8:9], v[46:47], s[40:41], v[136:137] op_sel_hi:[1,0,1]
	v_lshlrev_b32_e32 v166, 16, v148
	v_and_b32_e32 v167, 0xffff0000, v148
	v_lshlrev_b32_e32 v148, 16, v149
	v_and_b32_e32 v149, 0xffff0000, v149
	v_pk_mul_f32 v[12:13], v[12:13], v[162:163]
	v_pk_mul_f32 v[4:5], v[4:5], v[166:167]
	v_pk_mul_f32 v[6:7], v[6:7], v[148:149]
	v_pk_fma_f32 v[20:21], v[50:51], s[40:41], v[14:15] op_sel_hi:[1,0,1]
	v_pk_fma_f32 v[22:23], v[48:49], s[40:41], v[12:13] op_sel_hi:[1,0,1]
	v_pk_fma_f32 v[12:13], v[54:55], s[40:41], v[6:7] op_sel_hi:[1,0,1]
	v_pk_fma_f32 v[14:15], v[52:53], s[40:41], v[4:5] op_sel_hi:[1,0,1]
	v_pk_fma_f32 v[6:7], v[36:37], s[40:41], v[138:139] op_sel_hi:[1,0,1]
	v_mov_b32_e32 v37, v24
	v_pk_mov_b32 v[48:49], v[22:23], v[20:21] op_sel:[1,0]
	v_mov_b32_e32 v50, v22
	v_mov_b32_e32 v51, v21
	v_add_f32_e32 v52, v18, v19
	v_mov_b32_e32 v53, v12
	v_mov_b32_e32 v55, v13
	s_waitcnt vmcnt(1)
	v_pk_add_f32 v[92:93], v[92:93], 1.0 op_sel_hi:[1,0]
	s_waitcnt vmcnt(0)
	v_pk_fma_f32 v[92:93], v[92:93], v[134:135], v[120:121]
	v_mov_b32_e32 v120, 0
	v_cvt_pk_fp8_f32 v120, v92, v93
	v_pk_add_f32 v[94:95], v[94:95], 1.0 op_sel_hi:[1,0]
	v_lshl_add_u64 v[134:135], s[0:1], 0, v[86:87]
	v_pk_fma_f32 v[94:95], v[94:95], v[106:107], v[122:123]
	s_mov_b64 s[0:1], 0x8000
	v_cvt_pk_fp8_f32 v120, v94, v95 op_sel:[0,0,1]
	v_lshl_add_u64 v[122:123], v[88:89], 0, s[0:1]
	s_mov_b64 s[0:1], 0x6000
	global_store_dword v[134:135], v120, off
	global_load_dwordx4 v[150:153], v[112:113], off offset:1024
	global_load_dwordx4 v[154:157], v[114:115], off offset:1024
	v_lshl_add_u64 v[120:121], v[88:89], 0, s[0:1]
	v_pk_mul_f32 v[88:89], v[98:99], v[80:81] op_sel_hi:[1,0]
	s_lshl_b64 s[0:1], s[44:45], 12
	s_add_u32 s0, s3, s0
	s_addc_u32 s1, s41, s1
	s_waitcnt vmcnt(0)
	v_pk_fma_f32 v[106:107], v[152:153], v[96:97], v[156:157]
	v_pk_fma_f32 v[88:89], v[150:151], v[88:89], v[154:155]
	v_bfe_u32 v98, v106, 16, 1
	v_bfe_u32 v96, v88, 16, 1
	v_bfe_u32 v97, v89, 16, 1
	v_bfe_u32 v99, v107, 16, 1
	v_add3_u32 v96, v88, v96, s90
	v_add3_u32 v98, v106, v98, s90
	v_add3_u32 v97, v89, v97, s90
	v_add3_u32 v99, v107, v99, s90
	v_lshrrev_b32_e32 v96, 16, v96
	v_lshrrev_b32_e32 v98, 16, v98
	v_and_or_b32 v96, v97, s86, v96
	v_and_or_b32 v97, v99, s86, v98
	global_store_dwordx2 v[130:131], v[96:97], off offset:512
	global_load_dwordx4 v[96:99], v[122:123], off offset:1024
	s_nop 0
	global_load_dwordx4 v[150:153], v[120:121], off offset:1024
	v_mov_b32_e32 v154, 0
	s_waitcnt vmcnt(1)
	v_pk_add_f32 v[96:97], v[96:97], 1.0 op_sel_hi:[1,0]
	s_waitcnt vmcnt(0)
	v_pk_fma_f32 v[96:97], v[96:97], v[88:89], v[150:151]
	v_pk_add_f32 v[88:89], v[98:99], 1.0 op_sel_hi:[1,0]
	v_cvt_pk_fp8_f32 v154, v96, v97
	v_pk_fma_f32 v[98:99], v[88:89], v[106:107], v[152:153]
	v_pk_mul_f32 v[88:89], v[102:103], v[80:81] op_sel_hi:[1,0]
	v_cvt_pk_fp8_f32 v154, v98, v99 op_sel:[0,0,1]
	global_store_dword v[134:135], v154, off offset:256
	global_load_dwordx4 v[150:153], v[112:113], off offset:2048
	s_nop 0
	global_load_dwordx4 v[154:157], v[114:115], off offset:2048
	s_waitcnt vmcnt(0)
	v_pk_fma_f32 v[106:107], v[152:153], v[100:101], v[156:157]
	v_pk_fma_f32 v[88:89], v[150:151], v[88:89], v[154:155]
	v_bfe_u32 v102, v106, 16, 1
	v_bfe_u32 v100, v88, 16, 1
	v_bfe_u32 v101, v89, 16, 1
	v_bfe_u32 v103, v107, 16, 1
	v_add3_u32 v100, v88, v100, s90
	v_add3_u32 v102, v106, v102, s90
	v_add3_u32 v101, v89, v101, s90
	v_add3_u32 v103, v107, v103, s90
	v_lshrrev_b32_e32 v100, 16, v100
	v_lshrrev_b32_e32 v102, 16, v102
	v_and_or_b32 v100, v101, s86, v100
	v_and_or_b32 v101, v103, s86, v102
	global_store_dwordx2 v[130:131], v[100:101], off offset:1024
	global_load_dwordx4 v[100:103], v[122:123], off offset:2048
	s_nop 0
	global_load_dwordx4 v[150:153], v[120:121], off offset:2048
	v_mov_b32_e32 v154, 0
	s_waitcnt vmcnt(1)
	v_pk_add_f32 v[100:101], v[100:101], 1.0 op_sel_hi:[1,0]
	s_waitcnt vmcnt(0)
	v_pk_fma_f32 v[100:101], v[100:101], v[88:89], v[150:151]
	v_pk_add_f32 v[88:89], v[102:103], 1.0 op_sel_hi:[1,0]
	v_cvt_pk_fp8_f32 v154, v100, v101
	v_pk_fma_f32 v[102:103], v[88:89], v[106:107], v[152:153]
	v_pk_mul_f32 v[88:89], v[104:105], v[80:81] op_sel_hi:[1,0]
	v_cvt_pk_fp8_f32 v154, v102, v103 op_sel:[0,0,1]
	global_store_dword v[134:135], v154, off offset:512
	global_load_dwordx4 v[150:153], v[112:113], off offset:3072
	s_nop 0
	global_load_dwordx4 v[154:157], v[114:115], off offset:3072
	s_waitcnt vmcnt(0)
; #define GAS __attribute__((address_space(1)))
; #define LAS __attribute__((address_space(3)))
; __device__ __forceinline__ unsigned pk2(float lo, float hi) { return f2bf(lo) | (f2bf(hi) << 16); }
; __device__ __forceinline__ unsigned pk4_fp8(float a, float b, float c, float d) { int r = __builtin_amdgcn_cvt_pk_fp8_f32(a, b, 0, false); r = __builtin_amdgcn_cvt_pk_fp8_f32(c, d, r, true); return (unsigned)r; }
; __device__ __forceinline__ f32x4 bf4(unsigned a, unsigned b) { return (f32x4){bflo(a), bfhi(a), bflo(b), bfhi(b)}; }
; template <int l>
; __device__ __forceinline__ void layer_phases(Frame& F, const XcdBarrier& bar, const int lo, const int hi) {
;     ...
;                     for (int j = 0; j < 8; ++j) { const size_t off = (size_t)(m0 + 2 * rp + rr) * D + 4 * lq + 256 * j;
;                         f32x4 xv; if (l == 0) xv = __builtin_nontemporal_load((const GAS f32x4*)(xin + off)); else { const v2u xw_ = __builtin_nontemporal_load((const GAS v2u*)(xinb + off)); xv = bf4(xw_.x, xw_.y); } const v2u mw = __builtin_nontemporal_load((const GAS v2u*)(mixb + off)); const f32x4 gv = *(const GAS f32x4*)(mrow + 4096 + 4 * lq + 256 * j);
;                         vv[rr][j] = xv * ALPHA + gv * (f32x4){bflo(mw.x), bfhi(mw.x), bflo(mw.y), bfhi(mw.y)}; }
;     ...
; #pragma unroll
;                     for (int j = 0; j < 8; ++j) { const int k = 4 * lq + 256 * j;
;                         const f32x4 xv = v[j] * rstd * *(const GAS f32x4*)(g1 + k) + *(const GAS f32x4*)(b1 + k);
;                         { v2u xo; xo.x = pk2(xv.x, xv.y); xo.y = pk2(xv.z, xv.w); *(GAS v2u*)(x1 + (size_t)m * D + k) = xo; }
;                         const f32x4 hv = xv * (*(const GAS f32x4*)(mrow + 8192 + k) + 1.0f) + *(const GAS f32x4*)(mrow + 6144 + k);
;                         v2u o; o.x = pk2(hv.x, hv.y); o.y = pk2(hv.z, hv.w);
;                         *(GAS unsigned*)(h2q + (size_t)m * D + k) = pk4_fp8(hv.x, hv.y, hv.z, hv.w);
;                         const int chunk = (lq >> 1) + 32 * j;
;                         *(LAS v2u*)(h2s + rloc * 4096 + ((chunk ^ (rloc & 15)) << 4) + (lq & 1) * 8) = o; }
	v_pk_fma_f32 v[152:153], v[90:91], v[152:153], v[156:157]
	v_pk_fma_f32 v[150:151], v[88:89], v[150:151], v[154:155]
	v_bfe_u32 v90, v152, 16, 1
	v_bfe_u32 v88, v150, 16, 1
	v_bfe_u32 v89, v151, 16, 1
	v_bfe_u32 v91, v153, 16, 1
	v_add3_u32 v88, v150, v88, s90
	v_add3_u32 v90, v152, v90, s90
	v_add3_u32 v89, v151, v89, s90
	v_add3_u32 v91, v153, v91, s90
	v_lshrrev_b32_e32 v88, 16, v88
	v_lshrrev_b32_e32 v90, 16, v90
	v_and_or_b32 v88, v89, s86, v88
	v_and_or_b32 v89, v91, s86, v90
	global_store_dwordx2 v[130:131], v[88:89], off offset:1536
	global_load_dwordx4 v[88:91], v[122:123], off offset:3072
	s_nop 0
	global_load_dwordx4 v[104:107], v[120:121], off offset:3072
	v_mov_b32_e32 v154, 0
	s_waitcnt vmcnt(1)
	v_pk_add_f32 v[88:89], v[88:89], 1.0 op_sel_hi:[1,0]
	s_waitcnt vmcnt(0)
	v_pk_fma_f32 v[104:105], v[150:151], v[88:89], v[104:105]
	v_pk_add_f32 v[90:91], v[90:91], 1.0 op_sel_hi:[1,0]
	v_cvt_pk_fp8_f32 v154, v104, v105
	v_pk_fma_f32 v[106:107], v[152:153], v[90:91], v[106:107]
	v_add_co_u32_e32 v88, vcc, s87, v112
	v_cvt_pk_fp8_f32 v154, v106, v107 op_sel:[0,0,1]
	s_nop 0
	v_addc_co_u32_e32 v89, vcc, 0, v113, vcc
	v_add_co_u32_e32 v90, vcc, s87, v114
	global_store_dword v[134:135], v154, off offset:768
	s_nop 0
	v_addc_co_u32_e32 v91, vcc, 0, v115, vcc
	global_load_dwordx4 v[150:153], v[88:89], off
	global_load_dwordx4 v[154:157], v[90:91], off
	s_waitcnt vmcnt(0)
	v_pk_fma_f32 v[156:157], v[108:109], v[152:153], v[156:157]
	v_pk_fma_f32 v[154:155], v[110:111], v[150:151], v[154:155]
	v_bfe_u32 v110, v156, 16, 1
	v_bfe_u32 v108, v154, 16, 1
	v_bfe_u32 v109, v155, 16, 1
	v_bfe_u32 v111, v157, 16, 1
	v_add3_u32 v108, v154, v108, s90
	v_add3_u32 v110, v156, v110, s90
	v_add3_u32 v109, v155, v109, s90
	v_add3_u32 v111, v157, v111, s90
	v_lshrrev_b32_e32 v108, 16, v108
	v_lshrrev_b32_e32 v110, 16, v110
	v_and_or_b32 v108, v109, s86, v108
	v_and_or_b32 v109, v111, s86, v110
	global_store_dwordx2 v[130:131], v[108:109], off offset:2048
	global_load_dwordx4 v[108:111], v[82:83], off
	s_nop 0
	global_load_dwordx4 v[150:153], v[84:85], off
	s_waitcnt vmcnt(1)
	v_pk_add_f32 v[108:109], v[108:109], 1.0 op_sel_hi:[1,0]
	s_waitcnt vmcnt(0)
	v_pk_fma_f32 v[108:109], v[154:155], v[108:109], v[150:151]
	v_pk_add_f32 v[110:111], v[110:111], 1.0 op_sel_hi:[1,0]
	v_cvt_pk_fp8_f32 v158, v108, v109
	v_pk_fma_f32 v[110:111], v[156:157], v[110:111], v[152:153]
	s_nop 0
	v_cvt_pk_fp8_f32 v158, v110, v111 op_sel:[0,0,1]
	global_store_dword v[134:135], v158, off offset:1024
	global_load_dwordx4 v[150:153], v[88:89], off offset:1024
	global_load_dwordx4 v[154:157], v[90:91], off offset:1024
	v_mov_b32_e32 v158, 0
	s_waitcnt vmcnt(0)
	v_pk_fma_f32 v[156:157], v[116:117], v[152:153], v[156:157]
	v_pk_fma_f32 v[154:155], v[118:119], v[150:151], v[154:155]
	v_bfe_u32 v118, v156, 16, 1
	v_bfe_u32 v116, v154, 16, 1
	v_bfe_u32 v117, v155, 16, 1
	v_bfe_u32 v119, v157, 16, 1
	v_add3_u32 v116, v154, v116, s90
	v_add3_u32 v118, v156, v118, s90
	v_add3_u32 v117, v155, v117, s90
	v_add3_u32 v119, v157, v119, s90
	v_lshrrev_b32_e32 v116, 16, v116
	v_lshrrev_b32_e32 v118, 16, v118
	v_and_or_b32 v116, v117, s86, v116
	v_and_or_b32 v117, v119, s86, v118
	global_store_dwordx2 v[130:131], v[116:117], off offset:2560
	global_load_dwordx4 v[116:119], v[82:83], off offset:1024
	s_nop 0
	global_load_dwordx4 v[150:153], v[84:85], off offset:1024
	s_waitcnt vmcnt(1)
	v_pk_add_f32 v[116:117], v[116:117], 1.0 op_sel_hi:[1,0]
	s_waitcnt vmcnt(0)
	v_pk_fma_f32 v[116:117], v[154:155], v[116:117], v[150:151]
	v_pk_add_f32 v[118:119], v[118:119], 1.0 op_sel_hi:[1,0]
	v_cvt_pk_fp8_f32 v158, v116, v117
	v_pk_fma_f32 v[118:119], v[156:157], v[118:119], v[152:153]
	s_nop 0
	v_cvt_pk_fp8_f32 v158, v118, v119 op_sel:[0,0,1]
	global_store_dword v[134:135], v158, off offset:1280
	global_load_dwordx4 v[150:153], v[88:89], off offset:2048
	global_load_dwordx4 v[154:157], v[90:91], off offset:2048
	v_lshlrev_b32_e32 v158, 16, v140
	v_pk_mul_f32 v[0:1], v[0:1], v[158:159]
	v_lshlrev_b32_e32 v140, 16, v141
	v_pk_fma_f32 v[30:31], v[60:61], s[40:41], v[0:1] op_sel_hi:[1,0,1]
	v_and_b32_e32 v141, 0xffff0000, v141
	v_pk_mul_f32 v[2:3], v[2:3], v[140:141]
	v_pk_mul_f32 v[140:141], v[26:27], v[144:145]
	v_pk_fma_f32 v[26:27], v[56:57], s[40:41], v[16:17] op_sel_hi:[1,0,1]
	v_pk_fma_f32 v[16:17], v[42:43], s[40:41], v[10:11] op_sel_hi:[1,0,1]
	v_pk_fma_f32 v[10:11], v[44:45], s[40:41], v[132:133] op_sel_hi:[1,0,1]
	v_pk_mul_f32 v[144:145], v[28:29], v[172:173]
	v_pk_fma_f32 v[28:29], v[62:63], s[40:41], v[2:3] op_sel_hi:[1,0,1]
	v_pk_fma_f32 v[4:5], v[38:39], s[40:41], v[140:141] op_sel_hi:[1,0,1]
	v_pk_fma_f32 v[2:3], v[32:33], s[40:41], v[144:145] op_sel_hi:[1,0,1]
	v_mov_b32_e32 v32, v30
	v_mov_b32_e32 v33, v26
	v_mov_b32_e32 v36, v28
	v_mov_b32_e32 v38, v29
	v_mov_b32_e32 v39, v25
	v_add_f32_e32 v54, v16, v17
	v_mov_b32_e32 v57, v14
	v_pk_mov_b32 v[58:59], v[10:11], v[8:9] op_sel:[1,0]
	v_mov_b32_e32 v60, v10
	v_mov_b32_e32 v61, v9
	v_add_f32_e32 v62, v6, v7
	v_add_f32_e32 v132, v4, v5
	s_waitcnt vmcnt(0)
	v_pk_fma_f32 v[156:157], v[124:125], v[152:153], v[156:157]
	v_pk_fma_f32 v[154:155], v[126:127], v[150:151], v[154:155]
	v_bfe_u32 v126, v156, 16, 1
	v_bfe_u32 v124, v154, 16, 1
	v_bfe_u32 v125, v155, 16, 1
	v_bfe_u32 v127, v157, 16, 1
	v_add3_u32 v124, v154, v124, s90
	v_add3_u32 v126, v156, v126, s90
	v_add3_u32 v125, v155, v125, s90
	v_add3_u32 v127, v157, v127, s90
	v_lshrrev_b32_e32 v124, 16, v124
	v_lshrrev_b32_e32 v126, 16, v126
	v_and_or_b32 v124, v125, s86, v124
	v_and_or_b32 v125, v127, s86, v126
	global_store_dwordx2 v[130:131], v[124:125], off offset:3072
	global_load_dwordx4 v[124:127], v[82:83], off offset:2048
	s_nop 0
	global_load_dwordx4 v[150:153], v[84:85], off offset:2048
	s_waitcnt vmcnt(1)
; #define GAS __attribute__((address_space(1)))
; #define LAS __attribute__((address_space(3)))
; __device__ __forceinline__ unsigned pk2(float lo, float hi) { return f2bf(lo) | (f2bf(hi) << 16); }
; __device__ __forceinline__ unsigned pk4_fp8(float a, float b, float c, float d) { int r = __builtin_amdgcn_cvt_pk_fp8_f32(a, b, 0, false); r = __builtin_amdgcn_cvt_pk_fp8_f32(c, d, r, true); return (unsigned)r; }
; template <int l>
; __device__ __forceinline__ void layer_phases(Frame& F, const XcdBarrier& bar, const int lo, const int hi) {
;     ...
;                 for (int rq = 0; rq < 2; ++rq) { const int rr = 2 * rp + rq, m = m0 + rr, rloc = 4 * F.wave + rr;
;                     f32x4 (&v)[8] = vv[rq]; float s = 0.f;
; #pragma unroll
;                     for (int j = 0; j < 8; ++j) s += (v[j].x + v[j].y) + (v[j].z + v[j].w);
;                     const float mean = wave_sum(s) * (1.f / D); float s2 = 0.f;
; #pragma unroll
;                     for (int j = 0; j < 8; ++j) { v[j] = v[j] - mean; s2 += (v[j].x * v[j].x + v[j].y * v[j].y) + (v[j].z * v[j].z + v[j].w * v[j].w); }
;                     const float rstd = 1.f / sqrtf(wave_sum(s2) * (1.f / D) + LN_EPS);
; #pragma unroll
;                     for (int j = 0; j < 8; ++j) { const int k = 4 * lq + 256 * j;
;                         const f32x4 xv = v[j] * rstd * *(const GAS f32x4*)(g1 + k) + *(const GAS f32x4*)(b1 + k);
;                         { v2u xo; xo.x = pk2(xv.x, xv.y); xo.y = pk2(xv.z, xv.w); *(GAS v2u*)(x1 + (size_t)m * D + k) = xo; }
;                         const f32x4 hv = xv * (*(const GAS f32x4*)(mrow + 8192 + k) + 1.0f) + *(const GAS f32x4*)(mrow + 6144 + k);
;                         v2u o; o.x = pk2(hv.x, hv.y); o.y = pk2(hv.z, hv.w);
;                         *(GAS unsigned*)(h2q + (size_t)m * D + k) = pk4_fp8(hv.x, hv.y, hv.z, hv.w);
;                         const int chunk = (lq >> 1) + 32 * j;
;                         *(LAS v2u*)(h2s + rloc * 4096 + ((chunk ^ (rloc & 15)) << 4) + (lq & 1) * 8) = o; }
	v_pk_add_f32 v[0:1], v[124:125], 1.0 op_sel_hi:[1,0]
	s_waitcnt vmcnt(0)
	v_pk_fma_f32 v[124:125], v[154:155], v[0:1], v[150:151]
	v_pk_add_f32 v[0:1], v[126:127], 1.0 op_sel_hi:[1,0]
	v_cvt_pk_fp8_f32 v174, v124, v125
	v_pk_fma_f32 v[126:127], v[156:157], v[0:1], v[152:153]
	v_pk_fma_f32 v[0:1], v[34:35], s[40:41], v[142:143] op_sel_hi:[1,0,1]
	v_mov_b32_e32 v34, v31
	v_cvt_pk_fp8_f32 v174, v126, v127 op_sel:[0,0,1]
	v_mov_b32_e32 v35, v27
	v_pk_add_f32 v[32:33], v[32:33], v[34:35]
	v_pk_add_f32 v[34:35], v[36:37], v[38:39]
	global_store_dword v[134:135], v174, off offset:1536
	global_load_dwordx4 v[40:43], v[88:89], off offset:3072
	global_load_dwordx4 v[44:47], v[90:91], off offset:3072
	v_pk_add_f32 v[36:37], v[48:49], v[50:51]
	v_pk_add_f32 v[32:33], v[32:33], v[34:35]
	v_pk_add_f32 v[34:35], v[36:37], v[36:37] op_sel:[0,1] op_sel_hi:[1,0]
	v_add_f32_e32 v32, 0, v32
	v_mov_b32_e32 v35, v15
	v_add_f32_e32 v56, v32, v33
	v_pk_add_f32 v[38:39], v[52:53], v[54:55]
	v_pk_add_f32 v[32:33], v[56:57], v[34:35]
	v_pk_add_f32 v[48:49], v[58:59], v[60:61]
	v_pk_add_f32 v[32:33], v[32:33], v[38:39]
	v_pk_add_f32 v[36:37], v[48:49], v[48:49] op_sel:[0,1] op_sel_hi:[1,0]
	v_pk_add_f32 v[32:33], v[32:33], v[32:33] op_sel:[0,1] op_sel_hi:[1,0]
	v_mov_b32_e32 v63, v0
	v_mov_b32_e32 v133, v1
	v_mov_b32_e32 v37, v3
	v_mov_b32_e32 v33, v2
	v_pk_add_f32 v[50:51], v[62:63], v[132:133]
	v_pk_add_f32 v[32:33], v[32:33], v[36:37]
	v_pk_mul_f32 v[34:35], v[68:69], v[80:81] op_sel_hi:[1,0]
	v_pk_add_f32 v[32:33], v[32:33], v[50:51]
	s_waitcnt vmcnt(0)
	v_pk_fma_f32 v[42:43], v[34:35], v[42:43], v[46:47]
	v_add_f32_e32 v32, v32, v33
	ds_bpermute_b32 v33, v73, v32
	v_bfe_u32 v34, v42, 16, 1
	v_bfe_u32 v35, v43, 16, 1
	v_add3_u32 v34, v42, v34, s90
	v_add3_u32 v35, v43, v35, s90
	s_waitcnt lgkmcnt(0)
	v_add_f32_e32 v32, v32, v33
	ds_bpermute_b32 v33, v217, v32
	v_lshrrev_b32_e32 v34, 16, v34
	s_waitcnt lgkmcnt(0)
	v_add_f32_e32 v32, v32, v33
	ds_bpermute_b32 v33, v218, v32
	s_waitcnt lgkmcnt(0)
	v_add_f32_e32 v32, v32, v33
	ds_bpermute_b32 v33, v219, v32
	s_waitcnt lgkmcnt(0)
	v_add_f32_e32 v32, v32, v33
	ds_bpermute_b32 v33, v220, v32
	s_waitcnt lgkmcnt(0)
	v_add_f32_e32 v48, v32, v33
	v_pk_mul_f32 v[32:33], v[70:71], v[80:81] op_sel_hi:[1,0]
	v_mov_b32_e32 v71, 0
	v_pk_fma_f32 v[40:41], v[32:33], v[40:41], v[44:45]
	ds_bpermute_b32 v44, v221, v48
	v_bfe_u32 v32, v40, 16, 1
	v_bfe_u32 v33, v41, 16, 1
	v_add3_u32 v32, v40, v32, s90
	v_add3_u32 v33, v41, v33, s90
	v_lshrrev_b32_e32 v32, 16, v32
	v_and_or_b32 v32, v33, s86, v32
	v_and_or_b32 v33, v35, s86, v34
	global_store_dwordx2 v[130:131], v[32:33], off offset:3584
	global_load_dwordx4 v[32:35], v[82:83], off offset:3072
	s_nop 0
	global_load_dwordx4 v[36:39], v[84:85], off offset:3072
	s_waitcnt lgkmcnt(0)
	v_add_f32_e32 v44, v48, v44
	v_fmamk_f32 v29, v44, 0xba000000, v29
	v_fmamk_f32 v31, v44, 0xba000000, v31
	v_fmamk_f32 v25, v44, 0xba000000, v25
	v_fmamk_f32 v27, v44, 0xba000000, v27
	v_fmamk_f32 v23, v44, 0xba000000, v23
	v_fmac_f32_e32 v22, 0xba000000, v44
	v_fmamk_f32 v21, v44, 0xba000000, v21
	v_fmac_f32_e32 v20, 0xba000000, v44
	v_fmac_f32_e32 v28, 0xba000000, v44
	v_fmac_f32_e32 v30, 0xba000000, v44
	v_fmac_f32_e32 v24, 0xba000000, v44
	v_fmac_f32_e32 v26, 0xba000000, v44
	v_mov_b32_e32 v46, v31
	v_mov_b32_e32 v47, v27
	v_mov_b32_e32 v50, v29
	v_mov_b32_e32 v51, v25
	v_pk_mul_f32 v[52:53], v[20:21], v[20:21]
	v_pk_mul_f32 v[54:55], v[22:23], v[22:23]
	v_fmamk_f32 v19, v44, 0xba000000, v19
	v_fmac_f32_e32 v18, 0xba000000, v44
	v_fmamk_f32 v17, v44, 0xba000000, v17
	v_fmac_f32_e32 v16, 0xba000000, v44
	v_fmamk_f32 v13, v44, 0xba000000, v13
	v_fmac_f32_e32 v12, 0xba000000, v44
	v_fmamk_f32 v15, v44, 0xba000000, v15
	v_fmac_f32_e32 v14, 0xba000000, v44
	v_fmamk_f32 v11, v44, 0xba000000, v11
	v_fmac_f32_e32 v10, 0xba000000, v44
	v_fmamk_f32 v9, v44, 0xba000000, v9
	v_fmac_f32_e32 v8, 0xba000000, v44
	v_fmamk_f32 v7, v44, 0xba000000, v7
	v_fmac_f32_e32 v6, 0xba000000, v44
	v_fmamk_f32 v5, v44, 0xba000000, v5
	v_fmac_f32_e32 v4, 0xba000000, v44
	v_fmamk_f32 v1, v44, 0xba000000, v1
	v_fmac_f32_e32 v0, 0xba000000, v44
	v_fmamk_f32 v3, v44, 0xba000000, v3
	v_fmac_f32_e32 v2, 0xba000000, v44
	v_mov_b32_e32 v44, v30
	v_mov_b32_e32 v45, v26
	v_mov_b32_e32 v48, v28
	v_mov_b32_e32 v49, v24
	v_pk_mul_f32 v[46:47], v[46:47], v[46:47]
	v_pk_mul_f32 v[50:51], v[50:51], v[50:51]
	v_pk_mov_b32 v[130:131], v[54:55], v[52:53] op_sel:[1,0]
	v_mov_b32_e32 v55, v53
	v_mul_f32_e32 v56, v18, v18
	v_mul_f32_e32 v58, v16, v16
	v_pk_mul_f32 v[60:61], v[8:9], v[8:9]
	v_pk_mul_f32 v[62:63], v[10:11], v[10:11]
	v_mul_f32_e32 v68, v6, v6
	v_mul_f32_e32 v70, v4, v4
	v_pk_fma_f32 v[44:45], v[44:45], v[44:45], v[46:47]
	v_pk_fma_f32 v[46:47], v[48:49], v[48:49], v[50:51]
	v_pk_add_f32 v[48:49], v[130:131], v[54:55]
	v_pk_fma_f32 v[52:53], v[18:19], v[18:19], v[56:57] op_sel_hi:[1,1,0]
	v_pk_fma_f32 v[56:57], v[16:17], v[16:17], v[58:59] op_sel_hi:[1,1,0]
	v_pk_mov_b32 v[58:59], v[62:63], v[60:61] op_sel:[1,0]
	v_mov_b32_e32 v63, v61
	v_pk_fma_f32 v[60:61], v[6:7], v[6:7], v[68:69] op_sel_hi:[1,1,0]
	v_pk_fma_f32 v[68:69], v[4:5], v[4:5], v[70:71] op_sel_hi:[1,1,0]
	v_pk_add_f32 v[44:45], v[44:45], v[46:47]
	v_pk_add_f32 v[46:47], v[48:49], v[48:49] op_sel_hi:[0,1]
	v_pk_add_f32 v[44:45], v[44:45], v[44:45] op_sel_hi:[0,1]
	v_mul_f32_e32 v52, v14, v14
	v_mul_f32_e32 v56, v15, v15
	v_mul_f32_e32 v46, v12, v12
	v_mul_f32_e32 v44, v13, v13
	v_pk_add_f32 v[48:49], v[52:53], v[56:57]
	v_pk_add_f32 v[50:51], v[58:59], v[62:63]
	v_mul_f32_e32 v60, v2, v2
	v_pk_add_f32 v[50:51], v[50:51], v[50:51] op_sel_hi:[0,1]
	v_mul_f32_e32 v68, v3, v3
	v_mul_f32_e32 v50, v0, v0
	v_pk_add_f32 v[52:53], v[60:61], v[68:69]
	s_waitcnt vmcnt(1)
; #define GAS __attribute__((address_space(1)))
; __device__ __forceinline__ unsigned pk2(float lo, float hi) { return f2bf(lo) | (f2bf(hi) << 16); }
; __device__ __forceinline__ unsigned pk4_fp8(float a, float b, float c, float d) { int r = __builtin_amdgcn_cvt_pk_fp8_f32(a, b, 0, false); r = __builtin_amdgcn_cvt_pk_fp8_f32(c, d, r, true); return (unsigned)r; }
; template <int l>
; __device__ __forceinline__ void layer_phases(Frame& F, const XcdBarrier& bar, const int lo, const int hi) {
;     ...
;                     const float mean = wave_sum(s) * (1.f / D); float s2 = 0.f;
; #pragma unroll
;                     for (int j = 0; j < 8; ++j) { v[j] = v[j] - mean; s2 += (v[j].x * v[j].x + v[j].y * v[j].y) + (v[j].z * v[j].z + v[j].w * v[j].w); }
;                     const float rstd = 1.f / sqrtf(wave_sum(s2) * (1.f / D) + LN_EPS);
; #pragma unroll
;                     for (int j = 0; j < 8; ++j) { const int k = 4 * lq + 256 * j;
;                         const f32x4 xv = v[j] * rstd * *(const GAS f32x4*)(g1 + k) + *(const GAS f32x4*)(b1 + k);
;                         { v2u xo; xo.x = pk2(xv.x, xv.y); xo.y = pk2(xv.z, xv.w); *(GAS v2u*)(x1 + (size_t)m * D + k) = xo; }
;                         const f32x4 hv = xv * (*(const GAS f32x4*)(mrow + 8192 + k) + 1.0f) + *(const GAS f32x4*)(mrow + 6144 + k);
;                         v2u o; o.x = pk2(hv.x, hv.y); o.y = pk2(hv.z, hv.w);
;                         *(GAS unsigned*)(h2q + (size_t)m * D + k) = pk4_fp8(hv.x, hv.y, hv.z, hv.w);
	v_pk_add_f32 v[32:33], v[32:33], 1.0 op_sel_hi:[1,0]
	s_waitcnt vmcnt(0)
	v_pk_fma_f32 v[130:131], v[40:41], v[32:33], v[36:37]
	v_pk_add_f32 v[32:33], v[34:35], 1.0 op_sel_hi:[1,0]
	v_cvt_pk_fp8_f32 v71, v130, v131
	v_pk_fma_f32 v[132:133], v[42:43], v[32:33], v[38:39]
	v_pk_add_f32 v[32:33], v[46:47], v[44:45]
	v_cvt_pk_fp8_f32 v71, v132, v133 op_sel:[0,0,1]
	v_pk_add_f32 v[32:33], v[48:49], v[32:33]
	global_store_dword v[134:135], v71, off offset:1792
	global_load_dwordx4 v[36:39], v[112:113], off
	global_load_dwordx4 v[40:43], v[114:115], off
	v_pk_add_f32 v[32:33], v[32:33], v[32:33] op_sel_hi:[0,1]
	v_mul_f32_e32 v32, v1, v1
	v_pk_add_f32 v[32:33], v[50:51], v[32:33]
	s_nop 0
	v_pk_add_f32 v[32:33], v[52:53], v[32:33]
	s_nop 0
	v_add_f32_e32 v32, v32, v33
	ds_bpermute_b32 v33, v73, v32
	s_waitcnt lgkmcnt(0)
	v_add_f32_e32 v32, v32, v33
	ds_bpermute_b32 v33, v217, v32
	s_waitcnt lgkmcnt(0)
	v_add_f32_e32 v32, v32, v33
	ds_bpermute_b32 v33, v218, v32
	s_waitcnt lgkmcnt(0)
	v_add_f32_e32 v32, v32, v33
	ds_bpermute_b32 v33, v219, v32
	s_waitcnt lgkmcnt(0)
	v_add_f32_e32 v32, v32, v33
	ds_bpermute_b32 v33, v220, v32
	s_waitcnt lgkmcnt(0)
	v_add_f32_e32 v32, v32, v33
	ds_bpermute_b32 v33, v221, v32
	s_waitcnt lgkmcnt(0)
	v_add_f32_e32 v32, v32, v33
	v_fmamk_f32 v32, v32, 0x3a000000, v223
	v_mul_f32_e32 v33, 0x4f800000, v32
	v_cmp_gt_f32_e32 vcc, s89, v32
	s_nop 1
	v_cndmask_b32_e32 v32, v32, v33, vcc
	v_sqrt_f32_e32 v33, v32
	s_nop 0
	v_add_u32_e32 v34, -1, v33
	v_add_u32_e32 v35, 1, v33
	v_fma_f32 v44, -v34, v33, v32
	v_fma_f32 v45, -v35, v33, v32
	v_cmp_ge_f32_e64 s[14:15], 0, v44
	s_nop 1
	v_cndmask_b32_e64 v33, v33, v34, s[14:15]
	v_cmp_lt_f32_e64 s[14:15], 0, v45
	s_nop 1
	v_cndmask_b32_e64 v33, v33, v35, s[14:15]
	v_mul_f32_e32 v34, 0x37800000, v33
	v_cndmask_b32_e32 v33, v33, v34, vcc
	v_cmp_class_f32_e32 vcc, v32, v224
	s_nop 1
	v_cndmask_b32_e32 v34, v33, v32, vcc
	v_div_scale_f32 v35, s[14:15], v34, v34, 1.0
	v_rcp_f32_e32 v44, v35
	v_div_scale_f32 v45, vcc, 1.0, v34, 1.0
	v_lshl_add_u64 v[32:33], s[0:1], 0, v[128:129]
	v_fma_f32 v46, -v35, v44, 1.0
	v_fmac_f32_e32 v44, v46, v44
	v_mul_f32_e32 v46, v45, v44
	v_fma_f32 v47, -v35, v46, v45
	v_fmac_f32_e32 v46, v47, v44
	v_fma_f32 v35, -v35, v46, v45
	v_div_fmas_f32 v35, v35, v44, v46
	v_div_fixup_f32 v34, v35, v34, 1.0
	v_pk_mul_f32 v[30:31], v[30:31], v[34:35] op_sel_hi:[1,0]
	v_pk_mul_f32 v[28:29], v[28:29], v[34:35] op_sel_hi:[1,0]
	s_waitcnt vmcnt(0)
	v_pk_fma_f32 v[40:41], v[36:37], v[30:31], v[40:41]
	v_pk_fma_f32 v[42:43], v[38:39], v[28:29], v[42:43]
	v_bfe_u32 v28, v40, 16, 1
	v_bfe_u32 v30, v42, 16, 1
	v_bfe_u32 v29, v41, 16, 1
	v_bfe_u32 v31, v43, 16, 1
	v_add3_u32 v28, v40, v28, s90
	v_add3_u32 v30, v42, v30, s90
	v_add3_u32 v29, v41, v29, s90
	v_add3_u32 v31, v43, v31, s90
	v_lshrrev_b32_e32 v28, 16, v28
	v_lshrrev_b32_e32 v30, 16, v30
	v_and_or_b32 v28, v29, s86, v28
	v_and_or_b32 v29, v31, s86, v30
	global_store_dwordx2 v[32:33], v[28:29], off
	global_load_dwordx4 v[28:31], v[82:83], off offset:-4096
	s_nop 0
	global_load_dwordx4 v[36:39], v[84:85], off offset:-4096
	v_mov_b32_e32 v35, 0
	s_add_u32 s0, s50, s16
	s_addc_u32 s1, s51, s17
	s_or_b32 s46, s42, 2
	s_ashr_i32 s47, s46, 31
	s_lshl_b64 s[18:19], s[46:47], 11
	s_or_b32 s48, s42, 3
	s_ashr_i32 s49, s48, 31
	s_lshl_b64 s[16:17], s[48:49], 11
	s_waitcnt vmcnt(1)
	v_pk_add_f32 v[28:29], v[28:29], 1.0 op_sel_hi:[1,0]
	s_waitcnt vmcnt(0)
	v_pk_fma_f32 v[134:135], v[28:29], v[40:41], v[36:37]
	v_pk_add_f32 v[28:29], v[30:31], 1.0 op_sel_hi:[1,0]
	v_cvt_pk_fp8_f32 v35, v134, v135
	v_pk_fma_f32 v[136:137], v[28:29], v[42:43], v[38:39]
	v_lshl_add_u64 v[28:29], s[0:1], 0, v[86:87]
	s_lshl_b64 s[0:1], s[46:47], 12
	v_cvt_pk_fp8_f32 v35, v136, v137 op_sel:[0,0,1]
	s_add_u32 s0, s3, s0
	s_addc_u32 s1, s41, s1
	global_store_dword v[28:29], v35, off
	global_load_dwordx4 v[36:39], v[112:113], off offset:1024
	global_load_dwordx4 v[40:43], v[114:115], off offset:1024
	v_pk_mul_f32 v[26:27], v[26:27], v[34:35] op_sel_hi:[1,0]
	v_pk_mul_f32 v[24:25], v[24:25], v[34:35] op_sel_hi:[1,0]
	v_mov_b32_e32 v35, 0
	s_waitcnt vmcnt(0)
	v_pk_fma_f32 v[30:31], v[38:39], v[24:25], v[42:43]
	v_pk_fma_f32 v[40:41], v[36:37], v[26:27], v[40:41]
	v_bfe_u32 v26, v30, 16, 1
	v_bfe_u32 v24, v40, 16, 1
	v_bfe_u32 v25, v41, 16, 1
	v_bfe_u32 v27, v31, 16, 1
	v_add3_u32 v24, v40, v24, s90
	v_add3_u32 v26, v30, v26, s90
	v_add3_u32 v25, v41, v25, s90
	v_add3_u32 v27, v31, v27, s90
	v_lshrrev_b32_e32 v24, 16, v24
	v_lshrrev_b32_e32 v26, 16, v26
	v_and_or_b32 v24, v25, s86, v24
	v_and_or_b32 v25, v27, s86, v26
	global_store_dwordx2 v[32:33], v[24:25], off offset:512
	global_load_dwordx4 v[24:27], v[122:123], off offset:1024
	s_nop 0
	global_load_dwordx4 v[36:39], v[120:121], off offset:1024
	s_waitcnt vmcnt(1)
	v_pk_add_f32 v[24:25], v[24:25], 1.0 op_sel_hi:[1,0]
	s_waitcnt vmcnt(0)
	v_pk_fma_f32 v[138:139], v[24:25], v[40:41], v[36:37]
	v_pk_add_f32 v[24:25], v[26:27], 1.0 op_sel_hi:[1,0]
	v_cvt_pk_fp8_f32 v35, v138, v139
	v_pk_fma_f32 v[140:141], v[24:25], v[30:31], v[38:39]
	s_nop 0
	v_cvt_pk_fp8_f32 v35, v140, v141 op_sel:[0,0,1]
	global_store_dword v[28:29], v35, off offset:256
	global_load_dwordx4 v[24:27], v[112:113], off offset:2048
	global_load_dwordx4 v[36:39], v[114:115], off offset:2048
	v_pk_mul_f32 v[22:23], v[22:23], v[34:35] op_sel_hi:[1,0]
	v_pk_mul_f32 v[20:21], v[20:21], v[34:35] op_sel_hi:[1,0]
	v_mov_b32_e32 v35, 0
	s_waitcnt vmcnt(0)
; #define GAS __attribute__((address_space(1)))
; #define LAS __attribute__((address_space(3)))
; __device__ __forceinline__ unsigned pk2(float lo, float hi) { return f2bf(lo) | (f2bf(hi) << 16); }
; __device__ __forceinline__ unsigned pk4_fp8(float a, float b, float c, float d) { int r = __builtin_amdgcn_cvt_pk_fp8_f32(a, b, 0, false); r = __builtin_amdgcn_cvt_pk_fp8_f32(c, d, r, true); return (unsigned)r; }
; template <int l>
; __device__ __forceinline__ void layer_phases(Frame& F, const XcdBarrier& bar, const int lo, const int hi) {
;     ...
; #pragma unroll
;                     for (int j = 0; j < 8; ++j) { const int k = 4 * lq + 256 * j;
;                         const f32x4 xv = v[j] * rstd * *(const GAS f32x4*)(g1 + k) + *(const GAS f32x4*)(b1 + k);
;                         { v2u xo; xo.x = pk2(xv.x, xv.y); xo.y = pk2(xv.z, xv.w); *(GAS v2u*)(x1 + (size_t)m * D + k) = xo; }
;                         const f32x4 hv = xv * (*(const GAS f32x4*)(mrow + 8192 + k) + 1.0f) + *(const GAS f32x4*)(mrow + 6144 + k);
;                         v2u o; o.x = pk2(hv.x, hv.y); o.y = pk2(hv.z, hv.w);
;                         *(GAS unsigned*)(h2q + (size_t)m * D + k) = pk4_fp8(hv.x, hv.y, hv.z, hv.w);
;                         const int chunk = (lq >> 1) + 32 * j;
;                         *(LAS v2u*)(h2s + rloc * 4096 + ((chunk ^ (rloc & 15)) << 4) + (lq & 1) * 8) = o; }
	v_pk_fma_f32 v[30:31], v[26:27], v[20:21], v[38:39]
	v_pk_fma_f32 v[36:37], v[24:25], v[22:23], v[36:37]
	v_bfe_u32 v22, v30, 16, 1
	v_bfe_u32 v20, v36, 16, 1
	v_bfe_u32 v21, v37, 16, 1
	v_bfe_u32 v23, v31, 16, 1
	v_add3_u32 v20, v36, v20, s90
	v_add3_u32 v22, v30, v22, s90
	v_add3_u32 v21, v37, v21, s90
	v_add3_u32 v23, v31, v23, s90
	v_lshrrev_b32_e32 v20, 16, v20
	v_lshrrev_b32_e32 v22, 16, v22
	v_and_or_b32 v20, v21, s86, v20
	v_and_or_b32 v21, v23, s86, v22
	global_store_dwordx2 v[32:33], v[20:21], off offset:1024
	global_load_dwordx4 v[20:23], v[122:123], off offset:2048
	s_nop 0
	global_load_dwordx4 v[24:27], v[120:121], off offset:2048
	s_waitcnt vmcnt(1)
	v_pk_add_f32 v[20:21], v[20:21], 1.0 op_sel_hi:[1,0]
	s_waitcnt vmcnt(0)
	v_pk_fma_f32 v[142:143], v[20:21], v[36:37], v[24:25]
	v_pk_add_f32 v[20:21], v[22:23], 1.0 op_sel_hi:[1,0]
	v_cvt_pk_fp8_f32 v35, v142, v143
	v_pk_fma_f32 v[144:145], v[20:21], v[30:31], v[26:27]
	v_mov_b32_e32 v30, 0
	v_cvt_pk_fp8_f32 v35, v144, v145 op_sel:[0,0,1]
	global_store_dword v[28:29], v35, off offset:512
	global_load_dwordx4 v[20:23], v[112:113], off offset:3072
	global_load_dwordx4 v[24:27], v[114:115], off offset:3072
	v_pk_mul_f32 v[18:19], v[18:19], v[34:35] op_sel_hi:[1,0]
	v_pk_mul_f32 v[16:17], v[16:17], v[34:35] op_sel_hi:[1,0]
	v_pk_mul_f32 v[14:15], v[14:15], v[34:35] op_sel_hi:[1,0]
	v_pk_mul_f32 v[12:13], v[12:13], v[34:35] op_sel_hi:[1,0]
	v_pk_mul_f32 v[10:11], v[10:11], v[34:35] op_sel_hi:[1,0]
	v_pk_mul_f32 v[8:9], v[8:9], v[34:35] op_sel_hi:[1,0]
	v_pk_mul_f32 v[6:7], v[6:7], v[34:35] op_sel_hi:[1,0]
	v_pk_mul_f32 v[4:5], v[4:5], v[34:35] op_sel_hi:[1,0]
	v_pk_mul_f32 v[2:3], v[2:3], v[34:35] op_sel_hi:[1,0]
	v_pk_mul_f32 v[0:1], v[0:1], v[34:35] op_sel_hi:[1,0]
	s_waitcnt vmcnt(0)
	v_pk_fma_f32 v[26:27], v[16:17], v[22:23], v[26:27]
	v_pk_fma_f32 v[24:25], v[18:19], v[20:21], v[24:25]
	v_bfe_u32 v18, v26, 16, 1
	v_bfe_u32 v16, v24, 16, 1
	v_bfe_u32 v17, v25, 16, 1
	v_bfe_u32 v19, v27, 16, 1
	v_add3_u32 v16, v24, v16, s90
	v_add3_u32 v18, v26, v18, s90
	v_add3_u32 v17, v25, v17, s90
	v_add3_u32 v19, v27, v19, s90
	v_lshrrev_b32_e32 v16, 16, v16
	v_lshrrev_b32_e32 v18, 16, v18
	v_and_or_b32 v16, v17, s86, v16
	v_and_or_b32 v17, v19, s86, v18
	global_store_dwordx2 v[32:33], v[16:17], off offset:1536
	global_load_dwordx4 v[16:19], v[122:123], off offset:3072
	s_nop 0
	global_load_dwordx4 v[20:23], v[120:121], off offset:3072
	s_waitcnt vmcnt(1)
	v_pk_add_f32 v[16:17], v[16:17], 1.0 op_sel_hi:[1,0]
	s_waitcnt vmcnt(0)
	v_pk_fma_f32 v[146:147], v[24:25], v[16:17], v[20:21]
	v_pk_add_f32 v[16:17], v[18:19], 1.0 op_sel_hi:[1,0]
	v_cvt_pk_fp8_f32 v30, v146, v147
	v_pk_fma_f32 v[148:149], v[26:27], v[16:17], v[22:23]
	v_mov_b32_e32 v24, 0
	v_cvt_pk_fp8_f32 v30, v148, v149 op_sel:[0,0,1]
	global_store_dword v[28:29], v30, off offset:768
	global_load_dwordx4 v[16:19], v[88:89], off
	global_load_dwordx4 v[20:23], v[90:91], off
	s_waitcnt vmcnt(0)
	v_pk_fma_f32 v[22:23], v[12:13], v[18:19], v[22:23]
	v_pk_fma_f32 v[20:21], v[14:15], v[16:17], v[20:21]
	v_bfe_u32 v14, v22, 16, 1
	v_bfe_u32 v12, v20, 16, 1
	v_bfe_u32 v13, v21, 16, 1
	v_bfe_u32 v15, v23, 16, 1
	v_add3_u32 v12, v20, v12, s90
	v_add3_u32 v14, v22, v14, s90
	v_add3_u32 v13, v21, v13, s90
	v_add3_u32 v15, v23, v15, s90
	v_lshrrev_b32_e32 v12, 16, v12
	v_lshrrev_b32_e32 v14, 16, v14
	v_and_or_b32 v12, v13, s86, v12
	v_and_or_b32 v13, v15, s86, v14
	global_store_dwordx2 v[32:33], v[12:13], off offset:2048
	global_load_dwordx4 v[12:15], v[82:83], off
	s_nop 0
	global_load_dwordx4 v[16:19], v[84:85], off
	s_waitcnt vmcnt(1)
	v_pk_add_f32 v[12:13], v[12:13], 1.0 op_sel_hi:[1,0]
	s_waitcnt vmcnt(0)
	v_pk_fma_f32 v[150:151], v[20:21], v[12:13], v[16:17]
	v_pk_add_f32 v[12:13], v[14:15], 1.0 op_sel_hi:[1,0]
	v_cvt_pk_fp8_f32 v24, v150, v151
	v_pk_fma_f32 v[152:153], v[22:23], v[12:13], v[18:19]
	v_mov_b32_e32 v20, 0
	v_cvt_pk_fp8_f32 v24, v152, v153 op_sel:[0,0,1]
	global_store_dword v[28:29], v24, off offset:1024
	global_load_dwordx4 v[12:15], v[88:89], off offset:1024
	global_load_dwordx4 v[16:19], v[90:91], off offset:1024
	s_waitcnt vmcnt(0)
	v_pk_fma_f32 v[18:19], v[8:9], v[14:15], v[18:19]
	v_pk_fma_f32 v[16:17], v[10:11], v[12:13], v[16:17]
	v_bfe_u32 v10, v18, 16, 1
	v_bfe_u32 v8, v16, 16, 1
	v_bfe_u32 v9, v17, 16, 1
	v_bfe_u32 v11, v19, 16, 1
	v_add3_u32 v8, v16, v8, s90
	v_add3_u32 v10, v18, v10, s90
	v_add3_u32 v9, v17, v9, s90
	v_add3_u32 v11, v19, v11, s90
	v_lshrrev_b32_e32 v8, 16, v8
	v_lshrrev_b32_e32 v10, 16, v10
	v_and_or_b32 v8, v9, s86, v8
	v_and_or_b32 v9, v11, s86, v10
	global_store_dwordx2 v[32:33], v[8:9], off offset:2560
	global_load_dwordx4 v[8:11], v[82:83], off offset:1024
	s_nop 0
	global_load_dwordx4 v[12:15], v[84:85], off offset:1024
	s_waitcnt vmcnt(1)
	v_pk_add_f32 v[8:9], v[8:9], 1.0 op_sel_hi:[1,0]
	s_waitcnt vmcnt(0)
	v_pk_fma_f32 v[154:155], v[16:17], v[8:9], v[12:13]
	v_pk_add_f32 v[8:9], v[10:11], 1.0 op_sel_hi:[1,0]
	v_cvt_pk_fp8_f32 v20, v154, v155
	v_pk_fma_f32 v[156:157], v[18:19], v[8:9], v[14:15]
	v_mov_b32_e32 v16, 0
	v_cvt_pk_fp8_f32 v20, v156, v157 op_sel:[0,0,1]
	global_store_dword v[28:29], v20, off offset:1280
	global_load_dwordx4 v[8:11], v[88:89], off offset:2048
	global_load_dwordx4 v[12:15], v[90:91], off offset:2048
	s_waitcnt vmcnt(0)
	v_pk_fma_f32 v[14:15], v[4:5], v[10:11], v[14:15]
	v_pk_fma_f32 v[12:13], v[6:7], v[8:9], v[12:13]
	v_bfe_u32 v6, v14, 16, 1
	v_bfe_u32 v4, v12, 16, 1
	v_bfe_u32 v5, v13, 16, 1
	v_bfe_u32 v7, v15, 16, 1
	v_add3_u32 v4, v12, v4, s90
	v_add3_u32 v6, v14, v6, s90
	v_add3_u32 v5, v13, v5, s90
	v_add3_u32 v7, v15, v7, s90
	v_lshrrev_b32_e32 v4, 16, v4
	v_lshrrev_b32_e32 v6, 16, v6
	v_and_or_b32 v4, v5, s86, v4
	v_and_or_b32 v5, v7, s86, v6
	global_store_dwordx2 v[32:33], v[4:5], off offset:3072
	global_load_dwordx4 v[4:7], v[82:83], off offset:2048
	s_nop 0
	global_load_dwordx4 v[8:11], v[84:85], off offset:2048
	s_waitcnt vmcnt(1)
; #define GAS __attribute__((address_space(1)))
; #define LAS __attribute__((address_space(3)))
; __device__ __forceinline__ unsigned pk2(float lo, float hi) { return f2bf(lo) | (f2bf(hi) << 16); }
; __device__ __forceinline__ unsigned pk4_fp8(float a, float b, float c, float d) { int r = __builtin_amdgcn_cvt_pk_fp8_f32(a, b, 0, false); r = __builtin_amdgcn_cvt_pk_fp8_f32(c, d, r, true); return (unsigned)r; }
; __device__ __forceinline__ f32x4 bf4(unsigned a, unsigned b) { return (f32x4){bflo(a), bfhi(a), bflo(b), bfhi(b)}; }
; template <int l>
; __device__ __forceinline__ void layer_phases(Frame& F, const XcdBarrier& bar, const int lo, const int hi) {
;     ...
;                 for (int rp = 0; rp < 2; ++rp) {
;                 f32x4 vv[2][8];
; #pragma unroll
;                 for (int rr = 0; rr < 2; ++rr)
; #pragma unroll
;                     for (int j = 0; j < 8; ++j) { const size_t off = (size_t)(m0 + 2 * rp + rr) * D + 4 * lq + 256 * j;
;                         f32x4 xv; if (l == 0) xv = __builtin_nontemporal_load((const GAS f32x4*)(xin + off)); else { const v2u xw_ = __builtin_nontemporal_load((const GAS v2u*)(xinb + off)); xv = bf4(xw_.x, xw_.y); } const v2u mw = __builtin_nontemporal_load((const GAS v2u*)(mixb + off)); const f32x4 gv = *(const GAS f32x4*)(mrow + 4096 + 4 * lq + 256 * j);
;                         vv[rr][j] = xv * ALPHA + gv * (f32x4){bflo(mw.x), bfhi(mw.x), bflo(mw.y), bfhi(mw.y)}; }
;     ...
; #pragma unroll
;                     for (int j = 0; j < 8; ++j) { const int k = 4 * lq + 256 * j;
;                         const f32x4 xv = v[j] * rstd * *(const GAS f32x4*)(g1 + k) + *(const GAS f32x4*)(b1 + k);
;                         { v2u xo; xo.x = pk2(xv.x, xv.y); xo.y = pk2(xv.z, xv.w); *(GAS v2u*)(x1 + (size_t)m * D + k) = xo; }
;                         const f32x4 hv = xv * (*(const GAS f32x4*)(mrow + 8192 + k) + 1.0f) + *(const GAS f32x4*)(mrow + 6144 + k);
;                         v2u o; o.x = pk2(hv.x, hv.y); o.y = pk2(hv.z, hv.w);
;                         *(GAS unsigned*)(h2q + (size_t)m * D + k) = pk4_fp8(hv.x, hv.y, hv.z, hv.w);
;                         const int chunk = (lq >> 1) + 32 * j;
;                         *(LAS v2u*)(h2s + rloc * 4096 + ((chunk ^ (rloc & 15)) << 4) + (lq & 1) * 8) = o; }
	v_pk_add_f32 v[4:5], v[4:5], 1.0 op_sel_hi:[1,0]
	s_waitcnt vmcnt(0)
	v_pk_fma_f32 v[158:159], v[12:13], v[4:5], v[8:9]
	v_pk_add_f32 v[4:5], v[6:7], 1.0 op_sel_hi:[1,0]
	v_cvt_pk_fp8_f32 v16, v158, v159
	v_pk_fma_f32 v[160:161], v[14:15], v[4:5], v[10:11]
	v_mov_b32_e32 v12, 0
	v_cvt_pk_fp8_f32 v16, v160, v161 op_sel:[0,0,1]
	global_store_dword v[28:29], v16, off offset:1536
	global_load_dwordx4 v[4:7], v[88:89], off offset:3072
	global_load_dwordx4 v[8:11], v[90:91], off offset:3072
	s_waitcnt vmcnt(0)
	v_pk_fma_f32 v[10:11], v[0:1], v[6:7], v[10:11]
	v_pk_fma_f32 v[8:9], v[2:3], v[4:5], v[8:9]
	v_bfe_u32 v2, v10, 16, 1
	v_bfe_u32 v0, v8, 16, 1
	v_bfe_u32 v1, v9, 16, 1
	v_bfe_u32 v3, v11, 16, 1
	v_add3_u32 v0, v8, v0, s90
	v_add3_u32 v2, v10, v2, s90
	v_add3_u32 v1, v9, v1, s90
	v_add3_u32 v3, v11, v3, s90
	v_lshrrev_b32_e32 v0, 16, v0
	v_lshrrev_b32_e32 v2, 16, v2
	v_and_or_b32 v0, v1, s86, v0
	v_and_or_b32 v1, v3, s86, v2
	global_store_dwordx2 v[32:33], v[0:1], off offset:3584
	global_load_dwordx4 v[0:3], v[82:83], off offset:3072
	s_nop 0
	global_load_dwordx4 v[4:7], v[84:85], off offset:3072
	v_lshl_add_u64 v[32:33], s[18:19], 0, v[86:87]
	v_lshl_add_u64 v[48:49], v[32:33], 2, s[20:21]
	v_add_co_u32_e32 v60, vcc, s87, v48
	s_waitcnt vmcnt(1)
	v_pk_add_f32 v[0:1], v[0:1], 1.0 op_sel_hi:[1,0]
	s_waitcnt vmcnt(0)
	v_pk_fma_f32 v[162:163], v[8:9], v[0:1], v[4:5]
	v_pk_add_f32 v[0:1], v[2:3], 1.0 op_sel_hi:[1,0]
	v_cvt_pk_fp8_f32 v12, v162, v163
	v_pk_fma_f32 v[164:165], v[10:11], v[0:1], v[6:7]
	v_lshl_add_u64 v[0:1], v[32:33], 1, s[26:27]
	v_addc_co_u32_e32 v61, vcc, 0, v49, vcc
	v_cvt_pk_fp8_f32 v12, v164, v165 op_sel:[0,0,1]
	global_store_dword v[28:29], v12, off offset:1792
	global_load_dwordx2 v[68:69], v[0:1], off nt
	global_load_dwordx2 v[70:71], v[0:1], off offset:512 nt
	global_load_dwordx2 v[166:167], v[0:1], off offset:1024 nt
	global_load_dwordx2 v[168:169], v[0:1], off offset:1536 nt
	global_load_dwordx2 v[170:171], v[0:1], off offset:2048 nt
	global_load_dwordx2 v[172:173], v[0:1], off offset:2560 nt
	global_load_dwordx2 v[174:175], v[0:1], off offset:3072 nt
	global_load_dwordx2 v[176:177], v[0:1], off offset:3584 nt
	global_load_dwordx4 v[28:31], v[64:65], off offset:-4096
	global_load_dwordx4 v[24:27], v[66:67], off offset:1024
	global_load_dwordx4 v[20:23], v[66:67], off offset:2048
	global_load_dwordx4 v[16:19], v[66:67], off offset:3072
	global_load_dwordx4 v[12:15], v[64:65], off
	global_load_dwordx4 v[8:11], v[64:65], off offset:1024
	global_load_dwordx4 v[4:7], v[64:65], off offset:2048
	global_load_dwordx4 v[0:3], v[64:65], off offset:3072
	global_load_dwordx4 v[32:35], v[48:49], off nt
	global_load_dwordx4 v[36:39], v[48:49], off offset:1024 nt
	global_load_dwordx4 v[40:43], v[48:49], off offset:2048 nt
	global_load_dwordx4 v[44:47], v[48:49], off offset:3072 nt
	s_nop 0
	global_load_dwordx4 v[48:51], v[60:61], off nt
	global_load_dwordx4 v[52:55], v[60:61], off offset:1024 nt
	global_load_dwordx4 v[56:59], v[60:61], off offset:2048 nt
	s_nop 0
	global_load_dwordx4 v[60:63], v[60:61], off offset:3072 nt
	s_waitcnt vmcnt(23)
	v_lshlrev_b32_e32 v64, 16, v68
	v_and_b32_e32 v65, 0xffff0000, v68
	v_lshlrev_b32_e32 v66, 16, v69
	v_and_b32_e32 v67, 0xffff0000, v69
	s_waitcnt vmcnt(22)
	v_lshlrev_b32_e32 v68, 16, v70
	v_and_b32_e32 v69, 0xffff0000, v70
	v_lshlrev_b32_e32 v70, 16, v71
	v_and_b32_e32 v71, 0xffff0000, v71
	s_waitcnt vmcnt(21)
	v_lshlrev_b32_e32 v178, 16, v166
	v_and_b32_e32 v179, 0xffff0000, v166
	v_lshlrev_b32_e32 v166, 16, v167
	v_and_b32_e32 v167, 0xffff0000, v167
	s_waitcnt vmcnt(15)
	v_pk_mul_f32 v[64:65], v[28:29], v[64:65]
	v_pk_mul_f32 v[66:67], v[30:31], v[66:67]
	s_waitcnt vmcnt(14)
	v_pk_mul_f32 v[70:71], v[26:27], v[70:71]
	v_pk_mul_f32 v[68:69], v[24:25], v[68:69]
	v_lshlrev_b32_e32 v180, 16, v168
	v_and_b32_e32 v181, 0xffff0000, v168
	v_lshlrev_b32_e32 v168, 16, v169
	v_and_b32_e32 v169, 0xffff0000, v169
	s_waitcnt vmcnt(13)
	v_pk_mul_f32 v[166:167], v[22:23], v[166:167]
	v_pk_mul_f32 v[178:179], v[20:21], v[178:179]
	s_waitcnt vmcnt(7)
	v_pk_fma_f32 v[190:191], v[34:35], s[40:41], v[66:67] op_sel_hi:[1,0,1]
	v_pk_fma_f32 v[198:199], v[32:33], s[40:41], v[64:65] op_sel_hi:[1,0,1]
	s_waitcnt vmcnt(6)
	v_pk_fma_f32 v[192:193], v[38:39], s[40:41], v[70:71] op_sel_hi:[1,0,1]
	v_pk_fma_f32 v[194:195], v[36:37], s[40:41], v[68:69] op_sel_hi:[1,0,1]
	v_pk_mul_f32 v[196:197], v[18:19], v[168:169]
	s_waitcnt vmcnt(5)
	v_pk_fma_f32 v[166:167], v[42:43], s[40:41], v[166:167] op_sel_hi:[1,0,1]
	v_pk_fma_f32 v[168:169], v[40:41], s[40:41], v[178:179] op_sel_hi:[1,0,1]
	v_mov_b32_e32 v32, v198
	v_mov_b32_e32 v33, v194
	v_mov_b32_e32 v34, v199
	v_mov_b32_e32 v35, v195
	v_mov_b32_e32 v36, v190
	v_mov_b32_e32 v37, v192
	v_mov_b32_e32 v38, v191
	v_mov_b32_e32 v39, v193
	v_lshlrev_b32_e32 v182, 16, v170
	v_and_b32_e32 v183, 0xffff0000, v170
	v_lshlrev_b32_e32 v170, 16, v171
	v_and_b32_e32 v171, 0xffff0000, v171
	v_pk_mov_b32 v[40:41], v[168:169], v[166:167] op_sel:[1,0]
	v_mov_b32_e32 v42, v168
	v_mov_b32_e32 v43, v167
	v_pk_add_f32 v[32:33], v[32:33], v[34:35]
	v_pk_add_f32 v[34:35], v[36:37], v[38:39]
	v_lshlrev_b32_e32 v184, 16, v172
	v_and_b32_e32 v185, 0xffff0000, v172
	v_lshlrev_b32_e32 v172, 16, v173
	v_and_b32_e32 v173, 0xffff0000, v173
	v_lshlrev_b32_e32 v186, 16, v174
	v_and_b32_e32 v187, 0xffff0000, v174
	v_lshlrev_b32_e32 v174, 16, v175
	v_and_b32_e32 v175, 0xffff0000, v175
	v_lshlrev_b32_e32 v188, 16, v176
	v_and_b32_e32 v189, 0xffff0000, v176
	v_lshlrev_b32_e32 v176, 16, v177
	v_and_b32_e32 v177, 0xffff0000, v177
	v_pk_mul_f32 v[180:181], v[16:17], v[180:181]
	v_pk_mul_f32 v[182:183], v[12:13], v[182:183]
	v_pk_mul_f32 v[200:201], v[14:15], v[170:171]
	v_pk_add_f32 v[36:37], v[40:41], v[42:43]
	v_pk_add_f32 v[32:33], v[32:33], v[34:35]
	v_pk_mul_f32 v[184:185], v[8:9], v[184:185]
	v_pk_mul_f32 v[202:203], v[10:11], v[172:173]
	v_pk_mul_f32 v[204:205], v[4:5], v[186:187]
	v_pk_mul_f32 v[186:187], v[6:7], v[174:175]
	v_pk_mul_f32 v[208:209], v[2:3], v[176:177]
	s_waitcnt vmcnt(4)
; #define GAS __attribute__((address_space(1)))
; __device__ __forceinline__ f32x4 bf4(unsigned a, unsigned b) { return (f32x4){bflo(a), bfhi(a), bflo(b), bfhi(b)}; }
; template <int l>
; __device__ __forceinline__ void layer_phases(Frame& F, const XcdBarrier& bar, const int lo, const int hi) {
;     ...
;                     for (int j = 0; j < 8; ++j) { const size_t off = (size_t)(m0 + 2 * rp + rr) * D + 4 * lq + 256 * j;
;                         f32x4 xv; if (l == 0) xv = __builtin_nontemporal_load((const GAS f32x4*)(xin + off)); else { const v2u xw_ = __builtin_nontemporal_load((const GAS v2u*)(xinb + off)); xv = bf4(xw_.x, xw_.y); } const v2u mw = __builtin_nontemporal_load((const GAS v2u*)(mixb + off)); const f32x4 gv = *(const GAS f32x4*)(mrow + 4096 + 4 * lq + 256 * j);
;                         vv[rr][j] = xv * ALPHA + gv * (f32x4){bflo(mw.x), bfhi(mw.x), bflo(mw.y), bfhi(mw.y)}; }
; #pragma unroll
;                 for (int rq = 0; rq < 2; ++rq) { const int rr = 2 * rp + rq, m = m0 + rr, rloc = 4 * F.wave + rr;
;                     f32x4 (&v)[8] = vv[rq]; float s = 0.f;
; #pragma unroll
;                     for (int j = 0; j < 8; ++j) s += (v[j].x + v[j].y) + (v[j].z + v[j].w);
;                     const float mean = wave_sum(s) * (1.f / D); float s2 = 0.f;
; #pragma unroll
;                     for (int j = 0; j < 8; ++j) { v[j] = v[j] - mean; s2 += (v[j].x * v[j].x + v[j].y * v[j].y) + (v[j].z * v[j].z + v[j].w * v[j].w); }
	v_pk_fma_f32 v[170:171], v[46:47], s[40:41], v[196:197] op_sel_hi:[1,0,1]
	v_pk_fma_f32 v[172:173], v[44:45], s[40:41], v[180:181] op_sel_hi:[1,0,1]
	s_waitcnt vmcnt(3)
	v_pk_fma_f32 v[174:175], v[50:51], s[40:41], v[200:201] op_sel_hi:[1,0,1]
	v_pk_fma_f32 v[176:177], v[48:49], s[40:41], v[182:183] op_sel_hi:[1,0,1]
	v_pk_add_f32 v[34:35], v[36:37], v[36:37] op_sel:[0,1] op_sel_hi:[1,0]
	v_add_f32_e32 v32, 0, v32
	s_waitcnt vmcnt(2)
	v_pk_fma_f32 v[178:179], v[54:55], s[40:41], v[202:203] op_sel_hi:[1,0,1]
	v_pk_fma_f32 v[180:181], v[52:53], s[40:41], v[184:185] op_sel_hi:[1,0,1]
	v_add_f32_e32 v44, v172, v173
	v_add_f32_e32 v46, v170, v171
	v_mov_b32_e32 v49, v176
	v_mov_b32_e32 v45, v174
	v_mov_b32_e32 v47, v175
	v_mov_b32_e32 v35, v177
	v_add_f32_e32 v48, v32, v33
	v_pk_mov_b32 v[50:51], v[180:181], v[178:179] op_sel:[1,0]
	v_mov_b32_e32 v52, v180
	v_mov_b32_e32 v53, v179
	v_pk_add_f32 v[38:39], v[44:45], v[46:47]
	v_pk_add_f32 v[32:33], v[48:49], v[34:35]
	v_pk_mul_f32 v[206:207], v[0:1], v[188:189]
	v_pk_add_f32 v[40:41], v[50:51], v[52:53]
	v_pk_add_f32 v[32:33], v[32:33], v[38:39]
	s_waitcnt vmcnt(1)
	v_pk_fma_f32 v[186:187], v[58:59], s[40:41], v[186:187] op_sel_hi:[1,0,1]
	v_pk_fma_f32 v[188:189], v[56:57], s[40:41], v[204:205] op_sel_hi:[1,0,1]
	s_waitcnt vmcnt(0)
	v_pk_fma_f32 v[182:183], v[62:63], s[40:41], v[208:209] op_sel_hi:[1,0,1]
	v_pk_fma_f32 v[184:185], v[60:61], s[40:41], v[206:207] op_sel_hi:[1,0,1]
	v_pk_add_f32 v[36:37], v[40:41], v[40:41] op_sel:[0,1] op_sel_hi:[1,0]
	v_pk_add_f32 v[32:33], v[32:33], v[32:33] op_sel:[0,1] op_sel_hi:[1,0]
	v_add_f32_e32 v54, v188, v189
	v_add_f32_e32 v56, v186, v187
	v_mov_b32_e32 v55, v182
	v_mov_b32_e32 v57, v183
	v_mov_b32_e32 v37, v185
	v_mov_b32_e32 v33, v184
	v_pk_add_f32 v[42:43], v[54:55], v[56:57]
	v_pk_add_f32 v[32:33], v[32:33], v[36:37]
	global_load_dwordx4 v[64:67], v[112:113], off
	global_load_dwordx4 v[68:71], v[114:115], off
	v_pk_add_f32 v[32:33], v[32:33], v[42:43]
	v_lshl_add_u64 v[196:197], s[0:1], 0, v[128:129]
	v_add_f32_e32 v32, v32, v33
	ds_bpermute_b32 v33, v73, v32
	s_waitcnt lgkmcnt(0)
	v_add_f32_e32 v32, v32, v33
	ds_bpermute_b32 v33, v217, v32
	s_waitcnt lgkmcnt(0)
	v_add_f32_e32 v32, v32, v33
	ds_bpermute_b32 v33, v218, v32
	s_waitcnt lgkmcnt(0)
	v_add_f32_e32 v32, v32, v33
	ds_bpermute_b32 v33, v219, v32
	s_waitcnt lgkmcnt(0)
	v_add_f32_e32 v32, v32, v33
	ds_bpermute_b32 v33, v220, v32
	s_waitcnt lgkmcnt(0)
	v_add_f32_e32 v32, v32, v33
	ds_bpermute_b32 v33, v221, v32
	s_waitcnt lgkmcnt(0)
	v_add_f32_e32 v32, v32, v33
	v_fmamk_f32 v191, v32, 0xba000000, v191
	v_fmamk_f32 v199, v32, 0xba000000, v199
	v_fmamk_f32 v193, v32, 0xba000000, v193
	v_fmamk_f32 v195, v32, 0xba000000, v195
	v_fmac_f32_e32 v190, 0xba000000, v32
	v_fmac_f32_e32 v198, 0xba000000, v32
	v_fmac_f32_e32 v192, 0xba000000, v32
	v_fmac_f32_e32 v194, 0xba000000, v32
	v_fmamk_f32 v169, v32, 0xba000000, v169
	v_fmac_f32_e32 v168, 0xba000000, v32
	v_fmamk_f32 v167, v32, 0xba000000, v167
	v_fmac_f32_e32 v166, 0xba000000, v32
	v_mov_b32_e32 v34, v199
	v_mov_b32_e32 v35, v195
	v_mov_b32_e32 v38, v191
	v_mov_b32_e32 v39, v193
	v_fmamk_f32 v173, v32, 0xba000000, v173
	v_fmac_f32_e32 v172, 0xba000000, v32
	v_fmamk_f32 v171, v32, 0xba000000, v171
	v_fmac_f32_e32 v170, 0xba000000, v32
	v_fmamk_f32 v175, v32, 0xba000000, v175
	v_fmac_f32_e32 v174, 0xba000000, v32
	v_fmamk_f32 v177, v32, 0xba000000, v177
	v_fmac_f32_e32 v176, 0xba000000, v32
	v_fmamk_f32 v181, v32, 0xba000000, v181
	v_fmac_f32_e32 v180, 0xba000000, v32
	v_fmamk_f32 v179, v32, 0xba000000, v179
	v_fmac_f32_e32 v178, 0xba000000, v32
	v_fmamk_f32 v189, v32, 0xba000000, v189
	v_fmac_f32_e32 v188, 0xba000000, v32
	v_fmamk_f32 v187, v32, 0xba000000, v187
	v_fmac_f32_e32 v186, 0xba000000, v32
	v_fmamk_f32 v183, v32, 0xba000000, v183
	v_fmac_f32_e32 v182, 0xba000000, v32
	v_fmamk_f32 v185, v32, 0xba000000, v185
	v_fmac_f32_e32 v184, 0xba000000, v32
	v_mov_b32_e32 v32, v198
	v_mov_b32_e32 v33, v194
	v_mov_b32_e32 v36, v190
	v_mov_b32_e32 v37, v192
	v_pk_mul_f32 v[40:41], v[166:167], v[166:167]
	v_pk_mul_f32 v[42:43], v[168:169], v[168:169]
	v_pk_mul_f32 v[34:35], v[34:35], v[34:35]
	v_pk_mul_f32 v[38:39], v[38:39], v[38:39]
	v_pk_mov_b32 v[56:57], v[42:43], v[40:41] op_sel:[1,0]
	v_mov_b32_e32 v43, v41
	v_pk_fma_f32 v[32:33], v[32:33], v[32:33], v[34:35]
	v_pk_fma_f32 v[34:35], v[36:37], v[36:37], v[38:39]
	v_mul_f32_e32 v44, v172, v172
	v_mul_f32_e32 v46, v170, v170
	v_pk_add_f32 v[36:37], v[56:57], v[42:43]
	v_pk_add_f32 v[32:33], v[32:33], v[34:35]
	v_pk_fma_f32 v[40:41], v[172:173], v[172:173], v[44:45] op_sel_hi:[1,1,0]
	v_pk_fma_f32 v[44:45], v[170:171], v[170:171], v[46:47] op_sel_hi:[1,1,0]
	v_pk_add_f32 v[34:35], v[36:37], v[36:37] op_sel_hi:[0,1]
	v_pk_add_f32 v[32:33], v[32:33], v[32:33] op_sel_hi:[0,1]
	v_pk_mul_f32 v[48:49], v[178:179], v[178:179]
	v_pk_mul_f32 v[50:51], v[180:181], v[180:181]
	v_mul_f32_e32 v40, v176, v176
	v_mul_f32_e32 v44, v177, v177
	v_mul_f32_e32 v34, v174, v174
	v_mul_f32_e32 v32, v175, v175
	v_pk_mov_b32 v[46:47], v[50:51], v[48:49] op_sel:[1,0]
	v_mov_b32_e32 v51, v49
	v_pk_add_f32 v[36:37], v[40:41], v[44:45]
	v_pk_add_f32 v[32:33], v[34:35], v[32:33]
	v_mul_f32_e32 v52, v188, v188
	v_mul_f32_e32 v54, v186, v186
	v_pk_add_f32 v[38:39], v[46:47], v[50:51]
	v_pk_add_f32 v[32:33], v[36:37], v[32:33]
	v_pk_fma_f32 v[48:49], v[188:189], v[188:189], v[52:53] op_sel_hi:[1,1,0]
	v_pk_fma_f32 v[52:53], v[186:187], v[186:187], v[54:55] op_sel_hi:[1,1,0]
	v_pk_add_f32 v[38:39], v[38:39], v[38:39] op_sel_hi:[0,1]
	v_pk_add_f32 v[32:33], v[32:33], v[32:33] op_sel_hi:[0,1]
	v_mul_f32_e32 v48, v184, v184
	v_mul_f32_e32 v52, v185, v185
	v_mul_f32_e32 v38, v182, v182
	v_mul_f32_e32 v32, v183, v183
	v_pk_add_f32 v[40:41], v[48:49], v[52:53]
	v_pk_add_f32 v[32:33], v[38:39], v[32:33]
	s_nop 0
	v_pk_add_f32 v[32:33], v[40:41], v[32:33]
	s_nop 0
	v_add_f32_e32 v32, v32, v33
	ds_bpermute_b32 v33, v73, v32
	s_waitcnt lgkmcnt(0)
; #define GAS __attribute__((address_space(1)))
; __device__ __forceinline__ unsigned pk2(float lo, float hi) { return f2bf(lo) | (f2bf(hi) << 16); }
; __device__ __forceinline__ f32x4 bf4(unsigned a, unsigned b) { return (f32x4){bflo(a), bfhi(a), bflo(b), bfhi(b)}; }
; template <int l>
; __device__ __forceinline__ void layer_phases(Frame& F, const XcdBarrier& bar, const int lo, const int hi) {
;     ...
;                     for (int j = 0; j < 8; ++j) { const size_t off = (size_t)(m0 + 2 * rp + rr) * D + 4 * lq + 256 * j;
;                         f32x4 xv; if (l == 0) xv = __builtin_nontemporal_load((const GAS f32x4*)(xin + off)); else { const v2u xw_ = __builtin_nontemporal_load((const GAS v2u*)(xinb + off)); xv = bf4(xw_.x, xw_.y); } const v2u mw = __builtin_nontemporal_load((const GAS v2u*)(mixb + off)); const f32x4 gv = *(const GAS f32x4*)(mrow + 4096 + 4 * lq + 256 * j);
;                         vv[rr][j] = xv * ALPHA + gv * (f32x4){bflo(mw.x), bfhi(mw.x), bflo(mw.y), bfhi(mw.y)}; }
; #pragma unroll
;                 for (int rq = 0; rq < 2; ++rq) { const int rr = 2 * rp + rq, m = m0 + rr, rloc = 4 * F.wave + rr;
;                     f32x4 (&v)[8] = vv[rq]; float s = 0.f;
; #pragma unroll
;                     for (int j = 0; j < 8; ++j) s += (v[j].x + v[j].y) + (v[j].z + v[j].w);
;                     const float mean = wave_sum(s) * (1.f / D); float s2 = 0.f;
; #pragma unroll
;                     for (int j = 0; j < 8; ++j) { v[j] = v[j] - mean; s2 += (v[j].x * v[j].x + v[j].y * v[j].y) + (v[j].z * v[j].z + v[j].w * v[j].w); }
;                     const float rstd = 1.f / sqrtf(wave_sum(s2) * (1.f / D) + LN_EPS);
; #pragma unroll
;                     for (int j = 0; j < 8; ++j) { const int k = 4 * lq + 256 * j;
;                         const f32x4 xv = v[j] * rstd * *(const GAS f32x4*)(g1 + k) + *(const GAS f32x4*)(b1 + k);
;                         { v2u xo; xo.x = pk2(xv.x, xv.y); xo.y = pk2(xv.z, xv.w); *(GAS v2u*)(x1 + (size_t)m * D + k) = xo; }
;                         const f32x4 hv = xv * (*(const GAS f32x4*)(mrow + 8192 + k) + 1.0f) + *(const GAS f32x4*)(mrow + 6144 + k);
;                         v2u o; o.x = pk2(hv.x, hv.y); o.y = pk2(hv.z, hv.w);
;                         *(GAS unsigned*)(h2q + (size_t)m * D + k) = pk4_fp8(hv.x, hv.y, hv.z, hv.w);
	v_add_f32_e32 v34, v32, v33
	ds_bpermute_b32 v35, v217, v34
	v_lshl_add_u64 v[32:33], s[16:17], 0, v[86:87]
	v_lshl_add_u64 v[214:215], v[32:33], 1, s[26:27]
	s_waitcnt lgkmcnt(0)
	v_add_f32_e32 v36, v34, v35
	ds_bpermute_b32 v37, v218, v36
	v_lshl_add_u64 v[34:35], v[32:33], 2, s[20:21]
	v_add_co_u32_e32 v32, vcc, s87, v34
	global_load_dwordx4 v[44:47], v[34:35], off nt
	global_load_dwordx4 v[52:55], v[34:35], off offset:1024 nt
	global_load_dwordx4 v[48:51], v[34:35], off offset:2048 nt
	global_load_dwordx4 v[40:43], v[34:35], off offset:3072 nt
	s_waitcnt lgkmcnt(0)
	v_add_f32_e32 v36, v36, v37
	ds_bpermute_b32 v37, v219, v36
	v_addc_co_u32_e32 v33, vcc, 0, v35, vcc
	global_load_dwordx2 v[206:207], v[214:215], off nt
	global_load_dwordx2 v[204:205], v[214:215], off offset:512 nt
	global_load_dwordx2 v[202:203], v[214:215], off offset:1024 nt
	global_load_dwordx2 v[200:201], v[214:215], off offset:1536 nt
	s_waitcnt lgkmcnt(0)
	v_add_f32_e32 v36, v36, v37
	ds_bpermute_b32 v37, v220, v36
	s_waitcnt lgkmcnt(0)
	v_add_f32_e32 v34, v36, v37
	ds_bpermute_b32 v35, v221, v34
	s_waitcnt lgkmcnt(0)
	v_add_f32_e32 v34, v34, v35
	v_fmamk_f32 v34, v34, 0x3a000000, v223
	v_mul_f32_e32 v35, 0x4f800000, v34
	v_cmp_gt_f32_e32 vcc, s89, v34
	s_waitcnt vmcnt(2)
	v_and_b32_e32 v233, 0xffff0000, v204
	v_cndmask_b32_e32 v80, v34, v35, vcc
	v_sqrt_f32_e32 v208, v80
	global_load_dwordx4 v[56:59], v[32:33], off nt
	global_load_dwordx4 v[60:63], v[32:33], off offset:1024 nt
	global_load_dwordx4 v[36:39], v[32:33], off offset:2048 nt
	s_nop 0
	global_load_dwordx4 v[32:35], v[32:33], off offset:3072 nt
	s_waitcnt vmcnt(4)
	v_lshlrev_b32_e32 v236, 16, v200
	v_and_b32_e32 v237, 0xffff0000, v200
	v_add_u32_e32 v209, -1, v208
	v_add_u32_e32 v210, 1, v208
	v_fma_f32 v211, -v209, v208, v80
	v_fma_f32 v212, -v210, v208, v80
	v_cmp_ge_f32_e64 s[14:15], 0, v211
	v_lshlrev_b32_e32 v200, 16, v201
	v_and_b32_e32 v201, 0xffff0000, v201
	v_cndmask_b32_e64 v208, v208, v209, s[14:15]
	v_cmp_lt_f32_e64 s[14:15], 0, v212
	v_pk_mul_f32 v[18:19], v[18:19], v[200:201]
	v_lshlrev_b32_e32 v234, 16, v202
	v_cndmask_b32_e64 v208, v208, v210, s[14:15]
	v_mul_f32_e32 v209, 0x37800000, v208
	v_cndmask_b32_e32 v208, v208, v209, vcc
	v_cmp_class_f32_e32 vcc, v80, v224
	v_and_b32_e32 v235, 0xffff0000, v202
	v_lshlrev_b32_e32 v202, 16, v203
	v_cndmask_b32_e32 v80, v208, v80, vcc
	v_div_scale_f32 v228, s[0:1], v80, v80, 1.0
	v_rcp_f32_e32 v229, v228
	v_div_scale_f32 v230, vcc, 1.0, v80, 1.0
	global_load_dwordx2 v[208:209], v[214:215], off offset:2048 nt
	global_load_dwordx2 v[212:213], v[214:215], off offset:2560 nt
	global_load_dwordx2 v[210:211], v[214:215], off offset:3072 nt
	s_nop 0
	global_load_dwordx2 v[214:215], v[214:215], off offset:3584 nt
	v_fma_f32 v231, -v228, v229, 1.0
	v_fmac_f32_e32 v229, v231, v229
	v_mul_f32_e32 v231, v230, v229
	v_fma_f32 v232, -v228, v231, v230
	v_fmac_f32_e32 v231, v232, v229
	v_fma_f32 v228, -v228, v231, v230
	v_div_fmas_f32 v228, v228, v229, v231
	v_div_fixup_f32 v80, v228, v80, 1.0
	v_pk_mul_f32 v[198:199], v[198:199], v[80:81] op_sel_hi:[1,0]
	v_pk_mul_f32 v[190:191], v[190:191], v[80:81] op_sel_hi:[1,0]
	v_pk_fma_f32 v[198:199], v[64:65], v[198:199], v[68:69]
	v_pk_fma_f32 v[190:191], v[66:67], v[190:191], v[70:71]
	v_bfe_u32 v64, v198, 16, 1
	v_bfe_u32 v66, v190, 16, 1
	v_bfe_u32 v65, v199, 16, 1
	v_bfe_u32 v67, v191, 16, 1
	v_add3_u32 v64, v198, v64, s90
	v_add3_u32 v66, v190, v66, s90
	v_add3_u32 v65, v199, v65, s90
	v_add3_u32 v67, v191, v67, s90
	v_lshrrev_b32_e32 v64, 16, v64
	v_lshrrev_b32_e32 v66, 16, v66
	v_and_or_b32 v64, v65, s86, v64
	v_and_or_b32 v65, v67, s86, v66
	global_store_dwordx2 v[196:197], v[64:65], off
	global_load_dwordx4 v[64:67], v[82:83], off offset:-4096
	s_nop 0
	global_load_dwordx4 v[68:71], v[84:85], off offset:-4096
	v_mov_b32_e32 v228, 0
	s_add_u32 s0, s50, s18
	s_addc_u32 s1, s51, s19
	v_pk_mul_f32 v[194:195], v[194:195], v[80:81] op_sel_hi:[1,0]
	v_pk_mul_f32 v[192:193], v[192:193], v[80:81] op_sel_hi:[1,0]
	v_pk_mul_f32 v[168:169], v[168:169], v[80:81] op_sel_hi:[1,0]
	v_pk_mul_f32 v[166:167], v[166:167], v[80:81] op_sel_hi:[1,0]
	v_pk_mul_f32 v[172:173], v[172:173], v[80:81] op_sel_hi:[1,0]
	v_pk_mul_f32 v[170:171], v[170:171], v[80:81] op_sel_hi:[1,0]
	v_pk_mul_f32 v[176:177], v[176:177], v[80:81] op_sel_hi:[1,0]
	v_pk_mul_f32 v[174:175], v[174:175], v[80:81] op_sel_hi:[1,0]
	v_pk_mul_f32 v[180:181], v[180:181], v[80:81] op_sel_hi:[1,0]
	v_pk_mul_f32 v[178:179], v[178:179], v[80:81] op_sel_hi:[1,0]
	v_pk_mul_f32 v[188:189], v[188:189], v[80:81] op_sel_hi:[1,0]
	v_pk_mul_f32 v[186:187], v[186:187], v[80:81] op_sel_hi:[1,0]
	v_lshlrev_b32_e32 v232, 16, v204
	v_lshlrev_b32_e32 v204, 16, v205
	v_and_b32_e32 v205, 0xffff0000, v205
	v_and_b32_e32 v203, 0xffff0000, v203
	v_pk_mul_f32 v[26:27], v[26:27], v[204:205]
	v_pk_mul_f32 v[204:205], v[24:25], v[232:233]
	v_pk_mul_f32 v[16:17], v[16:17], v[236:237]
	v_pk_mul_f32 v[22:23], v[22:23], v[202:203]
	v_pk_mul_f32 v[202:203], v[20:21], v[234:235]
	v_pk_fma_f32 v[50:51], v[50:51], s[40:41], v[22:23] op_sel_hi:[1,0,1]
	v_pk_fma_f32 v[48:49], v[48:49], s[40:41], v[202:203] op_sel_hi:[1,0,1]
	s_waitcnt vmcnt(6)
	v_lshlrev_b32_e32 v238, 16, v208
	v_and_b32_e32 v239, 0xffff0000, v208
	v_lshlrev_b32_e32 v208, 16, v209
	s_waitcnt vmcnt(3)
; #define GAS __attribute__((address_space(1)))
; #define LAS __attribute__((address_space(3)))
; __device__ __forceinline__ unsigned pk2(float lo, float hi) { return f2bf(lo) | (f2bf(hi) << 16); }
; __device__ __forceinline__ unsigned pk4_fp8(float a, float b, float c, float d) { int r = __builtin_amdgcn_cvt_pk_fp8_f32(a, b, 0, false); r = __builtin_amdgcn_cvt_pk_fp8_f32(c, d, r, true); return (unsigned)r; }
; template <int l>
; __device__ __forceinline__ void layer_phases(Frame& F, const XcdBarrier& bar, const int lo, const int hi) {
;     ...
; #pragma unroll
;                     for (int j = 0; j < 8; ++j) { const int k = 4 * lq + 256 * j;
;                         const f32x4 xv = v[j] * rstd * *(const GAS f32x4*)(g1 + k) + *(const GAS f32x4*)(b1 + k);
;                         { v2u xo; xo.x = pk2(xv.x, xv.y); xo.y = pk2(xv.z, xv.w); *(GAS v2u*)(x1 + (size_t)m * D + k) = xo; }
;                         const f32x4 hv = xv * (*(const GAS f32x4*)(mrow + 8192 + k) + 1.0f) + *(const GAS f32x4*)(mrow + 6144 + k);
;                         v2u o; o.x = pk2(hv.x, hv.y); o.y = pk2(hv.z, hv.w);
;                         *(GAS unsigned*)(h2q + (size_t)m * D + k) = pk4_fp8(hv.x, hv.y, hv.z, hv.w);
;                         const int chunk = (lq >> 1) + 32 * j;
;                         *(LAS v2u*)(h2s + rloc * 4096 + ((chunk ^ (rloc & 15)) << 4) + (lq & 1) * 8) = o; }
	v_lshlrev_b32_e32 v244, 16, v214
	v_and_b32_e32 v245, 0xffff0000, v214
	v_pk_mul_f32 v[200:201], v[0:1], v[244:245]
	v_lshlrev_b32_e32 v214, 16, v215
	v_and_b32_e32 v215, 0xffff0000, v215
	v_and_b32_e32 v209, 0xffff0000, v209
	v_lshlrev_b32_e32 v240, 16, v212
	v_and_b32_e32 v241, 0xffff0000, v212
	v_lshlrev_b32_e32 v212, 16, v213
	v_and_b32_e32 v213, 0xffff0000, v213
	v_lshlrev_b32_e32 v242, 16, v210
	v_and_b32_e32 v243, 0xffff0000, v210
	v_lshlrev_b32_e32 v210, 16, v211
	v_and_b32_e32 v211, 0xffff0000, v211
	v_pk_mul_f32 v[12:13], v[12:13], v[238:239]
	v_pk_mul_f32 v[14:15], v[14:15], v[208:209]
	v_pk_mul_f32 v[8:9], v[8:9], v[240:241]
	v_pk_mul_f32 v[10:11], v[10:11], v[212:213]
	v_pk_mul_f32 v[4:5], v[4:5], v[242:243]
	v_pk_mul_f32 v[6:7], v[6:7], v[210:211]
	s_waitcnt vmcnt(1)
	v_pk_add_f32 v[64:65], v[64:65], 1.0 op_sel_hi:[1,0]
	s_waitcnt vmcnt(0)
	v_pk_fma_f32 v[64:65], v[64:65], v[198:199], v[68:69]
	v_pk_add_f32 v[66:67], v[66:67], 1.0 op_sel_hi:[1,0]
	v_cvt_pk_fp8_f32 v228, v64, v65
	v_pk_fma_f32 v[66:67], v[66:67], v[190:191], v[70:71]
	v_lshl_add_u64 v[190:191], s[0:1], 0, v[86:87]
	s_lshl_b64 s[0:1], s[48:49], 12
	v_cvt_pk_fp8_f32 v228, v66, v67 op_sel:[0,0,1]
	s_add_u32 s0, s3, s0
	s_addc_u32 s1, s41, s1
	global_store_dword v[190:191], v228, off
	global_load_dwordx4 v[68:71], v[112:113], off offset:1024
	s_nop 0
	global_load_dwordx4 v[228:231], v[114:115], off offset:1024
	s_waitcnt vmcnt(0)
	v_pk_fma_f32 v[198:199], v[70:71], v[192:193], v[230:231]
	v_pk_fma_f32 v[228:229], v[68:69], v[194:195], v[228:229]
	v_bfe_u32 v70, v198, 16, 1
	v_bfe_u32 v68, v228, 16, 1
	v_bfe_u32 v69, v229, 16, 1
	v_bfe_u32 v71, v199, 16, 1
	v_add3_u32 v68, v228, v68, s90
	v_add3_u32 v70, v198, v70, s90
	v_add3_u32 v69, v229, v69, s90
	v_add3_u32 v71, v199, v71, s90
	v_lshrrev_b32_e32 v68, 16, v68
	v_lshrrev_b32_e32 v70, 16, v70
	v_and_or_b32 v68, v69, s86, v68
	v_and_or_b32 v69, v71, s86, v70
	global_store_dwordx2 v[196:197], v[68:69], off offset:512
	global_load_dwordx4 v[68:71], v[122:123], off offset:1024
	s_nop 0
	global_load_dwordx4 v[192:195], v[120:121], off offset:1024
	v_mov_b32_e32 v230, 0
	s_waitcnt vmcnt(1)
	v_pk_add_f32 v[68:69], v[68:69], 1.0 op_sel_hi:[1,0]
	s_waitcnt vmcnt(0)
	v_pk_fma_f32 v[68:69], v[68:69], v[228:229], v[192:193]
	v_pk_add_f32 v[70:71], v[70:71], 1.0 op_sel_hi:[1,0]
	v_cvt_pk_fp8_f32 v230, v68, v69
	v_pk_fma_f32 v[70:71], v[70:71], v[198:199], v[194:195]
	s_nop 0
	v_cvt_pk_fp8_f32 v230, v70, v71 op_sel:[0,0,1]
	global_store_dword v[190:191], v230, off offset:256
	global_load_dwordx4 v[192:195], v[112:113], off offset:2048
	s_nop 0
	global_load_dwordx4 v[228:231], v[114:115], off offset:2048
	s_waitcnt vmcnt(0)
	v_pk_fma_f32 v[198:199], v[194:195], v[166:167], v[230:231]
	v_pk_fma_f32 v[228:229], v[192:193], v[168:169], v[228:229]
	v_bfe_u32 v168, v198, 16, 1
	v_bfe_u32 v166, v228, 16, 1
	v_bfe_u32 v167, v229, 16, 1
	v_bfe_u32 v169, v199, 16, 1
	v_add3_u32 v166, v228, v166, s90
	v_add3_u32 v168, v198, v168, s90
	v_add3_u32 v167, v229, v167, s90
	v_add3_u32 v169, v199, v169, s90
	v_lshrrev_b32_e32 v166, 16, v166
	v_lshrrev_b32_e32 v168, 16, v168
	v_and_or_b32 v166, v167, s86, v166
	v_and_or_b32 v167, v169, s86, v168
	global_store_dwordx2 v[196:197], v[166:167], off offset:1024
	global_load_dwordx4 v[166:169], v[122:123], off offset:2048
	s_nop 0
	global_load_dwordx4 v[192:195], v[120:121], off offset:2048
	v_mov_b32_e32 v230, 0
	s_waitcnt vmcnt(1)
	v_pk_add_f32 v[166:167], v[166:167], 1.0 op_sel_hi:[1,0]
	s_waitcnt vmcnt(0)
	v_pk_fma_f32 v[166:167], v[166:167], v[228:229], v[192:193]
	v_pk_add_f32 v[168:169], v[168:169], 1.0 op_sel_hi:[1,0]
	v_cvt_pk_fp8_f32 v230, v166, v167
	v_pk_fma_f32 v[168:169], v[168:169], v[198:199], v[194:195]
	s_nop 0
	v_cvt_pk_fp8_f32 v230, v168, v169 op_sel:[0,0,1]
	global_store_dword v[190:191], v230, off offset:512
	global_load_dwordx4 v[192:195], v[112:113], off offset:3072
	s_nop 0
	global_load_dwordx4 v[228:231], v[114:115], off offset:3072
	s_waitcnt vmcnt(0)
	v_pk_fma_f32 v[198:199], v[170:171], v[194:195], v[230:231]
	v_pk_fma_f32 v[228:229], v[172:173], v[192:193], v[228:229]
	v_bfe_u32 v172, v198, 16, 1
	v_bfe_u32 v170, v228, 16, 1
	v_bfe_u32 v171, v229, 16, 1
	v_bfe_u32 v173, v199, 16, 1
	v_add3_u32 v170, v228, v170, s90
	v_add3_u32 v172, v198, v172, s90
	v_add3_u32 v171, v229, v171, s90
	v_add3_u32 v173, v199, v173, s90
	v_lshrrev_b32_e32 v170, 16, v170
	v_lshrrev_b32_e32 v172, 16, v172
	v_and_or_b32 v170, v171, s86, v170
	v_and_or_b32 v171, v173, s86, v172
	global_store_dwordx2 v[196:197], v[170:171], off offset:1536
	global_load_dwordx4 v[170:173], v[122:123], off offset:3072
	s_nop 0
	global_load_dwordx4 v[192:195], v[120:121], off offset:3072
	v_mov_b32_e32 v230, 0
	s_waitcnt vmcnt(1)
	v_pk_add_f32 v[170:171], v[170:171], 1.0 op_sel_hi:[1,0]
	s_waitcnt vmcnt(0)
	v_pk_fma_f32 v[170:171], v[228:229], v[170:171], v[192:193]
	v_pk_add_f32 v[172:173], v[172:173], 1.0 op_sel_hi:[1,0]
	v_cvt_pk_fp8_f32 v230, v170, v171
	v_pk_fma_f32 v[172:173], v[198:199], v[172:173], v[194:195]
	s_nop 0
	v_cvt_pk_fp8_f32 v230, v172, v173 op_sel:[0,0,1]
	global_store_dword v[190:191], v230, off offset:768
	global_load_dwordx4 v[192:195], v[88:89], off
	s_nop 0
	global_load_dwordx4 v[228:231], v[90:91], off
	s_waitcnt vmcnt(0)
	v_pk_fma_f32 v[198:199], v[174:175], v[194:195], v[230:231]
	v_pk_fma_f32 v[228:229], v[176:177], v[192:193], v[228:229]
	v_bfe_u32 v176, v198, 16, 1
	v_bfe_u32 v174, v228, 16, 1
	v_bfe_u32 v175, v229, 16, 1
	v_bfe_u32 v177, v199, 16, 1
	v_add3_u32 v174, v228, v174, s90
	v_add3_u32 v176, v198, v176, s90
	v_add3_u32 v175, v229, v175, s90
	v_add3_u32 v177, v199, v177, s90
	v_lshrrev_b32_e32 v174, 16, v174
	v_lshrrev_b32_e32 v176, 16, v176
	v_and_or_b32 v174, v175, s86, v174
	v_and_or_b32 v175, v177, s86, v176
	global_store_dwordx2 v[196:197], v[174:175], off offset:2048
	global_load_dwordx4 v[174:177], v[82:83], off
	s_nop 0
	global_load_dwordx4 v[192:195], v[84:85], off
	v_mov_b32_e32 v230, 0
	s_waitcnt vmcnt(1)
; #define GAS __attribute__((address_space(1)))
; #define LAS __attribute__((address_space(3)))
; template <int l>
; __device__ __forceinline__ void layer_phases(Frame& F, const XcdBarrier& bar, const int lo, const int hi) {
;     ...
;                     for (int j = 0; j < 8; ++j) { const size_t off = (size_t)(m0 + 2 * rp + rr) * D + 4 * lq + 256 * j;
;                         f32x4 xv; if (l == 0) xv = __builtin_nontemporal_load((const GAS f32x4*)(xin + off)); else { const v2u xw_ = __builtin_nontemporal_load((const GAS v2u*)(xinb + off)); xv = bf4(xw_.x, xw_.y); } const v2u mw = __builtin_nontemporal_load((const GAS v2u*)(mixb + off)); const f32x4 gv = *(const GAS f32x4*)(mrow + 4096 + 4 * lq + 256 * j);
;                         vv[rr][j] = xv * ALPHA + gv * (f32x4){bflo(mw.x), bfhi(mw.x), bflo(mw.y), bfhi(mw.y)}; }
; #pragma unroll
;                 for (int rq = 0; rq < 2; ++rq) { const int rr = 2 * rp + rq, m = m0 + rr, rloc = 4 * F.wave + rr;
;                     f32x4 (&v)[8] = vv[rq]; float s = 0.f;
; #pragma unroll
;                     for (int j = 0; j < 8; ++j) s += (v[j].x + v[j].y) + (v[j].z + v[j].w);
;                     const float mean = wave_sum(s) * (1.f / D); float s2 = 0.f;
; #pragma unroll
;                     for (int j = 0; j < 8; ++j) { v[j] = v[j] - mean; s2 += (v[j].x * v[j].x + v[j].y * v[j].y) + (v[j].z * v[j].z + v[j].w * v[j].w); }
;                     const float rstd = 1.f / sqrtf(wave_sum(s2) * (1.f / D) + LN_EPS);
; #pragma unroll
;                     for (int j = 0; j < 8; ++j) { const int k = 4 * lq + 256 * j;
;                         const f32x4 xv = v[j] * rstd * *(const GAS f32x4*)(g1 + k) + *(const GAS f32x4*)(b1 + k);
;                         { v2u xo; xo.x = pk2(xv.x, xv.y); xo.y = pk2(xv.z, xv.w); *(GAS v2u*)(x1 + (size_t)m * D + k) = xo; }
;                         const f32x4 hv = xv * (*(const GAS f32x4*)(mrow + 8192 + k) + 1.0f) + *(const GAS f32x4*)(mrow + 6144 + k);
;                         v2u o; o.x = pk2(hv.x, hv.y); o.y = pk2(hv.z, hv.w);
;                         *(GAS unsigned*)(h2q + (size_t)m * D + k) = pk4_fp8(hv.x, hv.y, hv.z, hv.w);
;                         const int chunk = (lq >> 1) + 32 * j;
;                         *(LAS v2u*)(h2s + rloc * 4096 + ((chunk ^ (rloc & 15)) << 4) + (lq & 1) * 8) = o; }
	v_pk_add_f32 v[174:175], v[174:175], 1.0 op_sel_hi:[1,0]
	s_waitcnt vmcnt(0)
	v_pk_fma_f32 v[174:175], v[228:229], v[174:175], v[192:193]
	v_pk_add_f32 v[176:177], v[176:177], 1.0 op_sel_hi:[1,0]
	v_cvt_pk_fp8_f32 v230, v174, v175
	v_pk_fma_f32 v[176:177], v[198:199], v[176:177], v[194:195]
	s_nop 0
	v_cvt_pk_fp8_f32 v230, v176, v177 op_sel:[0,0,1]
	global_store_dword v[190:191], v230, off offset:1024
	global_load_dwordx4 v[192:195], v[88:89], off offset:1024
	s_nop 0
	global_load_dwordx4 v[228:231], v[90:91], off offset:1024
	s_waitcnt vmcnt(0)
	v_pk_fma_f32 v[198:199], v[178:179], v[194:195], v[230:231]
	v_pk_fma_f32 v[228:229], v[180:181], v[192:193], v[228:229]
	v_bfe_u32 v180, v198, 16, 1
	v_bfe_u32 v178, v228, 16, 1
	v_bfe_u32 v179, v229, 16, 1
	v_bfe_u32 v181, v199, 16, 1
	v_add3_u32 v178, v228, v178, s90
	v_add3_u32 v180, v198, v180, s90
	v_add3_u32 v179, v229, v179, s90
	v_add3_u32 v181, v199, v181, s90
	v_lshrrev_b32_e32 v178, 16, v178
	v_lshrrev_b32_e32 v180, 16, v180
	v_and_or_b32 v178, v179, s86, v178
	v_and_or_b32 v179, v181, s86, v180
	global_store_dwordx2 v[196:197], v[178:179], off offset:2560
	global_load_dwordx4 v[178:181], v[82:83], off offset:1024
	s_nop 0
	global_load_dwordx4 v[192:195], v[84:85], off offset:1024
	v_mov_b32_e32 v230, 0
	s_waitcnt vmcnt(1)
	v_pk_add_f32 v[178:179], v[178:179], 1.0 op_sel_hi:[1,0]
	s_waitcnt vmcnt(0)
	v_pk_fma_f32 v[178:179], v[228:229], v[178:179], v[192:193]
	v_pk_add_f32 v[180:181], v[180:181], 1.0 op_sel_hi:[1,0]
	v_cvt_pk_fp8_f32 v230, v178, v179
	v_pk_fma_f32 v[180:181], v[198:199], v[180:181], v[194:195]
	s_nop 0
	v_cvt_pk_fp8_f32 v230, v180, v181 op_sel:[0,0,1]
	global_store_dword v[190:191], v230, off offset:1280
	global_load_dwordx4 v[192:195], v[88:89], off offset:2048
	s_nop 0
	global_load_dwordx4 v[228:231], v[90:91], off offset:2048
	s_waitcnt vmcnt(0)
	v_pk_fma_f32 v[198:199], v[186:187], v[194:195], v[230:231]
	v_pk_fma_f32 v[228:229], v[188:189], v[192:193], v[228:229]
	v_bfe_u32 v188, v198, 16, 1
	v_bfe_u32 v186, v228, 16, 1
	v_bfe_u32 v187, v229, 16, 1
	v_bfe_u32 v189, v199, 16, 1
	v_add3_u32 v186, v228, v186, s90
	v_add3_u32 v188, v198, v188, s90
	v_add3_u32 v187, v229, v187, s90
	v_add3_u32 v189, v199, v189, s90
	v_lshrrev_b32_e32 v186, 16, v186
	v_lshrrev_b32_e32 v188, 16, v188
	v_and_or_b32 v186, v187, s86, v186
	v_and_or_b32 v187, v189, s86, v188
	global_store_dwordx2 v[196:197], v[186:187], off offset:3072
	global_load_dwordx4 v[186:189], v[82:83], off offset:2048
	s_nop 0
	global_load_dwordx4 v[192:195], v[84:85], off offset:2048
	v_lshlrev_b32_e32 v230, 16, v206
	v_and_b32_e32 v231, 0xffff0000, v206
	v_lshlrev_b32_e32 v206, 16, v207
	v_and_b32_e32 v207, 0xffff0000, v207
	v_pk_mul_f32 v[30:31], v[30:31], v[206:207]
	v_pk_mul_f32 v[206:207], v[2:3], v[214:215]
	v_pk_mul_f32 v[28:29], v[28:29], v[230:231]
	v_pk_fma_f32 v[20:21], v[46:47], s[40:41], v[30:31] op_sel_hi:[1,0,1]
	v_pk_fma_f32 v[24:25], v[44:45], s[40:41], v[28:29] op_sel_hi:[1,0,1]
	v_pk_fma_f32 v[28:29], v[54:55], s[40:41], v[26:27] op_sel_hi:[1,0,1]
	v_pk_fma_f32 v[30:31], v[52:53], s[40:41], v[204:205] op_sel_hi:[1,0,1]
	v_pk_fma_f32 v[44:45], v[42:43], s[40:41], v[18:19] op_sel_hi:[1,0,1]
	v_pk_fma_f32 v[46:47], v[40:41], s[40:41], v[16:17] op_sel_hi:[1,0,1]
	v_pk_fma_f32 v[40:41], v[58:59], s[40:41], v[14:15] op_sel_hi:[1,0,1]
	v_pk_fma_f32 v[42:43], v[56:57], s[40:41], v[12:13] op_sel_hi:[1,0,1]
	v_pk_fma_f32 v[12:13], v[62:63], s[40:41], v[10:11] op_sel_hi:[1,0,1]
	v_pk_fma_f32 v[14:15], v[60:61], s[40:41], v[8:9] op_sel_hi:[1,0,1]
	v_pk_fma_f32 v[8:9], v[38:39], s[40:41], v[6:7] op_sel_hi:[1,0,1]
	v_pk_fma_f32 v[10:11], v[36:37], s[40:41], v[4:5] op_sel_hi:[1,0,1]
	v_pk_fma_f32 v[4:5], v[34:35], s[40:41], v[206:207] op_sel_hi:[1,0,1]
	v_pk_fma_f32 v[6:7], v[32:33], s[40:41], v[200:201] op_sel_hi:[1,0,1]
	v_mov_b32_e32 v22, v24
	v_mov_b32_e32 v23, v30
	v_mov_b32_e32 v26, v25
	v_mov_b32_e32 v27, v31
	v_mov_b32_e32 v32, v20
	v_mov_b32_e32 v33, v28
	v_mov_b32_e32 v34, v21
	v_mov_b32_e32 v35, v29
	v_pk_mov_b32 v[36:37], v[48:49], v[50:51] op_sel:[1,0]
	v_mov_b32_e32 v38, v48
	v_mov_b32_e32 v39, v51
	v_pk_add_f32 v[22:23], v[22:23], v[26:27]
	v_pk_add_f32 v[26:27], v[32:33], v[34:35]
	v_pk_add_f32 v[32:33], v[36:37], v[38:39]
	v_pk_add_f32 v[22:23], v[22:23], v[26:27]
	v_pk_add_f32 v[26:27], v[32:33], v[32:33] op_sel:[0,1] op_sel_hi:[1,0]
	v_add_f32_e32 v22, 0, v22
	v_add_f32_e32 v56, v46, v47
	v_add_f32_e32 v58, v44, v45
	v_mov_b32_e32 v61, v42
	v_mov_b32_e32 v57, v40
	v_mov_b32_e32 v59, v41
	v_mov_b32_e32 v27, v43
	v_add_f32_e32 v60, v22, v23
	v_pk_mov_b32 v[62:63], v[14:15], v[12:13] op_sel:[1,0]
	v_pk_add_f32 v[34:35], v[56:57], v[58:59]
	v_pk_add_f32 v[22:23], v[60:61], v[26:27]
	v_pk_mul_f32 v[26:27], v[182:183], v[80:81] op_sel_hi:[1,0]
	v_pk_add_f32 v[22:23], v[22:23], v[34:35]
	s_waitcnt vmcnt(1)
	v_pk_add_f32 v[0:1], v[186:187], 1.0 op_sel_hi:[1,0]
	s_waitcnt vmcnt(0)
	v_pk_fma_f32 v[0:1], v[228:229], v[0:1], v[192:193]
	v_pk_add_f32 v[2:3], v[188:189], 1.0 op_sel_hi:[1,0]
	v_cvt_pk_fp8_f32 v246, v0, v1
	v_pk_fma_f32 v[2:3], v[198:199], v[2:3], v[194:195]
	v_mov_b32_e32 v186, v14
	v_mov_b32_e32 v187, v13
	v_cvt_pk_fp8_f32 v246, v2, v3 op_sel:[0,0,1]
	v_pk_add_f32 v[36:37], v[62:63], v[186:187]
	v_pk_add_f32 v[22:23], v[22:23], v[22:23] op_sel:[0,1] op_sel_hi:[1,0]
	v_pk_add_f32 v[32:33], v[36:37], v[36:37] op_sel:[0,1] op_sel_hi:[1,0]
	global_store_dword v[190:191], v246, off offset:1536
	global_load_dwordx4 v[16:19], v[88:89], off offset:3072
	global_load_dwordx4 v[52:55], v[90:91], off offset:3072
	v_add_f32_e32 v188, v10, v11
	v_add_f32_e32 v192, v8, v9
	v_mov_b32_e32 v189, v4
	v_mov_b32_e32 v193, v5
	v_mov_b32_e32 v33, v7
	v_mov_b32_e32 v23, v6
	v_pk_add_f32 v[38:39], v[188:189], v[192:193]
	v_pk_add_f32 v[22:23], v[22:23], v[32:33]
	v_mov_b32_e32 v192, 0
	v_pk_add_f32 v[22:23], v[22:23], v[38:39]
	s_waitcnt vmcnt(0)
; #define GAS __attribute__((address_space(1)))
; #define LAS __attribute__((address_space(3)))
; __device__ __forceinline__ unsigned pk2(float lo, float hi) { return f2bf(lo) | (f2bf(hi) << 16); }
; __device__ __forceinline__ unsigned pk4_fp8(float a, float b, float c, float d) { int r = __builtin_amdgcn_cvt_pk_fp8_f32(a, b, 0, false); r = __builtin_amdgcn_cvt_pk_fp8_f32(c, d, r, true); return (unsigned)r; }
; template <int l>
; __device__ __forceinline__ void layer_phases(Frame& F, const XcdBarrier& bar, const int lo, const int hi) {
;     ...
;                 for (int rq = 0; rq < 2; ++rq) { const int rr = 2 * rp + rq, m = m0 + rr, rloc = 4 * F.wave + rr;
;                     f32x4 (&v)[8] = vv[rq]; float s = 0.f;
; #pragma unroll
;                     for (int j = 0; j < 8; ++j) s += (v[j].x + v[j].y) + (v[j].z + v[j].w);
;                     const float mean = wave_sum(s) * (1.f / D); float s2 = 0.f;
; #pragma unroll
;                     for (int j = 0; j < 8; ++j) { v[j] = v[j] - mean; s2 += (v[j].x * v[j].x + v[j].y * v[j].y) + (v[j].z * v[j].z + v[j].w * v[j].w); }
;                     const float rstd = 1.f / sqrtf(wave_sum(s2) * (1.f / D) + LN_EPS);
; #pragma unroll
;                     for (int j = 0; j < 8; ++j) { const int k = 4 * lq + 256 * j;
;                         const f32x4 xv = v[j] * rstd * *(const GAS f32x4*)(g1 + k) + *(const GAS f32x4*)(b1 + k);
;                         { v2u xo; xo.x = pk2(xv.x, xv.y); xo.y = pk2(xv.z, xv.w); *(GAS v2u*)(x1 + (size_t)m * D + k) = xo; }
;                         const f32x4 hv = xv * (*(const GAS f32x4*)(mrow + 8192 + k) + 1.0f) + *(const GAS f32x4*)(mrow + 6144 + k);
;                         v2u o; o.x = pk2(hv.x, hv.y); o.y = pk2(hv.z, hv.w);
;                         *(GAS unsigned*)(h2q + (size_t)m * D + k) = pk4_fp8(hv.x, hv.y, hv.z, hv.w);
;                         const int chunk = (lq >> 1) + 32 * j;
;                         *(LAS v2u*)(h2s + rloc * 4096 + ((chunk ^ (rloc & 15)) << 4) + (lq & 1) * 8) = o; }
	v_pk_fma_f32 v[26:27], v[26:27], v[18:19], v[54:55]
	v_add_f32_e32 v22, v22, v23
	ds_bpermute_b32 v23, v73, v22
	v_bfe_u32 v18, v26, 16, 1
	v_bfe_u32 v19, v27, 16, 1
	v_add3_u32 v18, v26, v18, s90
	v_add3_u32 v19, v27, v19, s90
	s_waitcnt lgkmcnt(0)
	v_add_f32_e32 v22, v22, v23
	ds_bpermute_b32 v23, v217, v22
	v_lshrrev_b32_e32 v18, 16, v18
	s_waitcnt lgkmcnt(0)
	v_add_f32_e32 v22, v22, v23
	ds_bpermute_b32 v23, v218, v22
	s_waitcnt lgkmcnt(0)
	v_add_f32_e32 v22, v22, v23
	ds_bpermute_b32 v23, v219, v22
	s_waitcnt lgkmcnt(0)
	v_add_f32_e32 v22, v22, v23
	ds_bpermute_b32 v23, v220, v22
	s_waitcnt lgkmcnt(0)
	v_add_f32_e32 v36, v22, v23
	v_pk_mul_f32 v[22:23], v[184:185], v[80:81] op_sel_hi:[1,0]
	ds_bpermute_b32 v37, v221, v36
	v_pk_fma_f32 v[22:23], v[22:23], v[16:17], v[52:53]
	s_waitcnt lgkmcnt(0)
	v_add_f32_e32 v36, v36, v37
	v_bfe_u32 v16, v22, 16, 1
	v_bfe_u32 v17, v23, 16, 1
	v_add3_u32 v16, v22, v16, s90
	v_add3_u32 v17, v23, v17, s90
	v_lshrrev_b32_e32 v16, 16, v16
	v_and_or_b32 v16, v17, s86, v16
	v_and_or_b32 v17, v19, s86, v18
	global_store_dwordx2 v[196:197], v[16:17], off offset:3584
	global_load_dwordx4 v[16:19], v[82:83], off offset:3072
	s_nop 0
	global_load_dwordx4 v[32:35], v[84:85], off offset:3072
	v_fmamk_f32 v21, v36, 0xba000000, v21
	v_fmamk_f32 v25, v36, 0xba000000, v25
	v_fmamk_f32 v29, v36, 0xba000000, v29
	v_fmamk_f32 v31, v36, 0xba000000, v31
	v_fmac_f32_e32 v20, 0xba000000, v36
	v_fmac_f32_e32 v24, 0xba000000, v36
	v_fmac_f32_e32 v28, 0xba000000, v36
	v_fmac_f32_e32 v30, 0xba000000, v36
	v_fmamk_f32 v49, v36, 0xba000000, v49
	v_fmac_f32_e32 v48, 0xba000000, v36
	v_fmamk_f32 v51, v36, 0xba000000, v51
	v_fmac_f32_e32 v50, 0xba000000, v36
	v_mov_b32_e32 v38, v25
	v_mov_b32_e32 v39, v31
	v_mov_b32_e32 v54, v21
	v_mov_b32_e32 v55, v29
	v_fmamk_f32 v47, v36, 0xba000000, v47
	v_fmac_f32_e32 v46, 0xba000000, v36
	v_fmamk_f32 v45, v36, 0xba000000, v45
	v_fmac_f32_e32 v44, 0xba000000, v36
	v_fmamk_f32 v41, v36, 0xba000000, v41
	v_fmac_f32_e32 v40, 0xba000000, v36
	v_fmamk_f32 v43, v36, 0xba000000, v43
	v_fmac_f32_e32 v42, 0xba000000, v36
	v_fmamk_f32 v15, v36, 0xba000000, v15
	v_fmac_f32_e32 v14, 0xba000000, v36
	v_fmamk_f32 v13, v36, 0xba000000, v13
	v_fmac_f32_e32 v12, 0xba000000, v36
	v_fmamk_f32 v11, v36, 0xba000000, v11
	v_fmac_f32_e32 v10, 0xba000000, v36
	v_fmamk_f32 v9, v36, 0xba000000, v9
	v_fmac_f32_e32 v8, 0xba000000, v36
	v_fmamk_f32 v5, v36, 0xba000000, v5
	v_fmac_f32_e32 v4, 0xba000000, v36
	v_fmamk_f32 v7, v36, 0xba000000, v7
	v_fmac_f32_e32 v6, 0xba000000, v36
	v_mov_b32_e32 v36, v24
	v_mov_b32_e32 v37, v30
	v_mov_b32_e32 v52, v20
	v_mov_b32_e32 v53, v28
	v_pk_mul_f32 v[56:57], v[50:51], v[50:51]
	v_pk_mul_f32 v[58:59], v[48:49], v[48:49]
	v_pk_mul_f32 v[38:39], v[38:39], v[38:39]
	v_pk_mul_f32 v[54:55], v[54:55], v[54:55]
	v_pk_mov_b32 v[188:189], v[58:59], v[56:57] op_sel:[1,0]
	v_mov_b32_e32 v59, v57
	v_pk_fma_f32 v[36:37], v[36:37], v[36:37], v[38:39]
	v_pk_fma_f32 v[38:39], v[52:53], v[52:53], v[54:55]
	v_mul_f32_e32 v60, v46, v46
	v_mul_f32_e32 v62, v44, v44
	v_pk_mul_f32 v[182:183], v[12:13], v[12:13]
	v_pk_mul_f32 v[184:185], v[14:15], v[14:15]
	v_pk_add_f32 v[52:53], v[188:189], v[58:59]
	v_pk_add_f32 v[36:37], v[36:37], v[38:39]
	v_pk_fma_f32 v[56:57], v[46:47], v[46:47], v[60:61] op_sel_hi:[1,1,0]
	v_pk_fma_f32 v[60:61], v[44:45], v[44:45], v[62:63] op_sel_hi:[1,1,0]
	v_pk_mov_b32 v[62:63], v[184:185], v[182:183] op_sel:[1,0]
	v_mov_b32_e32 v185, v183
	v_pk_add_f32 v[38:39], v[52:53], v[52:53] op_sel_hi:[0,1]
	v_pk_add_f32 v[36:37], v[36:37], v[36:37] op_sel_hi:[0,1]
	v_pk_add_f32 v[54:55], v[62:63], v[184:185]
	v_mul_f32_e32 v38, v40, v40
	v_mul_f32_e32 v36, v41, v41
	v_pk_add_f32 v[58:59], v[54:55], v[54:55] op_sel_hi:[0,1]
	v_mul_f32_e32 v56, v42, v42
	v_mul_f32_e32 v60, v43, v43
	v_pk_add_f32 v[56:57], v[56:57], v[60:61]
	v_mul_f32_e32 v80, v10, v10
	v_mul_f32_e32 v186, v8, v8
	v_pk_fma_f32 v[182:183], v[10:11], v[10:11], v[80:81] op_sel_hi:[1,1,0]
	v_pk_fma_f32 v[186:187], v[8:9], v[8:9], v[186:187] op_sel_hi:[1,1,0]
	v_mul_f32_e32 v182, v6, v6
	v_mul_f32_e32 v186, v7, v7
	v_mul_f32_e32 v58, v4, v4
	v_pk_add_f32 v[60:61], v[182:183], v[186:187]
	v_mov_b32_e32 v62, 0
	v_lshlrev_b32_e32 v80, 4, v227
	s_waitcnt vmcnt(1)
	v_pk_add_f32 v[16:17], v[16:17], 1.0 op_sel_hi:[1,0]
	s_waitcnt vmcnt(0)
	v_pk_fma_f32 v[16:17], v[22:23], v[16:17], v[32:33]
	v_pk_add_f32 v[18:19], v[18:19], 1.0 op_sel_hi:[1,0]
	v_cvt_pk_fp8_f32 v192, v16, v17
	v_pk_fma_f32 v[18:19], v[26:27], v[18:19], v[34:35]
	v_pk_add_f32 v[22:23], v[38:39], v[36:37]
	v_cvt_pk_fp8_f32 v192, v18, v19 op_sel:[0,0,1]
	v_pk_add_f32 v[22:23], v[56:57], v[22:23]
	v_mov_b32_e32 v56, 0
	v_pk_add_f32 v[22:23], v[22:23], v[22:23] op_sel_hi:[0,1]
	global_store_dword v[190:191], v192, off offset:1792
	global_load_dwordx4 v[34:37], v[112:113], off
	global_load_dwordx4 v[52:55], v[114:115], off
	v_mul_f32_e32 v22, v5, v5
	v_pk_add_f32 v[22:23], v[58:59], v[22:23]
	v_lshlrev_b32_e32 v57, 3, v227
	v_pk_add_f32 v[22:23], v[60:61], v[22:23]
	v_and_b32_e32 v63, 8, v57
	v_add_f32_e32 v22, v22, v23
	ds_bpermute_b32 v23, v73, v22
	v_add_u32_e32 v63, 0, v63
	v_lshrrev_b32_e32 v61, 1, v227
	v_mov_b32_e32 v60, 0
	s_waitcnt lgkmcnt(0)
	v_add_f32_e32 v22, v22, v23
	ds_bpermute_b32 v23, v217, v22
	s_waitcnt lgkmcnt(0)
	v_add_f32_e32 v22, v22, v23
	ds_bpermute_b32 v23, v218, v22
	s_waitcnt lgkmcnt(0)
	v_add_f32_e32 v22, v22, v23
	ds_bpermute_b32 v23, v219, v22
	s_waitcnt lgkmcnt(0)
	v_add_f32_e32 v22, v22, v23
	ds_bpermute_b32 v23, v220, v22
	s_waitcnt lgkmcnt(0)
	v_add_f32_e32 v22, v22, v23
	ds_bpermute_b32 v23, v221, v22
	s_waitcnt lgkmcnt(0)
; #define GAS __attribute__((address_space(1)))
; #define LAS __attribute__((address_space(3)))
; __device__ __forceinline__ unsigned pk2(float lo, float hi) { return f2bf(lo) | (f2bf(hi) << 16); }
; __device__ __forceinline__ unsigned pk4_fp8(float a, float b, float c, float d) { int r = __builtin_amdgcn_cvt_pk_fp8_f32(a, b, 0, false); r = __builtin_amdgcn_cvt_pk_fp8_f32(c, d, r, true); return (unsigned)r; }
; template <int l>
; __device__ __forceinline__ void layer_phases(Frame& F, const XcdBarrier& bar, const int lo, const int hi) {
;     ...
;                     const float rstd = 1.f / sqrtf(wave_sum(s2) * (1.f / D) + LN_EPS);
; #pragma unroll
;                     for (int j = 0; j < 8; ++j) { const int k = 4 * lq + 256 * j;
;                         const f32x4 xv = v[j] * rstd * *(const GAS f32x4*)(g1 + k) + *(const GAS f32x4*)(b1 + k);
;                         { v2u xo; xo.x = pk2(xv.x, xv.y); xo.y = pk2(xv.z, xv.w); *(GAS v2u*)(x1 + (size_t)m * D + k) = xo; }
;                         const f32x4 hv = xv * (*(const GAS f32x4*)(mrow + 8192 + k) + 1.0f) + *(const GAS f32x4*)(mrow + 6144 + k);
;                         v2u o; o.x = pk2(hv.x, hv.y); o.y = pk2(hv.z, hv.w);
;                         *(GAS unsigned*)(h2q + (size_t)m * D + k) = pk4_fp8(hv.x, hv.y, hv.z, hv.w);
;                         const int chunk = (lq >> 1) + 32 * j;
;                         *(LAS v2u*)(h2s + rloc * 4096 + ((chunk ^ (rloc & 15)) << 4) + (lq & 1) * 8) = o; }
	v_add_f32_e32 v22, v22, v23
	v_fmamk_f32 v22, v22, 0x3a000000, v223
	v_mul_f32_e32 v23, 0x4f800000, v22
	v_cmp_gt_f32_e32 vcc, s89, v22
	s_nop 1
	v_cndmask_b32_e32 v22, v22, v23, vcc
	v_sqrt_f32_e32 v23, v22
	s_nop 0
	v_add_u32_e32 v26, -1, v23
	v_add_u32_e32 v27, 1, v23
	v_fma_f32 v32, -v26, v23, v22
	v_fma_f32 v33, -v27, v23, v22
	v_cmp_ge_f32_e64 s[14:15], 0, v32
	s_nop 1
	v_cndmask_b32_e64 v23, v23, v26, s[14:15]
	v_cmp_lt_f32_e64 s[14:15], 0, v33
	s_nop 1
	v_cndmask_b32_e64 v23, v23, v27, s[14:15]
	v_mul_f32_e32 v26, 0x37800000, v23
	v_cndmask_b32_e32 v23, v23, v26, vcc
	v_cmp_class_f32_e32 vcc, v22, v224
	s_nop 1
	v_cndmask_b32_e32 v26, v23, v22, vcc
	v_div_scale_f32 v27, s[14:15], v26, v26, 1.0
	v_rcp_f32_e32 v32, v27
	v_div_scale_f32 v33, vcc, 1.0, v26, 1.0
	v_lshl_add_u64 v[22:23], s[0:1], 0, v[128:129]
	v_fma_f32 v38, -v27, v32, 1.0
	v_fmac_f32_e32 v32, v38, v32
	v_mul_f32_e32 v38, v33, v32
	v_fma_f32 v39, -v27, v38, v33
	v_fmac_f32_e32 v38, v39, v32
	v_fma_f32 v27, -v27, v38, v33
	v_div_fmas_f32 v27, v27, v32, v38
	v_div_fixup_f32 v32, v27, v26, 1.0
	v_pk_mul_f32 v[24:25], v[24:25], v[32:33] op_sel_hi:[1,0]
	v_pk_mul_f32 v[20:21], v[20:21], v[32:33] op_sel_hi:[1,0]
	s_waitcnt vmcnt(0)
	v_pk_fma_f32 v[38:39], v[34:35], v[24:25], v[52:53]
	v_pk_fma_f32 v[20:21], v[36:37], v[20:21], v[54:55]
	v_bfe_u32 v24, v38, 16, 1
	v_bfe_u32 v26, v20, 16, 1
	v_bfe_u32 v25, v39, 16, 1
	v_bfe_u32 v27, v21, 16, 1
	v_add3_u32 v24, v38, v24, s90
	v_add3_u32 v26, v20, v26, s90
	v_add3_u32 v25, v39, v25, s90
	v_add3_u32 v27, v21, v27, s90
	v_lshrrev_b32_e32 v24, 16, v24
	v_lshrrev_b32_e32 v26, 16, v26
	v_and_or_b32 v24, v25, s86, v24
	v_and_or_b32 v25, v27, s86, v26
	global_store_dwordx2 v[22:23], v[24:25], off
	global_load_dwordx4 v[24:27], v[82:83], off offset:-4096
	s_nop 0
	global_load_dwordx4 v[34:37], v[84:85], off offset:-4096
	v_mov_b32_e32 v33, 0
	s_add_u32 s0, s50, s16
	s_addc_u32 s1, s51, s17
	s_mov_b32 s14, 0x8000
	s_waitcnt vmcnt(1)
	v_pk_add_f32 v[24:25], v[24:25], 1.0 op_sel_hi:[1,0]
	s_waitcnt vmcnt(0)
	v_pk_fma_f32 v[24:25], v[24:25], v[38:39], v[34:35]
	v_pk_add_f32 v[26:27], v[26:27], 1.0 op_sel_hi:[1,0]
	v_cvt_pk_fp8_f32 v33, v24, v25
	v_pk_fma_f32 v[26:27], v[26:27], v[20:21], v[36:37]
	v_lshl_add_u64 v[20:21], s[0:1], 0, v[86:87]
	v_readlane_b32 s0, v248, 24
	v_cvt_pk_fp8_f32 v33, v26, v27 op_sel:[0,0,1]
	v_add_u32_e32 v87, 32, v61
	v_add_u32_e32 v199, s0, v63
	v_readlane_b32 s0, v248, 25
	global_store_dword v[20:21], v33, off
	global_load_dwordx4 v[34:37], v[112:113], off offset:1024
	global_load_dwordx4 v[52:55], v[114:115], off offset:1024
	v_pk_mul_f32 v[30:31], v[30:31], v[32:33] op_sel_hi:[1,0]
	v_pk_mul_f32 v[28:29], v[28:29], v[32:33] op_sel_hi:[1,0]
	v_mov_b32_e32 v33, 0
	v_add_u32_e32 v200, s0, v63
	v_readlane_b32 s0, v248, 26
	v_xor_b32_e32 v185, s66, v87
	v_xor_b32_e32 v192, s68, v87
	v_add_u32_e32 v201, s0, v63
	v_readlane_b32 s0, v248, 27
	v_lshl_add_u32 v185, v185, 4, v200
	v_lshl_add_u32 v192, v192, 4, v201
	v_add_u32_e32 v63, s0, v63
	v_xor_b32_e32 v86, s64, v61
	v_lshl_add_u32 v86, v86, 4, v199
	v_readlane_b32 s0, v248, 30
	s_waitcnt vmcnt(0)
	v_pk_fma_f32 v[38:39], v[36:37], v[28:29], v[54:55]
	v_pk_fma_f32 v[52:53], v[34:35], v[30:31], v[52:53]
	v_bfe_u32 v30, v38, 16, 1
	v_bfe_u32 v28, v52, 16, 1
	v_bfe_u32 v29, v53, 16, 1
	v_bfe_u32 v31, v39, 16, 1
	v_add3_u32 v28, v52, v28, s90
	v_add3_u32 v30, v38, v30, s90
	v_add3_u32 v29, v53, v29, s90
	v_add3_u32 v31, v39, v31, s90
	v_lshrrev_b32_e32 v28, 16, v28
	v_lshrrev_b32_e32 v30, 16, v30
	v_and_or_b32 v28, v29, s86, v28
	v_and_or_b32 v29, v31, s86, v30
	global_store_dwordx2 v[22:23], v[28:29], off offset:512
	global_load_dwordx4 v[28:31], v[122:123], off offset:1024
	s_nop 0
	global_load_dwordx4 v[34:37], v[120:121], off offset:1024
	s_waitcnt vmcnt(1)
	v_pk_add_f32 v[28:29], v[28:29], 1.0 op_sel_hi:[1,0]
	s_waitcnt vmcnt(0)
	v_pk_fma_f32 v[28:29], v[28:29], v[52:53], v[34:35]
	v_pk_add_f32 v[30:31], v[30:31], 1.0 op_sel_hi:[1,0]
	v_cvt_pk_fp8_f32 v33, v28, v29
	v_pk_fma_f32 v[30:31], v[30:31], v[38:39], v[36:37]
	s_nop 0
	v_cvt_pk_fp8_f32 v33, v30, v31 op_sel:[0,0,1]
	global_store_dword v[20:21], v33, off offset:256
	global_load_dwordx4 v[34:37], v[112:113], off offset:2048
	global_load_dwordx4 v[52:55], v[114:115], off offset:2048
	v_pk_mul_f32 v[38:39], v[48:49], v[32:33] op_sel_hi:[1,0]
	v_pk_mul_f32 v[48:49], v[50:51], v[32:33] op_sel_hi:[1,0]
	s_waitcnt vmcnt(0)
	v_pk_fma_f32 v[38:39], v[34:35], v[38:39], v[52:53]
	v_pk_fma_f32 v[54:55], v[36:37], v[48:49], v[54:55]
	v_bfe_u32 v33, v38, 16, 1
	v_bfe_u32 v35, v54, 16, 1
	v_bfe_u32 v34, v39, 16, 1
	v_bfe_u32 v36, v55, 16, 1
	v_add3_u32 v33, v38, v33, s90
	v_add3_u32 v35, v54, v35, s90
	v_add3_u32 v34, v39, v34, s90
	v_add3_u32 v36, v55, v36, s90
	v_lshrrev_b32_e32 v33, 16, v33
	v_lshrrev_b32_e32 v35, 16, v35
	v_and_or_b32 v34, v34, s86, v33
	v_and_or_b32 v35, v36, s86, v35
	global_store_dwordx2 v[22:23], v[34:35], off offset:1024
	global_load_dwordx4 v[34:37], v[122:123], off offset:2048
	s_nop 0
	global_load_dwordx4 v[48:51], v[120:121], off offset:2048
	v_mov_b32_e32 v33, 0
	s_waitcnt vmcnt(1)
	v_pk_add_f32 v[34:35], v[34:35], 1.0 op_sel_hi:[1,0]
	s_waitcnt vmcnt(0)
; #define GAS __attribute__((address_space(1)))
; #define LAS __attribute__((address_space(3)))
; __device__ __forceinline__ unsigned pk2(float lo, float hi) { return f2bf(lo) | (f2bf(hi) << 16); }
; __device__ __forceinline__ unsigned pk4_fp8(float a, float b, float c, float d) { int r = __builtin_amdgcn_cvt_pk_fp8_f32(a, b, 0, false); r = __builtin_amdgcn_cvt_pk_fp8_f32(c, d, r, true); return (unsigned)r; }
; template <int l>
; __device__ __forceinline__ void layer_phases(Frame& F, const XcdBarrier& bar, const int lo, const int hi) {
;     ...
;                     for (int j = 0; j < 8; ++j) { const int k = 4 * lq + 256 * j;
;                         const f32x4 xv = v[j] * rstd * *(const GAS f32x4*)(g1 + k) + *(const GAS f32x4*)(b1 + k);
;                         { v2u xo; xo.x = pk2(xv.x, xv.y); xo.y = pk2(xv.z, xv.w); *(GAS v2u*)(x1 + (size_t)m * D + k) = xo; }
;                         const f32x4 hv = xv * (*(const GAS f32x4*)(mrow + 8192 + k) + 1.0f) + *(const GAS f32x4*)(mrow + 6144 + k);
;                         v2u o; o.x = pk2(hv.x, hv.y); o.y = pk2(hv.z, hv.w);
;                         *(GAS unsigned*)(h2q + (size_t)m * D + k) = pk4_fp8(hv.x, hv.y, hv.z, hv.w);
;                         const int chunk = (lq >> 1) + 32 * j;
;                         *(LAS v2u*)(h2s + rloc * 4096 + ((chunk ^ (rloc & 15)) << 4) + (lq & 1) * 8) = o; }
	v_pk_fma_f32 v[34:35], v[34:35], v[38:39], v[48:49]
	v_pk_add_f32 v[36:37], v[36:37], 1.0 op_sel_hi:[1,0]
	v_cvt_pk_fp8_f32 v33, v34, v35
	v_pk_fma_f32 v[36:37], v[36:37], v[54:55], v[50:51]
	s_nop 0
	v_cvt_pk_fp8_f32 v33, v36, v37 op_sel:[0,0,1]
	global_store_dword v[20:21], v33, off offset:512
	global_load_dwordx4 v[48:51], v[112:113], off offset:3072
	global_load_dwordx4 v[52:55], v[114:115], off offset:3072
	v_pk_mul_f32 v[38:39], v[46:47], v[32:33] op_sel_hi:[1,0]
	v_pk_mul_f32 v[44:45], v[44:45], v[32:33] op_sel_hi:[1,0]
	v_add_u32_e32 v112, 64, v61
	v_add_u32_e32 v113, 0xa0, v61
	v_add_u32_e32 v114, 0xc0, v61
	v_add_u32_e32 v115, 0xe0, v61
	v_xor_b32_e32 v186, s66, v112
	v_xor_b32_e32 v189, s66, v113
	v_xor_b32_e32 v190, s66, v114
	v_xor_b32_e32 v191, s66, v115
	v_xor_b32_e32 v193, s68, v112
	v_xor_b32_e32 v196, s68, v113
	v_xor_b32_e32 v197, s68, v114
	v_xor_b32_e32 v198, s68, v115
	v_lshl_add_u32 v186, v186, 4, v200
	v_lshl_add_u32 v189, v189, 4, v200
	v_lshl_add_u32 v190, v190, 4, v200
	v_lshl_add_u32 v191, v191, 4, v200
	v_lshl_add_u32 v193, v193, 4, v201
	v_lshl_add_u32 v196, v196, 4, v201
	v_lshl_add_u32 v197, v197, 4, v201
	v_lshl_add_u32 v198, v198, 4, v201
	v_xor_b32_e32 v182, s64, v113
	v_xor_b32_e32 v183, s64, v114
	v_xor_b32_e32 v184, s64, v115
	v_xor_b32_e32 v113, s70, v113
	v_xor_b32_e32 v114, s70, v114
	v_xor_b32_e32 v115, s70, v115
	v_lshl_add_u32 v182, v182, 4, v199
	v_lshl_add_u32 v183, v183, 4, v199
	v_lshl_add_u32 v184, v184, 4, v199
	v_lshl_add_u32 v113, v113, 4, v63
	v_lshl_add_u32 v114, v114, 4, v63
	s_waitcnt vmcnt(0)
	v_pk_fma_f32 v[54:55], v[44:45], v[50:51], v[54:55]
	v_pk_fma_f32 v[38:39], v[38:39], v[48:49], v[52:53]
	v_bfe_u32 v45, v54, 16, 1
	v_bfe_u32 v33, v38, 16, 1
	v_bfe_u32 v44, v39, 16, 1
	v_bfe_u32 v46, v55, 16, 1
	v_add3_u32 v33, v38, v33, s90
	v_add3_u32 v45, v54, v45, s90
	v_add3_u32 v44, v39, v44, s90
	v_add3_u32 v46, v55, v46, s90
	v_lshrrev_b32_e32 v33, 16, v33
	v_lshrrev_b32_e32 v45, 16, v45
	v_and_or_b32 v44, v44, s86, v33
	v_and_or_b32 v45, v46, s86, v45
	global_store_dwordx2 v[22:23], v[44:45], off offset:1536
	global_load_dwordx4 v[44:47], v[122:123], off offset:3072
	s_nop 0
	global_load_dwordx4 v[48:51], v[120:121], off offset:3072
	v_mov_b32_e32 v33, 0
	v_xor_b32_e32 v120, s66, v61
	v_xor_b32_e32 v121, s68, v61
	v_lshl_add_u32 v120, v120, 4, v200
	v_lshl_add_u32 v121, v121, 4, v201
	v_xor_b32_e32 v122, s64, v87
	v_xor_b32_e32 v123, s64, v112
	v_xor_b32_e32 v87, s70, v87
	v_xor_b32_e32 v112, s70, v112
	v_lshl_add_u32 v122, v122, 4, v199
	v_lshl_add_u32 v123, v123, 4, v199
	v_lshl_add_u32 v87, v87, 4, v63
	v_lshl_add_u32 v112, v112, 4, v63
	s_waitcnt vmcnt(1)
	v_pk_add_f32 v[44:45], v[44:45], 1.0 op_sel_hi:[1,0]
	s_waitcnt vmcnt(0)
	v_pk_fma_f32 v[38:39], v[38:39], v[44:45], v[48:49]
	v_pk_add_f32 v[44:45], v[46:47], 1.0 op_sel_hi:[1,0]
	v_cvt_pk_fp8_f32 v33, v38, v39
	v_pk_fma_f32 v[44:45], v[54:55], v[44:45], v[50:51]
	v_ashrrev_i32_e32 v55, 5, v227
	v_and_b32_e32 v54, 31, v227
	v_cvt_pk_fp8_f32 v33, v44, v45 op_sel:[0,0,1]
	global_store_dword v[20:21], v33, off offset:768
	global_load_dwordx4 v[46:49], v[88:89], off
	global_load_dwordx4 v[50:53], v[90:91], off
	v_pk_mul_f32 v[42:43], v[42:43], v[32:33] op_sel_hi:[1,0]
	v_pk_mul_f32 v[40:41], v[40:41], v[32:33] op_sel_hi:[1,0]
	s_waitcnt vmcnt(0)
	v_pk_fma_f32 v[50:51], v[42:43], v[46:47], v[50:51]
	v_pk_fma_f32 v[52:53], v[40:41], v[48:49], v[52:53]
	v_bfe_u32 v33, v50, 16, 1
	v_bfe_u32 v41, v52, 16, 1
	v_bfe_u32 v40, v51, 16, 1
	v_bfe_u32 v42, v53, 16, 1
	v_add3_u32 v33, v50, v33, s90
	v_add3_u32 v41, v52, v41, s90
	v_add3_u32 v40, v51, v40, s90
	v_add3_u32 v42, v53, v42, s90
	v_lshrrev_b32_e32 v33, 16, v33
	v_lshrrev_b32_e32 v41, 16, v41
	v_and_or_b32 v40, v40, s86, v33
	v_and_or_b32 v41, v42, s86, v41
	global_store_dwordx2 v[22:23], v[40:41], off offset:2048
	global_load_dwordx4 v[40:43], v[82:83], off
	s_nop 0
	global_load_dwordx4 v[46:49], v[84:85], off
	v_mov_b32_e32 v33, 0
	v_pk_mul_f32 v[14:15], v[14:15], v[32:33] op_sel_hi:[1,0]
	v_pk_mul_f32 v[12:13], v[12:13], v[32:33] op_sel_hi:[1,0]
	v_pk_mul_f32 v[10:11], v[10:11], v[32:33] op_sel_hi:[1,0]
	v_pk_mul_f32 v[8:9], v[8:9], v[32:33] op_sel_hi:[1,0]
	s_waitcnt vmcnt(1)
	v_pk_add_f32 v[40:41], v[40:41], 1.0 op_sel_hi:[1,0]
	s_waitcnt vmcnt(0)
	v_pk_fma_f32 v[40:41], v[50:51], v[40:41], v[46:47]
	v_pk_add_f32 v[42:43], v[42:43], 1.0 op_sel_hi:[1,0]
	v_cvt_pk_fp8_f32 v56, v40, v41
	v_pk_fma_f32 v[42:43], v[52:53], v[42:43], v[48:49]
	v_add_u32_e32 v50, 0x60, v61
	v_add_u32_e32 v51, 0x80, v61
	v_cvt_pk_fp8_f32 v56, v42, v43 op_sel:[0,0,1]
	v_xor_b32_e32 v128, s64, v50
	v_xor_b32_e32 v129, s64, v51
	v_xor_b32_e32 v187, s66, v50
	global_store_dword v[20:21], v56, off offset:1024
	global_load_dwordx4 v[46:49], v[88:89], off offset:1024
	s_nop 0
	global_load_dwordx4 v[56:59], v[90:91], off offset:1024
	v_xor_b32_e32 v188, s66, v51
	v_xor_b32_e32 v194, s68, v50
	v_xor_b32_e32 v195, s68, v51
	v_xor_b32_e32 v50, s70, v50
	v_xor_b32_e32 v51, s70, v51
	v_lshl_add_u32 v187, v187, 4, v200
	v_lshl_add_u32 v188, v188, 4, v200
	v_lshl_add_u32 v194, v194, 4, v201
	v_lshl_add_u32 v195, v195, 4, v201
	v_lshl_add_u32 v200, v50, 4, v63
	v_lshl_add_u32 v201, v51, 4, v63
	v_and_b32_sdwa v50, v94, v226 dst_sel:DWORD dst_unused:UNUSED_PAD src0_sel:WORD_1 src1_sel:DWORD
	v_and_b32_sdwa v51, v92, v226 dst_sel:DWORD dst_unused:UNUSED_PAD src0_sel:WORD_1 src1_sel:DWORD
	v_add3_u32 v92, v92, v51, s90
	v_add3_u32 v94, v94, v50, s90
	v_xor_b32_e32 v61, s70, v61
	v_lshl_add_u32 v128, v128, 4, v199
	v_lshl_add_u32 v129, v129, 4, v199
	v_lshl_add_u32 v199, v61, 4, v63
	v_lshl_add_u32 v63, v115, 4, v63
	v_and_b32_sdwa v61, v95, v226 dst_sel:DWORD dst_unused:UNUSED_PAD src0_sel:WORD_1 src1_sel:DWORD
	v_and_b32_sdwa v115, v93, v226 dst_sel:DWORD dst_unused:UNUSED_PAD src0_sel:WORD_1 src1_sel:DWORD
	v_add3_u32 v61, v95, v61, s90
	v_lshl_add_u64 v[52:53], s[36:37], 0, v[80:81]
	s_waitcnt vmcnt(0)
; #define GAS __attribute__((address_space(1)))
; #define LAS __attribute__((address_space(3)))
; __device__ __forceinline__ unsigned pk2(float lo, float hi) { return f2bf(lo) | (f2bf(hi) << 16); }
; __device__ __forceinline__ unsigned pk4_fp8(float a, float b, float c, float d) { int r = __builtin_amdgcn_cvt_pk_fp8_f32(a, b, 0, false); r = __builtin_amdgcn_cvt_pk_fp8_f32(c, d, r, true); return (unsigned)r; }
; template <int l>
; __device__ __forceinline__ void layer_phases(Frame& F, const XcdBarrier& bar, const int lo, const int hi) {
;     ...
;                     for (int j = 0; j < 8; ++j) { const int k = 4 * lq + 256 * j;
;                         const f32x4 xv = v[j] * rstd * *(const GAS f32x4*)(g1 + k) + *(const GAS f32x4*)(b1 + k);
;                         { v2u xo; xo.x = pk2(xv.x, xv.y); xo.y = pk2(xv.z, xv.w); *(GAS v2u*)(x1 + (size_t)m * D + k) = xo; }
;                         const f32x4 hv = xv * (*(const GAS f32x4*)(mrow + 8192 + k) + 1.0f) + *(const GAS f32x4*)(mrow + 6144 + k);
;                         v2u o; o.x = pk2(hv.x, hv.y); o.y = pk2(hv.z, hv.w);
;                         *(GAS unsigned*)(h2q + (size_t)m * D + k) = pk4_fp8(hv.x, hv.y, hv.z, hv.w);
;                         const int chunk = (lq >> 1) + 32 * j;
;                         *(LAS v2u*)(h2s + rloc * 4096 + ((chunk ^ (rloc & 15)) << 4) + (lq & 1) * 8) = o; }
	v_pk_fma_f32 v[50:51], v[12:13], v[48:49], v[58:59]
	v_pk_fma_f32 v[56:57], v[14:15], v[46:47], v[56:57]
	v_bfe_u32 v14, v50, 16, 1
	v_bfe_u32 v12, v56, 16, 1
	v_bfe_u32 v13, v57, 16, 1
	v_bfe_u32 v15, v51, 16, 1
	v_add3_u32 v12, v56, v12, s90
	v_add3_u32 v14, v50, v14, s90
	v_add3_u32 v13, v57, v13, s90
	v_add3_u32 v15, v51, v15, s90
	v_lshrrev_b32_e32 v12, 16, v12
	v_lshrrev_b32_e32 v14, 16, v14
	v_and_or_b32 v12, v13, s86, v12
	v_and_or_b32 v13, v15, s86, v14
	global_store_dwordx2 v[22:23], v[12:13], off offset:2560
	global_load_dwordx4 v[12:15], v[82:83], off offset:1024
	s_nop 0
	global_load_dwordx4 v[46:49], v[84:85], off offset:1024
	v_add3_u32 v58, v93, v115, s90
	v_and_b32_e32 v59, 0xffff0000, v61
	v_and_b32_e32 v58, 0xffff0000, v58
	v_or_b32_sdwa v59, v59, v94 dst_sel:DWORD dst_unused:UNUSED_PAD src0_sel:DWORD src1_sel:WORD_1
	v_or_b32_sdwa v58, v58, v92 dst_sel:DWORD dst_unused:UNUSED_PAD src0_sel:DWORD src1_sel:WORD_1
	ds_write_b64 v86, v[58:59]
	v_and_b32_sdwa v59, v96, v226 dst_sel:DWORD dst_unused:UNUSED_PAD src0_sel:WORD_1 src1_sel:DWORD
	v_and_b32_sdwa v61, v99, v226 dst_sel:DWORD dst_unused:UNUSED_PAD src0_sel:WORD_1 src1_sel:DWORD
	v_and_b32_sdwa v86, v97, v226 dst_sel:DWORD dst_unused:UNUSED_PAD src0_sel:WORD_1 src1_sel:DWORD
	v_and_b32_sdwa v58, v98, v226 dst_sel:DWORD dst_unused:UNUSED_PAD src0_sel:WORD_1 src1_sel:DWORD
	v_add3_u32 v92, v96, v59, s90
	v_add3_u32 v59, v99, v61, s90
	v_add3_u32 v61, v97, v86, s90
	v_add3_u32 v58, v98, v58, s90
	v_and_b32_e32 v59, 0xffff0000, v59
	v_and_b32_e32 v61, 0xffff0000, v61
	v_or_b32_sdwa v59, v59, v58 dst_sel:DWORD dst_unused:UNUSED_PAD src0_sel:DWORD src1_sel:WORD_1
	v_or_b32_sdwa v58, v61, v92 dst_sel:DWORD dst_unused:UNUSED_PAD src0_sel:DWORD src1_sel:WORD_1
	ds_write_b64 v122, v[58:59]
	v_and_b32_sdwa v59, v100, v226 dst_sel:DWORD dst_unused:UNUSED_PAD src0_sel:WORD_1 src1_sel:DWORD
	v_and_b32_sdwa v61, v103, v226 dst_sel:DWORD dst_unused:UNUSED_PAD src0_sel:WORD_1 src1_sel:DWORD
	v_and_b32_sdwa v86, v101, v226 dst_sel:DWORD dst_unused:UNUSED_PAD src0_sel:WORD_1 src1_sel:DWORD
	v_and_b32_sdwa v58, v102, v226 dst_sel:DWORD dst_unused:UNUSED_PAD src0_sel:WORD_1 src1_sel:DWORD
	v_add3_u32 v92, v100, v59, s90
	v_add3_u32 v59, v103, v61, s90
	v_add3_u32 v61, v101, v86, s90
	v_add3_u32 v58, v102, v58, s90
	v_and_b32_e32 v59, 0xffff0000, v59
	v_and_b32_e32 v61, 0xffff0000, v61
	v_or_b32_sdwa v59, v59, v58 dst_sel:DWORD dst_unused:UNUSED_PAD src0_sel:DWORD src1_sel:WORD_1
	v_or_b32_sdwa v58, v61, v92 dst_sel:DWORD dst_unused:UNUSED_PAD src0_sel:DWORD src1_sel:WORD_1
	ds_write_b64 v123, v[58:59]
	v_and_b32_sdwa v59, v104, v226 dst_sel:DWORD dst_unused:UNUSED_PAD src0_sel:WORD_1 src1_sel:DWORD
	v_and_b32_sdwa v61, v107, v226 dst_sel:DWORD dst_unused:UNUSED_PAD src0_sel:WORD_1 src1_sel:DWORD
	v_and_b32_sdwa v86, v105, v226 dst_sel:DWORD dst_unused:UNUSED_PAD src0_sel:WORD_1 src1_sel:DWORD
	v_and_b32_sdwa v58, v106, v226 dst_sel:DWORD dst_unused:UNUSED_PAD src0_sel:WORD_1 src1_sel:DWORD
	v_add3_u32 v92, v104, v59, s90
	v_add3_u32 v59, v107, v61, s90
	v_add3_u32 v61, v105, v86, s90
	v_add3_u32 v58, v106, v58, s90
	v_and_b32_e32 v59, 0xffff0000, v59
	v_and_b32_e32 v61, 0xffff0000, v61
	v_or_b32_sdwa v59, v59, v58 dst_sel:DWORD dst_unused:UNUSED_PAD src0_sel:DWORD src1_sel:WORD_1
	v_or_b32_sdwa v58, v61, v92 dst_sel:DWORD dst_unused:UNUSED_PAD src0_sel:DWORD src1_sel:WORD_1
	ds_write_b64 v128, v[58:59]
	v_and_b32_sdwa v59, v108, v226 dst_sel:DWORD dst_unused:UNUSED_PAD src0_sel:WORD_1 src1_sel:DWORD
	v_and_b32_sdwa v61, v111, v226 dst_sel:DWORD dst_unused:UNUSED_PAD src0_sel:WORD_1 src1_sel:DWORD
	v_and_b32_sdwa v86, v109, v226 dst_sel:DWORD dst_unused:UNUSED_PAD src0_sel:WORD_1 src1_sel:DWORD
	v_and_b32_sdwa v58, v110, v226 dst_sel:DWORD dst_unused:UNUSED_PAD src0_sel:WORD_1 src1_sel:DWORD
	v_add3_u32 v92, v108, v59, s90
	v_add3_u32 v59, v111, v61, s90
	v_add3_u32 v61, v109, v86, s90
	v_add3_u32 v58, v110, v58, s90
	v_and_b32_e32 v59, 0xffff0000, v59
	v_and_b32_e32 v61, 0xffff0000, v61
	v_or_b32_sdwa v59, v59, v58 dst_sel:DWORD dst_unused:UNUSED_PAD src0_sel:DWORD src1_sel:WORD_1
	v_or_b32_sdwa v58, v61, v92 dst_sel:DWORD dst_unused:UNUSED_PAD src0_sel:DWORD src1_sel:WORD_1
	ds_write_b64 v129, v[58:59]
	v_and_b32_sdwa v59, v116, v226 dst_sel:DWORD dst_unused:UNUSED_PAD src0_sel:WORD_1 src1_sel:DWORD
	v_and_b32_sdwa v61, v119, v226 dst_sel:DWORD dst_unused:UNUSED_PAD src0_sel:WORD_1 src1_sel:DWORD
	v_and_b32_sdwa v86, v117, v226 dst_sel:DWORD dst_unused:UNUSED_PAD src0_sel:WORD_1 src1_sel:DWORD
	v_and_b32_sdwa v58, v118, v226 dst_sel:DWORD dst_unused:UNUSED_PAD src0_sel:WORD_1 src1_sel:DWORD
	v_add3_u32 v92, v116, v59, s90
	v_add3_u32 v59, v119, v61, s90
	v_add3_u32 v61, v117, v86, s90
	v_add3_u32 v58, v118, v58, s90
	v_and_b32_e32 v59, 0xffff0000, v59
	v_and_b32_e32 v61, 0xffff0000, v61
	v_or_b32_sdwa v59, v59, v58 dst_sel:DWORD dst_unused:UNUSED_PAD src0_sel:DWORD src1_sel:WORD_1
	v_or_b32_sdwa v58, v61, v92 dst_sel:DWORD dst_unused:UNUSED_PAD src0_sel:DWORD src1_sel:WORD_1
	ds_write_b64 v182, v[58:59]
	v_and_b32_sdwa v59, v124, v226 dst_sel:DWORD dst_unused:UNUSED_PAD src0_sel:WORD_1 src1_sel:DWORD
	v_and_b32_sdwa v61, v127, v226 dst_sel:DWORD dst_unused:UNUSED_PAD src0_sel:WORD_1 src1_sel:DWORD
	v_and_b32_sdwa v58, v126, v226 dst_sel:DWORD dst_unused:UNUSED_PAD src0_sel:WORD_1 src1_sel:DWORD
	v_and_b32_sdwa v86, v125, v226 dst_sel:DWORD dst_unused:UNUSED_PAD src0_sel:WORD_1 src1_sel:DWORD
	v_add3_u32 v92, v124, v59, s90
	v_add3_u32 v59, v127, v61, s90
	v_add3_u32 v58, v126, v58, s90
	s_waitcnt vmcnt(1)
	v_pk_add_f32 v[12:13], v[12:13], 1.0 op_sel_hi:[1,0]
	v_pk_add_f32 v[14:15], v[14:15], 1.0 op_sel_hi:[1,0]
	s_waitcnt vmcnt(0)
; #define GAS __attribute__((address_space(1)))
; #define LAS __attribute__((address_space(3)))
; __device__ __forceinline__ unsigned pk2(float lo, float hi) { return f2bf(lo) | (f2bf(hi) << 16); }
; __device__ __forceinline__ unsigned pk4_fp8(float a, float b, float c, float d) { int r = __builtin_amdgcn_cvt_pk_fp8_f32(a, b, 0, false); r = __builtin_amdgcn_cvt_pk_fp8_f32(c, d, r, true); return (unsigned)r; }
; template <int l>
; __device__ __forceinline__ void layer_phases(Frame& F, const XcdBarrier& bar, const int lo, const int hi) {
;     ...
;                     for (int j = 0; j < 8; ++j) { const int k = 4 * lq + 256 * j;
;                         const f32x4 xv = v[j] * rstd * *(const GAS f32x4*)(g1 + k) + *(const GAS f32x4*)(b1 + k);
;                         { v2u xo; xo.x = pk2(xv.x, xv.y); xo.y = pk2(xv.z, xv.w); *(GAS v2u*)(x1 + (size_t)m * D + k) = xo; }
;                         const f32x4 hv = xv * (*(const GAS f32x4*)(mrow + 8192 + k) + 1.0f) + *(const GAS f32x4*)(mrow + 6144 + k);
;                         v2u o; o.x = pk2(hv.x, hv.y); o.y = pk2(hv.z, hv.w);
;                         *(GAS unsigned*)(h2q + (size_t)m * D + k) = pk4_fp8(hv.x, hv.y, hv.z, hv.w);
;                         const int chunk = (lq >> 1) + 32 * j;
;                         *(LAS v2u*)(h2s + rloc * 4096 + ((chunk ^ (rloc & 15)) << 4) + (lq & 1) * 8) = o; }
	v_pk_fma_f32 v[12:13], v[56:57], v[12:13], v[46:47]
	v_pk_fma_f32 v[14:15], v[50:51], v[14:15], v[48:49]
	v_cvt_pk_fp8_f32 v60, v12, v13
	v_add3_u32 v46, v125, v86, s90
	v_and_b32_e32 v47, 0xffff0000, v59
	v_and_b32_e32 v50, 0xffff0000, v46
	v_cvt_pk_fp8_f32 v60, v14, v15 op_sel:[0,0,1]
	v_or_b32_sdwa v51, v47, v58 dst_sel:DWORD dst_unused:UNUSED_PAD src0_sel:DWORD src1_sel:WORD_1
	v_or_b32_sdwa v50, v50, v92 dst_sel:DWORD dst_unused:UNUSED_PAD src0_sel:DWORD src1_sel:WORD_1
	v_and_b32_sdwa v61, v131, v226 dst_sel:DWORD dst_unused:UNUSED_PAD src0_sel:WORD_1 src1_sel:DWORD
	global_store_dword v[20:21], v60, off offset:1280
	global_load_dwordx4 v[46:49], v[88:89], off offset:2048
	global_load_dwordx4 v[56:59], v[90:91], off offset:2048
	ds_write_b64 v183, v[50:51]
	v_and_b32_sdwa v51, v130, v226 dst_sel:DWORD dst_unused:UNUSED_PAD src0_sel:WORD_1 src1_sel:DWORD
	v_and_b32_sdwa v60, v133, v226 dst_sel:DWORD dst_unused:UNUSED_PAD src0_sel:WORD_1 src1_sel:DWORD
	v_and_b32_sdwa v50, v132, v226 dst_sel:DWORD dst_unused:UNUSED_PAD src0_sel:WORD_1 src1_sel:DWORD
	v_add3_u32 v86, v130, v51, s90
	v_add3_u32 v51, v133, v60, s90
	v_add3_u32 v60, v131, v61, s90
	v_add3_u32 v50, v132, v50, s90
	v_and_b32_e32 v51, 0xffff0000, v51
	v_and_b32_e32 v60, 0xffff0000, v60
	v_or_b32_sdwa v51, v51, v50 dst_sel:DWORD dst_unused:UNUSED_PAD src0_sel:DWORD src1_sel:WORD_1
	v_or_b32_sdwa v50, v60, v86 dst_sel:DWORD dst_unused:UNUSED_PAD src0_sel:DWORD src1_sel:WORD_1
	ds_write_b64 v184, v[50:51]
	v_and_b32_sdwa v51, v134, v226 dst_sel:DWORD dst_unused:UNUSED_PAD src0_sel:WORD_1 src1_sel:DWORD
	v_and_b32_sdwa v60, v137, v226 dst_sel:DWORD dst_unused:UNUSED_PAD src0_sel:WORD_1 src1_sel:DWORD
	v_and_b32_sdwa v61, v135, v226 dst_sel:DWORD dst_unused:UNUSED_PAD src0_sel:WORD_1 src1_sel:DWORD
	v_and_b32_sdwa v50, v136, v226 dst_sel:DWORD dst_unused:UNUSED_PAD src0_sel:WORD_1 src1_sel:DWORD
	v_add3_u32 v86, v134, v51, s90
	v_add3_u32 v51, v137, v60, s90
	v_add3_u32 v60, v135, v61, s90
	v_add3_u32 v50, v136, v50, s90
	v_and_b32_e32 v51, 0xffff0000, v51
	v_and_b32_e32 v60, 0xffff0000, v60
	v_or_b32_sdwa v51, v51, v50 dst_sel:DWORD dst_unused:UNUSED_PAD src0_sel:DWORD src1_sel:WORD_1
	v_or_b32_sdwa v50, v60, v86 dst_sel:DWORD dst_unused:UNUSED_PAD src0_sel:DWORD src1_sel:WORD_1
	ds_write_b64 v120, v[50:51]
	v_and_b32_sdwa v51, v138, v226 dst_sel:DWORD dst_unused:UNUSED_PAD src0_sel:WORD_1 src1_sel:DWORD
	v_and_b32_sdwa v60, v141, v226 dst_sel:DWORD dst_unused:UNUSED_PAD src0_sel:WORD_1 src1_sel:DWORD
	v_and_b32_sdwa v61, v139, v226 dst_sel:DWORD dst_unused:UNUSED_PAD src0_sel:WORD_1 src1_sel:DWORD
	v_and_b32_sdwa v50, v140, v226 dst_sel:DWORD dst_unused:UNUSED_PAD src0_sel:WORD_1 src1_sel:DWORD
	v_add3_u32 v86, v138, v51, s90
	v_add3_u32 v51, v141, v60, s90
	v_add3_u32 v60, v139, v61, s90
	v_add3_u32 v50, v140, v50, s90
	v_and_b32_e32 v51, 0xffff0000, v51
	v_and_b32_e32 v60, 0xffff0000, v60
	v_or_b32_sdwa v51, v51, v50 dst_sel:DWORD dst_unused:UNUSED_PAD src0_sel:DWORD src1_sel:WORD_1
	v_or_b32_sdwa v50, v60, v86 dst_sel:DWORD dst_unused:UNUSED_PAD src0_sel:DWORD src1_sel:WORD_1
	ds_write_b64 v185, v[50:51]
	v_and_b32_sdwa v51, v142, v226 dst_sel:DWORD dst_unused:UNUSED_PAD src0_sel:WORD_1 src1_sel:DWORD
	v_and_b32_sdwa v60, v145, v226 dst_sel:DWORD dst_unused:UNUSED_PAD src0_sel:WORD_1 src1_sel:DWORD
	v_and_b32_sdwa v61, v143, v226 dst_sel:DWORD dst_unused:UNUSED_PAD src0_sel:WORD_1 src1_sel:DWORD
	v_and_b32_sdwa v50, v144, v226 dst_sel:DWORD dst_unused:UNUSED_PAD src0_sel:WORD_1 src1_sel:DWORD
	v_add3_u32 v86, v142, v51, s90
	v_add3_u32 v51, v145, v60, s90
	v_add3_u32 v60, v143, v61, s90
	v_add3_u32 v50, v144, v50, s90
	v_and_b32_e32 v51, 0xffff0000, v51
	v_and_b32_e32 v60, 0xffff0000, v60
	v_or_b32_sdwa v51, v51, v50 dst_sel:DWORD dst_unused:UNUSED_PAD src0_sel:DWORD src1_sel:WORD_1
	v_or_b32_sdwa v50, v60, v86 dst_sel:DWORD dst_unused:UNUSED_PAD src0_sel:DWORD src1_sel:WORD_1
	ds_write_b64 v186, v[50:51]
	v_and_b32_sdwa v51, v146, v226 dst_sel:DWORD dst_unused:UNUSED_PAD src0_sel:WORD_1 src1_sel:DWORD
	v_and_b32_sdwa v60, v149, v226 dst_sel:DWORD dst_unused:UNUSED_PAD src0_sel:WORD_1 src1_sel:DWORD
	v_and_b32_sdwa v61, v147, v226 dst_sel:DWORD dst_unused:UNUSED_PAD src0_sel:WORD_1 src1_sel:DWORD
	v_and_b32_sdwa v50, v148, v226 dst_sel:DWORD dst_unused:UNUSED_PAD src0_sel:WORD_1 src1_sel:DWORD
	v_add3_u32 v86, v146, v51, s90
	v_add3_u32 v51, v149, v60, s90
	v_add3_u32 v60, v147, v61, s90
	v_add3_u32 v50, v148, v50, s90
	v_and_b32_e32 v51, 0xffff0000, v51
	v_and_b32_e32 v60, 0xffff0000, v60
	v_or_b32_sdwa v51, v51, v50 dst_sel:DWORD dst_unused:UNUSED_PAD src0_sel:DWORD src1_sel:WORD_1
	v_or_b32_sdwa v50, v60, v86 dst_sel:DWORD dst_unused:UNUSED_PAD src0_sel:DWORD src1_sel:WORD_1
	ds_write_b64 v187, v[50:51]
	v_and_b32_sdwa v50, v152, v226 dst_sel:DWORD dst_unused:UNUSED_PAD src0_sel:WORD_1 src1_sel:DWORD
	v_and_b32_sdwa v51, v150, v226 dst_sel:DWORD dst_unused:UNUSED_PAD src0_sel:WORD_1 src1_sel:DWORD
	v_and_b32_sdwa v60, v153, v226 dst_sel:DWORD dst_unused:UNUSED_PAD src0_sel:WORD_1 src1_sel:DWORD
	v_and_b32_sdwa v61, v151, v226 dst_sel:DWORD dst_unused:UNUSED_PAD src0_sel:WORD_1 src1_sel:DWORD
	v_add3_u32 v86, v150, v51, s90
	v_add3_u32 v92, v152, v50, s90
	v_add3_u32 v50, v153, v60, s90
	v_add3_u32 v51, v151, v61, s90
	v_and_b32_e32 v60, 0xffff0000, v50
	v_and_b32_e32 v61, 0xffff0000, v51
	s_waitcnt vmcnt(0)
; #define GAS __attribute__((address_space(1)))
; #define LAS __attribute__((address_space(3)))
; __device__ __forceinline__ unsigned pk2(float lo, float hi) { return f2bf(lo) | (f2bf(hi) << 16); }
; __device__ __forceinline__ unsigned pk4_fp8(float a, float b, float c, float d) { int r = __builtin_amdgcn_cvt_pk_fp8_f32(a, b, 0, false); r = __builtin_amdgcn_cvt_pk_fp8_f32(c, d, r, true); return (unsigned)r; }
; template <int l>
; __device__ __forceinline__ void layer_phases(Frame& F, const XcdBarrier& bar, const int lo, const int hi) {
;     ...
;                     for (int j = 0; j < 8; ++j) { const int k = 4 * lq + 256 * j;
;                         const f32x4 xv = v[j] * rstd * *(const GAS f32x4*)(g1 + k) + *(const GAS f32x4*)(b1 + k);
;                         { v2u xo; xo.x = pk2(xv.x, xv.y); xo.y = pk2(xv.z, xv.w); *(GAS v2u*)(x1 + (size_t)m * D + k) = xo; }
;                         const f32x4 hv = xv * (*(const GAS f32x4*)(mrow + 8192 + k) + 1.0f) + *(const GAS f32x4*)(mrow + 6144 + k);
;                         v2u o; o.x = pk2(hv.x, hv.y); o.y = pk2(hv.z, hv.w);
;                         *(GAS unsigned*)(h2q + (size_t)m * D + k) = pk4_fp8(hv.x, hv.y, hv.z, hv.w);
;                         const int chunk = (lq >> 1) + 32 * j;
;                         *(LAS v2u*)(h2s + rloc * 4096 + ((chunk ^ (rloc & 15)) << 4) + (lq & 1) * 8) = o; }
	v_pk_fma_f32 v[50:51], v[8:9], v[48:49], v[58:59]
	v_pk_fma_f32 v[56:57], v[10:11], v[46:47], v[56:57]
	v_bfe_u32 v10, v50, 16, 1
	v_bfe_u32 v8, v56, 16, 1
	v_bfe_u32 v9, v57, 16, 1
	v_bfe_u32 v11, v51, 16, 1
	v_add3_u32 v8, v56, v8, s90
	v_add3_u32 v10, v50, v10, s90
	v_add3_u32 v9, v57, v9, s90
	v_add3_u32 v11, v51, v11, s90
	v_lshrrev_b32_e32 v8, 16, v8
	v_lshrrev_b32_e32 v10, 16, v10
	v_and_or_b32 v8, v9, s86, v8
	v_and_or_b32 v9, v11, s86, v10
	global_store_dwordx2 v[22:23], v[8:9], off offset:3072
	global_load_dwordx4 v[8:11], v[82:83], off offset:2048
	s_nop 0
	global_load_dwordx4 v[46:49], v[84:85], off offset:2048
	v_or_b32_sdwa v59, v60, v92 dst_sel:DWORD dst_unused:UNUSED_PAD src0_sel:DWORD src1_sel:WORD_1
	v_or_b32_sdwa v58, v61, v86 dst_sel:DWORD dst_unused:UNUSED_PAD src0_sel:DWORD src1_sel:WORD_1
	ds_write_b64 v188, v[58:59]
	v_and_b32_sdwa v59, v154, v226 dst_sel:DWORD dst_unused:UNUSED_PAD src0_sel:WORD_1 src1_sel:DWORD
	v_and_b32_sdwa v60, v157, v226 dst_sel:DWORD dst_unused:UNUSED_PAD src0_sel:WORD_1 src1_sel:DWORD
	v_and_b32_sdwa v61, v155, v226 dst_sel:DWORD dst_unused:UNUSED_PAD src0_sel:WORD_1 src1_sel:DWORD
	v_and_b32_sdwa v58, v156, v226 dst_sel:DWORD dst_unused:UNUSED_PAD src0_sel:WORD_1 src1_sel:DWORD
	v_add3_u32 v86, v154, v59, s90
	v_add3_u32 v59, v157, v60, s90
	v_add3_u32 v60, v155, v61, s90
	v_add3_u32 v58, v156, v58, s90
	v_and_b32_e32 v59, 0xffff0000, v59
	v_and_b32_e32 v60, 0xffff0000, v60
	v_or_b32_sdwa v59, v59, v58 dst_sel:DWORD dst_unused:UNUSED_PAD src0_sel:DWORD src1_sel:WORD_1
	v_or_b32_sdwa v58, v60, v86 dst_sel:DWORD dst_unused:UNUSED_PAD src0_sel:DWORD src1_sel:WORD_1
	ds_write_b64 v189, v[58:59]
	v_and_b32_sdwa v59, v158, v226 dst_sel:DWORD dst_unused:UNUSED_PAD src0_sel:WORD_1 src1_sel:DWORD
	v_and_b32_sdwa v60, v161, v226 dst_sel:DWORD dst_unused:UNUSED_PAD src0_sel:WORD_1 src1_sel:DWORD
	v_and_b32_sdwa v61, v159, v226 dst_sel:DWORD dst_unused:UNUSED_PAD src0_sel:WORD_1 src1_sel:DWORD
	v_and_b32_sdwa v58, v160, v226 dst_sel:DWORD dst_unused:UNUSED_PAD src0_sel:WORD_1 src1_sel:DWORD
	v_add3_u32 v86, v158, v59, s90
	v_add3_u32 v59, v161, v60, s90
	v_add3_u32 v60, v159, v61, s90
	v_add3_u32 v58, v160, v58, s90
	v_and_b32_e32 v59, 0xffff0000, v59
	v_and_b32_e32 v60, 0xffff0000, v60
	v_or_b32_sdwa v59, v59, v58 dst_sel:DWORD dst_unused:UNUSED_PAD src0_sel:DWORD src1_sel:WORD_1
	v_or_b32_sdwa v58, v60, v86 dst_sel:DWORD dst_unused:UNUSED_PAD src0_sel:DWORD src1_sel:WORD_1
	ds_write_b64 v190, v[58:59]
	v_and_b32_sdwa v59, v162, v226 dst_sel:DWORD dst_unused:UNUSED_PAD src0_sel:WORD_1 src1_sel:DWORD
	v_and_b32_sdwa v60, v165, v226 dst_sel:DWORD dst_unused:UNUSED_PAD src0_sel:WORD_1 src1_sel:DWORD
	v_and_b32_sdwa v61, v163, v226 dst_sel:DWORD dst_unused:UNUSED_PAD src0_sel:WORD_1 src1_sel:DWORD
	v_and_b32_sdwa v58, v164, v226 dst_sel:DWORD dst_unused:UNUSED_PAD src0_sel:WORD_1 src1_sel:DWORD
	v_add3_u32 v86, v162, v59, s90
	v_add3_u32 v59, v165, v60, s90
	v_add3_u32 v60, v163, v61, s90
	v_add3_u32 v58, v164, v58, s90
	v_and_b32_e32 v59, 0xffff0000, v59
	v_and_b32_e32 v60, 0xffff0000, v60
	v_or_b32_sdwa v59, v59, v58 dst_sel:DWORD dst_unused:UNUSED_PAD src0_sel:DWORD src1_sel:WORD_1
	v_or_b32_sdwa v58, v60, v86 dst_sel:DWORD dst_unused:UNUSED_PAD src0_sel:DWORD src1_sel:WORD_1
	ds_write_b64 v191, v[58:59]
	v_pk_mul_f32 v[58:59], v[6:7], v[32:33] op_sel_hi:[1,0]
	v_pk_mul_f32 v[60:61], v[4:5], v[32:33] op_sel_hi:[1,0]
	v_and_b32_sdwa v5, v64, v226 dst_sel:DWORD dst_unused:UNUSED_PAD src0_sel:WORD_1 src1_sel:DWORD
	v_and_b32_sdwa v6, v67, v226 dst_sel:DWORD dst_unused:UNUSED_PAD src0_sel:WORD_1 src1_sel:DWORD
	v_and_b32_sdwa v7, v65, v226 dst_sel:DWORD dst_unused:UNUSED_PAD src0_sel:WORD_1 src1_sel:DWORD
	v_and_b32_sdwa v4, v66, v226 dst_sel:DWORD dst_unused:UNUSED_PAD src0_sel:WORD_1 src1_sel:DWORD
	v_add3_u32 v32, v64, v5, s90
	v_add3_u32 v5, v67, v6, s90
	v_add3_u32 v6, v65, v7, s90
	v_add3_u32 v4, v66, v4, s90
	v_and_b32_e32 v5, 0xffff0000, v5
	v_and_b32_e32 v6, 0xffff0000, v6
	v_or_b32_sdwa v5, v5, v4 dst_sel:DWORD dst_unused:UNUSED_PAD src0_sel:DWORD src1_sel:WORD_1
	v_or_b32_sdwa v4, v6, v32 dst_sel:DWORD dst_unused:UNUSED_PAD src0_sel:DWORD src1_sel:WORD_1
	ds_write_b64 v121, v[4:5]
	v_and_b32_sdwa v5, v68, v226 dst_sel:DWORD dst_unused:UNUSED_PAD src0_sel:WORD_1 src1_sel:DWORD
	v_and_b32_sdwa v6, v71, v226 dst_sel:DWORD dst_unused:UNUSED_PAD src0_sel:WORD_1 src1_sel:DWORD
	v_and_b32_sdwa v7, v69, v226 dst_sel:DWORD dst_unused:UNUSED_PAD src0_sel:WORD_1 src1_sel:DWORD
	v_and_b32_sdwa v4, v70, v226 dst_sel:DWORD dst_unused:UNUSED_PAD src0_sel:WORD_1 src1_sel:DWORD
	v_add3_u32 v32, v68, v5, s90
	v_add3_u32 v5, v71, v6, s90
	v_add3_u32 v6, v69, v7, s90
	v_add3_u32 v4, v70, v4, s90
	v_and_b32_e32 v5, 0xffff0000, v5
	v_and_b32_e32 v6, 0xffff0000, v6
	v_or_b32_sdwa v5, v5, v4 dst_sel:DWORD dst_unused:UNUSED_PAD src0_sel:DWORD src1_sel:WORD_1
	v_or_b32_sdwa v4, v6, v32 dst_sel:DWORD dst_unused:UNUSED_PAD src0_sel:DWORD src1_sel:WORD_1
	ds_write_b64 v192, v[4:5]
	v_and_b32_sdwa v4, v168, v226 dst_sel:DWORD dst_unused:UNUSED_PAD src0_sel:WORD_1 src1_sel:DWORD
	v_and_b32_sdwa v5, v166, v226 dst_sel:DWORD dst_unused:UNUSED_PAD src0_sel:WORD_1 src1_sel:DWORD
	v_add3_u32 v32, v166, v5, s90
	v_add3_u32 v64, v168, v4, s90
	v_and_b32_sdwa v6, v169, v226 dst_sel:DWORD dst_unused:UNUSED_PAD src0_sel:WORD_1 src1_sel:DWORD
	v_and_b32_sdwa v7, v167, v226 dst_sel:DWORD dst_unused:UNUSED_PAD src0_sel:WORD_1 src1_sel:DWORD
	v_add3_u32 v6, v169, v6, s90
	v_add3_u32 v7, v167, v7, s90
	s_waitcnt vmcnt(1)
	v_pk_add_f32 v[4:5], v[8:9], 1.0 op_sel_hi:[1,0]
	v_and_b32_e32 v6, 0xffff0000, v6
	s_waitcnt vmcnt(0)
; #define GAS __attribute__((address_space(1)))
; #define LAS __attribute__((address_space(3)))
; __device__ __forceinline__ unsigned pk2(float lo, float hi) { return f2bf(lo) | (f2bf(hi) << 16); }
; __device__ __forceinline__ unsigned pk4_fp8(float a, float b, float c, float d) { int r = __builtin_amdgcn_cvt_pk_fp8_f32(a, b, 0, false); r = __builtin_amdgcn_cvt_pk_fp8_f32(c, d, r, true); return (unsigned)r; }
; template <int l>
; __device__ __forceinline__ void layer_phases(Frame& F, const XcdBarrier& bar, const int lo, const int hi) {
;     ...
;                     for (int j = 0; j < 8; ++j) { const int k = 4 * lq + 256 * j;
;                         const f32x4 xv = v[j] * rstd * *(const GAS f32x4*)(g1 + k) + *(const GAS f32x4*)(b1 + k);
;                         { v2u xo; xo.x = pk2(xv.x, xv.y); xo.y = pk2(xv.z, xv.w); *(GAS v2u*)(x1 + (size_t)m * D + k) = xo; }
;                         const f32x4 hv = xv * (*(const GAS f32x4*)(mrow + 8192 + k) + 1.0f) + *(const GAS f32x4*)(mrow + 6144 + k);
;                         v2u o; o.x = pk2(hv.x, hv.y); o.y = pk2(hv.z, hv.w);
;                         *(GAS unsigned*)(h2q + (size_t)m * D + k) = pk4_fp8(hv.x, hv.y, hv.z, hv.w);
;                         const int chunk = (lq >> 1) + 32 * j;
;                         *(LAS v2u*)(h2s + rloc * 4096 + ((chunk ^ (rloc & 15)) << 4) + (lq & 1) * 8) = o; }
	v_pk_fma_f32 v[46:47], v[56:57], v[4:5], v[46:47]
	v_pk_add_f32 v[4:5], v[10:11], 1.0 op_sel_hi:[1,0]
	v_cvt_pk_fp8_f32 v62, v46, v47
	v_pk_fma_f32 v[48:49], v[50:51], v[4:5], v[48:49]
	v_and_b32_e32 v4, 0xffff0000, v7
	v_or_b32_sdwa v51, v6, v64 dst_sel:DWORD dst_unused:UNUSED_PAD src0_sel:DWORD src1_sel:WORD_1
	v_cvt_pk_fp8_f32 v62, v48, v49 op_sel:[0,0,1]
	v_or_b32_sdwa v50, v4, v32 dst_sel:DWORD dst_unused:UNUSED_PAD src0_sel:DWORD src1_sel:WORD_1
	v_and_b32_sdwa v56, v171, v226 dst_sel:DWORD dst_unused:UNUSED_PAD src0_sel:WORD_1 src1_sel:DWORD
	v_and_b32_sdwa v32, v172, v226 dst_sel:DWORD dst_unused:UNUSED_PAD src0_sel:WORD_1 src1_sel:DWORD
	global_store_dword v[20:21], v62, off offset:1536
	global_load_dwordx4 v[4:7], v[88:89], off offset:3072
	global_load_dwordx4 v[8:11], v[90:91], off offset:3072
	ds_write_b64 v193, v[50:51]
	v_and_b32_sdwa v51, v173, v226 dst_sel:DWORD dst_unused:UNUSED_PAD src0_sel:WORD_1 src1_sel:DWORD
	v_and_b32_sdwa v50, v170, v226 dst_sel:DWORD dst_unused:UNUSED_PAD src0_sel:WORD_1 src1_sel:DWORD
	v_add3_u32 v51, v173, v51, s90
	v_add3_u32 v56, v171, v56, s90
	v_add3_u32 v50, v170, v50, s90
	v_add3_u32 v32, v172, v32, s90
	v_and_b32_e32 v51, 0xffff0000, v51
	v_and_b32_e32 v56, 0xffff0000, v56
	v_or_b32_sdwa v51, v51, v32 dst_sel:DWORD dst_unused:UNUSED_PAD src0_sel:DWORD src1_sel:WORD_1
	v_or_b32_sdwa v50, v56, v50 dst_sel:DWORD dst_unused:UNUSED_PAD src0_sel:DWORD src1_sel:WORD_1
	ds_write_b64 v194, v[50:51]
	v_and_b32_sdwa v51, v177, v226 dst_sel:DWORD dst_unused:UNUSED_PAD src0_sel:WORD_1 src1_sel:DWORD
	v_and_b32_sdwa v56, v175, v226 dst_sel:DWORD dst_unused:UNUSED_PAD src0_sel:WORD_1 src1_sel:DWORD
	v_and_b32_sdwa v32, v176, v226 dst_sel:DWORD dst_unused:UNUSED_PAD src0_sel:WORD_1 src1_sel:DWORD
	v_and_b32_sdwa v50, v174, v226 dst_sel:DWORD dst_unused:UNUSED_PAD src0_sel:WORD_1 src1_sel:DWORD
	v_add3_u32 v51, v177, v51, s90
	v_add3_u32 v56, v175, v56, s90
	v_add3_u32 v50, v174, v50, s90
	v_add3_u32 v32, v176, v32, s90
	v_and_b32_e32 v51, 0xffff0000, v51
	v_and_b32_e32 v56, 0xffff0000, v56
	v_or_b32_sdwa v51, v51, v32 dst_sel:DWORD dst_unused:UNUSED_PAD src0_sel:DWORD src1_sel:WORD_1
	v_or_b32_sdwa v50, v56, v50 dst_sel:DWORD dst_unused:UNUSED_PAD src0_sel:DWORD src1_sel:WORD_1
	ds_write_b64 v195, v[50:51]
	v_and_b32_sdwa v51, v181, v226 dst_sel:DWORD dst_unused:UNUSED_PAD src0_sel:WORD_1 src1_sel:DWORD
	v_and_b32_sdwa v56, v179, v226 dst_sel:DWORD dst_unused:UNUSED_PAD src0_sel:WORD_1 src1_sel:DWORD
	v_and_b32_sdwa v32, v180, v226 dst_sel:DWORD dst_unused:UNUSED_PAD src0_sel:WORD_1 src1_sel:DWORD
	v_and_b32_sdwa v50, v178, v226 dst_sel:DWORD dst_unused:UNUSED_PAD src0_sel:WORD_1 src1_sel:DWORD
	v_add3_u32 v51, v181, v51, s90
	v_add3_u32 v56, v179, v56, s90
	v_add3_u32 v50, v178, v50, s90
	v_add3_u32 v32, v180, v32, s90
	v_and_b32_e32 v51, 0xffff0000, v51
	v_and_b32_e32 v56, 0xffff0000, v56
	v_or_b32_sdwa v51, v51, v32 dst_sel:DWORD dst_unused:UNUSED_PAD src0_sel:DWORD src1_sel:WORD_1
	v_or_b32_sdwa v50, v56, v50 dst_sel:DWORD dst_unused:UNUSED_PAD src0_sel:DWORD src1_sel:WORD_1
	ds_write_b64 v196, v[50:51]
	v_and_b32_sdwa v51, v3, v226 dst_sel:DWORD dst_unused:UNUSED_PAD src0_sel:WORD_1 src1_sel:DWORD
	v_and_b32_sdwa v56, v1, v226 dst_sel:DWORD dst_unused:UNUSED_PAD src0_sel:WORD_1 src1_sel:DWORD
	v_and_b32_sdwa v32, v2, v226 dst_sel:DWORD dst_unused:UNUSED_PAD src0_sel:WORD_1 src1_sel:DWORD
	v_and_b32_sdwa v50, v0, v226 dst_sel:DWORD dst_unused:UNUSED_PAD src0_sel:WORD_1 src1_sel:DWORD
	v_add3_u32 v3, v3, v51, s90
	v_add3_u32 v1, v1, v56, s90
	v_add3_u32 v0, v0, v50, s90
	v_add3_u32 v2, v2, v32, s90
	v_and_b32_e32 v3, 0xffff0000, v3
	v_and_b32_e32 v32, 0xffff0000, v1
	v_or_b32_sdwa v1, v3, v2 dst_sel:DWORD dst_unused:UNUSED_PAD src0_sel:DWORD src1_sel:WORD_1
	v_or_b32_sdwa v0, v32, v0 dst_sel:DWORD dst_unused:UNUSED_PAD src0_sel:DWORD src1_sel:WORD_1
	ds_write_b64 v197, v[0:1]
	v_and_b32_sdwa v1, v16, v226 dst_sel:DWORD dst_unused:UNUSED_PAD src0_sel:WORD_1 src1_sel:DWORD
	v_and_b32_sdwa v2, v19, v226 dst_sel:DWORD dst_unused:UNUSED_PAD src0_sel:WORD_1 src1_sel:DWORD
	v_and_b32_sdwa v3, v17, v226 dst_sel:DWORD dst_unused:UNUSED_PAD src0_sel:WORD_1 src1_sel:DWORD
	v_and_b32_sdwa v0, v18, v226 dst_sel:DWORD dst_unused:UNUSED_PAD src0_sel:WORD_1 src1_sel:DWORD
	v_add3_u32 v16, v16, v1, s90
	v_add3_u32 v1, v19, v2, s90
	v_add3_u32 v2, v17, v3, s90
	v_add3_u32 v0, v18, v0, s90
	v_and_b32_e32 v1, 0xffff0000, v1
	v_and_b32_e32 v2, 0xffff0000, v2
	v_or_b32_sdwa v1, v1, v0 dst_sel:DWORD dst_unused:UNUSED_PAD src0_sel:DWORD src1_sel:WORD_1
	v_or_b32_sdwa v0, v2, v16 dst_sel:DWORD dst_unused:UNUSED_PAD src0_sel:DWORD src1_sel:WORD_1
	ds_write_b64 v198, v[0:1]
	v_and_b32_sdwa v1, v24, v226 dst_sel:DWORD dst_unused:UNUSED_PAD src0_sel:WORD_1 src1_sel:DWORD
	v_and_b32_sdwa v2, v27, v226 dst_sel:DWORD dst_unused:UNUSED_PAD src0_sel:WORD_1 src1_sel:DWORD
	v_and_b32_sdwa v3, v25, v226 dst_sel:DWORD dst_unused:UNUSED_PAD src0_sel:WORD_1 src1_sel:DWORD
	v_and_b32_sdwa v0, v26, v226 dst_sel:DWORD dst_unused:UNUSED_PAD src0_sel:WORD_1 src1_sel:DWORD
	v_add3_u32 v16, v24, v1, s90
	v_add3_u32 v1, v27, v2, s90
	v_add3_u32 v2, v25, v3, s90
	v_add3_u32 v0, v26, v0, s90
	v_and_b32_e32 v1, 0xffff0000, v1
	v_and_b32_e32 v2, 0xffff0000, v2
	v_or_b32_sdwa v1, v1, v0 dst_sel:DWORD dst_unused:UNUSED_PAD src0_sel:DWORD src1_sel:WORD_1
	v_or_b32_sdwa v0, v2, v16 dst_sel:DWORD dst_unused:UNUSED_PAD src0_sel:DWORD src1_sel:WORD_1
	ds_write_b64 v199, v[0:1]
	v_and_b32_sdwa v17, v28, v226 dst_sel:DWORD dst_unused:UNUSED_PAD src0_sel:WORD_1 src1_sel:DWORD
	v_and_b32_sdwa v18, v31, v226 dst_sel:DWORD dst_unused:UNUSED_PAD src0_sel:WORD_1 src1_sel:DWORD
	s_waitcnt vmcnt(0)
; #define GAS __attribute__((address_space(1)))
; #define LAS __attribute__((address_space(3)))
; __device__ __forceinline__ unsigned pk2(float lo, float hi) { return f2bf(lo) | (f2bf(hi) << 16); }
; __device__ __forceinline__ unsigned pk4_fp8(float a, float b, float c, float d) { int r = __builtin_amdgcn_cvt_pk_fp8_f32(a, b, 0, false); r = __builtin_amdgcn_cvt_pk_fp8_f32(c, d, r, true); return (unsigned)r; }
; template <int l>
; __device__ __forceinline__ void layer_phases(Frame& F, const XcdBarrier& bar, const int lo, const int hi) {
;     ...
;                     for (int j = 0; j < 8; ++j) { const int k = 4 * lq + 256 * j;
;                         const f32x4 xv = v[j] * rstd * *(const GAS f32x4*)(g1 + k) + *(const GAS f32x4*)(b1 + k);
;                         { v2u xo; xo.x = pk2(xv.x, xv.y); xo.y = pk2(xv.z, xv.w); *(GAS v2u*)(x1 + (size_t)m * D + k) = xo; }
;                         const f32x4 hv = xv * (*(const GAS f32x4*)(mrow + 8192 + k) + 1.0f) + *(const GAS f32x4*)(mrow + 6144 + k);
;                         v2u o; o.x = pk2(hv.x, hv.y); o.y = pk2(hv.z, hv.w);
;                         *(GAS unsigned*)(h2q + (size_t)m * D + k) = pk4_fp8(hv.x, hv.y, hv.z, hv.w);
;                         const int chunk = (lq >> 1) + 32 * j;
;                         *(LAS v2u*)(h2s + rloc * 4096 + ((chunk ^ (rloc & 15)) << 4) + (lq & 1) * 8) = o; }
	v_pk_fma_f32 v[10:11], v[60:61], v[6:7], v[10:11]
	v_pk_fma_f32 v[8:9], v[58:59], v[4:5], v[8:9]
	v_bfe_u32 v2, v10, 16, 1
	v_bfe_u32 v0, v8, 16, 1
	v_bfe_u32 v1, v9, 16, 1
	v_bfe_u32 v3, v11, 16, 1
	v_add3_u32 v0, v8, v0, s90
	v_add3_u32 v2, v10, v2, s90
	v_add3_u32 v1, v9, v1, s90
	v_add3_u32 v3, v11, v3, s90
	v_lshrrev_b32_e32 v0, 16, v0
	v_lshrrev_b32_e32 v2, 16, v2
	v_and_or_b32 v0, v1, s86, v0
	v_and_or_b32 v1, v3, s86, v2
	global_store_dwordx2 v[22:23], v[0:1], off offset:3584
	global_load_dwordx4 v[0:3], v[82:83], off offset:3072
	v_and_b32_sdwa v19, v29, v226 dst_sel:DWORD dst_unused:UNUSED_PAD src0_sel:WORD_1 src1_sel:DWORD
	global_load_dwordx4 v[4:7], v[84:85], off offset:3072
	v_and_b32_sdwa v16, v30, v226 dst_sel:DWORD dst_unused:UNUSED_PAD src0_sel:WORD_1 src1_sel:DWORD
	v_add3_u32 v22, v28, v17, s90
	v_add3_u32 v17, v31, v18, s90
	v_add3_u32 v18, v29, v19, s90
	v_add3_u32 v16, v30, v16, s90
	v_and_b32_e32 v17, 0xffff0000, v17
	v_and_b32_e32 v18, 0xffff0000, v18
	v_or_b32_sdwa v17, v17, v16 dst_sel:DWORD dst_unused:UNUSED_PAD src0_sel:DWORD src1_sel:WORD_1
	v_or_b32_sdwa v16, v18, v22 dst_sel:DWORD dst_unused:UNUSED_PAD src0_sel:DWORD src1_sel:WORD_1
	ds_write_b64 v87, v[16:17]
	v_and_b32_sdwa v17, v34, v226 dst_sel:DWORD dst_unused:UNUSED_PAD src0_sel:WORD_1 src1_sel:DWORD
	v_and_b32_sdwa v18, v37, v226 dst_sel:DWORD dst_unused:UNUSED_PAD src0_sel:WORD_1 src1_sel:DWORD
	v_and_b32_sdwa v19, v35, v226 dst_sel:DWORD dst_unused:UNUSED_PAD src0_sel:WORD_1 src1_sel:DWORD
	v_and_b32_sdwa v16, v36, v226 dst_sel:DWORD dst_unused:UNUSED_PAD src0_sel:WORD_1 src1_sel:DWORD
	v_add3_u32 v22, v34, v17, s90
	v_add3_u32 v17, v37, v18, s90
	v_add3_u32 v18, v35, v19, s90
	v_add3_u32 v16, v36, v16, s90
	v_and_b32_e32 v17, 0xffff0000, v17
	v_and_b32_e32 v18, 0xffff0000, v18
	v_or_b32_sdwa v17, v17, v16 dst_sel:DWORD dst_unused:UNUSED_PAD src0_sel:DWORD src1_sel:WORD_1
	v_or_b32_sdwa v16, v18, v22 dst_sel:DWORD dst_unused:UNUSED_PAD src0_sel:DWORD src1_sel:WORD_1
	ds_write_b64 v112, v[16:17]
	v_and_b32_sdwa v17, v38, v226 dst_sel:DWORD dst_unused:UNUSED_PAD src0_sel:WORD_1 src1_sel:DWORD
	v_and_b32_sdwa v18, v45, v226 dst_sel:DWORD dst_unused:UNUSED_PAD src0_sel:WORD_1 src1_sel:DWORD
	v_and_b32_sdwa v19, v39, v226 dst_sel:DWORD dst_unused:UNUSED_PAD src0_sel:WORD_1 src1_sel:DWORD
	v_and_b32_sdwa v16, v44, v226 dst_sel:DWORD dst_unused:UNUSED_PAD src0_sel:WORD_1 src1_sel:DWORD
	v_add3_u32 v22, v38, v17, s90
	v_add3_u32 v17, v45, v18, s90
	v_add3_u32 v18, v39, v19, s90
	v_add3_u32 v16, v44, v16, s90
	v_and_b32_e32 v17, 0xffff0000, v17
	v_and_b32_e32 v18, 0xffff0000, v18
	v_or_b32_sdwa v17, v17, v16 dst_sel:DWORD dst_unused:UNUSED_PAD src0_sel:DWORD src1_sel:WORD_1
	v_or_b32_sdwa v16, v18, v22 dst_sel:DWORD dst_unused:UNUSED_PAD src0_sel:DWORD src1_sel:WORD_1
	ds_write_b64 v200, v[16:17]
	v_and_b32_sdwa v17, v40, v226 dst_sel:DWORD dst_unused:UNUSED_PAD src0_sel:WORD_1 src1_sel:DWORD
	v_and_b32_sdwa v18, v43, v226 dst_sel:DWORD dst_unused:UNUSED_PAD src0_sel:WORD_1 src1_sel:DWORD
	v_and_b32_sdwa v19, v41, v226 dst_sel:DWORD dst_unused:UNUSED_PAD src0_sel:WORD_1 src1_sel:DWORD
	v_and_b32_sdwa v16, v42, v226 dst_sel:DWORD dst_unused:UNUSED_PAD src0_sel:WORD_1 src1_sel:DWORD
	v_add3_u32 v22, v40, v17, s90
	v_add3_u32 v17, v43, v18, s90
	v_add3_u32 v18, v41, v19, s90
	v_add3_u32 v16, v42, v16, s90
	v_and_b32_e32 v17, 0xffff0000, v17
	v_and_b32_e32 v18, 0xffff0000, v18
	v_or_b32_sdwa v17, v17, v16 dst_sel:DWORD dst_unused:UNUSED_PAD src0_sel:DWORD src1_sel:WORD_1
	v_or_b32_sdwa v16, v18, v22 dst_sel:DWORD dst_unused:UNUSED_PAD src0_sel:DWORD src1_sel:WORD_1
	v_and_b32_sdwa v18, v15, v226 dst_sel:DWORD dst_unused:UNUSED_PAD src0_sel:WORD_1 src1_sel:DWORD
	v_and_b32_sdwa v19, v13, v226 dst_sel:DWORD dst_unused:UNUSED_PAD src0_sel:WORD_1 src1_sel:DWORD
	ds_write_b64 v201, v[16:17]
	v_and_b32_sdwa v16, v14, v226 dst_sel:DWORD dst_unused:UNUSED_PAD src0_sel:WORD_1 src1_sel:DWORD
	v_and_b32_sdwa v17, v12, v226 dst_sel:DWORD dst_unused:UNUSED_PAD src0_sel:WORD_1 src1_sel:DWORD
	v_add3_u32 v15, v15, v18, s90
	v_add3_u32 v13, v13, v19, s90
	v_add3_u32 v12, v12, v17, s90
	v_add3_u32 v14, v14, v16, s90
	v_and_b32_e32 v15, 0xffff0000, v15
	v_and_b32_e32 v16, 0xffff0000, v13
	v_or_b32_sdwa v13, v15, v14 dst_sel:DWORD dst_unused:UNUSED_PAD src0_sel:DWORD src1_sel:WORD_1
	v_or_b32_sdwa v12, v16, v12 dst_sel:DWORD dst_unused:UNUSED_PAD src0_sel:DWORD src1_sel:WORD_1
	ds_write_b64 v113, v[12:13]
	v_and_b32_sdwa v13, v46, v226 dst_sel:DWORD dst_unused:UNUSED_PAD src0_sel:WORD_1 src1_sel:DWORD
	v_and_b32_sdwa v14, v49, v226 dst_sel:DWORD dst_unused:UNUSED_PAD src0_sel:WORD_1 src1_sel:DWORD
	v_and_b32_sdwa v15, v47, v226 dst_sel:DWORD dst_unused:UNUSED_PAD src0_sel:WORD_1 src1_sel:DWORD
	v_and_b32_sdwa v12, v48, v226 dst_sel:DWORD dst_unused:UNUSED_PAD src0_sel:WORD_1 src1_sel:DWORD
	v_add3_u32 v16, v46, v13, s90
	v_add3_u32 v13, v49, v14, s90
	v_add3_u32 v14, v47, v15, s90
	v_add3_u32 v12, v48, v12, s90
	v_and_b32_e32 v13, 0xffff0000, v13
	v_and_b32_e32 v14, 0xffff0000, v14
	v_or_b32_sdwa v13, v13, v12 dst_sel:DWORD dst_unused:UNUSED_PAD src0_sel:DWORD src1_sel:WORD_1
	v_or_b32_sdwa v12, v14, v16 dst_sel:DWORD dst_unused:UNUSED_PAD src0_sel:DWORD src1_sel:WORD_1
	ds_write_b64 v114, v[12:13]
	v_add_u32_e32 v57, s0, v55
	s_movk_i32 s0, 0x2000
	s_waitcnt vmcnt(1)
	v_pk_add_f32 v[0:1], v[0:1], 1.0 op_sel_hi:[1,0]
	v_pk_add_f32 v[2:3], v[2:3], 1.0 op_sel_hi:[1,0]
	s_waitcnt vmcnt(0)
; #define LAS __attribute__((address_space(3)))
; #define P5_LDB(dst, q0) do { _Pragma("unroll") for (int q_ = 0; q_ < 4; ++q_) _Pragma("unroll") for (int c_ = 0; c_ < 4; ++c_) dst[q_][c_] = *(const GAS bf16x8*)(wbase + (size_t)((q0) + q_) * 4096 + c_ * 1024); } while (0)
; template <int l>
; __device__ __forceinline__ void layer_phases(Frame& F, const XcdBarrier& bar, const int lo, const int hi) {
;     ...
;                         *(LAS v2u*)(h2s + rloc * 4096 + ((chunk ^ (rloc & 15)) << 4) + (lq & 1) * 8) = o; }
;     ...
;                 bf16x8 bqa[4][4], bqb[4][4];
;                 const unsigned lo_ = lq * 16;
;                 const unsigned char* wbase = wrf + (size_t)(16 * F.wave) * 4096 + lo_;
;     ...
;                 asm volatile("" ::: "memory");
;                 P5_LDB(bqa, 0); P5_LDB(bqb, 4);
;                 __syncthreads();
;                 att::f32x16 acc0 = att::f32x16{}, acc1 = att::f32x16{};
;                 P5_MMA(bqa, 0); asm volatile("" ::: "memory"); P5_LDB(bqa, 8);
;                 P5_MMA(bqb, 4); asm volatile("" ::: "memory"); P5_LDB(bqb, 12);
;                 P5_MMA(bqa, 8); P5_MMA(bqb, 12);
	v_pk_fma_f32 v[0:1], v[8:9], v[0:1], v[4:5]
	v_pk_fma_f32 v[2:3], v[10:11], v[2:3], v[6:7]
	v_cvt_pk_fp8_f32 v33, v0, v1
	v_and_b32_sdwa v5, v0, v226 dst_sel:DWORD dst_unused:UNUSED_PAD src0_sel:WORD_1 src1_sel:DWORD
	v_and_b32_sdwa v6, v3, v226 dst_sel:DWORD dst_unused:UNUSED_PAD src0_sel:WORD_1 src1_sel:DWORD
	v_and_b32_sdwa v7, v1, v226 dst_sel:DWORD dst_unused:UNUSED_PAD src0_sel:WORD_1 src1_sel:DWORD
	v_cvt_pk_fp8_f32 v33, v2, v3 op_sel:[0,0,1]
	v_and_b32_sdwa v4, v2, v226 dst_sel:DWORD dst_unused:UNUSED_PAD src0_sel:WORD_1 src1_sel:DWORD
	v_add3_u32 v0, v0, v5, s90
	v_add3_u32 v5, v3, v6, s90
	v_add3_u32 v1, v1, v7, s90
	v_add3_u32 v4, v2, v4, s90
	v_and_b32_e32 v5, 0xffff0000, v5
	v_and_b32_e32 v6, 0xffff0000, v1
	v_or_b32_sdwa v1, v5, v4 dst_sel:DWORD dst_unused:UNUSED_PAD src0_sel:DWORD src1_sel:WORD_1
	v_or_b32_sdwa v0, v6, v0 dst_sel:DWORD dst_unused:UNUSED_PAD src0_sel:DWORD src1_sel:WORD_1
	ds_write_b64 v63, v[0:1]
	global_store_dword v[20:21], v33, off offset:1792
	global_load_dwordx4 v[0:3], v80, s[36:37]
	global_load_dwordx4 v[36:39], v80, s[36:37] offset:1024
	global_load_dwordx4 v[16:19], v80, s[36:37] offset:2048
	global_load_dwordx4 v[32:35], v80, s[36:37] offset:3072
	v_add_co_u32_e32 v4, vcc, s87, v52
	v_lshl_add_u32 v56, v54, 12, 0
	s_nop 0
	v_addc_co_u32_e32 v5, vcc, 0, v53, vcc
	v_add_co_u32_e32 v8, vcc, s0, v52
	s_movk_i32 s0, 0x3000
	s_nop 0
	v_addc_co_u32_e32 v9, vcc, 0, v53, vcc
	global_load_dwordx4 v[40:43], v[8:9], off offset:-4096
	global_load_dwordx4 v[58:61], v[4:5], off offset:1024
	global_load_dwordx4 v[62:65], v[4:5], off offset:2048
	v_add_co_u32_e32 v12, vcc, s0, v52
	s_movk_i32 s0, 0x6000
	s_nop 0
	v_addc_co_u32_e32 v13, vcc, 0, v53, vcc
	v_add_co_u32_e32 v10, vcc, s85, v52
	v_bitop3_b32 v22, v57, v227, 15 bitop3:0x78
	s_nop 0
	v_addc_co_u32_e32 v11, vcc, 0, v53, vcc
	v_add_co_u32_e32 v6, vcc, s22, v52
	v_lshl_add_u32 v22, v22, 4, v56
	s_nop 0
	v_addc_co_u32_e32 v7, vcc, 0, v53, vcc
	v_add_co_u32_e32 v20, vcc, s0, v52
	v_readlane_b32 s0, v248, 28
	s_nop 0
	v_addc_co_u32_e32 v21, vcc, 0, v53, vcc
	v_add_co_u32_e32 v14, vcc, s28, v52
	s_nop 1
	v_addc_co_u32_e32 v15, vcc, 0, v53, vcc
	v_add_co_u32_e32 v70, vcc, s14, v52
	s_nop 1
	v_addc_co_u32_e32 v71, vcc, 0, v53, vcc
	global_load_dwordx4 v[66:69], v[8:9], off
	global_load_dwordx4 v[82:85], v[8:9], off offset:1024
	global_load_dwordx4 v[86:89], v[8:9], off offset:2048
	global_load_dwordx4 v[90:93], v[8:9], off offset:3072
	global_load_dwordx4 v[94:97], v[10:11], off offset:-4096
	global_load_dwordx4 v[98:101], v[4:5], off offset:3072
	global_load_dwordx4 v[102:105], v[12:13], off offset:1024
	global_load_dwordx4 v[106:109], v[12:13], off offset:2048
	global_load_dwordx4 v[110:113], v[12:13], off offset:3072
	global_load_dwordx4 v[114:117], v[10:11], off
	global_load_dwordx4 v[118:121], v[10:11], off offset:1024
	global_load_dwordx4 v[122:125], v[10:11], off offset:2048
	global_load_dwordx4 v[126:129], v[10:11], off offset:3072
	global_load_dwordx4 v[130:133], v[6:7], off offset:1024
	global_load_dwordx4 v[134:137], v[6:7], off offset:2048
	global_load_dwordx4 v[138:141], v[20:21], off offset:-4096
	global_load_dwordx4 v[142:145], v[20:21], off
	global_load_dwordx4 v[146:149], v[20:21], off offset:1024
	global_load_dwordx4 v[150:153], v[20:21], off offset:2048
	global_load_dwordx4 v[154:157], v[20:21], off offset:3072
	global_load_dwordx4 v[158:161], v[70:71], off offset:-4096
	global_load_dwordx4 v[162:165], v[6:7], off offset:3072
	global_load_dwordx4 v[48:51], v[14:15], off offset:1024
	global_load_dwordx4 v[166:169], v[14:15], off offset:2048
	global_load_dwordx4 v[44:47], v[14:15], off offset:3072
	s_waitcnt lgkmcnt(0)
	s_barrier
	ds_read_b128 v[170:173], v22
	v_add_u32_e32 v4, 2, v57
	v_bitop3_b32 v4, v4, v227, 15 bitop3:0x78
	v_lshl_add_u32 v4, v4, 4, v56
	ds_read_b128 v[174:177], v4
	s_waitcnt vmcnt(31) lgkmcnt(1)
	v_mfma_f32_32x32x16_bf16 v[0:15], v[170:173], v[0:3], 0
	s_waitcnt vmcnt(29)
	v_mfma_f32_32x32x16_bf16 v[16:31], v[170:173], v[16:19], 0
	v_mfma_f32_32x32x16_bf16 v[0:15], v[170:173], v[36:39], v[0:15]
	v_add_u32_e32 v36, 6, v57
	v_bitop3_b32 v36, v36, v227, 15 bitop3:0x78
	v_lshl_add_u32 v36, v36, 4, v56
	ds_read_b128 v[36:39], v36
	s_waitcnt vmcnt(28)
	v_mfma_f32_32x32x16_bf16 v[16:31], v[170:173], v[32:35], v[16:31]
	v_add_u32_e32 v32, 4, v57
	v_bitop3_b32 v32, v32, v227, 15 bitop3:0x78
	v_lshl_add_u32 v32, v32, 4, v56
	ds_read_b128 v[32:35], v32
	s_waitcnt vmcnt(27) lgkmcnt(2)
	v_mfma_f32_32x32x16_bf16 v[0:15], v[174:177], v[40:43], v[0:15]
	v_add_u32_e32 v40, s0, v55
	s_mov_b32 s0, 0xa000
	s_waitcnt vmcnt(25)
	v_mfma_f32_32x32x16_bf16 v[16:31], v[174:177], v[62:65], v[16:31]
	v_mfma_f32_32x32x16_bf16 v[0:15], v[174:177], v[58:61], v[0:15]
	global_load_dwordx4 v[58:61], v[70:71], off offset:2048
	s_waitcnt vmcnt(20)
	v_mfma_f32_32x32x16_bf16 v[16:31], v[174:177], v[98:101], v[16:31]
	s_waitcnt lgkmcnt(0)
	v_mfma_f32_32x32x16_bf16 v[0:15], v[32:35], v[66:69], v[0:15]
	v_mfma_f32_32x32x16_bf16 v[16:31], v[32:35], v[86:89], v[16:31]
	v_mfma_f32_32x32x16_bf16 v[0:15], v[32:35], v[82:85], v[0:15]
	v_mfma_f32_32x32x16_bf16 v[16:31], v[32:35], v[90:93], v[16:31]
	v_bitop3_b32 v32, v40, v227, 15 bitop3:0x78
	v_lshl_add_u32 v32, v32, 4, v56
	ds_read_b128 v[32:35], v32
	v_mfma_f32_32x32x16_bf16 v[0:15], v[36:39], v[94:97], v[0:15]
	s_waitcnt vmcnt(18)
	v_mfma_f32_32x32x16_bf16 v[16:31], v[36:39], v[106:109], v[16:31]
	v_mfma_f32_32x32x16_bf16 v[0:15], v[36:39], v[102:105], v[0:15]
	s_waitcnt vmcnt(17)
	v_mfma_f32_32x32x16_bf16 v[16:31], v[36:39], v[110:113], v[16:31]
	v_add_u32_e32 v36, 2, v40
	v_bitop3_b32 v36, v36, v227, 15 bitop3:0x78
	v_lshl_add_u32 v36, v36, 4, v56
	ds_read_b128 v[36:39], v36
	s_waitcnt vmcnt(16) lgkmcnt(1)
; #define P5_LDB(dst, q0) do { _Pragma("unroll") for (int q_ = 0; q_ < 4; ++q_) _Pragma("unroll") for (int c_ = 0; c_ < 4; ++c_) dst[q_][c_] = *(const GAS bf16x8*)(wbase + (size_t)((q0) + q_) * 4096 + c_ * 1024); } while (0)
; template <int l>
; __device__ __forceinline__ void layer_phases(Frame& F, const XcdBarrier& bar, const int lo, const int hi) {
;     ...
;                 asm volatile("" ::: "memory");
;                 P5_LDB(bqa, 0); P5_LDB(bqb, 4);
;                 __syncthreads();
;                 att::f32x16 acc0 = att::f32x16{}, acc1 = att::f32x16{};
;                 P5_MMA(bqa, 0); asm volatile("" ::: "memory"); P5_LDB(bqa, 8);
;                 P5_MMA(bqb, 4); asm volatile("" ::: "memory"); P5_LDB(bqb, 12);
;                 P5_MMA(bqa, 8); P5_MMA(bqb, 12);
	v_mfma_f32_32x32x16_bf16 v[0:15], v[32:35], v[114:117], v[0:15]
	s_waitcnt vmcnt(14)
	v_mfma_f32_32x32x16_bf16 v[16:31], v[32:35], v[122:125], v[16:31]
	v_mfma_f32_32x32x16_bf16 v[0:15], v[32:35], v[118:121], v[0:15]
	s_waitcnt vmcnt(13)
	v_mfma_f32_32x32x16_bf16 v[16:31], v[32:35], v[126:129], v[16:31]
	v_add_u32_e32 v32, 4, v40
	v_bitop3_b32 v32, v32, v227, 15 bitop3:0x78
	v_lshl_add_u32 v32, v32, 4, v56
	ds_read_b128 v[32:35], v32
	v_add_u32_e32 v40, 6, v40
	v_bitop3_b32 v40, v40, v227, 15 bitop3:0x78
	v_lshl_add_u32 v40, v40, 4, v56
	s_waitcnt vmcnt(10) lgkmcnt(1)
	v_mfma_f32_32x32x16_bf16 v[0:15], v[36:39], v[138:141], v[0:15]
	ds_read_b128 v[40:43], v40
	v_mfma_f32_32x32x16_bf16 v[16:31], v[36:39], v[134:137], v[16:31]
	v_mfma_f32_32x32x16_bf16 v[0:15], v[36:39], v[130:133], v[0:15]
	s_waitcnt vmcnt(4)
	v_mfma_f32_32x32x16_bf16 v[16:31], v[36:39], v[162:165], v[16:31]
	global_load_dwordx4 v[36:39], v[70:71], off
	global_load_dwordx4 v[62:65], v[70:71], off offset:1024
	global_load_dwordx4 v[66:69], v[70:71], off offset:3072
	v_add_co_u32_e32 v70, vcc, s0, v52
	v_readlane_b32 s0, v248, 29
	s_nop 0
	v_addc_co_u32_e32 v71, vcc, 0, v53, vcc
	s_waitcnt lgkmcnt(1)
	v_mfma_f32_32x32x16_bf16 v[0:15], v[32:35], v[142:145], v[0:15]
	v_add_co_u32_e32 v90, vcc, s23, v52
	global_load_dwordx4 v[82:85], v[70:71], off offset:-4096
	global_load_dwordx4 v[94:97], v[70:71], off
	v_addc_co_u32_e32 v91, vcc, 0, v53, vcc
	global_load_dwordx4 v[86:89], v[90:91], off offset:1024
	v_mfma_f32_32x32x16_bf16 v[16:31], v[32:35], v[150:153], v[16:31]
	v_add_u32_e32 v57, s0, v55
	s_mov_b32 s0, 0xb000
	v_add_co_u32_e32 v118, vcc, s0, v52
	s_mov_b32 s0, 0xc000
	s_nop 0
	v_addc_co_u32_e32 v119, vcc, 0, v53, vcc
	v_mfma_f32_32x32x16_bf16 v[0:15], v[32:35], v[146:149], v[0:15]
	v_add_co_u32_e32 v122, vcc, s0, v52
	v_bitop3_b32 v80, v57, v227, 15 bitop3:0x78
	s_nop 0
	v_addc_co_u32_e32 v123, vcc, 0, v53, vcc
	v_lshl_add_u32 v80, v80, 4, v56
	v_readlane_b32 s0, v248, 31
	v_mfma_f32_32x32x16_bf16 v[16:31], v[32:35], v[154:157], v[16:31]
	global_load_dwordx4 v[32:35], v[90:91], off offset:2048
	s_nop 0
	global_load_dwordx4 v[90:93], v[90:91], off offset:3072
	s_waitcnt lgkmcnt(0)
	v_mfma_f32_32x32x16_bf16 v[0:15], v[40:43], v[158:161], v[0:15]
	s_waitcnt vmcnt(11)
	v_mfma_f32_32x32x16_bf16 v[0:15], v[40:43], v[48:51], v[0:15]
	global_load_dwordx4 v[48:51], v[70:71], off offset:1024
	global_load_dwordx4 v[98:101], v[70:71], off offset:2048
	global_load_dwordx4 v[102:105], v[70:71], off offset:3072
	global_load_dwordx4 v[106:109], v[122:123], off offset:-4096
	global_load_dwordx4 v[110:113], v[118:119], off offset:1024
	global_load_dwordx4 v[114:117], v[118:119], off offset:2048
	s_nop 0
	global_load_dwordx4 v[118:121], v[118:119], off offset:3072
	s_waitcnt vmcnt(17)
	v_mfma_f32_32x32x16_bf16 v[16:31], v[40:43], v[166:169], v[16:31]
	s_waitcnt vmcnt(16)
	v_mfma_f32_32x32x16_bf16 v[16:31], v[40:43], v[44:47], v[16:31]
	ds_read_b128 v[40:43], v80
	v_add_u32_e32 v44, 2, v57
	v_bitop3_b32 v44, v44, v227, 15 bitop3:0x78
	v_lshl_add_u32 v44, v44, 4, v56
	ds_read_b128 v[44:47], v44
	s_waitcnt vmcnt(14) lgkmcnt(1)
	v_mfma_f32_32x32x16_bf16 v[0:15], v[40:43], v[36:39], v[0:15]
	v_add_u32_e32 v36, 6, v57
	v_bitop3_b32 v36, v36, v227, 15 bitop3:0x78
	v_lshl_add_u32 v36, v36, 4, v56
	ds_read_b128 v[36:39], v36
	v_mfma_f32_32x32x16_bf16 v[16:31], v[40:43], v[58:61], v[16:31]
	s_waitcnt vmcnt(13)
	v_mfma_f32_32x32x16_bf16 v[0:15], v[40:43], v[62:65], v[0:15]
	s_waitcnt vmcnt(12)
	v_mfma_f32_32x32x16_bf16 v[16:31], v[40:43], v[66:69], v[16:31]
	global_load_dwordx4 v[40:43], v[122:123], off offset:2048
	s_waitcnt vmcnt(12) lgkmcnt(1)
	v_mfma_f32_32x32x16_bf16 v[0:15], v[44:47], v[82:85], v[0:15]
	s_waitcnt vmcnt(9)
	v_mfma_f32_32x32x16_bf16 v[16:31], v[44:47], v[32:35], v[16:31]
	v_add_u32_e32 v32, 4, v57
	v_bitop3_b32 v32, v32, v227, 15 bitop3:0x78
	v_lshl_add_u32 v32, v32, 4, v56
	ds_read_b128 v[32:35], v32
	v_add_u32_e32 v57, s0, v55
	s_mov_b32 s0, 0xe000
	v_add_co_u32_e32 v58, vcc, s0, v52
	v_mfma_f32_32x32x16_bf16 v[0:15], v[44:47], v[86:89], v[0:15]
	s_nop 0
	v_addc_co_u32_e32 v59, vcc, 0, v53, vcc
	s_mov_b32 s0, 0xd000
	v_add_co_u32_e32 v60, vcc, s0, v52
	s_mov_b32 s0, 0xf000
	s_nop 0
	v_addc_co_u32_e32 v61, vcc, 0, v53, vcc
	s_waitcnt vmcnt(8)
	v_mfma_f32_32x32x16_bf16 v[16:31], v[44:47], v[90:93], v[16:31]
	v_bitop3_b32 v44, v57, v227, 15 bitop3:0x78
	v_lshl_add_u32 v44, v44, 4, v56
	ds_read_b128 v[44:47], v44
	v_add_co_u32_e32 v52, vcc, s0, v52
	v_readlane_b32 s0, v248, 32
	s_nop 0
	v_addc_co_u32_e32 v53, vcc, 0, v53, vcc
	s_waitcnt lgkmcnt(1)
	v_mfma_f32_32x32x16_bf16 v[0:15], v[32:35], v[94:97], v[0:15]
	s_waitcnt vmcnt(6)
	v_mfma_f32_32x32x16_bf16 v[16:31], v[32:35], v[98:101], v[16:31]
	v_mfma_f32_32x32x16_bf16 v[0:15], v[32:35], v[48:51], v[0:15]
	v_add_u32_e32 v48, 2, v57
	v_bitop3_b32 v48, v48, v227, 15 bitop3:0x78
	v_lshl_add_u32 v48, v48, 4, v56
	ds_read_b128 v[48:51], v48
	s_waitcnt vmcnt(5)
	v_mfma_f32_32x32x16_bf16 v[16:31], v[32:35], v[102:105], v[16:31]
	global_load_dwordx4 v[32:35], v[122:123], off
	s_waitcnt vmcnt(5)
	v_mfma_f32_32x32x16_bf16 v[0:15], v[36:39], v[106:109], v[0:15]
	s_waitcnt vmcnt(3)
	v_mfma_f32_32x32x16_bf16 v[16:31], v[36:39], v[114:117], v[16:31]
	v_mfma_f32_32x32x16_bf16 v[0:15], v[36:39], v[110:113], v[0:15]
	s_waitcnt vmcnt(2)
	v_mfma_f32_32x32x16_bf16 v[16:31], v[36:39], v[118:121], v[16:31]
	global_load_dwordx4 v[36:39], v[122:123], off offset:1024
	s_waitcnt vmcnt(1) lgkmcnt(1)
	v_mfma_f32_32x32x16_bf16 v[0:15], v[44:47], v[32:35], v[0:15]
	global_load_dwordx4 v[32:35], v[122:123], off offset:3072
	s_waitcnt vmcnt(1)
; __device__ __forceinline__ int crow(int r, int hi) { return (r & 3) + 8 * (r >> 2) + 4 * hi; }
; #define P5_LDB(dst, q0) do { _Pragma("unroll") for (int q_ = 0; q_ < 4; ++q_) _Pragma("unroll") for (int c_ = 0; c_ < 4; ++c_) dst[q_][c_] = *(const GAS bf16x8*)(wbase + (size_t)((q0) + q_) * 4096 + c_ * 1024); } while (0)
; template <int l>
; __device__ __forceinline__ void layer_phases(Frame& F, const XcdBarrier& bar, const int lo, const int hi) {
;     ...
;                 P5_MMA(bqa, 0); asm volatile("" ::: "memory"); P5_LDB(bqa, 8);
;                 P5_MMA(bqb, 4); asm volatile("" ::: "memory"); P5_LDB(bqb, 12);
;                 P5_MMA(bqa, 8); P5_MMA(bqb, 12);
;     ...
;                 __syncthreads();
; #pragma unroll
;                 for (int r = 0; r < 16; ++r) { const int row = att::crow(r, hi5); part[(F.wave * 32 + row) * 64 + r32] = acc0[r]; part[(F.wave * 32 + row) * 64 + 32 + r32] = acc1[r]; }
;                 __syncthreads();
;                 float score[4]; unsigned key[4]; int ek[4][6]; float sk[4][6];
; #pragma unroll
;                 for (int rr = 0; rr < 4; ++rr) { const int rloc = 4 * F.wave + rr; float lg = 0.f;
; #pragma unroll
;                     for (int w = 0; w < 8; ++w) lg += part[(w * 32 + rloc) * 64 + F.lane];
	v_mfma_f32_32x32x16_bf16 v[0:15], v[44:47], v[36:39], v[0:15]
	global_load_dwordx4 v[36:39], v[58:59], off offset:-4096
	v_mfma_f32_32x32x16_bf16 v[16:31], v[44:47], v[40:43], v[16:31]
	s_waitcnt vmcnt(1)
	v_mfma_f32_32x32x16_bf16 v[16:31], v[44:47], v[32:35], v[16:31]
	global_load_dwordx4 v[32:35], v[60:61], off offset:2048
	global_load_dwordx4 v[40:43], v[58:59], off
	s_waitcnt vmcnt(2) lgkmcnt(0)
	v_mfma_f32_32x32x16_bf16 v[0:15], v[48:51], v[36:39], v[0:15]
	global_load_dwordx4 v[36:39], v[60:61], off offset:1024
	s_waitcnt vmcnt(2)
	v_mfma_f32_32x32x16_bf16 v[16:31], v[48:51], v[32:35], v[16:31]
	global_load_dwordx4 v[32:35], v[60:61], off offset:3072
	s_waitcnt vmcnt(0)
	v_mfma_f32_32x32x16_bf16 v[16:31], v[48:51], v[32:35], v[16:31]
	global_load_dwordx4 v[32:35], v[58:59], off offset:2048
	v_mfma_f32_32x32x16_bf16 v[0:15], v[48:51], v[36:39], v[0:15]
	v_add_u32_e32 v36, 4, v57
	v_bitop3_b32 v36, v36, v227, 15 bitop3:0x78
	v_lshl_add_u32 v44, v36, 4, v56
	ds_read_b128 v[44:47], v44
	v_add_u32_e32 v48, 6, v57
	v_bitop3_b32 v48, v48, v227, 15 bitop3:0x78
	v_lshl_add_u32 v48, v48, 4, v56
	ds_read_b128 v[48:51], v48
	s_waitcnt lgkmcnt(1)
	v_mfma_f32_32x32x16_bf16 v[0:15], v[44:47], v[40:43], v[0:15]
	global_load_dwordx4 v[40:43], v[58:59], off offset:1024
	global_load_dwordx4 v[36:39], v[52:53], off
	s_waitcnt vmcnt(2)
	v_mfma_f32_32x32x16_bf16 v[16:31], v[44:47], v[32:35], v[16:31]
	global_load_dwordx4 v[32:35], v[58:59], off offset:3072
	s_waitcnt vmcnt(0)
	v_mfma_f32_32x32x16_bf16 v[16:31], v[44:47], v[32:35], v[16:31]
	global_load_dwordx4 v[32:35], v[52:53], off offset:2048
	v_mfma_f32_32x32x16_bf16 v[0:15], v[44:47], v[40:43], v[0:15]
	v_lshlrev_b32_e32 v40, 10, v55
	v_lshlrev_b32_e32 v41, 2, v54
	s_waitcnt lgkmcnt(0)
	v_mfma_f32_32x32x16_bf16 v[0:15], v[48:51], v[36:39], v[0:15]
	global_load_dwordx4 v[36:39], v[52:53], off offset:1024
	s_waitcnt vmcnt(1)
	v_mfma_f32_32x32x16_bf16 v[16:31], v[48:51], v[32:35], v[16:31]
	global_load_dwordx4 v[32:35], v[52:53], off offset:3072
	s_barrier
	s_waitcnt vmcnt(1)
	v_mfma_f32_32x32x16_bf16 v[0:15], v[48:51], v[36:39], v[0:15]
	v_add3_u32 v36, s0, v40, v41
	v_add_u32_e32 v37, 0x800, v36
	v_add_u32_e32 v38, 0x1000, v36
	v_add_u32_e32 v39, 0x1800, v36
	s_waitcnt vmcnt(0)
	v_mfma_f32_32x32x16_bf16 v[16:31], v[48:51], v[32:35], v[16:31]
	s_nop 11
	ds_write2_b32 v36, v0, v16 offset1:32
	ds_write2_b32 v36, v1, v17 offset0:64 offset1:96
	ds_write2_b32 v36, v2, v18 offset0:128 offset1:160
	ds_write2_b32 v36, v3, v19 offset0:192 offset1:224
	ds_write2_b32 v37, v4, v20 offset1:32
	ds_write2_b32 v37, v5, v21 offset0:64 offset1:96
	ds_write2_b32 v37, v6, v22 offset0:128 offset1:160
	ds_write2_b32 v37, v7, v23 offset0:192 offset1:224
	ds_write2_b32 v38, v8, v24 offset1:32
	ds_write2_b32 v38, v9, v25 offset0:64 offset1:96
	ds_write2_b32 v38, v10, v26 offset0:128 offset1:160
	ds_write2_b32 v38, v11, v27 offset0:192 offset1:224
	ds_write2_b32 v39, v12, v28 offset1:32
	ds_write2_b32 v39, v13, v29 offset0:64 offset1:96
	ds_write2_b32 v39, v14, v30 offset0:128 offset1:160
	ds_write2_b32 v39, v15, v31 offset0:192 offset1:224
	s_waitcnt lgkmcnt(0)
	s_barrier
	ds_read2st64_b32 v[0:1], v225 offset1:1
	ds_read2st64_b32 v[2:3], v225 offset0:32 offset1:33
	ds_read2st64_b32 v[4:5], v225 offset0:34 offset1:35
	ds_read2st64_b32 v[6:7], v225 offset0:2 offset1:3
	ds_read2st64_b32 v[8:9], v225 offset0:64 offset1:65
	ds_read2st64_b32 v[10:11], v225 offset0:96 offset1:97
	ds_read2st64_b32 v[12:13], v225 offset0:98 offset1:99
	ds_read2st64_b32 v[14:15], v225 offset0:66 offset1:67
	ds_read2st64_b32 v[16:17], v225 offset0:128 offset1:129
	ds_read2st64_b32 v[18:19], v225 offset0:160 offset1:161
	ds_read2st64_b32 v[20:21], v225 offset0:162 offset1:163
	ds_read2st64_b32 v[22:23], v225 offset0:130 offset1:131
	ds_read2st64_b32 v[24:25], v225 offset0:192 offset1:193
	ds_read2st64_b32 v[26:27], v225 offset0:224 offset1:225
	ds_read2st64_b32 v[28:29], v225 offset0:226 offset1:227
	ds_read2st64_b32 v[30:31], v225 offset0:194 offset1:195
	s_waitcnt lgkmcnt(14)
	v_add_f32_e32 v0, 0, v0
	v_add_f32_e32 v1, 0, v1
	v_add_f32_e32 v0, v0, v2
	v_add_f32_e32 v1, v1, v3
	s_waitcnt lgkmcnt(12)
	v_add_f32_e32 v6, 0, v6
	v_add_f32_e32 v7, 0, v7
	s_waitcnt lgkmcnt(11)
	v_add_f32_e32 v0, v0, v8
	v_add_f32_e32 v1, v1, v9
	v_add_f32_e32 v2, v6, v4
	v_add_f32_e32 v3, v7, v5
	s_waitcnt lgkmcnt(10)
	v_add_f32_e32 v0, v0, v10
	v_add_f32_e32 v1, v1, v11
	s_waitcnt lgkmcnt(8)
	v_add_f32_e32 v2, v2, v14
	v_add_f32_e32 v3, v3, v15
	s_waitcnt lgkmcnt(7)
	v_add_f32_e32 v0, v0, v16
	v_add_f32_e32 v1, v1, v17
	v_add_f32_e32 v2, v2, v12
	v_add_f32_e32 v3, v3, v13
	s_waitcnt lgkmcnt(6)
	v_add_f32_e32 v0, v0, v18
	v_add_f32_e32 v1, v1, v19
	s_waitcnt lgkmcnt(4)
	v_add_f32_e32 v2, v2, v22
	v_add_f32_e32 v3, v3, v23
	s_waitcnt lgkmcnt(3)
	v_add_f32_e32 v0, v0, v24
	v_add_f32_e32 v1, v1, v25
	v_add_f32_e32 v2, v2, v20
	v_add_f32_e32 v3, v3, v21
	s_waitcnt lgkmcnt(2)
	v_add_f32_e32 v0, v0, v26
	v_add_f32_e32 v1, v1, v27
	s_waitcnt lgkmcnt(0)
; template <int l>
; __device__ __forceinline__ void layer_phases(Frame& F, const XcdBarrier& bar, const int lo, const int hi) {
;     ...
;                 for (int rr = 0; rr < 4; ++rr) { const int rloc = 4 * F.wave + rr; float lg = 0.f;
; #pragma unroll
;                     for (int w = 0; w < 8; ++w) lg += part[(w * 32 + rloc) * 64 + F.lane];
;                     score[rr] = 1.0f / (1.0f + __expf(-lg)); const float sel = score[rr] + rb;
;                     unsigned ob = __float_as_uint(sel); ob = (ob & 0x80000000u) ? ~ob : (ob | 0x80000000u);
;                     key[rr] = (ob & ~63u) | (unsigned)(63 - F.lane); }
; #pragma unroll
;                 for (int k = 0; k < 6; ++k) {
;                     unsigned mx[4];
; #pragma unroll
;                     for (int rr = 0; rr < 4; ++rr) mx[rr] = key[rr];
; #pragma unroll
;                     for (int o = 1; o < 64; o <<= 1) {
; #pragma unroll
;                         for (int rr = 0; rr < 4; ++rr) { const unsigned t = __shfl_xor(mx[rr], o); mx[rr] = t > mx[rr] ? t : mx[rr]; } }
; #pragma unroll
;                     for (int rr = 0; rr < 4; ++rr) { const int win = 63 - (int)(__builtin_amdgcn_readfirstlane((int)mx[rr]) & 63);
;                         ek[rr][k] = win; sk[rr][k] = __uint_as_float((unsigned)__builtin_amdgcn_readlane((int)__float_as_uint(score[rr]), win)); if (F.lane == win) key[rr] = 0u; }
	v_add_f32_e32 v2, v2, v30
	v_add_f32_e32 v3, v3, v31
	v_mul_f32_e32 v0, 0xbfb8aa3b, v0
	v_mul_f32_e32 v4, 0xbfb8aa3b, v1
	v_add_f32_e32 v2, v2, v28
	v_add_f32_e32 v3, v3, v29
	v_exp_f32_e32 v1, v0
	v_exp_f32_e32 v0, v4
	v_mul_f32_e32 v2, 0xbfb8aa3b, v2
	v_mul_f32_e32 v5, 0xbfb8aa3b, v3
	v_exp_f32_e32 v3, v2
	v_exp_f32_e32 v2, v5
	v_pk_add_f32 v[0:1], v[0:1], 1.0 op_sel_hi:[1,0]
	v_pk_add_f32 v[2:3], v[2:3], 1.0 op_sel_hi:[1,0]
	v_div_scale_f32 v4, s[0:1], v1, v1, 1.0
	v_div_scale_f32 v6, s[0:1], v0, v0, 1.0
	v_rcp_f32_e32 v12, v4
	v_div_scale_f32 v8, s[0:1], v3, v3, 1.0
	v_rcp_f32_e32 v13, v6
	v_div_scale_f32 v10, s[0:1], v2, v2, 1.0
	v_rcp_f32_e32 v14, v8
	v_rcp_f32_e32 v15, v10
	v_fma_f32 v16, -v4, v12, 1.0
	v_div_scale_f32 v5, vcc, 1.0, v1, 1.0
	v_fma_f32 v17, -v6, v13, 1.0
	v_fmac_f32_e32 v12, v16, v12
	v_div_scale_f32 v7, s[14:15], 1.0, v0, 1.0
	v_fma_f32 v18, -v8, v14, 1.0
	v_fmac_f32_e32 v13, v17, v13
	v_mul_f32_e32 v16, v5, v12
	v_div_scale_f32 v9, s[16:17], 1.0, v3, 1.0
	v_fma_f32 v19, -v10, v15, 1.0
	v_fmac_f32_e32 v14, v18, v14
	v_mul_f32_e32 v17, v7, v13
	v_fma_f32 v20, -v4, v16, v5
	v_div_scale_f32 v11, s[18:19], 1.0, v2, 1.0
	v_fmac_f32_e32 v15, v19, v15
	v_mul_f32_e32 v18, v9, v14
	v_fma_f32 v21, -v6, v17, v7
	v_fmac_f32_e32 v16, v20, v12
	v_mul_f32_e32 v19, v11, v15
	v_fma_f32 v22, -v8, v18, v9
	v_fmac_f32_e32 v17, v21, v13
	v_fma_f32 v4, -v4, v16, v5
	v_fma_f32 v23, -v10, v19, v11
	v_fmac_f32_e32 v18, v22, v14
	v_fma_f32 v5, -v6, v17, v7
	v_div_fmas_f32 v4, v4, v12, v16
	s_mov_b64 vcc, s[14:15]
	v_fmac_f32_e32 v19, v23, v15
	v_fma_f32 v6, -v8, v18, v9
	v_div_fixup_f32 v1, v4, v1, 1.0
	v_div_fmas_f32 v4, v5, v13, v17
	s_mov_b64 vcc, s[16:17]
	v_fma_f32 v7, -v10, v19, v11
	v_div_fixup_f32 v0, v4, v0, 1.0
	v_div_fmas_f32 v6, v6, v14, v18
	s_mov_b64 vcc, s[18:19]
	v_pk_add_f32 v[4:5], v[74:75], v[0:1]
	v_div_fixup_f32 v3, v6, v3, 1.0
	v_div_fmas_f32 v6, v7, v15, v19
	v_not_b32_e32 v7, v5
	v_or_b32_e32 v8, 0x80000000, v5
	v_div_fixup_f32 v2, v6, v2, 1.0
	v_cmp_gt_i32_e32 vcc, 0, v5
	v_not_b32_e32 v9, v4
	v_or_b32_e32 v10, 0x80000000, v4
	v_cndmask_b32_e32 v6, v8, v7, vcc
	v_cmp_gt_i32_e32 vcc, 0, v4
	v_pk_add_f32 v[4:5], v[74:75], v[2:3]
	v_and_or_b32 v6, v6, s93, v222
	v_cndmask_b32_e32 v7, v10, v9, vcc
	v_not_b32_e32 v8, v5
	v_or_b32_e32 v9, 0x80000000, v5
	v_cmp_gt_i32_e32 vcc, 0, v5
	v_and_or_b32 v7, v7, s93, v222
	v_not_b32_e32 v10, v4
	v_or_b32_e32 v11, 0x80000000, v4
	v_cndmask_b32_e32 v5, v9, v8, vcc
	v_cmp_gt_i32_e32 vcc, 0, v4
	ds_bpermute_b32 v8, v73, v6
	ds_bpermute_b32 v9, v73, v7
	v_cndmask_b32_e32 v4, v11, v10, vcc
	v_and_or_b32 v5, v5, s93, v222
	v_and_or_b32 v4, v4, s93, v222
	ds_bpermute_b32 v10, v73, v5
	ds_bpermute_b32 v11, v73, v4
	s_waitcnt lgkmcnt(3)
	v_max_u32_e32 v8, v8, v6
	s_waitcnt lgkmcnt(2)
	v_max_u32_e32 v9, v9, v7
	ds_bpermute_b32 v12, v217, v8
	ds_bpermute_b32 v13, v217, v9
	s_waitcnt lgkmcnt(3)
	v_max_u32_e32 v10, v10, v5
	s_waitcnt lgkmcnt(2)
	v_max_u32_e32 v11, v11, v4
	ds_bpermute_b32 v14, v217, v10
	ds_bpermute_b32 v15, v217, v11
	s_waitcnt lgkmcnt(3)
	v_max_u32_e32 v8, v12, v8
	s_waitcnt lgkmcnt(2)
	v_max_u32_e32 v9, v13, v9
	ds_bpermute_b32 v12, v218, v8
	ds_bpermute_b32 v13, v218, v9
	s_waitcnt lgkmcnt(3)
	v_max_u32_e32 v10, v14, v10
	s_waitcnt lgkmcnt(2)
	v_max_u32_e32 v11, v15, v11
	ds_bpermute_b32 v14, v218, v10
	ds_bpermute_b32 v15, v218, v11
	s_waitcnt lgkmcnt(3)
	v_max_u32_e32 v8, v12, v8
	s_waitcnt lgkmcnt(2)
	v_max_u32_e32 v9, v13, v9
	ds_bpermute_b32 v12, v219, v8
	ds_bpermute_b32 v13, v219, v9
	s_waitcnt lgkmcnt(3)
	v_max_u32_e32 v10, v14, v10
	s_waitcnt lgkmcnt(2)
	v_max_u32_e32 v11, v15, v11
	ds_bpermute_b32 v14, v219, v10
	ds_bpermute_b32 v15, v219, v11
	s_waitcnt lgkmcnt(3)
	v_max_u32_e32 v8, v12, v8
	s_waitcnt lgkmcnt(2)
	v_max_u32_e32 v9, v13, v9
	ds_bpermute_b32 v12, v220, v8
	ds_bpermute_b32 v13, v220, v9
	s_waitcnt lgkmcnt(3)
	v_max_u32_e32 v10, v14, v10
	s_waitcnt lgkmcnt(2)
	v_max_u32_e32 v11, v15, v11
	ds_bpermute_b32 v14, v220, v10
	ds_bpermute_b32 v15, v220, v11
	s_waitcnt lgkmcnt(3)
	v_max_u32_e32 v8, v12, v8
	s_waitcnt lgkmcnt(2)
	v_max_u32_e32 v9, v13, v9
	ds_bpermute_b32 v12, v221, v8
	ds_bpermute_b32 v13, v221, v9
	s_waitcnt lgkmcnt(3)
	v_max_u32_e32 v10, v14, v10
	s_waitcnt lgkmcnt(2)
	v_max_u32_e32 v11, v15, v11
	ds_bpermute_b32 v14, v221, v10
	ds_bpermute_b32 v15, v221, v11
	s_waitcnt lgkmcnt(3)
	v_max_u32_e32 v8, v12, v8
	s_waitcnt lgkmcnt(2)
	v_max_u32_e32 v9, v13, v9
	v_readfirstlane_b32 s0, v8
	v_readfirstlane_b32 s1, v9
	s_waitcnt lgkmcnt(1)
	v_max_u32_e32 v8, v14, v10
	s_andn2_b32 s16, 63, s0
	s_waitcnt lgkmcnt(0)
	v_max_u32_e32 v9, v15, v11
	s_andn2_b32 s82, 63, s1
	v_cmp_ne_u32_e32 vcc, s16, v72
	v_readfirstlane_b32 s0, v8
	v_readfirstlane_b32 s1, v9
	v_cndmask_b32_e32 v6, 0, v6, vcc
	v_cmp_ne_u32_e32 vcc, s82, v72
	s_andn2_b32 s45, 63, s0
	s_andn2_b32 s19, 63, s1
	v_cndmask_b32_e32 v7, 0, v7, vcc
	ds_bpermute_b32 v8, v73, v6
	v_cmp_ne_u32_e32 vcc, s45, v72
	ds_bpermute_b32 v9, v73, v7
	v_readlane_b32 s95, v1, s16
	v_cndmask_b32_e32 v5, 0, v5, vcc
	v_cmp_ne_u32_e32 vcc, s19, v72
	ds_bpermute_b32 v10, v73, v5
	s_waitcnt lgkmcnt(2)
	v_max_u32_e32 v8, v8, v6
	v_cndmask_b32_e32 v4, 0, v4, vcc
	ds_bpermute_b32 v11, v73, v4
	s_waitcnt lgkmcnt(2)
	v_max_u32_e32 v9, v9, v7
	ds_bpermute_b32 v12, v217, v8
	ds_bpermute_b32 v13, v217, v9
	s_waitcnt lgkmcnt(3)
	v_max_u32_e32 v10, v10, v5
	s_waitcnt lgkmcnt(2)
	v_max_u32_e32 v11, v11, v4
	ds_bpermute_b32 v14, v217, v10
	ds_bpermute_b32 v15, v217, v11
	s_waitcnt lgkmcnt(3)
	v_max_u32_e32 v8, v12, v8
	s_waitcnt lgkmcnt(2)
	v_max_u32_e32 v9, v13, v9
	ds_bpermute_b32 v12, v218, v8
	ds_bpermute_b32 v13, v218, v9
	s_waitcnt lgkmcnt(3)
; template <int l>
; __device__ __forceinline__ void layer_phases(Frame& F, const XcdBarrier& bar, const int lo, const int hi) {
;     ...
; #pragma unroll
;                 for (int k = 0; k < 6; ++k) {
;                     unsigned mx[4];
; #pragma unroll
;                     for (int rr = 0; rr < 4; ++rr) mx[rr] = key[rr];
; #pragma unroll
;                     for (int o = 1; o < 64; o <<= 1) {
; #pragma unroll
;                         for (int rr = 0; rr < 4; ++rr) { const unsigned t = __shfl_xor(mx[rr], o); mx[rr] = t > mx[rr] ? t : mx[rr]; } }
; #pragma unroll
;                     for (int rr = 0; rr < 4; ++rr) { const int win = 63 - (int)(__builtin_amdgcn_readfirstlane((int)mx[rr]) & 63);
;                         ek[rr][k] = win; sk[rr][k] = __uint_as_float((unsigned)__builtin_amdgcn_readlane((int)__float_as_uint(score[rr]), win)); if (F.lane == win) key[rr] = 0u; }
	v_max_u32_e32 v10, v14, v10
	s_waitcnt lgkmcnt(2)
	v_max_u32_e32 v11, v15, v11
	ds_bpermute_b32 v14, v218, v10
	ds_bpermute_b32 v15, v218, v11
	s_waitcnt lgkmcnt(3)
	v_max_u32_e32 v8, v12, v8
	s_waitcnt lgkmcnt(2)
	v_max_u32_e32 v9, v13, v9
	ds_bpermute_b32 v12, v219, v8
	ds_bpermute_b32 v13, v219, v9
	s_waitcnt lgkmcnt(3)
	v_max_u32_e32 v10, v14, v10
	s_waitcnt lgkmcnt(2)
	v_max_u32_e32 v11, v15, v11
	ds_bpermute_b32 v14, v219, v10
	ds_bpermute_b32 v15, v219, v11
	s_waitcnt lgkmcnt(3)
	v_max_u32_e32 v8, v12, v8
	s_waitcnt lgkmcnt(2)
	v_max_u32_e32 v9, v13, v9
	ds_bpermute_b32 v12, v220, v8
	ds_bpermute_b32 v13, v220, v9
	s_waitcnt lgkmcnt(3)
	v_max_u32_e32 v10, v14, v10
	s_waitcnt lgkmcnt(2)
	v_max_u32_e32 v11, v15, v11
	ds_bpermute_b32 v14, v220, v10
	ds_bpermute_b32 v15, v220, v11
	s_waitcnt lgkmcnt(3)
	v_max_u32_e32 v8, v12, v8
	s_waitcnt lgkmcnt(2)
	v_max_u32_e32 v9, v13, v9
	ds_bpermute_b32 v12, v221, v8
	ds_bpermute_b32 v13, v221, v9
	s_waitcnt lgkmcnt(3)
	v_max_u32_e32 v10, v14, v10
	s_waitcnt lgkmcnt(2)
	v_max_u32_e32 v11, v15, v11
	ds_bpermute_b32 v14, v221, v10
	ds_bpermute_b32 v15, v221, v11
	s_waitcnt lgkmcnt(3)
	v_max_u32_e32 v8, v12, v8
	s_waitcnt lgkmcnt(2)
	v_max_u32_e32 v9, v13, v9
	v_readfirstlane_b32 s0, v8
	v_readfirstlane_b32 s1, v9
	s_waitcnt lgkmcnt(1)
	v_max_u32_e32 v8, v14, v10
	s_andn2_b32 s17, 63, s0
	s_waitcnt lgkmcnt(0)
	v_max_u32_e32 v9, v15, v11
	s_andn2_b32 s60, 63, s1
	v_cmp_ne_u32_e32 vcc, s17, v72
	v_readfirstlane_b32 s0, v8
	v_readfirstlane_b32 s1, v9
	v_cndmask_b32_e32 v6, 0, v6, vcc
	v_cmp_ne_u32_e32 vcc, s60, v72
	s_andn2_b32 s97, 63, s0
	s_andn2_b32 s49, 63, s1
	v_cndmask_b32_e32 v7, 0, v7, vcc
	ds_bpermute_b32 v8, v73, v6
	v_cmp_ne_u32_e32 vcc, s97, v72
	ds_bpermute_b32 v9, v73, v7
	v_readlane_b32 s47, v0, s82
	v_cndmask_b32_e32 v5, 0, v5, vcc
	v_cmp_ne_u32_e32 vcc, s49, v72
	ds_bpermute_b32 v10, v73, v5
	s_waitcnt lgkmcnt(2)
	v_max_u32_e32 v8, v8, v6
	v_cndmask_b32_e32 v4, 0, v4, vcc
	ds_bpermute_b32 v11, v73, v4
	s_waitcnt lgkmcnt(2)
	v_max_u32_e32 v9, v9, v7
	ds_bpermute_b32 v12, v217, v8
	ds_bpermute_b32 v13, v217, v9
	s_waitcnt lgkmcnt(3)
	v_max_u32_e32 v10, v10, v5
	s_waitcnt lgkmcnt(2)
	v_max_u32_e32 v11, v11, v4
	ds_bpermute_b32 v14, v217, v10
	ds_bpermute_b32 v15, v217, v11
	s_waitcnt lgkmcnt(3)
	v_max_u32_e32 v8, v12, v8
	s_waitcnt lgkmcnt(2)
	v_max_u32_e32 v9, v13, v9
	ds_bpermute_b32 v12, v218, v8
	ds_bpermute_b32 v13, v218, v9
	s_waitcnt lgkmcnt(3)
	v_max_u32_e32 v10, v14, v10
	s_waitcnt lgkmcnt(2)
	v_max_u32_e32 v11, v15, v11
	ds_bpermute_b32 v14, v218, v10
	ds_bpermute_b32 v15, v218, v11
	s_waitcnt lgkmcnt(3)
	v_max_u32_e32 v8, v12, v8
	s_waitcnt lgkmcnt(2)
	v_max_u32_e32 v9, v13, v9
	ds_bpermute_b32 v12, v219, v8
	ds_bpermute_b32 v13, v219, v9
	s_waitcnt lgkmcnt(3)
	v_max_u32_e32 v10, v14, v10
	s_waitcnt lgkmcnt(2)
	v_max_u32_e32 v11, v15, v11
	ds_bpermute_b32 v14, v219, v10
	ds_bpermute_b32 v15, v219, v11
	s_waitcnt lgkmcnt(3)
	v_max_u32_e32 v8, v12, v8
	s_waitcnt lgkmcnt(2)
	v_max_u32_e32 v9, v13, v9
	ds_bpermute_b32 v12, v220, v8
	ds_bpermute_b32 v13, v220, v9
	s_waitcnt lgkmcnt(3)
	v_max_u32_e32 v10, v14, v10
	s_waitcnt lgkmcnt(2)
	v_max_u32_e32 v11, v15, v11
	ds_bpermute_b32 v14, v220, v10
	ds_bpermute_b32 v15, v220, v11
	s_waitcnt lgkmcnt(3)
	v_max_u32_e32 v8, v12, v8
	s_waitcnt lgkmcnt(2)
	v_max_u32_e32 v9, v13, v9
	ds_bpermute_b32 v12, v221, v8
	ds_bpermute_b32 v13, v221, v9
	s_waitcnt lgkmcnt(3)
	v_max_u32_e32 v10, v14, v10
	s_waitcnt lgkmcnt(2)
	v_max_u32_e32 v11, v15, v11
	ds_bpermute_b32 v14, v221, v10
	ds_bpermute_b32 v15, v221, v11
	s_waitcnt lgkmcnt(3)
	v_max_u32_e32 v8, v12, v8
	s_waitcnt lgkmcnt(2)
	v_max_u32_e32 v9, v13, v9
	v_readfirstlane_b32 s0, v8
	v_readfirstlane_b32 s1, v9
	s_waitcnt lgkmcnt(1)
	v_max_u32_e32 v8, v14, v10
	s_andn2_b32 s80, 63, s0
	s_waitcnt lgkmcnt(0)
	v_max_u32_e32 v9, v15, v11
	s_andn2_b32 s33, 63, s1
	v_cmp_ne_u32_e32 vcc, s80, v72
	v_readfirstlane_b32 s0, v8
	v_readfirstlane_b32 s1, v9
	v_cndmask_b32_e32 v6, 0, v6, vcc
	v_cmp_ne_u32_e32 vcc, s33, v72
	s_andn2_b32 s61, 63, s0
	s_andn2_b32 s96, 63, s1
	v_cndmask_b32_e32 v7, 0, v7, vcc
	ds_bpermute_b32 v8, v73, v6
	v_cmp_ne_u32_e32 vcc, s61, v72
	ds_bpermute_b32 v9, v73, v7
	v_readlane_b32 s43, v3, s45
	v_cndmask_b32_e32 v5, 0, v5, vcc
	v_cmp_ne_u32_e32 vcc, s96, v72
	ds_bpermute_b32 v10, v73, v5
	s_waitcnt lgkmcnt(2)
	v_max_u32_e32 v8, v8, v6
	v_cndmask_b32_e32 v4, 0, v4, vcc
	ds_bpermute_b32 v11, v73, v4
	s_waitcnt lgkmcnt(2)
	v_max_u32_e32 v9, v9, v7
	ds_bpermute_b32 v12, v217, v8
	ds_bpermute_b32 v13, v217, v9
	s_waitcnt lgkmcnt(3)
	v_max_u32_e32 v10, v10, v5
	s_waitcnt lgkmcnt(2)
	v_max_u32_e32 v11, v11, v4
	ds_bpermute_b32 v14, v217, v10
	ds_bpermute_b32 v15, v217, v11
	s_waitcnt lgkmcnt(3)
	v_max_u32_e32 v8, v12, v8
	s_waitcnt lgkmcnt(2)
	v_max_u32_e32 v9, v13, v9
	ds_bpermute_b32 v12, v218, v8
	ds_bpermute_b32 v13, v218, v9
	s_waitcnt lgkmcnt(3)
	v_max_u32_e32 v10, v14, v10
	s_waitcnt lgkmcnt(2)
	v_max_u32_e32 v11, v15, v11
	ds_bpermute_b32 v14, v218, v10
	ds_bpermute_b32 v15, v218, v11
	s_waitcnt lgkmcnt(3)
	v_max_u32_e32 v8, v12, v8
	s_waitcnt lgkmcnt(2)
	v_max_u32_e32 v9, v13, v9
	ds_bpermute_b32 v12, v219, v8
	ds_bpermute_b32 v13, v219, v9
	s_waitcnt lgkmcnt(3)
	v_max_u32_e32 v10, v14, v10
	s_waitcnt lgkmcnt(2)
	v_max_u32_e32 v11, v15, v11
	ds_bpermute_b32 v14, v219, v10
	ds_bpermute_b32 v15, v219, v11
	s_waitcnt lgkmcnt(3)
	v_max_u32_e32 v8, v12, v8
	s_waitcnt lgkmcnt(2)
	v_max_u32_e32 v9, v13, v9
	ds_bpermute_b32 v12, v220, v8
	ds_bpermute_b32 v13, v220, v9
	s_waitcnt lgkmcnt(3)
	v_max_u32_e32 v10, v14, v10
	s_waitcnt lgkmcnt(2)
; template <int l>
; __device__ __forceinline__ void layer_phases(Frame& F, const XcdBarrier& bar, const int lo, const int hi) {
;     ...
; #pragma unroll
;                 for (int k = 0; k < 6; ++k) {
;                     unsigned mx[4];
; #pragma unroll
;                     for (int rr = 0; rr < 4; ++rr) mx[rr] = key[rr];
; #pragma unroll
;                     for (int o = 1; o < 64; o <<= 1) {
; #pragma unroll
;                         for (int rr = 0; rr < 4; ++rr) { const unsigned t = __shfl_xor(mx[rr], o); mx[rr] = t > mx[rr] ? t : mx[rr]; } }
; #pragma unroll
;                     for (int rr = 0; rr < 4; ++rr) { const int win = 63 - (int)(__builtin_amdgcn_readfirstlane((int)mx[rr]) & 63);
;                         ek[rr][k] = win; sk[rr][k] = __uint_as_float((unsigned)__builtin_amdgcn_readlane((int)__float_as_uint(score[rr]), win)); if (F.lane == win) key[rr] = 0u; }
;                 }
; #pragma unroll
;                 for (int rr = 0; rr < 4; ++rr) { const int m = m0 + rr;
;                     const float ssum = ((sk[rr][0] + sk[rr][1]) + (sk[rr][2] + sk[rr][3])) + (sk[rr][4] + sk[rr][5]);
;                     if (F.lane < 6 && rep == 0) { int e = ek[rr][0]; float sc = sk[rr][0];
	v_max_u32_e32 v11, v15, v11
	ds_bpermute_b32 v14, v220, v10
	ds_bpermute_b32 v15, v220, v11
	s_waitcnt lgkmcnt(3)
	v_max_u32_e32 v8, v12, v8
	s_waitcnt lgkmcnt(2)
	v_max_u32_e32 v9, v13, v9
	ds_bpermute_b32 v12, v221, v8
	ds_bpermute_b32 v13, v221, v9
	s_waitcnt lgkmcnt(3)
	v_max_u32_e32 v10, v14, v10
	s_waitcnt lgkmcnt(2)
	v_max_u32_e32 v11, v15, v11
	ds_bpermute_b32 v14, v221, v10
	ds_bpermute_b32 v15, v221, v11
	s_waitcnt lgkmcnt(3)
	v_max_u32_e32 v8, v12, v8
	s_waitcnt lgkmcnt(2)
	v_max_u32_e32 v9, v13, v9
	v_readfirstlane_b32 s0, v8
	v_readfirstlane_b32 s1, v9
	s_waitcnt lgkmcnt(1)
	v_max_u32_e32 v8, v14, v10
	s_andn2_b32 s92, 63, s0
	s_waitcnt lgkmcnt(0)
	v_max_u32_e32 v9, v15, v11
	s_andn2_b32 s77, 63, s1
	v_cmp_ne_u32_e32 vcc, s92, v72
	v_readfirstlane_b32 s0, v8
	v_readfirstlane_b32 s1, v9
	v_cndmask_b32_e32 v6, 0, v6, vcc
	v_cmp_ne_u32_e32 vcc, s77, v72
	s_andn2_b32 s79, 63, s0
	s_andn2_b32 s63, 63, s1
	v_cndmask_b32_e32 v7, 0, v7, vcc
	ds_bpermute_b32 v8, v73, v6
	v_cmp_ne_u32_e32 vcc, s79, v72
	ds_bpermute_b32 v9, v73, v7
	v_readlane_b32 s18, v2, s19
	v_cndmask_b32_e32 v5, 0, v5, vcc
	v_cmp_ne_u32_e32 vcc, s63, v72
	ds_bpermute_b32 v10, v73, v5
	s_waitcnt lgkmcnt(2)
	v_max_u32_e32 v8, v8, v6
	v_cndmask_b32_e32 v4, 0, v4, vcc
	ds_bpermute_b32 v11, v73, v4
	s_waitcnt lgkmcnt(2)
	v_max_u32_e32 v9, v9, v7
	ds_bpermute_b32 v12, v217, v8
	ds_bpermute_b32 v13, v217, v9
	s_waitcnt lgkmcnt(3)
	v_max_u32_e32 v10, v10, v5
	s_waitcnt lgkmcnt(2)
	v_max_u32_e32 v11, v11, v4
	ds_bpermute_b32 v14, v217, v10
	ds_bpermute_b32 v15, v217, v11
	s_waitcnt lgkmcnt(3)
	v_max_u32_e32 v8, v12, v8
	s_waitcnt lgkmcnt(2)
	v_max_u32_e32 v9, v13, v9
	ds_bpermute_b32 v12, v218, v8
	ds_bpermute_b32 v13, v218, v9
	s_waitcnt lgkmcnt(3)
	v_max_u32_e32 v10, v14, v10
	s_waitcnt lgkmcnt(2)
	v_max_u32_e32 v11, v15, v11
	ds_bpermute_b32 v14, v218, v10
	ds_bpermute_b32 v15, v218, v11
	s_waitcnt lgkmcnt(3)
	v_max_u32_e32 v8, v12, v8
	s_waitcnt lgkmcnt(2)
	v_max_u32_e32 v9, v13, v9
	ds_bpermute_b32 v12, v219, v8
	ds_bpermute_b32 v13, v219, v9
	s_waitcnt lgkmcnt(3)
	v_max_u32_e32 v10, v14, v10
	s_waitcnt lgkmcnt(2)
	v_max_u32_e32 v11, v15, v11
	ds_bpermute_b32 v14, v219, v10
	ds_bpermute_b32 v15, v219, v11
	s_waitcnt lgkmcnt(3)
	v_max_u32_e32 v8, v12, v8
	s_waitcnt lgkmcnt(2)
	v_max_u32_e32 v9, v13, v9
	ds_bpermute_b32 v12, v220, v8
	ds_bpermute_b32 v13, v220, v9
	s_waitcnt lgkmcnt(3)
	v_max_u32_e32 v10, v14, v10
	s_waitcnt lgkmcnt(2)
	v_max_u32_e32 v11, v15, v11
	ds_bpermute_b32 v14, v220, v10
	ds_bpermute_b32 v15, v220, v11
	s_waitcnt lgkmcnt(3)
	v_max_u32_e32 v8, v12, v8
	s_waitcnt lgkmcnt(2)
	v_max_u32_e32 v9, v13, v9
	ds_bpermute_b32 v12, v221, v8
	ds_bpermute_b32 v13, v221, v9
	s_waitcnt lgkmcnt(3)
	v_max_u32_e32 v10, v14, v10
	s_waitcnt lgkmcnt(2)
	v_max_u32_e32 v11, v15, v11
	ds_bpermute_b32 v14, v221, v10
	ds_bpermute_b32 v15, v221, v11
	s_waitcnt lgkmcnt(3)
	v_max_u32_e32 v8, v12, v8
	s_waitcnt lgkmcnt(2)
	v_max_u32_e32 v9, v13, v9
	v_readfirstlane_b32 s0, v8
	v_readfirstlane_b32 s1, v9
	s_waitcnt lgkmcnt(1)
	v_max_u32_e32 v8, v14, v10
	s_andn2_b32 s53, 63, s0
	s_waitcnt lgkmcnt(0)
	v_max_u32_e32 v9, v15, v11
	s_andn2_b32 s91, 63, s1
	v_cmp_ne_u32_e32 vcc, s53, v72
	v_readfirstlane_b32 s0, v8
	v_readfirstlane_b32 s1, v9
	v_cndmask_b32_e32 v6, 0, v6, vcc
	v_cmp_ne_u32_e32 vcc, s91, v72
	s_andn2_b32 s59, 63, s0
	s_andn2_b32 s78, 63, s1
	v_cndmask_b32_e32 v7, 0, v7, vcc
	v_cmp_ne_u32_e32 vcc, s59, v72
	ds_bpermute_b32 v8, v73, v6
	ds_bpermute_b32 v9, v73, v7
	v_cndmask_b32_e32 v5, 0, v5, vcc
	v_cmp_ne_u32_e32 vcc, s78, v72
	ds_bpermute_b32 v10, v73, v5
	s_waitcnt lgkmcnt(2)
	v_max_u32_e32 v6, v8, v6
	v_cndmask_b32_e32 v4, 0, v4, vcc
	ds_bpermute_b32 v11, v73, v4
	s_waitcnt lgkmcnt(2)
	v_max_u32_e32 v7, v9, v7
	ds_bpermute_b32 v8, v217, v6
	ds_bpermute_b32 v9, v217, v7
	s_waitcnt lgkmcnt(3)
	v_max_u32_e32 v5, v10, v5
	s_waitcnt lgkmcnt(2)
	v_max_u32_e32 v4, v11, v4
	ds_bpermute_b32 v10, v217, v5
	ds_bpermute_b32 v11, v217, v4
	s_waitcnt lgkmcnt(3)
	v_max_u32_e32 v6, v8, v6
	s_waitcnt lgkmcnt(2)
	v_max_u32_e32 v7, v9, v7
	ds_bpermute_b32 v8, v218, v6
	ds_bpermute_b32 v9, v218, v7
	s_waitcnt lgkmcnt(3)
	v_max_u32_e32 v5, v10, v5
	s_waitcnt lgkmcnt(2)
	v_max_u32_e32 v4, v11, v4
	ds_bpermute_b32 v10, v218, v5
	ds_bpermute_b32 v11, v218, v4
	s_waitcnt lgkmcnt(3)
	v_max_u32_e32 v6, v8, v6
	s_waitcnt lgkmcnt(2)
	v_max_u32_e32 v7, v9, v7
	ds_bpermute_b32 v8, v219, v6
	ds_bpermute_b32 v9, v219, v7
	s_waitcnt lgkmcnt(3)
	v_max_u32_e32 v5, v10, v5
	s_waitcnt lgkmcnt(2)
	v_max_u32_e32 v4, v11, v4
	ds_bpermute_b32 v10, v219, v5
	ds_bpermute_b32 v11, v219, v4
	s_waitcnt lgkmcnt(3)
	v_max_u32_e32 v6, v8, v6
	s_waitcnt lgkmcnt(2)
	v_max_u32_e32 v7, v9, v7
	ds_bpermute_b32 v8, v220, v6
	ds_bpermute_b32 v9, v220, v7
	s_waitcnt lgkmcnt(3)
	v_max_u32_e32 v5, v10, v5
	s_waitcnt lgkmcnt(2)
	v_max_u32_e32 v4, v11, v4
	ds_bpermute_b32 v10, v220, v5
	ds_bpermute_b32 v11, v220, v4
	s_waitcnt lgkmcnt(3)
	v_max_u32_e32 v6, v8, v6
	s_waitcnt lgkmcnt(2)
	v_max_u32_e32 v7, v9, v7
	ds_bpermute_b32 v8, v221, v6
	ds_bpermute_b32 v9, v221, v7
	s_waitcnt lgkmcnt(3)
	v_max_u32_e32 v5, v10, v5
	s_waitcnt lgkmcnt(2)
	v_max_u32_e32 v4, v11, v4
	ds_bpermute_b32 v10, v221, v5
	ds_bpermute_b32 v11, v221, v4
	s_waitcnt lgkmcnt(3)
	v_max_u32_e32 v6, v8, v6
	s_waitcnt lgkmcnt(2)
	v_max_u32_e32 v7, v9, v7
	v_readfirstlane_b32 s0, v6
	v_readfirstlane_b32 s1, v7
	s_waitcnt lgkmcnt(1)
	v_max_u32_e32 v5, v10, v5
	s_waitcnt lgkmcnt(0)
	v_max_u32_e32 v4, v11, v4
	s_andn2_b32 vcc_lo, 63, s0
	s_andn2_b32 s52, 63, s1
	v_readfirstlane_b32 s0, v5
	v_readfirstlane_b32 s1, v4
	s_andn2_b32 s88, 63, s0
	s_andn2_b32 s58, 63, s1
	v_readlane_b32 s81, v1, s17
	v_readlane_b32 s62, v0, s60
	v_readlane_b32 s55, v3, s97
	v_readlane_b32 s34, v2, s49
	v_readlane_b32 s0, v1, s80
	v_readlane_b32 s72, v0, s33
	v_readlane_b32 s65, v3, s61
	v_readlane_b32 s35, v2, s96
	v_readlane_b32 s29, v1, s92
	v_readlane_b32 s1, v0, s77
	v_readlane_b32 s73, v3, s79
	v_readlane_b32 s67, v2, s63
	v_readlane_b32 s31, v1, s53
	v_readlane_b32 s28, v0, s91
	v_readlane_b32 s75, v3, s59
	v_readlane_b32 s69, v2, s78
	v_readlane_b32 s71, v1, vcc_lo
	v_readlane_b32 s30, v0, s52
	v_readlane_b32 s84, v3, s88
	v_readlane_b32 s74, v2, s58
	s_mov_b64 s[14:15], exec
	v_readlane_b32 s22, v248, 34
	v_readlane_b32 s23, v248, 35
	s_and_b64 s[22:23], s[14:15], s[22:23]
	s_mov_b64 exec, s[22:23]
	s_cbranch_execz .LBB0_609
; template <int l>
; __device__ __forceinline__ void layer_phases(Frame& F, const XcdBarrier& bar, const int lo, const int hi) {
;     ...
;                 for (int rr = 0; rr < 4; ++rr) { const int m = m0 + rr;
;                     const float ssum = ((sk[rr][0] + sk[rr][1]) + (sk[rr][2] + sk[rr][3])) + (sk[rr][4] + sk[rr][5]);
;                     if (F.lane < 6 && rep == 0) { int e = ek[rr][0]; float sc = sk[rr][0];
; #pragma unroll
;                         for (int k = 1; k < 6; ++k) if (F.lane == k) { e = ek[rr][k]; sc = sk[rr][k]; }
;                         const unsigned pos = __hip_atomic_fetch_add(F.ctl + CW_CURSOR + (l * 64 + e) * 16, 1u, RLX_AGENT);
;                         if (pos < (unsigned)LISTCAP) { list[(size_t)e * LISTCAP + pos] = m; list2[(size_t)e * LISTCAP + pos] = m * 7 + F.lane; }
;                         tinfo[(size_t)m * 6 + F.lane] = e | (int)(pos << 8); gates[(size_t)m * 6 + F.lane] = sc / ssum * ROUTED_SCALE; }
	v_mov_b32_e32 v40, s16
	v_mov_b32_e32 v48, s17
	v_cndmask_b32_e64 v40, v40, v48, s[4:5]
	v_mov_b32_e32 v48, s80
	v_cndmask_b32_e64 v40, v40, v48, s[6:7]
	v_mov_b32_e32 v48, s92
	v_cndmask_b32_e64 v40, v40, v48, s[8:9]
	v_mov_b32_e32 v48, s53
	v_cndmask_b32_e64 v40, v40, v48, s[10:11]
	v_mov_b32_e32 v48, vcc_lo
	v_cndmask_b32_e64 v40, v40, v48, s[12:13]
	v_lshlrev_b32_e32 v34, 6, v40
	global_atomic_add v44, v34, v226, s[38:39] sc0
	v_mov_b32_e32 v41, s82
	v_mov_b32_e32 v48, s60
	v_cndmask_b32_e64 v41, v41, v48, s[4:5]
	v_mov_b32_e32 v48, s33
	v_cndmask_b32_e64 v41, v41, v48, s[6:7]
	v_mov_b32_e32 v48, s77
	v_cndmask_b32_e64 v41, v41, v48, s[8:9]
	v_mov_b32_e32 v48, s91
	v_cndmask_b32_e64 v41, v41, v48, s[10:11]
	v_mov_b32_e32 v48, s52
	v_cndmask_b32_e64 v41, v41, v48, s[12:13]
	v_lshlrev_b32_e32 v34, 6, v41
	global_atomic_add v45, v34, v226, s[38:39] sc0
	v_mov_b32_e32 v42, s45
	v_mov_b32_e32 v48, s97
	v_cndmask_b32_e64 v42, v42, v48, s[4:5]
	v_mov_b32_e32 v48, s61
	v_cndmask_b32_e64 v42, v42, v48, s[6:7]
	v_mov_b32_e32 v48, s79
	v_cndmask_b32_e64 v42, v42, v48, s[8:9]
	v_mov_b32_e32 v48, s59
	v_cndmask_b32_e64 v42, v42, v48, s[10:11]
	v_mov_b32_e32 v48, s88
	v_cndmask_b32_e64 v42, v42, v48, s[12:13]
	v_lshlrev_b32_e32 v34, 6, v42
	global_atomic_add v46, v34, v226, s[38:39] sc0
	v_mov_b32_e32 v43, s19
	v_mov_b32_e32 v48, s49
	v_cndmask_b32_e64 v43, v43, v48, s[4:5]
	v_mov_b32_e32 v48, s96
	v_cndmask_b32_e64 v43, v43, v48, s[6:7]
	v_mov_b32_e32 v48, s63
	v_cndmask_b32_e64 v43, v43, v48, s[8:9]
	v_mov_b32_e32 v48, s78
	v_cndmask_b32_e64 v43, v43, v48, s[10:11]
	v_mov_b32_e32 v48, s58
	v_cndmask_b32_e64 v43, v43, v48, s[12:13]
	v_lshlrev_b32_e32 v34, 6, v43
	global_atomic_add v47, v34, v226, s[38:39] sc0
	s_waitcnt vmcnt(0)
	v_mov_b32_e32 v0, v40
	v_mov_b32_e32 v80, v44
	v_cmp_gt_u32_e32 vcc, s85, v80
	s_and_saveexec_b64 s[16:17], vcc
	s_cbranch_execz .LBB0_615
	v_lshlrev_b64 v[2:3], 2, v[80:81]
	v_readlane_b32 s22, v248, 15
	v_lshl_or_b32 v2, v0, 16, v2
	v_readlane_b32 s23, v248, 16
	v_mov_b32_e32 v1, s42
	s_nop 0
	v_lshl_add_u64 v[4:5], s[22:23], 0, v[2:3]
	global_store_dword v[4:5], v1, off
	v_mad_u64_u32 v[4:5], s[22:23], s42, 7, v[72:73]
	v_readlane_b32 s22, v248, 17
	v_readlane_b32 s23, v248, 18
	s_nop 1
	v_lshl_add_u64 v[2:3], s[22:23], 0, v[2:3]
	global_store_dword v[2:3], v4, off
.LBB0_615:
	s_or_b64 exec, exec, s[16:17]
	v_mov_b32_e32 v1, s95
	v_mov_b32_e32 v2, s81
	v_cndmask_b32_e64 v1, v1, v2, s[4:5]
	v_mov_b32_e32 v3, s0
	v_cndmask_b32_e64 v1, v1, v3, s[6:7]
	v_mov_b32_e32 v3, s29
	v_cndmask_b32_e64 v1, v1, v3, s[8:9]
	v_mov_b32_e32 v4, s31
	v_cndmask_b32_e64 v1, v1, v4, s[10:11]
	v_mov_b32_e32 v4, s71
	v_cndmask_b32_e64 v5, v1, v4, s[12:13]
	v_add_f32_e32 v1, s95, v2
	v_add_f32_e32 v2, s0, v3
	v_add_f32_e32 v1, v1, v2
	v_add_f32_e32 v2, s31, v4
	v_add_f32_e32 v2, v1, v2
	v_div_scale_f32 v4, s[16:17], v2, v2, v5
	v_rcp_f32_e32 v6, v4
	v_lshl_or_b32 v3, v80, 8, v0
	v_mad_i64_i32 v[0:1], s[16:17], s42, 24, v[76:77]
	global_store_dword v[0:1], v3, off
	v_fma_f32 v0, -v4, v6, 1.0
	v_fmac_f32_e32 v6, v0, v6
	v_div_scale_f32 v0, vcc, v5, v2, v5
	v_mul_f32_e32 v1, v0, v6
	v_fma_f32 v3, -v4, v1, v0
	v_fmac_f32_e32 v1, v3, v6
	v_fma_f32 v0, -v4, v1, v0
	v_div_fmas_f32 v0, v0, v6, v1
	v_div_fixup_f32 v0, v0, v2, v5
	v_mul_f32_e32 v2, 0x40200000, v0
	v_mad_i64_i32 v[0:1], s[16:17], s42, 24, v[78:79]
	global_store_dword v[0:1], v2, off
	v_mov_b32_e32 v0, v41
	v_mov_b32_e32 v80, v45
	v_cmp_gt_u32_e32 vcc, s85, v80
	s_and_saveexec_b64 s[16:17], vcc
	s_cbranch_execz .LBB0_617
	v_lshlrev_b64 v[2:3], 2, v[80:81]
	v_readlane_b32 s22, v248, 15
	v_lshl_or_b32 v2, v0, 16, v2
	v_readlane_b32 s23, v248, 16
	v_mov_b32_e32 v1, s44
	s_nop 0
	v_lshl_add_u64 v[4:5], s[22:23], 0, v[2:3]
	global_store_dword v[4:5], v1, off
	v_mad_u64_u32 v[4:5], s[22:23], s44, 7, v[72:73]
	v_readlane_b32 s22, v248, 17
	v_readlane_b32 s23, v248, 18
	s_nop 1
	v_lshl_add_u64 v[2:3], s[22:23], 0, v[2:3]
	global_store_dword v[2:3], v4, off
; template <int l>
; __device__ __forceinline__ void layer_phases(Frame& F, const XcdBarrier& bar, const int lo, const int hi) {
;     ...
;                 for (int rr = 0; rr < 4; ++rr) { const int m = m0 + rr;
;                     const float ssum = ((sk[rr][0] + sk[rr][1]) + (sk[rr][2] + sk[rr][3])) + (sk[rr][4] + sk[rr][5]);
;                     if (F.lane < 6 && rep == 0) { int e = ek[rr][0]; float sc = sk[rr][0];
; #pragma unroll
;                         for (int k = 1; k < 6; ++k) if (F.lane == k) { e = ek[rr][k]; sc = sk[rr][k]; }
;                         const unsigned pos = __hip_atomic_fetch_add(F.ctl + CW_CURSOR + (l * 64 + e) * 16, 1u, RLX_AGENT);
;                         if (pos < (unsigned)LISTCAP) { list[(size_t)e * LISTCAP + pos] = m; list2[(size_t)e * LISTCAP + pos] = m * 7 + F.lane; }
;                         tinfo[(size_t)m * 6 + F.lane] = e | (int)(pos << 8); gates[(size_t)m * 6 + F.lane] = sc / ssum * ROUTED_SCALE; }
.LBB0_617:
	s_or_b64 exec, exec, s[16:17]
	v_mov_b32_e32 v1, s62
	v_mov_b32_e32 v3, s1
	v_add_f32_e32 v2, s47, v1
	v_add_f32_e32 v4, s72, v3
	v_add_f32_e32 v2, v2, v4
	v_mov_b32_e32 v4, s30
	v_add_f32_e32 v5, s28, v4
	v_add_f32_e32 v2, v2, v5
	v_mov_b32_e32 v5, s47
	v_cndmask_b32_e64 v1, v5, v1, s[4:5]
	v_mov_b32_e32 v5, s72
	v_cndmask_b32_e64 v1, v1, v5, s[6:7]
	v_cndmask_b32_e64 v1, v1, v3, s[8:9]
	v_mov_b32_e32 v3, s28
	v_cndmask_b32_e64 v1, v1, v3, s[10:11]
	v_cndmask_b32_e64 v3, v1, v4, s[12:13]
	v_div_scale_f32 v5, s[0:1], v2, v2, v3
	v_rcp_f32_e32 v6, v5
	v_lshl_or_b32 v4, v80, 8, v0
	v_mad_i64_i32 v[0:1], s[0:1], s44, 24, v[76:77]
	global_store_dword v[0:1], v4, off
	v_fma_f32 v0, -v5, v6, 1.0
	v_fmac_f32_e32 v6, v0, v6
	v_div_scale_f32 v0, vcc, v3, v2, v3
	v_mul_f32_e32 v1, v0, v6
	v_fma_f32 v4, -v5, v1, v0
	v_fmac_f32_e32 v1, v4, v6
	v_fma_f32 v0, -v5, v1, v0
	v_div_fmas_f32 v0, v0, v6, v1
	v_div_fixup_f32 v0, v0, v2, v3
	v_mul_f32_e32 v2, 0x40200000, v0
	v_mad_i64_i32 v[0:1], s[0:1], s44, 24, v[78:79]
	global_store_dword v[0:1], v2, off
	v_mov_b32_e32 v0, v42
	v_mov_b32_e32 v80, v46
	v_cmp_gt_u32_e32 vcc, s85, v80
	s_and_saveexec_b64 s[16:17], vcc
	s_cbranch_execz .LBB0_619
	v_lshlrev_b64 v[2:3], 2, v[80:81]
	v_readlane_b32 s0, v248, 15
	v_lshl_or_b32 v2, v0, 16, v2
	v_readlane_b32 s1, v248, 16
	v_mov_b32_e32 v1, s46
	s_nop 0
	v_lshl_add_u64 v[4:5], s[0:1], 0, v[2:3]
	global_store_dword v[4:5], v1, off
	v_mad_u64_u32 v[4:5], s[0:1], s46, 7, v[72:73]
	v_readlane_b32 s0, v248, 17
	v_readlane_b32 s1, v248, 18
	s_nop 1
	v_lshl_add_u64 v[2:3], s[0:1], 0, v[2:3]
	global_store_dword v[2:3], v4, off
.LBB0_619:
	s_or_b64 exec, exec, s[16:17]
	v_mov_b32_e32 v1, s55
	v_mov_b32_e32 v3, s73
	v_add_f32_e32 v2, s43, v1
	v_add_f32_e32 v4, s65, v3
	v_add_f32_e32 v2, v2, v4
	v_mov_b32_e32 v4, s84
	v_add_f32_e32 v5, s75, v4
	v_add_f32_e32 v2, v2, v5
	v_mov_b32_e32 v5, s43
	v_cndmask_b32_e64 v1, v5, v1, s[4:5]
	v_mov_b32_e32 v5, s65
	v_cndmask_b32_e64 v1, v1, v5, s[6:7]
	v_cndmask_b32_e64 v1, v1, v3, s[8:9]
	v_mov_b32_e32 v3, s75
	v_cndmask_b32_e64 v1, v1, v3, s[10:11]
	v_cndmask_b32_e64 v3, v1, v4, s[12:13]
	v_div_scale_f32 v5, s[0:1], v2, v2, v3
	v_rcp_f32_e32 v6, v5
	v_lshl_or_b32 v4, v80, 8, v0
	v_mad_i64_i32 v[0:1], s[0:1], s46, 24, v[76:77]
	global_store_dword v[0:1], v4, off
	v_fma_f32 v0, -v5, v6, 1.0
	v_fmac_f32_e32 v6, v0, v6
	v_div_scale_f32 v0, vcc, v3, v2, v3
	v_mul_f32_e32 v1, v0, v6
	v_fma_f32 v4, -v5, v1, v0
	v_fmac_f32_e32 v1, v4, v6
	v_fma_f32 v0, -v5, v1, v0
	v_div_fmas_f32 v0, v0, v6, v1
	v_div_fixup_f32 v0, v0, v2, v3
	v_mul_f32_e32 v2, 0x40200000, v0
	v_mad_i64_i32 v[0:1], s[0:1], s46, 24, v[78:79]
	global_store_dword v[0:1], v2, off
	v_mov_b32_e32 v0, v43
	v_mov_b32_e32 v80, v47
	v_cmp_gt_u32_e32 vcc, s85, v80
	s_and_saveexec_b64 s[16:17], vcc
	s_cbranch_execz .LBB0_608
	v_lshlrev_b64 v[2:3], 2, v[80:81]
	v_readlane_b32 s0, v248, 15
	v_lshl_or_b32 v2, v0, 16, v2
	v_readlane_b32 s1, v248, 16
	v_mov_b32_e32 v1, s48
	s_nop 0
	v_lshl_add_u64 v[4:5], s[0:1], 0, v[2:3]
	global_store_dword v[4:5], v1, off
	v_mad_u64_u32 v[4:5], s[0:1], s48, 7, v[72:73]
	v_readlane_b32 s0, v248, 17
	v_readlane_b32 s1, v248, 18
	s_nop 1
	v_lshl_add_u64 v[2:3], s[0:1], 0, v[2:3]
	global_store_dword v[2:3], v4, off
	s_branch .LBB0_608

; #define GAS __attribute__((address_space(1)))
; __device__ __forceinline__ f32x4 bf4(unsigned a, unsigned b) { return (f32x4){bflo(a), bfhi(a), bflo(b), bfhi(b)}; }
; __device__ __forceinline__ int affine_item(int item_, int G) { if (G != 256) return item_; const int c = item_ & 255, i = item_ >> 8; return 64 * (c & 7) + (c >> 3) + 32 * i; }
; template <int l>
; __device__ __forceinline__ void layer_phases(Frame& F, const XcdBarrier& bar, const int lo, const int hi) {
;     ...
;             for (int item_ = blockIdx.x; item_ < T / 32; item_ += F.G) {
;                 const int item = affine_item(item_, F.G);
;                 const int m0 = item * 32 + 4 * F.wave;
;                 int lq = F.lane; asm volatile("" : "+v"(lq));
;                 const int r32 = lq & 31, hi5 = lq >> 5;
;                 const float* mrow = (const float*)(ws + WS_MOD) + ((size_t)l * 8 + (m0 >> 11)) * 12288;
; #pragma unroll
;                 for (int rp = 0; rp < 2; ++rp) {
;                 f32x4 vv[2][8];
; #pragma unroll
;                 for (int rr = 0; rr < 2; ++rr)
; #pragma unroll
;                     for (int j = 0; j < 8; ++j) { const size_t off = (size_t)(m0 + 2 * rp + rr) * D + 4 * lq + 256 * j;
;                         f32x4 xv; if (l == 0) xv = __builtin_nontemporal_load((const GAS f32x4*)(xin + off)); else { const v2u xw_ = __builtin_nontemporal_load((const GAS v2u*)(xinb + off)); xv = bf4(xw_.x, xw_.y); } const v2u mw = __builtin_nontemporal_load((const GAS v2u*)(mixb + off)); const f32x4 gv = *(const GAS f32x4*)(mrow + 4096 + 4 * lq + 256 * j);
;                         vv[rr][j] = xv * ALPHA + gv * (f32x4){bflo(mw.x), bfhi(mw.x), bflo(mw.y), bfhi(mw.y)}; }
.LBB0_1522:
	s_lshl_b32 s0, s0, 5
	s_add_i32 s40, s0, s52
	s_ashr_i32 s0, s40, 11
	s_add_i32 s0, s0, 8
	s_mul_hi_i32 s1, s0, 0xc000
	s_mul_i32 s0, s0, 0xc000
	v_readlane_b32 s14, v248, 17
	v_mov_b32_e32 v204, v52
	s_add_u32 s0, s14, s0
	v_readlane_b32 s14, v248, 19
	s_addc_u32 s1, s14, s1
	v_lshlrev_b32_e32 v36, 2, v204
	s_ashr_i32 s41, s40, 31
	v_ashrrev_i32_e32 v37, 31, v36
	s_lshl_b64 s[18:19], s[40:41], 11
	v_lshl_add_u64 v[0:1], s[18:19], 0, v[36:37]
	v_lshlrev_b64 v[32:33], 2, v[36:37]
	v_lshlrev_b64 v[0:1], 1, v[0:1]
	v_lshl_add_u64 v[38:39], s[0:1], 0, v[32:33]
	s_movk_i32 s24, 0x5000
	v_lshl_add_u64 v[34:35], s[22:23], 0, v[0:1]
	v_add_co_u32_e32 v126, vcc, s24, v38
	global_load_dwordx2 v[40:41], v[34:35], off nt
	v_lshl_add_u64 v[42:43], s[20:21], 0, v[0:1]
	v_addc_co_u32_e32 v127, vcc, 0, v39, vcc
	global_load_dwordx2 v[44:45], v[42:43], off nt
	global_load_dwordx2 v[46:47], v[34:35], off offset:512 nt
	global_load_dwordx2 v[48:49], v[42:43], off offset:512 nt
	global_load_dwordx2 v[50:51], v[34:35], off offset:1024 nt
	global_load_dwordx2 v[62:63], v[42:43], off offset:1024 nt
	global_load_dwordx2 v[64:65], v[34:35], off offset:1536 nt
	global_load_dwordx2 v[66:67], v[42:43], off offset:1536 nt
	global_load_dwordx4 v[0:3], v[126:127], off offset:-4096
	s_mov_b64 s[0:1], 0x4000
	v_lshl_add_u64 v[128:129], v[38:39], 0, s[0:1]
	global_load_dwordx4 v[12:15], v[128:129], off offset:1024
	global_load_dwordx4 v[8:11], v[128:129], off offset:2048
	global_load_dwordx4 v[4:7], v[128:129], off offset:3072
	global_load_dwordx2 v[68:69], v[34:35], off offset:2048 nt
	global_load_dwordx2 v[70:71], v[42:43], off offset:2048 nt
	global_load_dwordx4 v[16:19], v[126:127], off
	global_load_dwordx2 v[72:73], v[34:35], off offset:2560 nt
	global_load_dwordx2 v[74:75], v[42:43], off offset:2560 nt
	global_load_dwordx4 v[28:31], v[126:127], off offset:1024
	global_load_dwordx4 v[24:27], v[126:127], off offset:2048
	global_load_dwordx4 v[20:23], v[126:127], off offset:3072
	global_load_dwordx2 v[80:81], v[34:35], off offset:3072 nt
	global_load_dwordx2 v[82:83], v[34:35], off offset:3584 nt
	global_load_dwordx2 v[86:87], v[42:43], off offset:3072 nt
	global_load_dwordx2 v[88:89], v[42:43], off offset:3584 nt
	v_readlane_b32 s0, v248, 20
	v_readlane_b32 s1, v248, 21
	s_or_b32 s42, s40, 1
	s_ashr_i32 s43, s42, 31
	s_lshl_b64 s[16:17], s[42:43], 11
	s_mov_b32 s25, 0x9000
	s_movk_i32 s26, 0x7000
	v_mov_b32_e32 v142, 0
	v_mov_b32_e32 v174, 0
	s_waitcnt vmcnt(21)
	v_lshlrev_b32_e32 v76, 16, v46
	v_lshlrev_b32_e32 v42, 16, v40
	v_and_b32_e32 v43, 0xffff0000, v40
	v_lshlrev_b32_e32 v34, 16, v41
	v_and_b32_e32 v35, 0xffff0000, v41
	v_lshlrev_b32_e32 v40, 16, v44
	v_and_b32_e32 v41, 0xffff0000, v44
	v_lshlrev_b32_e32 v44, 16, v45
	v_and_b32_e32 v45, 0xffff0000, v45
	s_waitcnt vmcnt(16)
	v_lshlrev_b32_e32 v94, 16, v66
	v_and_b32_e32 v95, 0xffff0000, v66
	v_lshlrev_b32_e32 v66, 16, v67
	v_and_b32_e32 v67, 0xffff0000, v67
	s_waitcnt vmcnt(15)
	v_pk_mul_f32 v[44:45], v[2:3], v[44:45]
	v_lshlrev_b32_e32 v78, 16, v48
	v_and_b32_e32 v79, 0xffff0000, v48
	v_lshlrev_b32_e32 v48, 16, v49
	v_and_b32_e32 v49, 0xffff0000, v49
	v_lshlrev_b32_e32 v92, 16, v64
	v_and_b32_e32 v93, 0xffff0000, v64
	v_lshlrev_b32_e32 v64, 16, v65
	v_and_b32_e32 v65, 0xffff0000, v65
	v_pk_mul_f32 v[40:41], v[0:1], v[40:41]
	s_waitcnt vmcnt(12)
	v_pk_mul_f32 v[66:67], v[6:7], v[66:67]
	v_pk_fma_f32 v[34:35], v[34:35], s[38:39], v[44:45] op_sel_hi:[1,0,1]
	v_pk_mul_f32 v[44:45], v[4:5], v[94:95]
	v_and_b32_e32 v77, 0xffff0000, v46
	v_lshlrev_b32_e32 v46, 16, v47
	v_and_b32_e32 v47, 0xffff0000, v47
	v_pk_mul_f32 v[48:49], v[14:15], v[48:49]
	v_pk_mul_f32 v[78:79], v[12:13], v[78:79]
	v_pk_fma_f32 v[42:43], v[42:43], s[38:39], v[40:41] op_sel_hi:[1,0,1]
	v_pk_fma_f32 v[40:41], v[64:65], s[38:39], v[66:67] op_sel_hi:[1,0,1]
	v_pk_fma_f32 v[64:65], v[92:93], s[38:39], v[44:45] op_sel_hi:[1,0,1]
	s_waitcnt vmcnt(11)
	v_lshlrev_b32_e32 v44, 16, v68
	v_and_b32_e32 v45, 0xffff0000, v68
	v_lshlrev_b32_e32 v66, 16, v69
	v_and_b32_e32 v67, 0xffff0000, v69
	s_waitcnt vmcnt(10)
	v_lshlrev_b32_e32 v68, 16, v70
	v_and_b32_e32 v69, 0xffff0000, v70
	v_pk_fma_f32 v[46:47], v[46:47], s[38:39], v[48:49] op_sel_hi:[1,0,1]
	v_pk_fma_f32 v[48:49], v[76:77], s[38:39], v[78:79] op_sel_hi:[1,0,1]
	v_lshlrev_b32_e32 v70, 16, v71
	v_and_b32_e32 v71, 0xffff0000, v71
	s_waitcnt vmcnt(9)
	v_pk_mul_f32 v[76:77], v[16:17], v[68:69]
	s_waitcnt vmcnt(7)
	v_lshlrev_b32_e32 v78, 16, v74
	v_and_b32_e32 v79, 0xffff0000, v74
	v_lshlrev_b32_e32 v74, 16, v75
	v_and_b32_e32 v75, 0xffff0000, v75
	v_pk_mul_f32 v[68:69], v[18:19], v[70:71]
	v_pk_fma_f32 v[70:71], v[44:45], s[38:39], v[76:77] op_sel_hi:[1,0,1]
	v_lshlrev_b32_e32 v76, 16, v72
	v_and_b32_e32 v77, 0xffff0000, v72
	v_lshlrev_b32_e32 v72, 16, v73
	v_and_b32_e32 v73, 0xffff0000, v73
	s_waitcnt vmcnt(6)
	v_pk_mul_f32 v[74:75], v[30:31], v[74:75]
	v_pk_mul_f32 v[78:79], v[28:29], v[78:79]
	v_lshlrev_b32_e32 v90, 16, v62
	v_pk_fma_f32 v[76:77], v[76:77], s[38:39], v[78:79] op_sel_hi:[1,0,1]
	v_pk_fma_f32 v[78:79], v[72:73], s[38:39], v[74:75] op_sel_hi:[1,0,1]
	s_waitcnt vmcnt(3)
	v_lshlrev_b32_e32 v72, 16, v80
	v_and_b32_e32 v73, 0xffff0000, v80
	v_lshlrev_b32_e32 v74, 16, v81
	v_and_b32_e32 v75, 0xffff0000, v81
	s_waitcnt vmcnt(1)
	v_lshlrev_b32_e32 v80, 16, v86
	v_and_b32_e32 v81, 0xffff0000, v86
	v_lshlrev_b32_e32 v86, 16, v87
	v_and_b32_e32 v87, 0xffff0000, v87
	v_pk_mul_f32 v[80:81], v[24:25], v[80:81]
	v_pk_mul_f32 v[86:87], v[26:27], v[86:87]
	v_and_b32_e32 v91, 0xffff0000, v62
	v_lshlrev_b32_e32 v62, 16, v63
	v_and_b32_e32 v63, 0xffff0000, v63
	v_pk_fma_f32 v[86:87], v[74:75], s[38:39], v[86:87] op_sel_hi:[1,0,1]
	v_pk_fma_f32 v[94:95], v[72:73], s[38:39], v[80:81] op_sel_hi:[1,0,1]
	v_lshlrev_b32_e32 v72, 16, v82
	v_and_b32_e32 v73, 0xffff0000, v82
	v_lshlrev_b32_e32 v74, 16, v83
	v_and_b32_e32 v75, 0xffff0000, v83
	s_waitcnt vmcnt(0)
; #define GAS __attribute__((address_space(1)))
; __device__ __forceinline__ f32x4 bf4(unsigned a, unsigned b) { return (f32x4){bflo(a), bfhi(a), bflo(b), bfhi(b)}; }
; template <int l>
; __device__ __forceinline__ void layer_phases(Frame& F, const XcdBarrier& bar, const int lo, const int hi) {
;     ...
;                     for (int j = 0; j < 8; ++j) { const size_t off = (size_t)(m0 + 2 * rp + rr) * D + 4 * lq + 256 * j;
;                         f32x4 xv; if (l == 0) xv = __builtin_nontemporal_load((const GAS f32x4*)(xin + off)); else { const v2u xw_ = __builtin_nontemporal_load((const GAS v2u*)(xinb + off)); xv = bf4(xw_.x, xw_.y); } const v2u mw = __builtin_nontemporal_load((const GAS v2u*)(mixb + off)); const f32x4 gv = *(const GAS f32x4*)(mrow + 4096 + 4 * lq + 256 * j);
;                         vv[rr][j] = xv * ALPHA + gv * (f32x4){bflo(mw.x), bfhi(mw.x), bflo(mw.y), bfhi(mw.y)}; }
; #pragma unroll
;                 for (int rq = 0; rq < 2; ++rq) { const int rr = 2 * rp + rq, m = m0 + rr, rloc = 4 * F.wave + rr;
;                     f32x4 (&v)[8] = vv[rq]; float s = 0.f;
; #pragma unroll
;                     for (int j = 0; j < 8; ++j) s += (v[j].x + v[j].y) + (v[j].z + v[j].w);
;                     const float mean = wave_sum(s) * (1.f / D); float s2 = 0.f;
; #pragma unroll
;                     for (int j = 0; j < 8; ++j) { v[j] = v[j] - mean; s2 += (v[j].x * v[j].x + v[j].y * v[j].y) + (v[j].z * v[j].z + v[j].w * v[j].w); }
;                     const float rstd = 1.f / sqrtf(wave_sum(s2) * (1.f / D) + LN_EPS);
	v_lshlrev_b32_e32 v80, 16, v88
	v_and_b32_e32 v81, 0xffff0000, v88
	v_lshlrev_b32_e32 v82, 16, v89
	v_and_b32_e32 v83, 0xffff0000, v89
	v_lshlrev_b32_e32 v84, 16, v50
	v_and_b32_e32 v85, 0xffff0000, v50
	v_lshlrev_b32_e32 v50, 16, v51
	v_and_b32_e32 v51, 0xffff0000, v51
	v_pk_mul_f32 v[62:63], v[10:11], v[62:63]
	v_pk_mul_f32 v[90:91], v[8:9], v[90:91]
	v_pk_mul_f32 v[80:81], v[20:21], v[80:81]
	v_pk_mul_f32 v[82:83], v[22:23], v[82:83]
	v_pk_fma_f32 v[50:51], v[50:51], s[38:39], v[62:63] op_sel_hi:[1,0,1]
	v_pk_fma_f32 v[62:63], v[84:85], s[38:39], v[90:91] op_sel_hi:[1,0,1]
	v_pk_fma_f32 v[90:91], v[74:75], s[38:39], v[82:83] op_sel_hi:[1,0,1]
	v_pk_fma_f32 v[92:93], v[72:73], s[38:39], v[80:81] op_sel_hi:[1,0,1]
	v_mov_b32_e32 v72, v42
	v_mov_b32_e32 v73, v48
	v_mov_b32_e32 v74, v43
	v_mov_b32_e32 v75, v49
	v_pk_add_f32 v[72:73], v[72:73], v[74:75]
	v_mov_b32_e32 v74, v34
	v_mov_b32_e32 v75, v46
	v_mov_b32_e32 v80, v35
	v_mov_b32_e32 v81, v47
	v_pk_add_f32 v[74:75], v[74:75], v[80:81]
	v_mov_b32_e32 v80, v62
	v_pk_add_f32 v[72:73], v[72:73], v[74:75]
	v_pk_mov_b32 v[74:75], v[62:63], v[50:51] op_sel:[1,0]
	v_mov_b32_e32 v81, v51
	v_pk_add_f32 v[74:75], v[74:75], v[80:81]
	v_pk_fma_f32 v[68:69], v[66:67], s[38:39], v[68:69] op_sel_hi:[1,0,1]
	v_add_f32_e32 v60, 0, v72
	v_pk_add_f32 v[74:75], v[74:75], v[74:75] op_sel:[0,1] op_sel_hi:[1,0]
	v_add_f32_e32 v72, v60, v73
	v_add_f32_e32 v80, v64, v65
	v_add_f32_e32 v82, v40, v41
	v_mov_b32_e32 v73, v70
	v_mov_b32_e32 v75, v71
	v_mov_b32_e32 v81, v68
	v_mov_b32_e32 v83, v69
	v_pk_add_f32 v[72:73], v[72:73], v[74:75]
	v_pk_add_f32 v[74:75], v[80:81], v[82:83]
	v_mov_b32_e32 v80, v76
	v_pk_add_f32 v[72:73], v[72:73], v[74:75]
	v_pk_mov_b32 v[74:75], v[76:77], v[78:79] op_sel:[1,0]
	v_mov_b32_e32 v81, v79
	v_pk_add_f32 v[74:75], v[74:75], v[80:81]
	v_pk_add_f32 v[72:73], v[72:73], v[72:73] op_sel:[0,1] op_sel_hi:[1,0]
	v_pk_add_f32 v[74:75], v[74:75], v[74:75] op_sel:[0,1] op_sel_hi:[1,0]
	v_add_f32_e32 v80, v94, v95
	v_add_f32_e32 v82, v86, v87
	v_mov_b32_e32 v73, v92
	v_mov_b32_e32 v75, v93
	v_mov_b32_e32 v81, v90
	v_mov_b32_e32 v83, v91
	v_pk_add_f32 v[72:73], v[72:73], v[74:75]
	v_pk_add_f32 v[74:75], v[80:81], v[82:83]
	v_lshl_add_u64 v[44:45], s[16:17], 0, v[36:37]
	v_pk_add_f32 v[72:73], v[72:73], v[74:75]
	v_lshlrev_b64 v[66:67], 1, v[44:45]
	v_add_f32_e32 v60, v72, v73
	ds_bpermute_b32 v72, v53, v60
	v_lshl_add_u64 v[44:45], s[22:23], 0, v[66:67]
	global_load_dwordx2 v[84:85], v[44:45], off nt
	s_waitcnt lgkmcnt(0)
	v_add_f32_e32 v60, v60, v72
	ds_bpermute_b32 v72, v194, v60
	s_waitcnt lgkmcnt(0)
	v_add_f32_e32 v60, v60, v72
	ds_bpermute_b32 v72, v195, v60
	s_waitcnt lgkmcnt(0)
	v_add_f32_e32 v60, v60, v72
	ds_bpermute_b32 v72, v196, v60
	s_waitcnt lgkmcnt(0)
	v_add_f32_e32 v60, v60, v72
	ds_bpermute_b32 v72, v197, v60
	s_waitcnt lgkmcnt(0)
	v_add_f32_e32 v60, v60, v72
	ds_bpermute_b32 v72, v198, v60
	s_waitcnt lgkmcnt(0)
	v_add_f32_e32 v88, v60, v72
	v_fmamk_f32 v43, v88, 0xba000000, v43
	v_fmamk_f32 v49, v88, 0xba000000, v49
	v_fmamk_f32 v35, v88, 0xba000000, v35
	v_fmac_f32_e32 v42, 0xba000000, v88
	v_fmamk_f32 v47, v88, 0xba000000, v47
	v_fmac_f32_e32 v48, 0xba000000, v88
	v_mov_b32_e32 v74, v43
	v_mov_b32_e32 v75, v49
	v_fmac_f32_e32 v34, 0xba000000, v88
	v_fmac_f32_e32 v46, 0xba000000, v88
	v_mov_b32_e32 v72, v42
	v_mov_b32_e32 v73, v48
	v_pk_mul_f32 v[74:75], v[74:75], v[74:75]
	v_mov_b32_e32 v80, v35
	v_mov_b32_e32 v81, v47
	v_pk_fma_f32 v[72:73], v[72:73], v[72:73], v[74:75]
	v_mov_b32_e32 v74, v34
	v_mov_b32_e32 v75, v46
	v_pk_mul_f32 v[80:81], v[80:81], v[80:81]
	v_fmamk_f32 v63, v88, 0xba000000, v63
	v_pk_fma_f32 v[74:75], v[74:75], v[74:75], v[80:81]
	v_fmac_f32_e32 v62, 0xba000000, v88
	v_fmamk_f32 v51, v88, 0xba000000, v51
	v_fmac_f32_e32 v50, 0xba000000, v88
	v_pk_add_f32 v[72:73], v[72:73], v[74:75]
	v_pk_mul_f32 v[74:75], v[50:51], v[50:51]
	v_pk_mul_f32 v[80:81], v[62:63], v[62:63]
	v_fmac_f32_e32 v64, 0xba000000, v88
	v_pk_mov_b32 v[82:83], v[80:81], v[74:75] op_sel:[1,0]
	v_mov_b32_e32 v81, v75
	v_fmamk_f32 v65, v88, 0xba000000, v65
	v_fmac_f32_e32 v40, 0xba000000, v88
	v_mul_f32_e32 v60, v64, v64
	v_pk_add_f32 v[74:75], v[82:83], v[80:81]
	v_fmamk_f32 v41, v88, 0xba000000, v41
	v_pk_fma_f32 v[80:81], v[64:65], v[64:65], v[60:61] op_sel_hi:[1,1,0]
	v_mul_f32_e32 v60, v40, v40
	v_pk_add_f32 v[72:73], v[72:73], v[72:73] op_sel_hi:[0,1]
	v_pk_add_f32 v[74:75], v[74:75], v[74:75] op_sel_hi:[0,1]
	v_pk_fma_f32 v[82:83], v[40:41], v[40:41], v[60:61] op_sel_hi:[1,1,0]
	v_fmamk_f32 v69, v88, 0xba000000, v69
	v_fmac_f32_e32 v68, 0xba000000, v88
	v_fmamk_f32 v71, v88, 0xba000000, v71
	v_fmac_f32_e32 v70, 0xba000000, v88
	v_mul_f32_e32 v80, v70, v70
	v_mul_f32_e32 v82, v71, v71
	v_mul_f32_e32 v74, v68, v68
	v_mul_f32_e32 v72, v69, v69
	v_pk_add_f32 v[80:81], v[80:81], v[82:83]
	v_pk_add_f32 v[72:73], v[74:75], v[72:73]
	v_fmamk_f32 v77, v88, 0xba000000, v77
	v_fmac_f32_e32 v76, 0xba000000, v88
	v_fmamk_f32 v79, v88, 0xba000000, v79
	v_fmac_f32_e32 v78, 0xba000000, v88
	v_pk_add_f32 v[72:73], v[80:81], v[72:73]
	v_pk_mul_f32 v[74:75], v[78:79], v[78:79]
	v_pk_mul_f32 v[80:81], v[76:77], v[76:77]
	v_fmac_f32_e32 v94, 0xba000000, v88
	v_pk_mov_b32 v[82:83], v[80:81], v[74:75] op_sel:[1,0]
	v_mov_b32_e32 v81, v75
	v_fmamk_f32 v95, v88, 0xba000000, v95
	v_fmac_f32_e32 v86, 0xba000000, v88
	v_mul_f32_e32 v60, v94, v94
	v_pk_add_f32 v[74:75], v[82:83], v[80:81]
	v_fmamk_f32 v87, v88, 0xba000000, v87
	v_pk_fma_f32 v[80:81], v[94:95], v[94:95], v[60:61] op_sel_hi:[1,1,0]
	v_mul_f32_e32 v60, v86, v86
	v_pk_add_f32 v[72:73], v[72:73], v[72:73] op_sel_hi:[0,1]
	v_pk_add_f32 v[74:75], v[74:75], v[74:75] op_sel_hi:[0,1]
	v_pk_fma_f32 v[82:83], v[86:87], v[86:87], v[60:61] op_sel_hi:[1,1,0]
	v_fmamk_f32 v91, v88, 0xba000000, v91
	v_fmac_f32_e32 v90, 0xba000000, v88
	v_fmamk_f32 v93, v88, 0xba000000, v93
	v_fmac_f32_e32 v92, 0xba000000, v88
	v_mul_f32_e32 v80, v92, v92
	v_mul_f32_e32 v82, v93, v93
	v_mul_f32_e32 v74, v90, v90
	v_mul_f32_e32 v72, v91, v91
	v_pk_add_f32 v[80:81], v[80:81], v[82:83]
	v_pk_add_f32 v[72:73], v[74:75], v[72:73]
	v_lshl_add_u64 v[74:75], s[30:31], 0, v[32:33]
	v_pk_add_f32 v[72:73], v[80:81], v[72:73]
	global_load_dwordx4 v[96:99], v[74:75], off
	v_add_f32_e32 v60, v72, v73
	v_lshl_add_u64 v[72:73], s[0:1], 0, v[32:33]
	global_load_dwordx4 v[80:83], v[72:73], off
	ds_bpermute_b32 v32, v53, v60
	global_load_dwordx2 v[124:125], v[44:45], off offset:512 nt
	global_load_dwordx2 v[118:119], v[44:45], off offset:1024 nt
	global_load_dwordx2 v[112:113], v[44:45], off offset:1536 nt
	global_load_dwordx2 v[104:105], v[44:45], off offset:2048 nt
	s_waitcnt vmcnt(6)
; #define GAS __attribute__((address_space(1)))
; __device__ __forceinline__ unsigned pk2(float lo, float hi) { return f2bf(lo) | (f2bf(hi) << 16); }
; __device__ __forceinline__ f32x4 bf4(unsigned a, unsigned b) { return (f32x4){bflo(a), bfhi(a), bflo(b), bfhi(b)}; }
; template <int l>
; __device__ __forceinline__ void layer_phases(Frame& F, const XcdBarrier& bar, const int lo, const int hi) {
;     ...
;                         f32x4 xv; if (l == 0) xv = __builtin_nontemporal_load((const GAS f32x4*)(xin + off)); else { const v2u xw_ = __builtin_nontemporal_load((const GAS v2u*)(xinb + off)); xv = bf4(xw_.x, xw_.y); } const v2u mw = __builtin_nontemporal_load((const GAS v2u*)(mixb + off)); const f32x4 gv = *(const GAS f32x4*)(mrow + 4096 + 4 * lq + 256 * j);
;                         vv[rr][j] = xv * ALPHA + gv * (f32x4){bflo(mw.x), bfhi(mw.x), bflo(mw.y), bfhi(mw.y)}; }
; #pragma unroll
;                 for (int rq = 0; rq < 2; ++rq) { const int rr = 2 * rp + rq, m = m0 + rr, rloc = 4 * F.wave + rr;
;                     f32x4 (&v)[8] = vv[rq]; float s = 0.f;
; #pragma unroll
;                     for (int j = 0; j < 8; ++j) s += (v[j].x + v[j].y) + (v[j].z + v[j].w);
;                     const float mean = wave_sum(s) * (1.f / D); float s2 = 0.f;
; #pragma unroll
;                     for (int j = 0; j < 8; ++j) { v[j] = v[j] - mean; s2 += (v[j].x * v[j].x + v[j].y * v[j].y) + (v[j].z * v[j].z + v[j].w * v[j].w); }
;                     const float rstd = 1.f / sqrtf(wave_sum(s2) * (1.f / D) + LN_EPS);
; #pragma unroll
;                     for (int j = 0; j < 8; ++j) { const int k = 4 * lq + 256 * j;
;                         const f32x4 xv = v[j] * rstd * *(const GAS f32x4*)(g1 + k) + *(const GAS f32x4*)(b1 + k);
;                         { v2u xo; xo.x = pk2(xv.x, xv.y); xo.y = pk2(xv.z, xv.w); *(GAS v2u*)(x1 + (size_t)m * D + k) = xo; }
	v_and_b32_e32 v143, 0xffff0000, v84
	v_lshlrev_b32_e32 v144, 16, v85
	v_and_b32_e32 v145, 0xffff0000, v85
	s_waitcnt lgkmcnt(0)
	v_add_f32_e32 v32, v60, v32
	ds_bpermute_b32 v33, v194, v32
	s_waitcnt lgkmcnt(0)
	v_add_f32_e32 v32, v32, v33
	ds_bpermute_b32 v33, v195, v32
	s_waitcnt lgkmcnt(0)
	v_add_f32_e32 v60, v32, v33
	ds_bpermute_b32 v88, v196, v60
	v_lshl_add_u64 v[32:33], s[20:21], 0, v[66:67]
	global_load_dwordx2 v[130:131], v[32:33], off offset:512 nt
	global_load_dwordx2 v[120:121], v[32:33], off offset:1024 nt
	global_load_dwordx2 v[114:115], v[32:33], off offset:1536 nt
	global_load_dwordx2 v[106:107], v[32:33], off offset:2048 nt
	global_load_dwordx2 v[132:133], v[32:33], off nt
	global_load_dwordx2 v[110:111], v[44:45], off offset:2560 nt
	global_load_dwordx2 v[102:103], v[44:45], off offset:3072 nt
	global_load_dwordx2 v[100:101], v[44:45], off offset:3584 nt
	global_load_dwordx2 v[122:123], v[32:33], off offset:2560 nt
	global_load_dwordx2 v[116:117], v[32:33], off offset:3072 nt
	global_load_dwordx2 v[108:109], v[32:33], off offset:3584 nt
	s_waitcnt lgkmcnt(0)
	v_add_f32_e32 v60, v60, v88
	ds_bpermute_b32 v66, v197, v60
	v_lshlrev_b64 v[88:89], 1, v[36:37]
	s_waitcnt lgkmcnt(0)
	v_add_f32_e32 v60, v60, v66
	ds_bpermute_b32 v66, v198, v60
	s_waitcnt lgkmcnt(0)
	v_add_f32_e32 v60, v60, v66
	v_fmamk_f32 v60, v60, 0x3a000000, v200
	v_mul_f32_e32 v66, 0x4f800000, v60
	v_cmp_gt_f32_e32 vcc, s85, v60
	s_waitcnt vmcnt(14)
	v_lshlrev_b32_e32 v150, 16, v124
	v_cndmask_b32_e32 v60, v60, v66, vcc
	v_sqrt_f32_e32 v66, v60
	v_and_b32_e32 v151, 0xffff0000, v124
	s_waitcnt vmcnt(11)
	v_lshlrev_b32_e32 v158, 16, v104
	v_and_b32_e32 v159, 0xffff0000, v104
	v_add_u32_e32 v44, -1, v66
	v_fma_f32 v45, -v44, v66, v60
	v_cmp_ge_f32_e64 s[14:15], 0, v45
	v_add_u32_e32 v45, 1, v66
	v_lshlrev_b32_e32 v104, 16, v105
	v_cndmask_b32_e64 v44, v66, v44, s[14:15]
	v_fma_f32 v66, -v45, v66, v60
	v_cmp_lt_f32_e64 s[14:15], 0, v66
	v_and_b32_e32 v105, 0xffff0000, v105
	v_lshlrev_b32_e32 v124, 16, v125
	v_cndmask_b32_e64 v44, v44, v45, s[14:15]
	v_mul_f32_e32 v45, 0x37800000, v44
	v_cndmask_b32_e32 v44, v44, v45, vcc
	v_cmp_class_f32_e32 vcc, v60, v201
	s_waitcnt vmcnt(6)
	v_lshlrev_b32_e32 v146, 16, v132
	v_and_b32_e32 v147, 0xffff0000, v132
	v_cndmask_b32_e32 v44, v44, v60, vcc
	v_div_scale_f32 v45, s[0:1], v44, v44, 1.0
	v_rcp_f32_e32 v60, v45
	s_lshl_b64 s[0:1], s[40:41], 12
	s_add_u32 s0, s3, s0
	s_addc_u32 s1, s39, s1
	v_fma_f32 v32, -v45, v60, 1.0
	v_fmac_f32_e32 v60, v32, v60
	v_div_scale_f32 v32, vcc, 1.0, v44, 1.0
	v_mul_f32_e32 v33, v32, v60
	v_fma_f32 v66, -v45, v33, v32
	v_fmac_f32_e32 v33, v66, v60
	v_fma_f32 v32, -v45, v33, v32
	v_div_fmas_f32 v32, v32, v60, v33
	v_div_fixup_f32 v60, v32, v44, 1.0
	v_pk_mul_f32 v[32:33], v[42:43], v[60:61] op_sel_hi:[1,0]
	v_pk_mul_f32 v[34:35], v[34:35], v[60:61] op_sel_hi:[1,0]
	v_pk_fma_f32 v[96:97], v[80:81], v[32:33], v[96:97]
	v_pk_fma_f32 v[66:67], v[82:83], v[34:35], v[98:99]
	v_bfe_u32 v32, v96, 16, 1
	v_add3_u32 v32, v96, v32, s86
	v_bfe_u32 v33, v97, 16, 1
	v_lshrrev_b32_e32 v32, 16, v32
	v_add3_u32 v33, v97, v33, s86
	v_and_or_b32 v32, v33, s82, v32
	v_bfe_u32 v33, v66, 16, 1
	v_add3_u32 v33, v66, v33, s86
	v_bfe_u32 v34, v67, 16, 1
	v_lshrrev_b32_e32 v33, 16, v33
	v_add3_u32 v34, v67, v34, s86
	v_and_or_b32 v33, v34, s82, v33
	v_lshl_add_u64 v[98:99], s[0:1], 0, v[88:89]
	global_store_dwordx2 v[98:99], v[32:33], off
	v_add_co_u32_e32 v32, vcc, s25, v38
	s_add_u32 s0, s48, s18
	s_nop 0
	v_addc_co_u32_e32 v33, vcc, 0, v39, vcc
	v_add_co_u32_e32 v34, vcc, s26, v38
	s_addc_u32 s1, s49, s19
	s_nop 0
	v_addc_co_u32_e32 v35, vcc, 0, v39, vcc
	global_load_dwordx4 v[42:45], v[32:33], off offset:-4096
	global_load_dwordx4 v[80:83], v[34:35], off offset:-4096
	v_pk_mul_f32 v[46:47], v[46:47], v[60:61] op_sel_hi:[1,0]
	v_pk_mul_f32 v[50:51], v[50:51], v[60:61] op_sel_hi:[1,0]
	v_pk_mul_f32 v[40:41], v[40:41], v[60:61] op_sel_hi:[1,0]
	v_pk_mul_f32 v[70:71], v[70:71], v[60:61] op_sel_hi:[1,0]
	v_pk_mul_f32 v[68:69], v[68:69], v[60:61] op_sel_hi:[1,0]
	v_pk_mul_f32 v[76:77], v[76:77], v[60:61] op_sel_hi:[1,0]
	v_pk_mul_f32 v[78:79], v[78:79], v[60:61] op_sel_hi:[1,0]
	v_pk_mul_f32 v[86:87], v[86:87], v[60:61] op_sel_hi:[1,0]
	v_lshlrev_b32_e32 v148, 16, v133
	v_and_b32_e32 v149, 0xffff0000, v133
	v_lshlrev_b32_e32 v152, 16, v120
	v_and_b32_e32 v153, 0xffff0000, v120
	v_lshlrev_b32_e32 v120, 16, v121
	v_and_b32_e32 v121, 0xffff0000, v121
	s_waitcnt vmcnt(5)
	v_lshlrev_b32_e32 v164, 16, v122
	v_and_b32_e32 v165, 0xffff0000, v122
	v_lshlrev_b32_e32 v122, 16, v123
	v_and_b32_e32 v123, 0xffff0000, v123
	v_pk_mul_f32 v[0:1], v[0:1], v[146:147]
	v_pk_mul_f32 v[10:11], v[10:11], v[120:121]
	v_pk_mul_f32 v[120:121], v[30:31], v[122:123]
	v_lshlrev_b32_e32 v160, 16, v106
	v_and_b32_e32 v161, 0xffff0000, v106
	v_lshlrev_b32_e32 v106, 16, v107
	v_and_b32_e32 v107, 0xffff0000, v107
	v_lshlrev_b32_e32 v166, 16, v102
	v_and_b32_e32 v167, 0xffff0000, v102
	v_lshlrev_b32_e32 v168, 16, v103
	v_and_b32_e32 v169, 0xffff0000, v103
	s_waitcnt vmcnt(4)
	v_lshlrev_b32_e32 v102, 16, v116
	v_and_b32_e32 v103, 0xffff0000, v116
	v_lshlrev_b32_e32 v116, 16, v117
	v_and_b32_e32 v117, 0xffff0000, v117
	v_lshlrev_b32_e32 v170, 16, v100
	v_and_b32_e32 v171, 0xffff0000, v100
	v_lshlrev_b32_e32 v172, 16, v101
	v_and_b32_e32 v173, 0xffff0000, v101
	s_waitcnt vmcnt(3)
; #define GAS __attribute__((address_space(1)))
; __device__ __forceinline__ unsigned pk2(float lo, float hi) { return f2bf(lo) | (f2bf(hi) << 16); }
; __device__ __forceinline__ unsigned pk4_fp8(float a, float b, float c, float d) { int r = __builtin_amdgcn_cvt_pk_fp8_f32(a, b, 0, false); r = __builtin_amdgcn_cvt_pk_fp8_f32(c, d, r, true); return (unsigned)r; }
; template <int l>
; __device__ __forceinline__ void layer_phases(Frame& F, const XcdBarrier& bar, const int lo, const int hi) {
;     ...
;                     const float rstd = 1.f / sqrtf(wave_sum(s2) * (1.f / D) + LN_EPS);
; #pragma unroll
;                     for (int j = 0; j < 8; ++j) { const int k = 4 * lq + 256 * j;
;                         const f32x4 xv = v[j] * rstd * *(const GAS f32x4*)(g1 + k) + *(const GAS f32x4*)(b1 + k);
;                         { v2u xo; xo.x = pk2(xv.x, xv.y); xo.y = pk2(xv.z, xv.w); *(GAS v2u*)(x1 + (size_t)m * D + k) = xo; }
;                         const f32x4 hv = xv * (*(const GAS f32x4*)(mrow + 8192 + k) + 1.0f) + *(const GAS f32x4*)(mrow + 6144 + k);
;                         v2u o; o.x = pk2(hv.x, hv.y); o.y = pk2(hv.z, hv.w);
;                         *(GAS unsigned*)(h2q + (size_t)m * D + k) = pk4_fp8(hv.x, hv.y, hv.z, hv.w);
	v_lshlrev_b32_e32 v100, 16, v108
	v_and_b32_e32 v101, 0xffff0000, v108
	v_pk_mul_f32 v[106:107], v[18:19], v[106:107]
	v_pk_mul_f32 v[116:117], v[26:27], v[116:117]
	v_and_b32_e32 v125, 0xffff0000, v125
	v_lshlrev_b32_e32 v156, 16, v114
	v_and_b32_e32 v157, 0xffff0000, v114
	v_lshlrev_b32_e32 v114, 16, v115
	v_and_b32_e32 v115, 0xffff0000, v115
	v_lshlrev_b32_e32 v108, 16, v109
	v_and_b32_e32 v109, 0xffff0000, v109
	v_pk_mul_f32 v[2:3], v[2:3], v[148:149]
	v_lshlrev_b32_e32 v154, 16, v112
	v_and_b32_e32 v155, 0xffff0000, v112
	v_lshlrev_b32_e32 v112, 16, v113
	v_and_b32_e32 v113, 0xffff0000, v113
	v_lshlrev_b32_e32 v162, 16, v110
	v_and_b32_e32 v163, 0xffff0000, v110
	v_lshlrev_b32_e32 v110, 16, v111
	v_and_b32_e32 v111, 0xffff0000, v111
	v_pk_mul_f32 v[8:9], v[8:9], v[152:153]
	v_pk_mul_f32 v[6:7], v[6:7], v[114:115]
	v_pk_mul_f32 v[122:123], v[28:29], v[164:165]
	v_pk_mul_f32 v[108:109], v[22:23], v[108:109]
	v_pk_fma_f32 v[28:29], v[144:145], s[38:39], v[2:3] op_sel_hi:[1,0,1]
	v_pk_mul_f32 v[4:5], v[4:5], v[156:157]
	v_pk_mul_f32 v[114:115], v[16:17], v[160:161]
	v_pk_fma_f32 v[16:17], v[112:113], s[38:39], v[6:7] op_sel_hi:[1,0,1]
	v_mov_b32_e32 v112, v29
	v_pk_fma_f32 v[18:19], v[154:155], s[38:39], v[4:5] op_sel_hi:[1,0,1]
	v_pk_fma_f32 v[4:5], v[168:169], s[38:39], v[116:117] op_sel_hi:[1,0,1]
	v_pk_mul_f32 v[92:93], v[92:93], v[60:61] op_sel_hi:[1,0]
	v_pk_mul_f32 v[90:91], v[90:91], v[60:61] op_sel_hi:[1,0]
	s_waitcnt vmcnt(1)
	v_pk_add_f32 v[42:43], v[42:43], 1.0 op_sel_hi:[1,0]
	s_waitcnt vmcnt(0)
	v_pk_fma_f32 v[42:43], v[42:43], v[96:97], v[80:81]
	v_mov_b32_e32 v80, 0
	v_cvt_pk_fp8_f32 v80, v42, v43
	v_pk_add_f32 v[44:45], v[44:45], 1.0 op_sel_hi:[1,0]
	v_lshl_add_u64 v[96:97], s[0:1], 0, v[36:37]
	v_pk_fma_f32 v[44:45], v[44:45], v[66:67], v[82:83]
	s_mov_b64 s[0:1], 0x8000
	v_cvt_pk_fp8_f32 v80, v44, v45 op_sel:[0,0,1]
	v_lshl_add_u64 v[82:83], v[38:39], 0, s[0:1]
	s_mov_b64 s[0:1], 0x6000
	global_store_dword v[96:97], v80, off
	global_load_dwordx4 v[134:137], v[72:73], off offset:1024
	global_load_dwordx4 v[138:141], v[74:75], off offset:1024
	v_lshl_add_u64 v[80:81], v[38:39], 0, s[0:1]
	v_pk_mul_f32 v[38:39], v[48:49], v[60:61] op_sel_hi:[1,0]
	s_lshl_b64 s[0:1], s[42:43], 12
	s_add_u32 s0, s3, s0
	s_addc_u32 s1, s39, s1
	s_waitcnt vmcnt(0)
	v_pk_fma_f32 v[38:39], v[134:135], v[38:39], v[138:139]
	v_pk_fma_f32 v[66:67], v[136:137], v[46:47], v[140:141]
	v_bfe_u32 v46, v38, 16, 1
	v_add3_u32 v46, v38, v46, s86
	v_bfe_u32 v47, v39, 16, 1
	v_lshrrev_b32_e32 v46, 16, v46
	v_add3_u32 v47, v39, v47, s86
	v_and_or_b32 v46, v47, s82, v46
	v_bfe_u32 v47, v66, 16, 1
	v_add3_u32 v47, v66, v47, s86
	v_bfe_u32 v48, v67, 16, 1
	v_lshrrev_b32_e32 v47, 16, v47
	v_add3_u32 v48, v67, v48, s86
	v_and_or_b32 v47, v48, s82, v47
	global_store_dwordx2 v[98:99], v[46:47], off offset:512
	global_load_dwordx4 v[46:49], v[82:83], off offset:1024
	s_nop 0
	global_load_dwordx4 v[134:137], v[80:81], off offset:1024
	v_mov_b32_e32 v138, 0
	s_waitcnt vmcnt(1)
	v_pk_add_f32 v[46:47], v[46:47], 1.0 op_sel_hi:[1,0]
	s_waitcnt vmcnt(0)
	v_pk_fma_f32 v[46:47], v[46:47], v[38:39], v[134:135]
	v_pk_add_f32 v[38:39], v[48:49], 1.0 op_sel_hi:[1,0]
	v_cvt_pk_fp8_f32 v138, v46, v47
	v_pk_fma_f32 v[48:49], v[38:39], v[66:67], v[136:137]
	v_pk_mul_f32 v[38:39], v[62:63], v[60:61] op_sel_hi:[1,0]
	v_cvt_pk_fp8_f32 v138, v48, v49 op_sel:[0,0,1]
	global_store_dword v[96:97], v138, off offset:256
	global_load_dwordx4 v[134:137], v[72:73], off offset:2048
	s_nop 0
	global_load_dwordx4 v[138:141], v[74:75], off offset:2048
	s_waitcnt vmcnt(0)
	v_pk_fma_f32 v[62:63], v[136:137], v[50:51], v[140:141]
	v_pk_fma_f32 v[38:39], v[134:135], v[38:39], v[138:139]
	v_bfe_u32 v66, v62, 16, 1
	v_bfe_u32 v50, v38, 16, 1
	v_bfe_u32 v51, v39, 16, 1
	v_bfe_u32 v67, v63, 16, 1
	v_add3_u32 v50, v38, v50, s86
	v_add3_u32 v66, v62, v66, s86
	v_add3_u32 v51, v39, v51, s86
	v_add3_u32 v67, v63, v67, s86
	v_lshrrev_b32_e32 v50, 16, v50
	v_lshrrev_b32_e32 v66, 16, v66
	v_and_or_b32 v50, v51, s82, v50
	v_and_or_b32 v51, v67, s82, v66
	global_store_dwordx2 v[98:99], v[50:51], off offset:1024
	global_load_dwordx4 v[134:137], v[82:83], off offset:2048
	global_load_dwordx4 v[138:141], v[80:81], off offset:2048
	v_mov_b32_e32 v66, 0
	s_waitcnt vmcnt(1)
	v_pk_add_f32 v[50:51], v[134:135], 1.0 op_sel_hi:[1,0]
	s_waitcnt vmcnt(0)
	v_pk_fma_f32 v[50:51], v[50:51], v[38:39], v[138:139]
	v_pk_add_f32 v[38:39], v[136:137], 1.0 op_sel_hi:[1,0]
	v_cvt_pk_fp8_f32 v66, v50, v51
	v_pk_fma_f32 v[62:63], v[38:39], v[62:63], v[140:141]
	v_pk_mul_f32 v[38:39], v[64:65], v[60:61] op_sel_hi:[1,0]
	v_cvt_pk_fp8_f32 v66, v62, v63 op_sel:[0,0,1]
	global_store_dword v[96:97], v66, off offset:512
	global_load_dwordx4 v[134:137], v[72:73], off offset:3072
	global_load_dwordx4 v[138:141], v[74:75], off offset:3072
	s_waitcnt vmcnt(0)
	v_pk_fma_f32 v[136:137], v[40:41], v[136:137], v[140:141]
	v_pk_fma_f32 v[134:135], v[38:39], v[134:135], v[138:139]
	v_bfe_u32 v40, v136, 16, 1
	v_bfe_u32 v38, v134, 16, 1
	v_bfe_u32 v39, v135, 16, 1
	v_bfe_u32 v41, v137, 16, 1
	v_add3_u32 v38, v134, v38, s86
	v_add3_u32 v40, v136, v40, s86
	v_add3_u32 v39, v135, v39, s86
	v_add3_u32 v41, v137, v41, s86
	v_lshrrev_b32_e32 v38, 16, v38
	v_lshrrev_b32_e32 v40, 16, v40
	v_and_or_b32 v38, v39, s82, v38
	v_and_or_b32 v39, v41, s82, v40
	global_store_dwordx2 v[98:99], v[38:39], off offset:1536
	global_load_dwordx4 v[38:41], v[82:83], off offset:3072
	s_nop 0
	global_load_dwordx4 v[64:67], v[80:81], off offset:3072
	v_mov_b32_e32 v138, 0
	s_waitcnt vmcnt(1)
	v_pk_add_f32 v[38:39], v[38:39], 1.0 op_sel_hi:[1,0]
	s_waitcnt vmcnt(0)
; #define GAS __attribute__((address_space(1)))
; __device__ __forceinline__ unsigned pk2(float lo, float hi) { return f2bf(lo) | (f2bf(hi) << 16); }
; __device__ __forceinline__ unsigned pk4_fp8(float a, float b, float c, float d) { int r = __builtin_amdgcn_cvt_pk_fp8_f32(a, b, 0, false); r = __builtin_amdgcn_cvt_pk_fp8_f32(c, d, r, true); return (unsigned)r; }
; template <int l>
; __device__ __forceinline__ void layer_phases(Frame& F, const XcdBarrier& bar, const int lo, const int hi) {
;     ...
;                     for (int j = 0; j < 8; ++j) { const int k = 4 * lq + 256 * j;
;                         const f32x4 xv = v[j] * rstd * *(const GAS f32x4*)(g1 + k) + *(const GAS f32x4*)(b1 + k);
;                         { v2u xo; xo.x = pk2(xv.x, xv.y); xo.y = pk2(xv.z, xv.w); *(GAS v2u*)(x1 + (size_t)m * D + k) = xo; }
;                         const f32x4 hv = xv * (*(const GAS f32x4*)(mrow + 8192 + k) + 1.0f) + *(const GAS f32x4*)(mrow + 6144 + k);
;                         v2u o; o.x = pk2(hv.x, hv.y); o.y = pk2(hv.z, hv.w);
;                         *(GAS unsigned*)(h2q + (size_t)m * D + k) = pk4_fp8(hv.x, hv.y, hv.z, hv.w);
;                         const int chunk = (lq >> 1) + 32 * j;
	v_pk_fma_f32 v[64:65], v[134:135], v[38:39], v[64:65]
	v_pk_add_f32 v[40:41], v[40:41], 1.0 op_sel_hi:[1,0]
	v_cvt_pk_fp8_f32 v138, v64, v65
	v_pk_fma_f32 v[66:67], v[136:137], v[40:41], v[66:67]
	v_add_co_u32_e32 v38, vcc, s87, v72
	v_cvt_pk_fp8_f32 v138, v66, v67 op_sel:[0,0,1]
	s_nop 0
	v_addc_co_u32_e32 v39, vcc, 0, v73, vcc
	v_add_co_u32_e32 v40, vcc, s87, v74
	global_store_dword v[96:97], v138, off offset:768
	s_nop 0
	v_addc_co_u32_e32 v41, vcc, 0, v75, vcc
	global_load_dwordx4 v[134:137], v[38:39], off
	global_load_dwordx4 v[138:141], v[40:41], off
	s_waitcnt vmcnt(0)
	v_pk_fma_f32 v[140:141], v[68:69], v[136:137], v[140:141]
	v_pk_fma_f32 v[138:139], v[70:71], v[134:135], v[138:139]
	v_bfe_u32 v70, v140, 16, 1
	v_bfe_u32 v68, v138, 16, 1
	v_bfe_u32 v69, v139, 16, 1
	v_bfe_u32 v71, v141, 16, 1
	v_add3_u32 v68, v138, v68, s86
	v_add3_u32 v70, v140, v70, s86
	v_add3_u32 v69, v139, v69, s86
	v_add3_u32 v71, v141, v71, s86
	v_lshrrev_b32_e32 v68, 16, v68
	v_lshrrev_b32_e32 v70, 16, v70
	v_and_or_b32 v68, v69, s82, v68
	v_and_or_b32 v69, v71, s82, v70
	global_store_dwordx2 v[98:99], v[68:69], off offset:2048
	global_load_dwordx4 v[68:71], v[32:33], off
	s_nop 0
	global_load_dwordx4 v[134:137], v[34:35], off
	s_waitcnt vmcnt(1)
	v_pk_add_f32 v[68:69], v[68:69], 1.0 op_sel_hi:[1,0]
	s_waitcnt vmcnt(0)
	v_pk_fma_f32 v[68:69], v[138:139], v[68:69], v[134:135]
	v_pk_add_f32 v[70:71], v[70:71], 1.0 op_sel_hi:[1,0]
	v_cvt_pk_fp8_f32 v142, v68, v69
	v_pk_fma_f32 v[70:71], v[140:141], v[70:71], v[136:137]
	s_nop 0
	v_cvt_pk_fp8_f32 v142, v70, v71 op_sel:[0,0,1]
	global_store_dword v[96:97], v142, off offset:1024
	global_load_dwordx4 v[134:137], v[38:39], off offset:1024
	global_load_dwordx4 v[138:141], v[40:41], off offset:1024
	v_mov_b32_e32 v142, 0
	s_waitcnt vmcnt(0)
	v_pk_fma_f32 v[140:141], v[78:79], v[136:137], v[140:141]
	v_pk_fma_f32 v[138:139], v[76:77], v[134:135], v[138:139]
	v_bfe_u32 v78, v140, 16, 1
	v_bfe_u32 v76, v138, 16, 1
	v_bfe_u32 v77, v139, 16, 1
	v_bfe_u32 v79, v141, 16, 1
	v_add3_u32 v76, v138, v76, s86
	v_add3_u32 v78, v140, v78, s86
	v_add3_u32 v77, v139, v77, s86
	v_add3_u32 v79, v141, v79, s86
	v_lshrrev_b32_e32 v76, 16, v76
	v_lshrrev_b32_e32 v78, 16, v78
	v_and_or_b32 v76, v77, s82, v76
	v_and_or_b32 v77, v79, s82, v78
	global_store_dwordx2 v[98:99], v[76:77], off offset:2560
	global_load_dwordx4 v[76:79], v[32:33], off offset:1024
	s_nop 0
	global_load_dwordx4 v[134:137], v[34:35], off offset:1024
	s_waitcnt vmcnt(1)
	v_pk_add_f32 v[76:77], v[76:77], 1.0 op_sel_hi:[1,0]
	s_waitcnt vmcnt(0)
	v_pk_fma_f32 v[76:77], v[138:139], v[76:77], v[134:135]
	v_pk_add_f32 v[78:79], v[78:79], 1.0 op_sel_hi:[1,0]
	v_cvt_pk_fp8_f32 v142, v76, v77
	v_pk_fma_f32 v[78:79], v[140:141], v[78:79], v[136:137]
	s_nop 0
	v_cvt_pk_fp8_f32 v142, v78, v79 op_sel:[0,0,1]
	global_store_dword v[96:97], v142, off offset:1280
	global_load_dwordx4 v[134:137], v[38:39], off offset:2048
	global_load_dwordx4 v[138:141], v[40:41], off offset:2048
	v_lshlrev_b32_e32 v142, 16, v84
	v_pk_mul_f32 v[84:85], v[94:95], v[60:61] op_sel_hi:[1,0]
	v_pk_fma_f32 v[30:31], v[142:143], s[38:39], v[0:1] op_sel_hi:[1,0,1]
	s_waitcnt vmcnt(0)
	v_pk_fma_f32 v[94:95], v[86:87], v[136:137], v[140:141]
	v_pk_fma_f32 v[136:137], v[84:85], v[134:135], v[138:139]
	v_bfe_u32 v86, v94, 16, 1
	v_bfe_u32 v84, v136, 16, 1
	v_bfe_u32 v85, v137, 16, 1
	v_bfe_u32 v87, v95, 16, 1
	v_add3_u32 v84, v136, v84, s86
	v_add3_u32 v86, v94, v86, s86
	v_add3_u32 v85, v137, v85, s86
	v_add3_u32 v87, v95, v87, s86
	v_lshrrev_b32_e32 v84, 16, v84
	v_lshrrev_b32_e32 v86, 16, v86
	v_and_or_b32 v84, v85, s82, v84
	v_and_or_b32 v85, v87, s82, v86
	global_store_dwordx2 v[98:99], v[84:85], off offset:3072
	global_load_dwordx4 v[84:87], v[32:33], off offset:2048
	s_nop 0
	global_load_dwordx4 v[132:135], v[34:35], off offset:2048
	v_lshlrev_b32_e32 v138, 16, v130
	v_and_b32_e32 v139, 0xffff0000, v130
	v_lshlrev_b32_e32 v130, 16, v131
	v_and_b32_e32 v131, 0xffff0000, v131
	v_pk_mul_f32 v[12:13], v[12:13], v[138:139]
	v_pk_mul_f32 v[14:15], v[14:15], v[130:131]
	v_pk_mul_f32 v[130:131], v[24:25], v[102:103]
	v_pk_mul_f32 v[138:139], v[20:21], v[100:101]
	v_pk_fma_f32 v[26:27], v[150:151], s[38:39], v[12:13] op_sel_hi:[1,0,1]
	v_pk_fma_f32 v[12:13], v[104:105], s[38:39], v[106:107] op_sel_hi:[1,0,1]
	v_lshlrev_b32_e32 v140, 16, v118
	v_and_b32_e32 v141, 0xffff0000, v118
	v_lshlrev_b32_e32 v118, 16, v119
	v_and_b32_e32 v119, 0xffff0000, v119
	v_pk_fma_f32 v[24:25], v[124:125], s[38:39], v[14:15] op_sel_hi:[1,0,1]
	v_pk_fma_f32 v[20:21], v[118:119], s[38:39], v[10:11] op_sel_hi:[1,0,1]
	v_pk_fma_f32 v[22:23], v[140:141], s[38:39], v[8:9] op_sel_hi:[1,0,1]
	v_pk_fma_f32 v[10:11], v[110:111], s[38:39], v[120:121] op_sel_hi:[1,0,1]
	v_mov_b32_e32 v110, v28
	v_mov_b32_e32 v111, v24
	v_mov_b32_e32 v113, v25
	v_pk_fma_f32 v[14:15], v[158:159], s[38:39], v[114:115] op_sel_hi:[1,0,1]
	v_pk_mov_b32 v[114:115], v[22:23], v[20:21] op_sel:[1,0]
	v_mov_b32_e32 v116, v22
	v_mov_b32_e32 v117, v21
	v_pk_fma_f32 v[8:9], v[162:163], s[38:39], v[122:123] op_sel_hi:[1,0,1]
	v_add_f32_e32 v118, v18, v19
	v_add_f32_e32 v120, v16, v17
	v_mov_b32_e32 v123, v14
	v_mov_b32_e32 v119, v12
	v_mov_b32_e32 v121, v13
	v_pk_fma_f32 v[6:7], v[166:167], s[38:39], v[130:131] op_sel_hi:[1,0,1]
	v_pk_mov_b32 v[124:125], v[8:9], v[10:11] op_sel:[1,0]
	v_mov_b32_e32 v130, v8
	v_mov_b32_e32 v131, v11
	v_pk_fma_f32 v[2:3], v[170:171], s[38:39], v[138:139] op_sel_hi:[1,0,1]
	s_waitcnt vmcnt(1)
	v_pk_add_f32 v[0:1], v[84:85], 1.0 op_sel_hi:[1,0]
	s_waitcnt vmcnt(0)
; #define GAS __attribute__((address_space(1)))
; __device__ __forceinline__ unsigned pk2(float lo, float hi) { return f2bf(lo) | (f2bf(hi) << 16); }
; __device__ __forceinline__ unsigned pk4_fp8(float a, float b, float c, float d) { int r = __builtin_amdgcn_cvt_pk_fp8_f32(a, b, 0, false); r = __builtin_amdgcn_cvt_pk_fp8_f32(c, d, r, true); return (unsigned)r; }
; __device__ __forceinline__ f32x4 bf4(unsigned a, unsigned b) { return (f32x4){bflo(a), bfhi(a), bflo(b), bfhi(b)}; }
; template <int l>
; __device__ __forceinline__ void layer_phases(Frame& F, const XcdBarrier& bar, const int lo, const int hi) {
;     ...
;                         f32x4 xv; if (l == 0) xv = __builtin_nontemporal_load((const GAS f32x4*)(xin + off)); else { const v2u xw_ = __builtin_nontemporal_load((const GAS v2u*)(xinb + off)); xv = bf4(xw_.x, xw_.y); } const v2u mw = __builtin_nontemporal_load((const GAS v2u*)(mixb + off)); const f32x4 gv = *(const GAS f32x4*)(mrow + 4096 + 4 * lq + 256 * j);
;                         vv[rr][j] = xv * ALPHA + gv * (f32x4){bflo(mw.x), bfhi(mw.x), bflo(mw.y), bfhi(mw.y)}; }
; #pragma unroll
;                 for (int rq = 0; rq < 2; ++rq) { const int rr = 2 * rp + rq, m = m0 + rr, rloc = 4 * F.wave + rr;
;                     f32x4 (&v)[8] = vv[rq]; float s = 0.f;
; #pragma unroll
;                     for (int j = 0; j < 8; ++j) s += (v[j].x + v[j].y) + (v[j].z + v[j].w);
;                     const float mean = wave_sum(s) * (1.f / D); float s2 = 0.f;
; #pragma unroll
;                     for (int j = 0; j < 8; ++j) { v[j] = v[j] - mean; s2 += (v[j].x * v[j].x + v[j].y * v[j].y) + (v[j].z * v[j].z + v[j].w * v[j].w); }
;                     const float rstd = 1.f / sqrtf(wave_sum(s2) * (1.f / D) + LN_EPS);
; #pragma unroll
;                     for (int j = 0; j < 8; ++j) { const int k = 4 * lq + 256 * j;
;                         const f32x4 xv = v[j] * rstd * *(const GAS f32x4*)(g1 + k) + *(const GAS f32x4*)(b1 + k);
;                         { v2u xo; xo.x = pk2(xv.x, xv.y); xo.y = pk2(xv.z, xv.w); *(GAS v2u*)(x1 + (size_t)m * D + k) = xo; }
;                         const f32x4 hv = xv * (*(const GAS f32x4*)(mrow + 8192 + k) + 1.0f) + *(const GAS f32x4*)(mrow + 6144 + k);
;                         v2u o; o.x = pk2(hv.x, hv.y); o.y = pk2(hv.z, hv.w);
;                         *(GAS unsigned*)(h2q + (size_t)m * D + k) = pk4_fp8(hv.x, hv.y, hv.z, hv.w);
	v_pk_fma_f32 v[84:85], v[136:137], v[0:1], v[132:133]
	v_pk_add_f32 v[0:1], v[86:87], 1.0 op_sel_hi:[1,0]
	v_cvt_pk_fp8_f32 v174, v84, v85
	v_pk_fma_f32 v[86:87], v[94:95], v[0:1], v[134:135]
	v_pk_fma_f32 v[0:1], v[172:173], s[38:39], v[108:109] op_sel_hi:[1,0,1]
	v_mov_b32_e32 v94, v30
	v_cvt_pk_fp8_f32 v174, v86, v87 op_sel:[0,0,1]
	v_mov_b32_e32 v95, v26
	v_mov_b32_e32 v108, v31
	v_mov_b32_e32 v109, v27
	global_store_dword v[96:97], v174, off offset:1536
	global_load_dwordx4 v[100:103], v[38:39], off offset:3072
	global_load_dwordx4 v[104:107], v[40:41], off offset:3072
	v_pk_add_f32 v[94:95], v[94:95], v[108:109]
	v_pk_add_f32 v[108:109], v[110:111], v[112:113]
	v_pk_add_f32 v[110:111], v[114:115], v[116:117]
	v_pk_add_f32 v[94:95], v[94:95], v[108:109]
	v_pk_add_f32 v[108:109], v[110:111], v[110:111] op_sel:[0,1] op_sel_hi:[1,0]
	v_add_f32_e32 v94, 0, v94
	v_mov_b32_e32 v109, v15
	v_add_f32_e32 v122, v94, v95
	v_pk_add_f32 v[112:113], v[118:119], v[120:121]
	v_pk_add_f32 v[94:95], v[122:123], v[108:109]
	v_pk_add_f32 v[114:115], v[124:125], v[130:131]
	v_pk_add_f32 v[94:95], v[94:95], v[112:113]
	v_pk_add_f32 v[110:111], v[114:115], v[114:115] op_sel:[0,1] op_sel_hi:[1,0]
	v_pk_add_f32 v[94:95], v[94:95], v[94:95] op_sel:[0,1] op_sel_hi:[1,0]
	v_add_f32_e32 v132, v6, v7
	v_add_f32_e32 v134, v4, v5
	v_mov_b32_e32 v133, v0
	v_mov_b32_e32 v135, v1
	v_mov_b32_e32 v111, v3
	v_mov_b32_e32 v95, v2
	v_pk_add_f32 v[116:117], v[132:133], v[134:135]
	v_pk_add_f32 v[94:95], v[94:95], v[110:111]
	v_mov_b32_e32 v125, 0
	v_pk_add_f32 v[94:95], v[94:95], v[116:117]
	s_nop 0
	v_add_f32_e32 v94, v94, v95
	ds_bpermute_b32 v95, v53, v94
	s_waitcnt lgkmcnt(0)
	v_add_f32_e32 v94, v94, v95
	ds_bpermute_b32 v95, v194, v94
	s_waitcnt lgkmcnt(0)
	v_add_f32_e32 v94, v94, v95
	ds_bpermute_b32 v95, v195, v94
	s_waitcnt lgkmcnt(0)
	v_add_f32_e32 v94, v94, v95
	ds_bpermute_b32 v95, v196, v94
	s_waitcnt lgkmcnt(0)
	v_add_f32_e32 v94, v94, v95
	ds_bpermute_b32 v95, v197, v94
	s_waitcnt lgkmcnt(0)
	v_add_f32_e32 v108, v94, v95
	s_waitcnt vmcnt(0)
	v_pk_fma_f32 v[94:95], v[90:91], v[102:103], v[106:107]
	v_pk_fma_f32 v[102:103], v[92:93], v[100:101], v[104:105]
	v_bfe_u32 v91, v94, 16, 1
	v_bfe_u32 v60, v102, 16, 1
	v_bfe_u32 v90, v103, 16, 1
	v_bfe_u32 v92, v95, 16, 1
	v_add3_u32 v60, v102, v60, s86
	v_add3_u32 v91, v94, v91, s86
	v_add3_u32 v90, v103, v90, s86
	v_add3_u32 v92, v95, v92, s86
	v_lshrrev_b32_e32 v60, 16, v60
	v_lshrrev_b32_e32 v91, 16, v91
	v_and_or_b32 v90, v90, s82, v60
	v_and_or_b32 v91, v92, s82, v91
	global_store_dwordx2 v[98:99], v[90:91], off offset:3584
	global_load_dwordx4 v[90:93], v[32:33], off offset:3072
	s_nop 0
	global_load_dwordx4 v[98:101], v[34:35], off offset:3072
	ds_bpermute_b32 v60, v198, v108
	s_waitcnt lgkmcnt(0)
	v_add_f32_e32 v60, v108, v60
	v_fmamk_f32 v9, v60, 0xba000000, v9
	v_fmac_f32_e32 v8, 0xba000000, v60
	v_fmamk_f32 v11, v60, 0xba000000, v11
	v_fmac_f32_e32 v10, 0xba000000, v60
	v_fmac_f32_e32 v6, 0xba000000, v60
	v_fmac_f32_e32 v4, 0xba000000, v60
	v_fmamk_f32 v7, v60, 0xba000000, v7
	v_fmamk_f32 v5, v60, 0xba000000, v5
	v_pk_mul_f32 v[118:119], v[10:11], v[10:11]
	v_pk_mul_f32 v[120:121], v[8:9], v[8:9]
	v_mul_f32_e32 v122, v6, v6
	v_mul_f32_e32 v124, v4, v4
	v_pk_mov_b32 v[132:133], v[120:121], v[118:119] op_sel:[1,0]
	v_mov_b32_e32 v121, v119
	v_pk_fma_f32 v[118:119], v[6:7], v[6:7], v[122:123] op_sel_hi:[1,1,0]
	v_pk_fma_f32 v[122:123], v[4:5], v[4:5], v[124:125] op_sel_hi:[1,1,0]
	v_fmamk_f32 v29, v60, 0xba000000, v29
	v_fmamk_f32 v31, v60, 0xba000000, v31
	v_fmamk_f32 v25, v60, 0xba000000, v25
	v_fmamk_f32 v27, v60, 0xba000000, v27
	v_fmac_f32_e32 v28, 0xba000000, v60
	v_fmac_f32_e32 v30, 0xba000000, v60
	v_fmac_f32_e32 v24, 0xba000000, v60
	v_fmac_f32_e32 v26, 0xba000000, v60
	v_fmamk_f32 v23, v60, 0xba000000, v23
	v_fmac_f32_e32 v22, 0xba000000, v60
	v_fmamk_f32 v21, v60, 0xba000000, v21
	v_fmac_f32_e32 v20, 0xba000000, v60
	v_mov_b32_e32 v106, v31
	v_mov_b32_e32 v107, v27
	v_mov_b32_e32 v110, v29
	v_mov_b32_e32 v111, v25
	v_mov_b32_e32 v104, v30
	v_mov_b32_e32 v105, v26
	v_mov_b32_e32 v108, v28
	v_mov_b32_e32 v109, v24
	v_pk_mul_f32 v[112:113], v[20:21], v[20:21]
	v_pk_mul_f32 v[114:115], v[22:23], v[22:23]
	v_pk_mul_f32 v[106:107], v[106:107], v[106:107]
	v_pk_mul_f32 v[110:111], v[110:111], v[110:111]
	v_fmac_f32_e32 v18, 0xba000000, v60
	v_fmac_f32_e32 v16, 0xba000000, v60
	v_pk_mov_b32 v[130:131], v[114:115], v[112:113] op_sel:[1,0]
	v_mov_b32_e32 v115, v113
	v_pk_fma_f32 v[104:105], v[104:105], v[104:105], v[106:107]
	v_pk_fma_f32 v[106:107], v[108:109], v[108:109], v[110:111]
	v_fmamk_f32 v19, v60, 0xba000000, v19
	v_fmamk_f32 v17, v60, 0xba000000, v17
	v_fmamk_f32 v13, v60, 0xba000000, v13
	v_fmac_f32_e32 v12, 0xba000000, v60
	v_fmamk_f32 v15, v60, 0xba000000, v15
	v_fmac_f32_e32 v14, 0xba000000, v60
	v_fmamk_f32 v1, v60, 0xba000000, v1
	v_fmac_f32_e32 v0, 0xba000000, v60
	v_fmamk_f32 v3, v60, 0xba000000, v3
	v_fmac_f32_e32 v2, 0xba000000, v60
	v_mul_f32_e32 v60, v18, v18
	v_mul_f32_e32 v116, v16, v16
	v_pk_add_f32 v[108:109], v[130:131], v[114:115]
	v_pk_add_f32 v[104:105], v[104:105], v[106:107]
	v_pk_fma_f32 v[112:113], v[18:19], v[18:19], v[60:61] op_sel_hi:[1,1,0]
	v_pk_fma_f32 v[116:117], v[16:17], v[16:17], v[116:117] op_sel_hi:[1,1,0]
	v_pk_add_f32 v[106:107], v[108:109], v[108:109] op_sel_hi:[0,1]
	v_pk_add_f32 v[104:105], v[104:105], v[104:105] op_sel_hi:[0,1]
	v_mul_f32_e32 v112, v14, v14
	v_mul_f32_e32 v116, v15, v15
	v_mul_f32_e32 v106, v12, v12
	v_mul_f32_e32 v104, v13, v13
	v_pk_add_f32 v[108:109], v[112:113], v[116:117]
	v_pk_add_f32 v[110:111], v[132:133], v[120:121]
	v_mul_f32_e32 v118, v2, v2
	v_pk_add_f32 v[110:111], v[110:111], v[110:111] op_sel_hi:[0,1]
	s_waitcnt vmcnt(1)
; #define GAS __attribute__((address_space(1)))
; #define LAS __attribute__((address_space(3)))
; __device__ __forceinline__ unsigned pk2(float lo, float hi) { return f2bf(lo) | (f2bf(hi) << 16); }
; __device__ __forceinline__ unsigned pk4_fp8(float a, float b, float c, float d) { int r = __builtin_amdgcn_cvt_pk_fp8_f32(a, b, 0, false); r = __builtin_amdgcn_cvt_pk_fp8_f32(c, d, r, true); return (unsigned)r; }
; template <int l>
; __device__ __forceinline__ void layer_phases(Frame& F, const XcdBarrier& bar, const int lo, const int hi) {
;     ...
;                     f32x4 (&v)[8] = vv[rq]; float s = 0.f;
; #pragma unroll
;                     for (int j = 0; j < 8; ++j) s += (v[j].x + v[j].y) + (v[j].z + v[j].w);
;                     const float mean = wave_sum(s) * (1.f / D); float s2 = 0.f;
; #pragma unroll
;                     for (int j = 0; j < 8; ++j) { v[j] = v[j] - mean; s2 += (v[j].x * v[j].x + v[j].y * v[j].y) + (v[j].z * v[j].z + v[j].w * v[j].w); }
;                     const float rstd = 1.f / sqrtf(wave_sum(s2) * (1.f / D) + LN_EPS);
; #pragma unroll
;                     for (int j = 0; j < 8; ++j) { const int k = 4 * lq + 256 * j;
;                         const f32x4 xv = v[j] * rstd * *(const GAS f32x4*)(g1 + k) + *(const GAS f32x4*)(b1 + k);
;                         { v2u xo; xo.x = pk2(xv.x, xv.y); xo.y = pk2(xv.z, xv.w); *(GAS v2u*)(x1 + (size_t)m * D + k) = xo; }
;                         const f32x4 hv = xv * (*(const GAS f32x4*)(mrow + 8192 + k) + 1.0f) + *(const GAS f32x4*)(mrow + 6144 + k);
;                         v2u o; o.x = pk2(hv.x, hv.y); o.y = pk2(hv.z, hv.w);
;                         *(GAS unsigned*)(h2q + (size_t)m * D + k) = pk4_fp8(hv.x, hv.y, hv.z, hv.w);
;                         const int chunk = (lq >> 1) + 32 * j;
;                         *(LAS v2u*)(h2s + rloc * 4096 + ((chunk ^ (rloc & 15)) << 4) + (lq & 1) * 8) = o; }
	v_pk_add_f32 v[90:91], v[90:91], 1.0 op_sel_hi:[1,0]
	v_pk_add_f32 v[92:93], v[92:93], 1.0 op_sel_hi:[1,0]
	s_waitcnt vmcnt(0)
	v_pk_fma_f32 v[90:91], v[102:103], v[90:91], v[98:99]
	v_pk_fma_f32 v[92:93], v[94:95], v[92:93], v[100:101]
	v_cvt_pk_fp8_f32 v125, v90, v91
	v_pk_add_f32 v[102:103], v[106:107], v[104:105]
	v_mul_f32_e32 v122, v3, v3
	v_pk_add_f32 v[102:103], v[108:109], v[102:103]
	v_cvt_pk_fp8_f32 v125, v92, v93 op_sel:[0,0,1]
	v_pk_add_f32 v[102:103], v[102:103], v[102:103] op_sel_hi:[0,1]
	v_mul_f32_e32 v110, v0, v0
	v_mul_f32_e32 v102, v1, v1
	global_store_dword v[96:97], v125, off offset:1792
	global_load_dwordx4 v[94:97], v[72:73], off
	s_nop 0
	global_load_dwordx4 v[98:101], v[74:75], off
	v_pk_add_f32 v[112:113], v[118:119], v[122:123]
	v_pk_add_f32 v[102:103], v[110:111], v[102:103]
	v_lshl_add_u64 v[122:123], s[0:1], 0, v[88:89]
	v_pk_add_f32 v[102:103], v[112:113], v[102:103]
	s_add_u32 s0, s48, s16
	v_add_f32_e32 v60, v102, v103
	ds_bpermute_b32 v102, v53, v60
	s_addc_u32 s1, s49, s17
	s_or_b32 s44, s40, 2
	s_ashr_i32 s45, s44, 31
	s_lshl_b64 s[18:19], s[44:45], 11
	s_waitcnt lgkmcnt(0)
	v_add_f32_e32 v60, v60, v102
	ds_bpermute_b32 v102, v194, v60
	s_or_b32 s46, s40, 3
	s_ashr_i32 s47, s46, 31
	s_lshl_b64 s[16:17], s[46:47], 11
	s_waitcnt lgkmcnt(0)
	v_add_f32_e32 v60, v60, v102
	ds_bpermute_b32 v102, v195, v60
	s_waitcnt lgkmcnt(0)
	v_add_f32_e32 v60, v60, v102
	ds_bpermute_b32 v102, v196, v60
	s_waitcnt lgkmcnt(0)
	v_add_f32_e32 v60, v60, v102
	ds_bpermute_b32 v102, v197, v60
	s_waitcnt lgkmcnt(0)
	v_add_f32_e32 v60, v60, v102
	ds_bpermute_b32 v102, v198, v60
	s_waitcnt lgkmcnt(0)
	v_add_f32_e32 v60, v60, v102
	v_fmamk_f32 v60, v60, 0x3a000000, v200
	v_mul_f32_e32 v102, 0x4f800000, v60
	v_cmp_gt_f32_e32 vcc, s85, v60
	s_nop 1
	v_cndmask_b32_e32 v60, v60, v102, vcc
	v_sqrt_f32_e32 v102, v60
	s_nop 0
	v_add_u32_e32 v103, -1, v102
	v_add_u32_e32 v104, 1, v102
	v_fma_f32 v105, -v103, v102, v60
	v_fma_f32 v106, -v104, v102, v60
	v_cmp_ge_f32_e64 s[14:15], 0, v105
	s_nop 1
	v_cndmask_b32_e64 v102, v102, v103, s[14:15]
	v_cmp_lt_f32_e64 s[14:15], 0, v106
	s_nop 1
	v_cndmask_b32_e64 v102, v102, v104, s[14:15]
	v_mul_f32_e32 v103, 0x37800000, v102
	v_cndmask_b32_e32 v102, v102, v103, vcc
	v_cmp_class_f32_e32 vcc, v60, v201
	s_nop 1
	v_cndmask_b32_e32 v60, v102, v60, vcc
	v_div_scale_f32 v102, s[14:15], v60, v60, 1.0
	v_rcp_f32_e32 v103, v102
	v_div_scale_f32 v104, vcc, 1.0, v60, 1.0
	v_fma_f32 v105, -v102, v103, 1.0
	v_fmac_f32_e32 v103, v105, v103
	v_mul_f32_e32 v105, v104, v103
	v_fma_f32 v106, -v102, v105, v104
	v_fmac_f32_e32 v105, v106, v103
	v_fma_f32 v102, -v102, v105, v104
	v_div_fmas_f32 v102, v102, v103, v105
	v_div_fixup_f32 v60, v102, v60, 1.0
	v_pk_mul_f32 v[30:31], v[30:31], v[60:61] op_sel_hi:[1,0]
	v_pk_mul_f32 v[28:29], v[28:29], v[60:61] op_sel_hi:[1,0]
	s_waitcnt vmcnt(0)
	v_pk_fma_f32 v[98:99], v[94:95], v[30:31], v[98:99]
	v_pk_fma_f32 v[100:101], v[96:97], v[28:29], v[100:101]
	v_bfe_u32 v28, v98, 16, 1
	v_bfe_u32 v30, v100, 16, 1
	v_bfe_u32 v29, v99, 16, 1
	v_bfe_u32 v31, v101, 16, 1
	v_add3_u32 v28, v98, v28, s86
	v_add3_u32 v30, v100, v30, s86
	v_add3_u32 v29, v99, v29, s86
	v_add3_u32 v31, v101, v31, s86
	v_lshrrev_b32_e32 v28, 16, v28
	v_lshrrev_b32_e32 v30, 16, v30
	v_and_or_b32 v28, v29, s82, v28
	v_and_or_b32 v29, v31, s82, v30
	global_store_dwordx2 v[122:123], v[28:29], off
	global_load_dwordx4 v[28:31], v[32:33], off offset:-4096
	s_nop 0
	global_load_dwordx4 v[94:97], v[34:35], off offset:-4096
	v_mov_b32_e32 v102, 0
	v_pk_mul_f32 v[26:27], v[26:27], v[60:61] op_sel_hi:[1,0]
	v_pk_mul_f32 v[24:25], v[24:25], v[60:61] op_sel_hi:[1,0]
	v_pk_mul_f32 v[22:23], v[22:23], v[60:61] op_sel_hi:[1,0]
	v_pk_mul_f32 v[20:21], v[20:21], v[60:61] op_sel_hi:[1,0]
	v_mov_b32_e32 v106, 0
	v_pk_mul_f32 v[18:19], v[18:19], v[60:61] op_sel_hi:[1,0]
	v_pk_mul_f32 v[16:17], v[16:17], v[60:61] op_sel_hi:[1,0]
	v_pk_mul_f32 v[14:15], v[14:15], v[60:61] op_sel_hi:[1,0]
	v_pk_mul_f32 v[12:13], v[12:13], v[60:61] op_sel_hi:[1,0]
	v_pk_mul_f32 v[8:9], v[8:9], v[60:61] op_sel_hi:[1,0]
	v_pk_mul_f32 v[10:11], v[10:11], v[60:61] op_sel_hi:[1,0]
	v_pk_mul_f32 v[6:7], v[6:7], v[60:61] op_sel_hi:[1,0]
	v_pk_mul_f32 v[4:5], v[4:5], v[60:61] op_sel_hi:[1,0]
	v_pk_mul_f32 v[2:3], v[2:3], v[60:61] op_sel_hi:[1,0]
	v_pk_mul_f32 v[0:1], v[0:1], v[60:61] op_sel_hi:[1,0]
	s_waitcnt vmcnt(1)
	v_pk_add_f32 v[28:29], v[28:29], 1.0 op_sel_hi:[1,0]
	s_waitcnt vmcnt(0)
	v_pk_fma_f32 v[94:95], v[28:29], v[98:99], v[94:95]
	v_pk_add_f32 v[28:29], v[30:31], 1.0 op_sel_hi:[1,0]
	v_cvt_pk_fp8_f32 v102, v94, v95
	v_pk_fma_f32 v[96:97], v[28:29], v[100:101], v[96:97]
	v_lshl_add_u64 v[28:29], s[0:1], 0, v[36:37]
	s_lshl_b64 s[0:1], s[44:45], 12
	v_cvt_pk_fp8_f32 v102, v96, v97 op_sel:[0,0,1]
	s_add_u32 s0, s3, s0
	s_addc_u32 s1, s39, s1
	global_store_dword v[28:29], v102, off
	global_load_dwordx4 v[98:101], v[72:73], off offset:1024
	s_nop 0
	global_load_dwordx4 v[102:105], v[74:75], off offset:1024
	s_waitcnt vmcnt(0)
	v_pk_fma_f32 v[30:31], v[100:101], v[24:25], v[104:105]
	v_pk_fma_f32 v[102:103], v[98:99], v[26:27], v[102:103]
	v_bfe_u32 v26, v30, 16, 1
	v_bfe_u32 v24, v102, 16, 1
	v_bfe_u32 v25, v103, 16, 1
	v_bfe_u32 v27, v31, 16, 1
	v_add3_u32 v24, v102, v24, s86
	v_add3_u32 v26, v30, v26, s86
	v_add3_u32 v25, v103, v25, s86
	v_add3_u32 v27, v31, v27, s86
	v_lshrrev_b32_e32 v24, 16, v24
	v_lshrrev_b32_e32 v26, 16, v26
	v_and_or_b32 v24, v25, s82, v24
	v_and_or_b32 v25, v27, s82, v26
	global_store_dwordx2 v[122:123], v[24:25], off offset:512
	global_load_dwordx4 v[24:27], v[82:83], off offset:1024
	s_nop 0
	global_load_dwordx4 v[98:101], v[80:81], off offset:1024
	v_mov_b32_e32 v104, 0
	s_waitcnt vmcnt(1)
; #define GAS __attribute__((address_space(1)))
; __device__ __forceinline__ unsigned pk2(float lo, float hi) { return f2bf(lo) | (f2bf(hi) << 16); }
; __device__ __forceinline__ unsigned pk4_fp8(float a, float b, float c, float d) { int r = __builtin_amdgcn_cvt_pk_fp8_f32(a, b, 0, false); r = __builtin_amdgcn_cvt_pk_fp8_f32(c, d, r, true); return (unsigned)r; }
; template <int l>
; __device__ __forceinline__ void layer_phases(Frame& F, const XcdBarrier& bar, const int lo, const int hi) {
;     ...
;                     for (int j = 0; j < 8; ++j) { const int k = 4 * lq + 256 * j;
;                         const f32x4 xv = v[j] * rstd * *(const GAS f32x4*)(g1 + k) + *(const GAS f32x4*)(b1 + k);
;                         { v2u xo; xo.x = pk2(xv.x, xv.y); xo.y = pk2(xv.z, xv.w); *(GAS v2u*)(x1 + (size_t)m * D + k) = xo; }
;                         const f32x4 hv = xv * (*(const GAS f32x4*)(mrow + 8192 + k) + 1.0f) + *(const GAS f32x4*)(mrow + 6144 + k);
;                         v2u o; o.x = pk2(hv.x, hv.y); o.y = pk2(hv.z, hv.w);
;                         *(GAS unsigned*)(h2q + (size_t)m * D + k) = pk4_fp8(hv.x, hv.y, hv.z, hv.w);
	v_pk_add_f32 v[24:25], v[24:25], 1.0 op_sel_hi:[1,0]
	s_waitcnt vmcnt(0)
	v_pk_fma_f32 v[98:99], v[24:25], v[102:103], v[98:99]
	v_pk_add_f32 v[24:25], v[26:27], 1.0 op_sel_hi:[1,0]
	v_cvt_pk_fp8_f32 v104, v98, v99
	v_pk_fma_f32 v[100:101], v[24:25], v[30:31], v[100:101]
	s_nop 0
	v_cvt_pk_fp8_f32 v104, v100, v101 op_sel:[0,0,1]
	global_store_dword v[28:29], v104, off offset:256
	global_load_dwordx4 v[24:27], v[72:73], off offset:2048
	s_nop 0
	global_load_dwordx4 v[102:105], v[74:75], off offset:2048
	s_waitcnt vmcnt(0)
	v_pk_fma_f32 v[30:31], v[26:27], v[20:21], v[104:105]
	v_pk_fma_f32 v[102:103], v[24:25], v[22:23], v[102:103]
	v_bfe_u32 v22, v30, 16, 1
	v_bfe_u32 v20, v102, 16, 1
	v_bfe_u32 v21, v103, 16, 1
	v_bfe_u32 v23, v31, 16, 1
	v_add3_u32 v20, v102, v20, s86
	v_add3_u32 v22, v30, v22, s86
	v_add3_u32 v21, v103, v21, s86
	v_add3_u32 v23, v31, v23, s86
	v_lshrrev_b32_e32 v20, 16, v20
	v_lshrrev_b32_e32 v22, 16, v22
	v_and_or_b32 v20, v21, s82, v20
	v_and_or_b32 v21, v23, s82, v22
	global_store_dwordx2 v[122:123], v[20:21], off offset:1024
	global_load_dwordx4 v[20:23], v[82:83], off offset:2048
	s_nop 0
	global_load_dwordx4 v[24:27], v[80:81], off offset:2048
	s_waitcnt vmcnt(1)
	v_pk_add_f32 v[20:21], v[20:21], 1.0 op_sel_hi:[1,0]
	s_waitcnt vmcnt(0)
	v_pk_fma_f32 v[102:103], v[20:21], v[102:103], v[24:25]
	v_pk_add_f32 v[20:21], v[22:23], 1.0 op_sel_hi:[1,0]
	v_cvt_pk_fp8_f32 v106, v102, v103
	v_pk_fma_f32 v[104:105], v[20:21], v[30:31], v[26:27]
	v_mov_b32_e32 v30, 0
	v_cvt_pk_fp8_f32 v106, v104, v105 op_sel:[0,0,1]
	global_store_dword v[28:29], v106, off offset:512
	global_load_dwordx4 v[20:23], v[72:73], off offset:3072
	global_load_dwordx4 v[24:27], v[74:75], off offset:3072
	s_waitcnt vmcnt(0)
	v_pk_fma_f32 v[26:27], v[16:17], v[22:23], v[26:27]
	v_pk_fma_f32 v[24:25], v[18:19], v[20:21], v[24:25]
	v_bfe_u32 v18, v26, 16, 1
	v_bfe_u32 v16, v24, 16, 1
	v_bfe_u32 v17, v25, 16, 1
	v_bfe_u32 v19, v27, 16, 1
	v_add3_u32 v16, v24, v16, s86
	v_add3_u32 v18, v26, v18, s86
	v_add3_u32 v17, v25, v17, s86
	v_add3_u32 v19, v27, v19, s86
	v_lshrrev_b32_e32 v16, 16, v16
	v_lshrrev_b32_e32 v18, 16, v18
	v_and_or_b32 v16, v17, s82, v16
	v_and_or_b32 v17, v19, s82, v18
	global_store_dwordx2 v[122:123], v[16:17], off offset:1536
	global_load_dwordx4 v[16:19], v[82:83], off offset:3072
	s_nop 0
	global_load_dwordx4 v[20:23], v[80:81], off offset:3072
	s_waitcnt vmcnt(1)
	v_pk_add_f32 v[16:17], v[16:17], 1.0 op_sel_hi:[1,0]
	s_waitcnt vmcnt(0)
	v_pk_fma_f32 v[106:107], v[24:25], v[16:17], v[20:21]
	v_pk_add_f32 v[16:17], v[18:19], 1.0 op_sel_hi:[1,0]
	v_cvt_pk_fp8_f32 v30, v106, v107
	v_pk_fma_f32 v[108:109], v[26:27], v[16:17], v[22:23]
	v_mov_b32_e32 v24, 0
	v_cvt_pk_fp8_f32 v30, v108, v109 op_sel:[0,0,1]
	global_store_dword v[28:29], v30, off offset:768
	global_load_dwordx4 v[16:19], v[38:39], off
	global_load_dwordx4 v[20:23], v[40:41], off
	s_waitcnt vmcnt(0)
	v_pk_fma_f32 v[22:23], v[12:13], v[18:19], v[22:23]
	v_pk_fma_f32 v[20:21], v[14:15], v[16:17], v[20:21]
	v_bfe_u32 v14, v22, 16, 1
	v_bfe_u32 v12, v20, 16, 1
	v_bfe_u32 v13, v21, 16, 1
	v_bfe_u32 v15, v23, 16, 1
	v_add3_u32 v12, v20, v12, s86
	v_add3_u32 v14, v22, v14, s86
	v_add3_u32 v13, v21, v13, s86
	v_add3_u32 v15, v23, v15, s86
	v_lshrrev_b32_e32 v12, 16, v12
	v_lshrrev_b32_e32 v14, 16, v14
	v_and_or_b32 v12, v13, s82, v12
	v_and_or_b32 v13, v15, s82, v14
	global_store_dwordx2 v[122:123], v[12:13], off offset:2048
	global_load_dwordx4 v[12:15], v[32:33], off
	s_nop 0
	global_load_dwordx4 v[16:19], v[34:35], off
	s_waitcnt vmcnt(1)
	v_pk_add_f32 v[12:13], v[12:13], 1.0 op_sel_hi:[1,0]
	s_waitcnt vmcnt(0)
	v_pk_fma_f32 v[110:111], v[20:21], v[12:13], v[16:17]
	v_pk_add_f32 v[12:13], v[14:15], 1.0 op_sel_hi:[1,0]
	v_cvt_pk_fp8_f32 v24, v110, v111
	v_pk_fma_f32 v[112:113], v[22:23], v[12:13], v[18:19]
	v_mov_b32_e32 v20, 0
	v_cvt_pk_fp8_f32 v24, v112, v113 op_sel:[0,0,1]
	global_store_dword v[28:29], v24, off offset:1024
	global_load_dwordx4 v[12:15], v[38:39], off offset:1024
	global_load_dwordx4 v[16:19], v[40:41], off offset:1024
	s_waitcnt vmcnt(0)
	v_pk_fma_f32 v[18:19], v[10:11], v[14:15], v[18:19]
	v_pk_fma_f32 v[16:17], v[8:9], v[12:13], v[16:17]
	v_bfe_u32 v10, v18, 16, 1
	v_bfe_u32 v8, v16, 16, 1
	v_bfe_u32 v9, v17, 16, 1
	v_bfe_u32 v11, v19, 16, 1
	v_add3_u32 v8, v16, v8, s86
	v_add3_u32 v10, v18, v10, s86
	v_add3_u32 v9, v17, v9, s86
	v_add3_u32 v11, v19, v11, s86
	v_lshrrev_b32_e32 v8, 16, v8
	v_lshrrev_b32_e32 v10, 16, v10
	v_and_or_b32 v8, v9, s82, v8
	v_and_or_b32 v9, v11, s82, v10
	global_store_dwordx2 v[122:123], v[8:9], off offset:2560
	global_load_dwordx4 v[8:11], v[32:33], off offset:1024
	s_nop 0
	global_load_dwordx4 v[12:15], v[34:35], off offset:1024
	s_waitcnt vmcnt(1)
	v_pk_add_f32 v[8:9], v[8:9], 1.0 op_sel_hi:[1,0]
	s_waitcnt vmcnt(0)
	v_pk_fma_f32 v[114:115], v[16:17], v[8:9], v[12:13]
	v_pk_add_f32 v[8:9], v[10:11], 1.0 op_sel_hi:[1,0]
	v_cvt_pk_fp8_f32 v20, v114, v115
	v_pk_fma_f32 v[116:117], v[18:19], v[8:9], v[14:15]
	v_mov_b32_e32 v16, 0
	v_cvt_pk_fp8_f32 v20, v116, v117 op_sel:[0,0,1]
	global_store_dword v[28:29], v20, off offset:1280
	global_load_dwordx4 v[8:11], v[38:39], off offset:2048
	global_load_dwordx4 v[12:15], v[40:41], off offset:2048
	s_waitcnt vmcnt(0)
	v_pk_fma_f32 v[14:15], v[4:5], v[10:11], v[14:15]
	v_pk_fma_f32 v[12:13], v[6:7], v[8:9], v[12:13]
	v_bfe_u32 v6, v14, 16, 1
	v_bfe_u32 v4, v12, 16, 1
	v_bfe_u32 v5, v13, 16, 1
	v_bfe_u32 v7, v15, 16, 1
	v_add3_u32 v4, v12, v4, s86
	v_add3_u32 v6, v14, v6, s86
	v_add3_u32 v5, v13, v5, s86
	v_add3_u32 v7, v15, v7, s86
	v_lshrrev_b32_e32 v4, 16, v4
	v_lshrrev_b32_e32 v6, 16, v6
	v_and_or_b32 v4, v5, s82, v4
	v_and_or_b32 v5, v7, s82, v6
	global_store_dwordx2 v[122:123], v[4:5], off offset:3072
	global_load_dwordx4 v[4:7], v[32:33], off offset:2048
	s_nop 0
	global_load_dwordx4 v[8:11], v[34:35], off offset:2048
	s_waitcnt vmcnt(1)
; #define GAS __attribute__((address_space(1)))
; __device__ __forceinline__ unsigned pk2(float lo, float hi) { return f2bf(lo) | (f2bf(hi) << 16); }
; __device__ __forceinline__ unsigned pk4_fp8(float a, float b, float c, float d) { int r = __builtin_amdgcn_cvt_pk_fp8_f32(a, b, 0, false); r = __builtin_amdgcn_cvt_pk_fp8_f32(c, d, r, true); return (unsigned)r; }
; __device__ __forceinline__ f32x4 bf4(unsigned a, unsigned b) { return (f32x4){bflo(a), bfhi(a), bflo(b), bfhi(b)}; }
; template <int l>
; __device__ __forceinline__ void layer_phases(Frame& F, const XcdBarrier& bar, const int lo, const int hi) {
;     ...
;                 for (int rr = 0; rr < 2; ++rr)
; #pragma unroll
;                     for (int j = 0; j < 8; ++j) { const size_t off = (size_t)(m0 + 2 * rp + rr) * D + 4 * lq + 256 * j;
;                         f32x4 xv; if (l == 0) xv = __builtin_nontemporal_load((const GAS f32x4*)(xin + off)); else { const v2u xw_ = __builtin_nontemporal_load((const GAS v2u*)(xinb + off)); xv = bf4(xw_.x, xw_.y); } const v2u mw = __builtin_nontemporal_load((const GAS v2u*)(mixb + off)); const f32x4 gv = *(const GAS f32x4*)(mrow + 4096 + 4 * lq + 256 * j);
;                         vv[rr][j] = xv * ALPHA + gv * (f32x4){bflo(mw.x), bfhi(mw.x), bflo(mw.y), bfhi(mw.y)}; }
; #pragma unroll
;                 for (int rq = 0; rq < 2; ++rq) { const int rr = 2 * rp + rq, m = m0 + rr, rloc = 4 * F.wave + rr;
;                     f32x4 (&v)[8] = vv[rq]; float s = 0.f;
; #pragma unroll
;                     for (int j = 0; j < 8; ++j) s += (v[j].x + v[j].y) + (v[j].z + v[j].w);
;     ...
;                     for (int j = 0; j < 8; ++j) { const int k = 4 * lq + 256 * j;
;                         const f32x4 xv = v[j] * rstd * *(const GAS f32x4*)(g1 + k) + *(const GAS f32x4*)(b1 + k);
;                         { v2u xo; xo.x = pk2(xv.x, xv.y); xo.y = pk2(xv.z, xv.w); *(GAS v2u*)(x1 + (size_t)m * D + k) = xo; }
;                         const f32x4 hv = xv * (*(const GAS f32x4*)(mrow + 8192 + k) + 1.0f) + *(const GAS f32x4*)(mrow + 6144 + k);
;                         v2u o; o.x = pk2(hv.x, hv.y); o.y = pk2(hv.z, hv.w);
;                         *(GAS unsigned*)(h2q + (size_t)m * D + k) = pk4_fp8(hv.x, hv.y, hv.z, hv.w);
	v_pk_add_f32 v[4:5], v[4:5], 1.0 op_sel_hi:[1,0]
	s_waitcnt vmcnt(0)
	v_pk_fma_f32 v[118:119], v[12:13], v[4:5], v[8:9]
	v_pk_add_f32 v[4:5], v[6:7], 1.0 op_sel_hi:[1,0]
	v_cvt_pk_fp8_f32 v16, v118, v119
	v_pk_fma_f32 v[120:121], v[14:15], v[4:5], v[10:11]
	v_mov_b32_e32 v12, 0
	v_cvt_pk_fp8_f32 v16, v120, v121 op_sel:[0,0,1]
	global_store_dword v[28:29], v16, off offset:1536
	global_load_dwordx4 v[4:7], v[38:39], off offset:3072
	global_load_dwordx4 v[8:11], v[40:41], off offset:3072
	s_waitcnt vmcnt(0)
	v_pk_fma_f32 v[10:11], v[0:1], v[6:7], v[10:11]
	v_pk_fma_f32 v[8:9], v[2:3], v[4:5], v[8:9]
	v_bfe_u32 v2, v10, 16, 1
	v_bfe_u32 v0, v8, 16, 1
	v_bfe_u32 v1, v9, 16, 1
	v_bfe_u32 v3, v11, 16, 1
	v_add3_u32 v0, v8, v0, s86
	v_add3_u32 v2, v10, v2, s86
	v_add3_u32 v1, v9, v1, s86
	v_add3_u32 v3, v11, v3, s86
	v_lshrrev_b32_e32 v0, 16, v0
	v_lshrrev_b32_e32 v2, 16, v2
	v_and_or_b32 v0, v1, s82, v0
	v_and_or_b32 v1, v3, s82, v2
	global_store_dwordx2 v[122:123], v[0:1], off offset:3584
	global_load_dwordx4 v[0:3], v[32:33], off offset:3072
	s_nop 0
	global_load_dwordx4 v[4:7], v[34:35], off offset:3072
	s_waitcnt vmcnt(1)
	v_pk_add_f32 v[0:1], v[0:1], 1.0 op_sel_hi:[1,0]
	s_waitcnt vmcnt(0)
	v_pk_fma_f32 v[122:123], v[8:9], v[0:1], v[4:5]
	v_pk_add_f32 v[0:1], v[2:3], 1.0 op_sel_hi:[1,0]
	v_cvt_pk_fp8_f32 v12, v122, v123
	v_pk_fma_f32 v[124:125], v[10:11], v[0:1], v[6:7]
	v_lshl_add_u64 v[0:1], s[18:19], 0, v[36:37]
	v_lshlrev_b64 v[0:1], 1, v[0:1]
	v_cvt_pk_fp8_f32 v12, v124, v125 op_sel:[0,0,1]
	v_lshl_add_u64 v[2:3], s[22:23], 0, v[0:1]
	v_lshl_add_u64 v[0:1], s[20:21], 0, v[0:1]
	global_store_dword v[28:29], v12, off offset:1792
	global_load_dwordx2 v[130:131], v[2:3], off nt
	global_load_dwordx2 v[132:133], v[0:1], off nt
	global_load_dwordx2 v[134:135], v[2:3], off offset:512 nt
	global_load_dwordx2 v[136:137], v[0:1], off offset:512 nt
	global_load_dwordx2 v[138:139], v[2:3], off offset:1024 nt
	global_load_dwordx2 v[140:141], v[0:1], off offset:1024 nt
	global_load_dwordx2 v[142:143], v[2:3], off offset:1536 nt
	global_load_dwordx2 v[144:145], v[0:1], off offset:1536 nt
	global_load_dwordx2 v[146:147], v[2:3], off offset:2048 nt
	global_load_dwordx2 v[148:149], v[0:1], off offset:2048 nt
	global_load_dwordx2 v[150:151], v[2:3], off offset:2560 nt
	global_load_dwordx2 v[152:153], v[0:1], off offset:2560 nt
	global_load_dwordx2 v[154:155], v[2:3], off offset:3072 nt
	global_load_dwordx2 v[156:157], v[0:1], off offset:3072 nt
	global_load_dwordx2 v[158:159], v[2:3], off offset:3584 nt
	global_load_dwordx2 v[160:161], v[0:1], off offset:3584 nt
	global_load_dwordx4 v[28:31], v[126:127], off offset:-4096
	global_load_dwordx4 v[24:27], v[128:129], off offset:1024
	global_load_dwordx4 v[20:23], v[128:129], off offset:2048
	global_load_dwordx4 v[16:19], v[128:129], off offset:3072
	global_load_dwordx4 v[12:15], v[126:127], off
	global_load_dwordx4 v[8:11], v[126:127], off offset:1024
	global_load_dwordx4 v[4:7], v[126:127], off offset:2048
	global_load_dwordx4 v[0:3], v[126:127], off offset:3072
	global_load_dwordx4 v[206:209], v[72:73], off
	global_load_dwordx4 v[210:213], v[74:75], off
	s_waitcnt vmcnt(23)
	v_lshlrev_b32_e32 v162, 16, v134
	s_waitcnt vmcnt(22)
	v_lshlrev_b32_e32 v164, 16, v136
	v_and_b32_e32 v165, 0xffff0000, v136
	v_lshlrev_b32_e32 v136, 16, v137
	v_and_b32_e32 v137, 0xffff0000, v137
	v_and_b32_e32 v163, 0xffff0000, v134
	v_lshlrev_b32_e32 v134, 16, v135
	v_and_b32_e32 v135, 0xffff0000, v135
	s_waitcnt vmcnt(20)
	v_lshlrev_b32_e32 v168, 16, v140
	v_and_b32_e32 v169, 0xffff0000, v140
	v_lshlrev_b32_e32 v140, 16, v141
	v_and_b32_e32 v141, 0xffff0000, v141
	s_waitcnt vmcnt(18)
	v_lshlrev_b32_e32 v172, 16, v144
	v_and_b32_e32 v173, 0xffff0000, v144
	v_lshlrev_b32_e32 v144, 16, v145
	v_and_b32_e32 v145, 0xffff0000, v145
	s_waitcnt vmcnt(16)
	v_lshlrev_b32_e32 v176, 16, v148
	v_and_b32_e32 v177, 0xffff0000, v148
	v_lshlrev_b32_e32 v148, 16, v149
	v_and_b32_e32 v149, 0xffff0000, v149
	v_lshlrev_b32_e32 v128, 16, v130
	v_and_b32_e32 v129, 0xffff0000, v130
	v_lshlrev_b32_e32 v126, 16, v131
	v_and_b32_e32 v127, 0xffff0000, v131
	v_lshlrev_b32_e32 v130, 16, v132
	v_and_b32_e32 v131, 0xffff0000, v132
	v_lshlrev_b32_e32 v132, 16, v133
	v_and_b32_e32 v133, 0xffff0000, v133
	s_waitcnt vmcnt(14)
	v_lshlrev_b32_e32 v180, 16, v152
	v_and_b32_e32 v181, 0xffff0000, v152
	v_lshlrev_b32_e32 v152, 16, v153
	v_and_b32_e32 v153, 0xffff0000, v153
	s_waitcnt vmcnt(10)
	v_lshlrev_b32_e32 v188, 16, v160
	v_and_b32_e32 v189, 0xffff0000, v160
	v_lshlrev_b32_e32 v160, 16, v161
	v_and_b32_e32 v161, 0xffff0000, v161
	s_waitcnt vmcnt(9)
	v_pk_mul_f32 v[130:131], v[28:29], v[130:131]
	v_pk_mul_f32 v[132:133], v[30:31], v[132:133]
	s_waitcnt vmcnt(8)
	v_pk_mul_f32 v[136:137], v[26:27], v[136:137]
	v_pk_mul_f32 v[164:165], v[24:25], v[164:165]
	v_lshlrev_b32_e32 v166, 16, v138
	v_and_b32_e32 v167, 0xffff0000, v138
	v_lshlrev_b32_e32 v138, 16, v139
	v_and_b32_e32 v139, 0xffff0000, v139
	v_lshlrev_b32_e32 v170, 16, v142
	v_and_b32_e32 v171, 0xffff0000, v142
	v_lshlrev_b32_e32 v142, 16, v143
	v_and_b32_e32 v143, 0xffff0000, v143
	v_lshlrev_b32_e32 v174, 16, v146
	v_and_b32_e32 v175, 0xffff0000, v146
	v_lshlrev_b32_e32 v146, 16, v147
	v_and_b32_e32 v147, 0xffff0000, v147
	v_lshlrev_b32_e32 v178, 16, v150
	v_and_b32_e32 v179, 0xffff0000, v150
	v_lshlrev_b32_e32 v150, 16, v151
	v_and_b32_e32 v151, 0xffff0000, v151
	v_lshlrev_b32_e32 v186, 16, v158
	v_and_b32_e32 v187, 0xffff0000, v158
	v_lshlrev_b32_e32 v158, 16, v159
	v_and_b32_e32 v159, 0xffff0000, v159
	s_waitcnt vmcnt(7)
	v_pk_mul_f32 v[140:141], v[22:23], v[140:141]
	v_pk_mul_f32 v[168:169], v[20:21], v[168:169]
	s_waitcnt vmcnt(6)
; template <int l>
; __device__ __forceinline__ void layer_phases(Frame& F, const XcdBarrier& bar, const int lo, const int hi) {
;     ...
;                         vv[rr][j] = xv * ALPHA + gv * (f32x4){bflo(mw.x), bfhi(mw.x), bflo(mw.y), bfhi(mw.y)}; }
; #pragma unroll
;                 for (int rq = 0; rq < 2; ++rq) { const int rr = 2 * rp + rq, m = m0 + rr, rloc = 4 * F.wave + rr;
;                     f32x4 (&v)[8] = vv[rq]; float s = 0.f;
; #pragma unroll
;                     for (int j = 0; j < 8; ++j) s += (v[j].x + v[j].y) + (v[j].z + v[j].w);
;                     const float mean = wave_sum(s) * (1.f / D); float s2 = 0.f;
; #pragma unroll
;                     for (int j = 0; j < 8; ++j) { v[j] = v[j] - mean; s2 += (v[j].x * v[j].x + v[j].y * v[j].y) + (v[j].z * v[j].z + v[j].w * v[j].w); }
	v_pk_mul_f32 v[144:145], v[18:19], v[144:145]
	s_waitcnt vmcnt(5)
	v_pk_mul_f32 v[148:149], v[14:15], v[148:149]
	s_waitcnt vmcnt(4)
	v_pk_mul_f32 v[152:153], v[10:11], v[152:153]
	s_waitcnt vmcnt(2)
	v_pk_mul_f32 v[160:161], v[2:3], v[160:161]
	v_pk_fma_f32 v[126:127], v[126:127], s[38:39], v[132:133] op_sel_hi:[1,0,1]
	v_pk_fma_f32 v[128:129], v[128:129], s[38:39], v[130:131] op_sel_hi:[1,0,1]
	v_pk_fma_f32 v[130:131], v[134:135], s[38:39], v[136:137] op_sel_hi:[1,0,1]
	v_pk_fma_f32 v[132:133], v[162:163], s[38:39], v[164:165] op_sel_hi:[1,0,1]
	v_pk_fma_f32 v[134:135], v[138:139], s[38:39], v[140:141] op_sel_hi:[1,0,1]
	v_pk_fma_f32 v[136:137], v[166:167], s[38:39], v[168:169] op_sel_hi:[1,0,1]
	v_pk_fma_f32 v[138:139], v[142:143], s[38:39], v[144:145] op_sel_hi:[1,0,1]
	v_pk_fma_f32 v[142:143], v[146:147], s[38:39], v[148:149] op_sel_hi:[1,0,1]
	v_pk_fma_f32 v[146:147], v[150:151], s[38:39], v[152:153] op_sel_hi:[1,0,1]
	v_pk_fma_f32 v[150:151], v[158:159], s[38:39], v[160:161] op_sel_hi:[1,0,1]
	v_mov_b32_e32 v158, v128
	v_mov_b32_e32 v159, v132
	v_mov_b32_e32 v160, v129
	v_mov_b32_e32 v161, v133
	v_mov_b32_e32 v162, v126
	v_mov_b32_e32 v163, v130
	v_mov_b32_e32 v164, v127
	v_mov_b32_e32 v165, v131
	v_pk_mov_b32 v[166:167], v[136:137], v[134:135] op_sel:[1,0]
	v_mov_b32_e32 v168, v136
	v_mov_b32_e32 v169, v135
	v_pk_add_f32 v[158:159], v[158:159], v[160:161]
	v_pk_add_f32 v[160:161], v[162:163], v[164:165]
	v_pk_mul_f32 v[172:173], v[16:17], v[172:173]
	v_pk_mul_f32 v[176:177], v[12:13], v[176:177]
	v_pk_add_f32 v[162:163], v[166:167], v[168:169]
	v_pk_add_f32 v[158:159], v[158:159], v[160:161]
	v_pk_mul_f32 v[180:181], v[8:9], v[180:181]
	v_pk_fma_f32 v[140:141], v[170:171], s[38:39], v[172:173] op_sel_hi:[1,0,1]
	v_pk_fma_f32 v[144:145], v[174:175], s[38:39], v[176:177] op_sel_hi:[1,0,1]
	v_pk_add_f32 v[160:161], v[162:163], v[162:163] op_sel:[0,1] op_sel_hi:[1,0]
	v_add_f32_e32 v60, 0, v158
	v_pk_fma_f32 v[148:149], v[178:179], s[38:39], v[180:181] op_sel_hi:[1,0,1]
	v_add_f32_e32 v170, v140, v141
	v_add_f32_e32 v172, v138, v139
	v_mov_b32_e32 v175, v144
	v_mov_b32_e32 v171, v142
	v_mov_b32_e32 v173, v143
	v_mov_b32_e32 v161, v145
	v_add_f32_e32 v174, v60, v159
	v_lshlrev_b32_e32 v184, 16, v156
	v_and_b32_e32 v185, 0xffff0000, v156
	v_lshlrev_b32_e32 v156, 16, v157
	v_and_b32_e32 v157, 0xffff0000, v157
	v_pk_mov_b32 v[176:177], v[148:149], v[146:147] op_sel:[1,0]
	v_mov_b32_e32 v178, v148
	v_mov_b32_e32 v179, v147
	v_pk_add_f32 v[164:165], v[170:171], v[172:173]
	v_pk_add_f32 v[158:159], v[174:175], v[160:161]
	v_lshlrev_b32_e32 v182, 16, v154
	v_and_b32_e32 v183, 0xffff0000, v154
	v_lshlrev_b32_e32 v154, 16, v155
	v_and_b32_e32 v155, 0xffff0000, v155
	v_pk_mul_f32 v[184:185], v[4:5], v[184:185]
	v_pk_mul_f32 v[156:157], v[6:7], v[156:157]
	v_pk_mul_f32 v[188:189], v[0:1], v[188:189]
	v_pk_add_f32 v[166:167], v[176:177], v[178:179]
	v_pk_add_f32 v[158:159], v[158:159], v[164:165]
	v_pk_fma_f32 v[154:155], v[154:155], s[38:39], v[156:157] op_sel_hi:[1,0,1]
	v_pk_fma_f32 v[156:157], v[182:183], s[38:39], v[184:185] op_sel_hi:[1,0,1]
	v_pk_fma_f32 v[152:153], v[186:187], s[38:39], v[188:189] op_sel_hi:[1,0,1]
	v_pk_add_f32 v[162:163], v[166:167], v[166:167] op_sel:[0,1] op_sel_hi:[1,0]
	v_pk_add_f32 v[158:159], v[158:159], v[158:159] op_sel:[0,1] op_sel_hi:[1,0]
	v_add_f32_e32 v180, v156, v157
	v_add_f32_e32 v182, v154, v155
	v_mov_b32_e32 v181, v150
	v_mov_b32_e32 v183, v151
	v_mov_b32_e32 v163, v153
	v_mov_b32_e32 v159, v152
	v_pk_add_f32 v[168:169], v[180:181], v[182:183]
	v_pk_add_f32 v[158:159], v[158:159], v[162:163]
	s_nop 0
	v_pk_add_f32 v[158:159], v[158:159], v[168:169]
	s_nop 0
	v_add_f32_e32 v60, v158, v159
	ds_bpermute_b32 v158, v53, v60
	s_waitcnt lgkmcnt(0)
	v_add_f32_e32 v60, v60, v158
	ds_bpermute_b32 v158, v194, v60
	s_waitcnt lgkmcnt(0)
	v_add_f32_e32 v60, v60, v158
	ds_bpermute_b32 v158, v195, v60
	s_waitcnt lgkmcnt(0)
	v_add_f32_e32 v60, v60, v158
	ds_bpermute_b32 v158, v196, v60
	s_waitcnt lgkmcnt(0)
	v_add_f32_e32 v60, v60, v158
	ds_bpermute_b32 v158, v197, v60
	s_waitcnt lgkmcnt(0)
	v_add_f32_e32 v60, v60, v158
	ds_bpermute_b32 v158, v198, v60
	s_waitcnt lgkmcnt(0)
	v_add_f32_e32 v60, v60, v158
	v_fmamk_f32 v127, v60, 0xba000000, v127
	v_fmamk_f32 v129, v60, 0xba000000, v129
	v_fmamk_f32 v131, v60, 0xba000000, v131
	v_fmamk_f32 v133, v60, 0xba000000, v133
	v_fmac_f32_e32 v126, 0xba000000, v60
	v_fmac_f32_e32 v128, 0xba000000, v60
	v_fmac_f32_e32 v130, 0xba000000, v60
	v_fmac_f32_e32 v132, 0xba000000, v60
	v_fmamk_f32 v137, v60, 0xba000000, v137
	v_fmac_f32_e32 v136, 0xba000000, v60
	v_fmamk_f32 v135, v60, 0xba000000, v135
	v_fmac_f32_e32 v134, 0xba000000, v60
	v_mov_b32_e32 v160, v129
	v_mov_b32_e32 v161, v133
	v_mov_b32_e32 v164, v127
	v_mov_b32_e32 v165, v131
	v_mov_b32_e32 v158, v128
	v_mov_b32_e32 v159, v132
	v_mov_b32_e32 v162, v126
	v_mov_b32_e32 v163, v130
	v_pk_mul_f32 v[166:167], v[134:135], v[134:135]
	v_pk_mul_f32 v[168:169], v[136:137], v[136:137]
	v_pk_mul_f32 v[160:161], v[160:161], v[160:161]
	v_pk_mul_f32 v[164:165], v[164:165], v[164:165]
	v_fmac_f32_e32 v140, 0xba000000, v60
	v_fmac_f32_e32 v138, 0xba000000, v60
	v_pk_mov_b32 v[180:181], v[168:169], v[166:167] op_sel:[1,0]
	v_mov_b32_e32 v169, v167
	v_pk_fma_f32 v[158:159], v[158:159], v[158:159], v[160:161]
	v_pk_fma_f32 v[160:161], v[162:163], v[162:163], v[164:165]
	v_fmamk_f32 v141, v60, 0xba000000, v141
	v_fmamk_f32 v139, v60, 0xba000000, v139
	v_fmamk_f32 v143, v60, 0xba000000, v143
	v_fmac_f32_e32 v142, 0xba000000, v60
	v_fmamk_f32 v145, v60, 0xba000000, v145
	v_fmac_f32_e32 v144, 0xba000000, v60
	v_fmamk_f32 v149, v60, 0xba000000, v149
; #define GAS __attribute__((address_space(1)))
; __device__ __forceinline__ unsigned pk2(float lo, float hi) { return f2bf(lo) | (f2bf(hi) << 16); }
; __device__ __forceinline__ unsigned pk4_fp8(float a, float b, float c, float d) { int r = __builtin_amdgcn_cvt_pk_fp8_f32(a, b, 0, false); r = __builtin_amdgcn_cvt_pk_fp8_f32(c, d, r, true); return (unsigned)r; }
; template <int l>
; __device__ __forceinline__ void layer_phases(Frame& F, const XcdBarrier& bar, const int lo, const int hi) {
;     ...
;                     const float mean = wave_sum(s) * (1.f / D); float s2 = 0.f;
; #pragma unroll
;                     for (int j = 0; j < 8; ++j) { v[j] = v[j] - mean; s2 += (v[j].x * v[j].x + v[j].y * v[j].y) + (v[j].z * v[j].z + v[j].w * v[j].w); }
;                     const float rstd = 1.f / sqrtf(wave_sum(s2) * (1.f / D) + LN_EPS);
; #pragma unroll
;                     for (int j = 0; j < 8; ++j) { const int k = 4 * lq + 256 * j;
;                         const f32x4 xv = v[j] * rstd * *(const GAS f32x4*)(g1 + k) + *(const GAS f32x4*)(b1 + k);
;                         { v2u xo; xo.x = pk2(xv.x, xv.y); xo.y = pk2(xv.z, xv.w); *(GAS v2u*)(x1 + (size_t)m * D + k) = xo; }
;                         const f32x4 hv = xv * (*(const GAS f32x4*)(mrow + 8192 + k) + 1.0f) + *(const GAS f32x4*)(mrow + 6144 + k);
;                         v2u o; o.x = pk2(hv.x, hv.y); o.y = pk2(hv.z, hv.w);
;                         *(GAS unsigned*)(h2q + (size_t)m * D + k) = pk4_fp8(hv.x, hv.y, hv.z, hv.w);
	v_fmac_f32_e32 v148, 0xba000000, v60
	v_fmamk_f32 v147, v60, 0xba000000, v147
	v_fmac_f32_e32 v146, 0xba000000, v60
	v_fmamk_f32 v157, v60, 0xba000000, v157
	v_fmac_f32_e32 v156, 0xba000000, v60
	v_fmamk_f32 v155, v60, 0xba000000, v155
	v_fmac_f32_e32 v154, 0xba000000, v60
	v_fmamk_f32 v151, v60, 0xba000000, v151
	v_fmac_f32_e32 v150, 0xba000000, v60
	v_fmamk_f32 v153, v60, 0xba000000, v153
	v_fmac_f32_e32 v152, 0xba000000, v60
	v_mul_f32_e32 v60, v140, v140
	v_mul_f32_e32 v170, v138, v138
	v_pk_add_f32 v[162:163], v[180:181], v[168:169]
	v_pk_add_f32 v[158:159], v[158:159], v[160:161]
	v_pk_fma_f32 v[166:167], v[140:141], v[140:141], v[60:61] op_sel_hi:[1,1,0]
	v_pk_fma_f32 v[170:171], v[138:139], v[138:139], v[170:171] op_sel_hi:[1,1,0]
	v_pk_add_f32 v[160:161], v[162:163], v[162:163] op_sel_hi:[0,1]
	v_pk_add_f32 v[158:159], v[158:159], v[158:159] op_sel_hi:[0,1]
	v_pk_mul_f32 v[172:173], v[146:147], v[146:147]
	v_pk_mul_f32 v[174:175], v[148:149], v[148:149]
	v_mul_f32_e32 v166, v144, v144
	v_mul_f32_e32 v170, v145, v145
	v_mul_f32_e32 v160, v142, v142
	v_mul_f32_e32 v158, v143, v143
	v_pk_mov_b32 v[182:183], v[174:175], v[172:173] op_sel:[1,0]
	v_mov_b32_e32 v175, v173
	v_pk_add_f32 v[162:163], v[166:167], v[170:171]
	v_pk_add_f32 v[158:159], v[160:161], v[158:159]
	v_mul_f32_e32 v176, v156, v156
	v_mul_f32_e32 v178, v154, v154
	v_pk_add_f32 v[164:165], v[182:183], v[174:175]
	v_pk_add_f32 v[158:159], v[162:163], v[158:159]
	v_pk_fma_f32 v[172:173], v[156:157], v[156:157], v[176:177] op_sel_hi:[1,1,0]
	v_pk_fma_f32 v[176:177], v[154:155], v[154:155], v[178:179] op_sel_hi:[1,1,0]
	v_pk_add_f32 v[164:165], v[164:165], v[164:165] op_sel_hi:[0,1]
	v_pk_add_f32 v[158:159], v[158:159], v[158:159] op_sel_hi:[0,1]
	v_mul_f32_e32 v172, v152, v152
	v_mul_f32_e32 v176, v153, v153
	v_mul_f32_e32 v164, v150, v150
	v_mul_f32_e32 v158, v151, v151
	v_pk_add_f32 v[166:167], v[172:173], v[176:177]
	v_pk_add_f32 v[158:159], v[164:165], v[158:159]
	s_nop 0
	v_pk_add_f32 v[158:159], v[166:167], v[158:159]
	s_nop 0
	v_add_f32_e32 v60, v158, v159
	ds_bpermute_b32 v158, v53, v60
	s_waitcnt lgkmcnt(0)
	v_add_f32_e32 v60, v60, v158
	ds_bpermute_b32 v158, v194, v60
	s_waitcnt lgkmcnt(0)
	v_add_f32_e32 v60, v60, v158
	ds_bpermute_b32 v160, v195, v60
	v_lshl_add_u64 v[158:159], s[16:17], 0, v[36:37]
	v_lshlrev_b64 v[158:159], 1, v[158:159]
	v_lshl_add_u64 v[162:163], s[22:23], 0, v[158:159]
	v_lshl_add_u64 v[158:159], s[20:21], 0, v[158:159]
	s_waitcnt lgkmcnt(0)
	v_add_f32_e32 v60, v60, v160
	ds_bpermute_b32 v164, v196, v60
	v_lshl_add_u64 v[160:161], s[0:1], 0, v[88:89]
	s_waitcnt lgkmcnt(0)
	v_add_f32_e32 v60, v60, v164
	ds_bpermute_b32 v166, v197, v60
	global_load_dwordx2 v[190:191], v[162:163], off nt
	global_load_dwordx2 v[176:177], v[162:163], off offset:512 nt
	global_load_dwordx2 v[170:171], v[162:163], off offset:1024 nt
	global_load_dwordx2 v[164:165], v[162:163], off offset:1536 nt
	global_load_dwordx2 v[192:193], v[158:159], off nt
	global_load_dwordx2 v[180:181], v[158:159], off offset:512 nt
	global_load_dwordx2 v[174:175], v[158:159], off offset:1024 nt
	global_load_dwordx2 v[168:169], v[158:159], off offset:1536 nt
	s_waitcnt lgkmcnt(0)
	v_add_f32_e32 v60, v60, v166
	ds_bpermute_b32 v166, v198, v60
	s_waitcnt lgkmcnt(0)
	v_add_f32_e32 v60, v60, v166
	v_fmamk_f32 v60, v60, 0x3a000000, v200
	v_mul_f32_e32 v166, 0x4f800000, v60
	v_cmp_gt_f32_e32 vcc, s85, v60
	s_waitcnt vmcnt(7)
	v_lshlrev_b32_e32 v218, 16, v191
	v_cndmask_b32_e32 v60, v60, v166, vcc
	v_sqrt_f32_e32 v182, v60
	global_load_dwordx2 v[178:179], v[162:163], off offset:2048 nt
	global_load_dwordx2 v[172:173], v[162:163], off offset:2560 nt
	global_load_dwordx2 v[166:167], v[162:163], off offset:3072 nt
	s_nop 0
	global_load_dwordx2 v[162:163], v[162:163], off offset:3584 nt
	v_and_b32_e32 v219, 0xffff0000, v191
	s_waitcnt vmcnt(7)
	v_lshlrev_b32_e32 v220, 16, v192
	v_add_u32_e32 v183, -1, v182
	v_add_u32_e32 v184, 1, v182
	v_fma_f32 v185, -v183, v182, v60
	v_fma_f32 v186, -v184, v182, v60
	v_cmp_ge_f32_e64 s[14:15], 0, v185
	v_and_b32_e32 v221, 0xffff0000, v192
	v_lshlrev_b32_e32 v222, 16, v193
	v_cndmask_b32_e64 v182, v182, v183, s[14:15]
	v_cmp_lt_f32_e64 s[14:15], 0, v186
	v_and_b32_e32 v223, 0xffff0000, v193
	s_waitcnt vmcnt(5)
	v_lshlrev_b32_e32 v226, 16, v174
	v_cndmask_b32_e64 v182, v182, v184, s[14:15]
	v_mul_f32_e32 v183, 0x37800000, v182
	v_cndmask_b32_e32 v182, v182, v183, vcc
	v_cmp_class_f32_e32 vcc, v60, v201
	v_and_b32_e32 v227, 0xffff0000, v174
	v_lshlrev_b32_e32 v174, 16, v175
	v_cndmask_b32_e32 v60, v182, v60, vcc
	v_div_scale_f32 v205, s[0:1], v60, v60, 1.0
	v_rcp_f32_e32 v214, v205
	global_load_dwordx2 v[188:189], v[158:159], off offset:2048 nt
	global_load_dwordx2 v[186:187], v[158:159], off offset:2560 nt
	global_load_dwordx2 v[182:183], v[158:159], off offset:3072 nt
	global_load_dwordx2 v[184:185], v[158:159], off offset:3584 nt
	v_div_scale_f32 v158, vcc, 1.0, v60, 1.0
	v_fma_f32 v159, -v205, v214, 1.0
	v_fmac_f32_e32 v214, v159, v214
	v_mul_f32_e32 v159, v158, v214
	v_fma_f32 v215, -v205, v159, v158
	v_fmac_f32_e32 v159, v215, v214
	v_fma_f32 v158, -v205, v159, v158
	v_div_fmas_f32 v158, v158, v214, v159
	v_div_fixup_f32 v60, v158, v60, 1.0
	v_pk_mul_f32 v[128:129], v[128:129], v[60:61] op_sel_hi:[1,0]
	v_pk_mul_f32 v[126:127], v[126:127], v[60:61] op_sel_hi:[1,0]
	v_pk_fma_f32 v[210:211], v[206:207], v[128:129], v[210:211]
	v_pk_fma_f32 v[158:159], v[208:209], v[126:127], v[212:213]
	v_bfe_u32 v126, v210, 16, 1
	v_bfe_u32 v128, v158, 16, 1
	v_bfe_u32 v127, v211, 16, 1
	v_bfe_u32 v129, v159, 16, 1
	v_add3_u32 v126, v210, v126, s86
	v_add3_u32 v128, v158, v128, s86
	v_add3_u32 v127, v211, v127, s86
	v_add3_u32 v129, v159, v129, s86
	v_lshrrev_b32_e32 v126, 16, v126
	v_lshrrev_b32_e32 v128, 16, v128
	v_and_or_b32 v126, v127, s82, v126
	v_and_or_b32 v127, v129, s82, v128
	global_store_dwordx2 v[160:161], v[126:127], off
	global_load_dwordx4 v[126:129], v[32:33], off offset:-4096
	s_nop 0
	global_load_dwordx4 v[206:209], v[34:35], off offset:-4096
	v_mov_b32_e32 v205, 0
	s_add_u32 s0, s48, s18
	s_addc_u32 s1, s49, s19
	v_pk_mul_f32 v[132:133], v[132:133], v[60:61] op_sel_hi:[1,0]
	v_pk_mul_f32 v[130:131], v[130:131], v[60:61] op_sel_hi:[1,0]
	v_pk_mul_f32 v[136:137], v[136:137], v[60:61] op_sel_hi:[1,0]
	v_pk_mul_f32 v[134:135], v[134:135], v[60:61] op_sel_hi:[1,0]
	v_pk_mul_f32 v[140:141], v[140:141], v[60:61] op_sel_hi:[1,0]
	v_pk_mul_f32 v[138:139], v[138:139], v[60:61] op_sel_hi:[1,0]
	v_pk_mul_f32 v[144:145], v[144:145], v[60:61] op_sel_hi:[1,0]
	v_pk_mul_f32 v[142:143], v[142:143], v[60:61] op_sel_hi:[1,0]
	v_pk_mul_f32 v[148:149], v[148:149], v[60:61] op_sel_hi:[1,0]
	v_pk_mul_f32 v[146:147], v[146:147], v[60:61] op_sel_hi:[1,0]
	v_pk_mul_f32 v[156:157], v[156:157], v[60:61] op_sel_hi:[1,0]
	v_pk_mul_f32 v[154:155], v[154:155], v[60:61] op_sel_hi:[1,0]
	v_lshlrev_b32_e32 v214, 16, v190
	v_and_b32_e32 v215, 0xffff0000, v190
	v_and_b32_e32 v175, 0xffff0000, v175
	s_waitcnt vmcnt(11)
; #define GAS __attribute__((address_space(1)))
; __device__ __forceinline__ unsigned pk2(float lo, float hi) { return f2bf(lo) | (f2bf(hi) << 16); }
; __device__ __forceinline__ unsigned pk4_fp8(float a, float b, float c, float d) { int r = __builtin_amdgcn_cvt_pk_fp8_f32(a, b, 0, false); r = __builtin_amdgcn_cvt_pk_fp8_f32(c, d, r, true); return (unsigned)r; }
; __device__ __forceinline__ f32x4 bf4(unsigned a, unsigned b) { return (f32x4){bflo(a), bfhi(a), bflo(b), bfhi(b)}; }
; template <int l>
; __device__ __forceinline__ void layer_phases(Frame& F, const XcdBarrier& bar, const int lo, const int hi) {
;     ...
;                     for (int j = 0; j < 8; ++j) { const size_t off = (size_t)(m0 + 2 * rp + rr) * D + 4 * lq + 256 * j;
;                         f32x4 xv; if (l == 0) xv = __builtin_nontemporal_load((const GAS f32x4*)(xin + off)); else { const v2u xw_ = __builtin_nontemporal_load((const GAS v2u*)(xinb + off)); xv = bf4(xw_.x, xw_.y); } const v2u mw = __builtin_nontemporal_load((const GAS v2u*)(mixb + off)); const f32x4 gv = *(const GAS f32x4*)(mrow + 4096 + 4 * lq + 256 * j);
;                         vv[rr][j] = xv * ALPHA + gv * (f32x4){bflo(mw.x), bfhi(mw.x), bflo(mw.y), bfhi(mw.y)}; }
;     ...
;                     for (int j = 0; j < 8; ++j) { const int k = 4 * lq + 256 * j;
;                         const f32x4 xv = v[j] * rstd * *(const GAS f32x4*)(g1 + k) + *(const GAS f32x4*)(b1 + k);
;                         { v2u xo; xo.x = pk2(xv.x, xv.y); xo.y = pk2(xv.z, xv.w); *(GAS v2u*)(x1 + (size_t)m * D + k) = xo; }
;                         const f32x4 hv = xv * (*(const GAS f32x4*)(mrow + 8192 + k) + 1.0f) + *(const GAS f32x4*)(mrow + 6144 + k);
;                         v2u o; o.x = pk2(hv.x, hv.y); o.y = pk2(hv.z, hv.w);
;                         *(GAS unsigned*)(h2q + (size_t)m * D + k) = pk4_fp8(hv.x, hv.y, hv.z, hv.w);
	v_lshlrev_b32_e32 v230, 16, v168
	v_and_b32_e32 v231, 0xffff0000, v168
	v_lshlrev_b32_e32 v168, 16, v169
	v_and_b32_e32 v169, 0xffff0000, v169
	v_lshlrev_b32_e32 v228, 16, v164
	v_and_b32_e32 v229, 0xffff0000, v164
	v_lshlrev_b32_e32 v164, 16, v165
	v_and_b32_e32 v165, 0xffff0000, v165
	s_waitcnt vmcnt(8)
	v_lshlrev_b32_e32 v240, 16, v166
	v_and_b32_e32 v241, 0xffff0000, v166
	v_lshlrev_b32_e32 v242, 16, v167
	v_and_b32_e32 v243, 0xffff0000, v167
	s_waitcnt vmcnt(7)
	v_lshlrev_b32_e32 v244, 16, v162
	v_and_b32_e32 v245, 0xffff0000, v162
	v_lshlrev_b32_e32 v246, 16, v163
	v_and_b32_e32 v247, 0xffff0000, v163
	v_lshlrev_b32_e32 v232, 16, v178
	v_and_b32_e32 v233, 0xffff0000, v178
	v_lshlrev_b32_e32 v236, 16, v172
	v_and_b32_e32 v237, 0xffff0000, v172
	v_lshlrev_b32_e32 v172, 16, v173
	v_and_b32_e32 v173, 0xffff0000, v173
	v_pk_mul_f32 v[22:23], v[22:23], v[174:175]
	v_pk_mul_f32 v[18:19], v[18:19], v[168:169]
	v_pk_mul_f32 v[16:17], v[16:17], v[230:231]
	v_lshlrev_b32_e32 v224, 16, v176
	v_and_b32_e32 v225, 0xffff0000, v176
	v_lshlrev_b32_e32 v176, 16, v177
	v_and_b32_e32 v177, 0xffff0000, v177
	v_pk_mul_f32 v[28:29], v[28:29], v[220:221]
	s_waitcnt vmcnt(6)
	v_lshlrev_b32_e32 v234, 16, v188
	v_and_b32_e32 v235, 0xffff0000, v188
	s_waitcnt vmcnt(4)
	v_lshlrev_b32_e32 v166, 16, v182
	v_and_b32_e32 v167, 0xffff0000, v182
	v_lshlrev_b32_e32 v182, 16, v183
	v_and_b32_e32 v183, 0xffff0000, v183
	s_waitcnt vmcnt(3)
	v_lshlrev_b32_e32 v162, 16, v184
	v_and_b32_e32 v163, 0xffff0000, v184
	v_pk_mul_f32 v[6:7], v[6:7], v[182:183]
	v_pk_mul_f32 v[182:183], v[0:1], v[162:163]
	v_lshlrev_b32_e32 v184, 16, v185
	v_and_b32_e32 v185, 0xffff0000, v185
	v_pk_mul_f32 v[184:185], v[2:3], v[184:185]
	v_lshlrev_b32_e32 v238, 16, v186
	v_and_b32_e32 v239, 0xffff0000, v186
	v_lshlrev_b32_e32 v186, 16, v187
	v_and_b32_e32 v187, 0xffff0000, v187
	v_pk_mul_f32 v[12:13], v[12:13], v[234:235]
	v_pk_mul_f32 v[10:11], v[10:11], v[186:187]
	v_pk_mul_f32 v[4:5], v[4:5], v[166:167]
	v_pk_fma_f32 v[162:163], v[164:165], s[38:39], v[18:19] op_sel_hi:[1,0,1]
	v_pk_fma_f32 v[164:165], v[228:229], s[38:39], v[16:17] op_sel_hi:[1,0,1]
	v_pk_mul_f32 v[30:31], v[30:31], v[222:223]
	v_lshlrev_b32_e32 v188, 16, v189
	v_and_b32_e32 v189, 0xffff0000, v189
	v_pk_mul_f32 v[174:175], v[20:21], v[226:227]
	v_pk_fma_f32 v[20:21], v[218:219], s[38:39], v[30:31] op_sel_hi:[1,0,1]
	v_lshlrev_b32_e32 v178, 16, v179
	v_and_b32_e32 v179, 0xffff0000, v179
	v_pk_mul_f32 v[14:15], v[14:15], v[188:189]
	s_waitcnt vmcnt(1)
	v_pk_add_f32 v[126:127], v[126:127], 1.0 op_sel_hi:[1,0]
	v_pk_add_f32 v[128:129], v[128:129], 1.0 op_sel_hi:[1,0]
	s_waitcnt vmcnt(0)
	v_pk_fma_f32 v[126:127], v[126:127], v[210:211], v[206:207]
	v_pk_fma_f32 v[128:129], v[128:129], v[158:159], v[208:209]
	v_cvt_pk_fp8_f32 v205, v126, v127
	v_lshl_add_u64 v[158:159], s[0:1], 0, v[36:37]
	v_pk_mul_f32 v[8:9], v[8:9], v[238:239]
	s_lshl_b64 s[0:1], s[46:47], 12
	v_cvt_pk_fp8_f32 v205, v128, v129 op_sel:[0,0,1]
	s_add_u32 s0, s3, s0
	s_addc_u32 s1, s39, s1
	global_store_dword v[158:159], v205, off
	global_load_dwordx4 v[206:209], v[72:73], off offset:1024
	global_load_dwordx4 v[210:213], v[74:75], off offset:1024
	v_mov_b32_e32 v205, 0
	s_waitcnt vmcnt(0)
	v_pk_fma_f32 v[212:213], v[208:209], v[130:131], v[212:213]
	v_pk_fma_f32 v[210:211], v[206:207], v[132:133], v[210:211]
	v_bfe_u32 v132, v212, 16, 1
	v_bfe_u32 v130, v210, 16, 1
	v_bfe_u32 v131, v211, 16, 1
	v_bfe_u32 v133, v213, 16, 1
	v_add3_u32 v130, v210, v130, s86
	v_add3_u32 v132, v212, v132, s86
	v_add3_u32 v131, v211, v131, s86
	v_add3_u32 v133, v213, v133, s86
	v_lshrrev_b32_e32 v130, 16, v130
	v_lshrrev_b32_e32 v132, 16, v132
	v_and_or_b32 v130, v131, s82, v130
	v_and_or_b32 v131, v133, s82, v132
	global_store_dwordx2 v[160:161], v[130:131], off offset:512
	global_load_dwordx4 v[130:133], v[82:83], off offset:1024
	s_nop 0
	global_load_dwordx4 v[206:209], v[80:81], off offset:1024
	s_waitcnt vmcnt(1)
	v_pk_add_f32 v[130:131], v[130:131], 1.0 op_sel_hi:[1,0]
	s_waitcnt vmcnt(0)
	v_pk_fma_f32 v[130:131], v[130:131], v[210:211], v[206:207]
	v_pk_add_f32 v[132:133], v[132:133], 1.0 op_sel_hi:[1,0]
	v_cvt_pk_fp8_f32 v205, v130, v131
	v_pk_fma_f32 v[132:133], v[132:133], v[212:213], v[208:209]
	s_nop 0
	v_cvt_pk_fp8_f32 v205, v132, v133 op_sel:[0,0,1]
	global_store_dword v[158:159], v205, off offset:256
	global_load_dwordx4 v[206:209], v[72:73], off offset:2048
	global_load_dwordx4 v[210:213], v[74:75], off offset:2048
	v_mov_b32_e32 v205, 0
	s_waitcnt vmcnt(0)
	v_pk_fma_f32 v[212:213], v[208:209], v[134:135], v[212:213]
	v_pk_fma_f32 v[210:211], v[206:207], v[136:137], v[210:211]
	v_bfe_u32 v136, v212, 16, 1
	v_bfe_u32 v134, v210, 16, 1
	v_bfe_u32 v135, v211, 16, 1
	v_bfe_u32 v137, v213, 16, 1
	v_add3_u32 v134, v210, v134, s86
	v_add3_u32 v136, v212, v136, s86
	v_add3_u32 v135, v211, v135, s86
	v_add3_u32 v137, v213, v137, s86
	v_lshrrev_b32_e32 v134, 16, v134
	v_lshrrev_b32_e32 v136, 16, v136
	v_and_or_b32 v134, v135, s82, v134
	v_and_or_b32 v135, v137, s82, v136
	global_store_dwordx2 v[160:161], v[134:135], off offset:1024
	global_load_dwordx4 v[134:137], v[82:83], off offset:2048
	s_nop 0
	global_load_dwordx4 v[206:209], v[80:81], off offset:2048
	s_waitcnt vmcnt(1)
	v_pk_add_f32 v[134:135], v[134:135], 1.0 op_sel_hi:[1,0]
	s_waitcnt vmcnt(0)
	v_pk_fma_f32 v[134:135], v[134:135], v[210:211], v[206:207]
	v_pk_add_f32 v[136:137], v[136:137], 1.0 op_sel_hi:[1,0]
	v_cvt_pk_fp8_f32 v205, v134, v135
	v_pk_fma_f32 v[136:137], v[136:137], v[212:213], v[208:209]
	s_nop 0
	v_cvt_pk_fp8_f32 v205, v136, v137 op_sel:[0,0,1]
	global_store_dword v[158:159], v205, off offset:512
	global_load_dwordx4 v[206:209], v[72:73], off offset:3072
	global_load_dwordx4 v[210:213], v[74:75], off offset:3072
	v_mov_b32_e32 v205, 0
	s_waitcnt vmcnt(0)
; #define GAS __attribute__((address_space(1)))
; __device__ __forceinline__ unsigned pk2(float lo, float hi) { return f2bf(lo) | (f2bf(hi) << 16); }
; __device__ __forceinline__ unsigned pk4_fp8(float a, float b, float c, float d) { int r = __builtin_amdgcn_cvt_pk_fp8_f32(a, b, 0, false); r = __builtin_amdgcn_cvt_pk_fp8_f32(c, d, r, true); return (unsigned)r; }
; __device__ __forceinline__ f32x4 bf4(unsigned a, unsigned b) { return (f32x4){bflo(a), bfhi(a), bflo(b), bfhi(b)}; }
; template <int l>
; __device__ __forceinline__ void layer_phases(Frame& F, const XcdBarrier& bar, const int lo, const int hi) {
;     ...
;                     for (int j = 0; j < 8; ++j) { const size_t off = (size_t)(m0 + 2 * rp + rr) * D + 4 * lq + 256 * j;
;                         f32x4 xv; if (l == 0) xv = __builtin_nontemporal_load((const GAS f32x4*)(xin + off)); else { const v2u xw_ = __builtin_nontemporal_load((const GAS v2u*)(xinb + off)); xv = bf4(xw_.x, xw_.y); } const v2u mw = __builtin_nontemporal_load((const GAS v2u*)(mixb + off)); const f32x4 gv = *(const GAS f32x4*)(mrow + 4096 + 4 * lq + 256 * j);
;                         vv[rr][j] = xv * ALPHA + gv * (f32x4){bflo(mw.x), bfhi(mw.x), bflo(mw.y), bfhi(mw.y)}; }
;     ...
;                     for (int j = 0; j < 8; ++j) { const int k = 4 * lq + 256 * j;
;                         const f32x4 xv = v[j] * rstd * *(const GAS f32x4*)(g1 + k) + *(const GAS f32x4*)(b1 + k);
;                         { v2u xo; xo.x = pk2(xv.x, xv.y); xo.y = pk2(xv.z, xv.w); *(GAS v2u*)(x1 + (size_t)m * D + k) = xo; }
;                         const f32x4 hv = xv * (*(const GAS f32x4*)(mrow + 8192 + k) + 1.0f) + *(const GAS f32x4*)(mrow + 6144 + k);
;                         v2u o; o.x = pk2(hv.x, hv.y); o.y = pk2(hv.z, hv.w);
;                         *(GAS unsigned*)(h2q + (size_t)m * D + k) = pk4_fp8(hv.x, hv.y, hv.z, hv.w);
	v_pk_fma_f32 v[212:213], v[138:139], v[208:209], v[212:213]
	v_pk_fma_f32 v[210:211], v[140:141], v[206:207], v[210:211]
	v_bfe_u32 v140, v212, 16, 1
	v_bfe_u32 v138, v210, 16, 1
	v_bfe_u32 v139, v211, 16, 1
	v_bfe_u32 v141, v213, 16, 1
	v_add3_u32 v138, v210, v138, s86
	v_add3_u32 v140, v212, v140, s86
	v_add3_u32 v139, v211, v139, s86
	v_add3_u32 v141, v213, v141, s86
	v_lshrrev_b32_e32 v138, 16, v138
	v_lshrrev_b32_e32 v140, 16, v140
	v_and_or_b32 v138, v139, s82, v138
	v_and_or_b32 v139, v141, s82, v140
	global_store_dwordx2 v[160:161], v[138:139], off offset:1536
	global_load_dwordx4 v[138:141], v[82:83], off offset:3072
	s_nop 0
	global_load_dwordx4 v[206:209], v[80:81], off offset:3072
	s_waitcnt vmcnt(1)
	v_pk_add_f32 v[138:139], v[138:139], 1.0 op_sel_hi:[1,0]
	s_waitcnt vmcnt(0)
	v_pk_fma_f32 v[138:139], v[210:211], v[138:139], v[206:207]
	v_pk_add_f32 v[140:141], v[140:141], 1.0 op_sel_hi:[1,0]
	v_cvt_pk_fp8_f32 v205, v138, v139
	v_pk_fma_f32 v[140:141], v[212:213], v[140:141], v[208:209]
	s_nop 0
	v_cvt_pk_fp8_f32 v205, v140, v141 op_sel:[0,0,1]
	global_store_dword v[158:159], v205, off offset:768
	global_load_dwordx4 v[206:209], v[38:39], off
	global_load_dwordx4 v[210:213], v[40:41], off
	v_mov_b32_e32 v205, 0
	s_waitcnt vmcnt(0)
	v_pk_fma_f32 v[212:213], v[142:143], v[208:209], v[212:213]
	v_pk_fma_f32 v[210:211], v[144:145], v[206:207], v[210:211]
	v_bfe_u32 v144, v212, 16, 1
	v_bfe_u32 v142, v210, 16, 1
	v_bfe_u32 v143, v211, 16, 1
	v_bfe_u32 v145, v213, 16, 1
	v_add3_u32 v142, v210, v142, s86
	v_add3_u32 v144, v212, v144, s86
	v_add3_u32 v143, v211, v143, s86
	v_add3_u32 v145, v213, v145, s86
	v_lshrrev_b32_e32 v142, 16, v142
	v_lshrrev_b32_e32 v144, 16, v144
	v_and_or_b32 v142, v143, s82, v142
	v_and_or_b32 v143, v145, s82, v144
	global_store_dwordx2 v[160:161], v[142:143], off offset:2048
	global_load_dwordx4 v[142:145], v[32:33], off
	s_nop 0
	global_load_dwordx4 v[206:209], v[34:35], off
	s_waitcnt vmcnt(1)
	v_pk_add_f32 v[142:143], v[142:143], 1.0 op_sel_hi:[1,0]
	s_waitcnt vmcnt(0)
	v_pk_fma_f32 v[142:143], v[210:211], v[142:143], v[206:207]
	v_pk_add_f32 v[144:145], v[144:145], 1.0 op_sel_hi:[1,0]
	v_cvt_pk_fp8_f32 v205, v142, v143
	v_pk_fma_f32 v[144:145], v[212:213], v[144:145], v[208:209]
	s_nop 0
	v_cvt_pk_fp8_f32 v205, v144, v145 op_sel:[0,0,1]
	global_store_dword v[158:159], v205, off offset:1024
	global_load_dwordx4 v[206:209], v[38:39], off offset:1024
	global_load_dwordx4 v[210:213], v[40:41], off offset:1024
	v_mov_b32_e32 v205, 0
	s_waitcnt vmcnt(0)
	v_pk_fma_f32 v[212:213], v[146:147], v[208:209], v[212:213]
	v_pk_fma_f32 v[210:211], v[148:149], v[206:207], v[210:211]
	v_bfe_u32 v148, v212, 16, 1
	v_bfe_u32 v146, v210, 16, 1
	v_bfe_u32 v147, v211, 16, 1
	v_bfe_u32 v149, v213, 16, 1
	v_add3_u32 v146, v210, v146, s86
	v_add3_u32 v148, v212, v148, s86
	v_add3_u32 v147, v211, v147, s86
	v_add3_u32 v149, v213, v149, s86
	v_lshrrev_b32_e32 v146, 16, v146
	v_lshrrev_b32_e32 v148, 16, v148
	v_and_or_b32 v146, v147, s82, v146
	v_and_or_b32 v147, v149, s82, v148
	global_store_dwordx2 v[160:161], v[146:147], off offset:2560
	global_load_dwordx4 v[146:149], v[32:33], off offset:1024
	s_nop 0
	global_load_dwordx4 v[206:209], v[34:35], off offset:1024
	s_waitcnt vmcnt(1)
	v_pk_add_f32 v[146:147], v[146:147], 1.0 op_sel_hi:[1,0]
	s_waitcnt vmcnt(0)
	v_pk_fma_f32 v[146:147], v[210:211], v[146:147], v[206:207]
	v_pk_add_f32 v[148:149], v[148:149], 1.0 op_sel_hi:[1,0]
	v_cvt_pk_fp8_f32 v205, v146, v147
	v_pk_fma_f32 v[148:149], v[212:213], v[148:149], v[208:209]
	s_nop 0
	v_cvt_pk_fp8_f32 v205, v148, v149 op_sel:[0,0,1]
	global_store_dword v[158:159], v205, off offset:1280
	global_load_dwordx4 v[206:209], v[38:39], off offset:2048
	global_load_dwordx4 v[210:213], v[40:41], off offset:2048
	v_mov_b32_e32 v205, 0
	s_waitcnt vmcnt(0)
	v_pk_fma_f32 v[208:209], v[154:155], v[208:209], v[212:213]
	v_pk_fma_f32 v[206:207], v[156:157], v[206:207], v[210:211]
	v_bfe_u32 v156, v208, 16, 1
	v_bfe_u32 v154, v206, 16, 1
	v_bfe_u32 v155, v207, 16, 1
	v_bfe_u32 v157, v209, 16, 1
	v_add3_u32 v154, v206, v154, s86
	v_add3_u32 v156, v208, v156, s86
	v_add3_u32 v155, v207, v155, s86
	v_add3_u32 v157, v209, v157, s86
	v_lshrrev_b32_e32 v154, 16, v154
	v_lshrrev_b32_e32 v156, 16, v156
	v_and_or_b32 v154, v155, s82, v154
	v_and_or_b32 v155, v157, s82, v156
	global_store_dwordx2 v[160:161], v[154:155], off offset:3072
	global_load_dwordx4 v[154:157], v[32:33], off offset:2048
	s_nop 0
	global_load_dwordx4 v[190:193], v[34:35], off offset:2048
	v_lshlrev_b32_e32 v212, 16, v170
	v_and_b32_e32 v213, 0xffff0000, v170
	v_lshlrev_b32_e32 v170, 16, v171
	v_and_b32_e32 v171, 0xffff0000, v171
	v_pk_fma_f32 v[166:167], v[170:171], s[38:39], v[22:23] op_sel_hi:[1,0,1]
	v_lshlrev_b32_e32 v210, 16, v180
	v_and_b32_e32 v211, 0xffff0000, v180
	v_lshlrev_b32_e32 v180, 16, v181
	v_and_b32_e32 v181, 0xffff0000, v181
	v_pk_mul_f32 v[26:27], v[26:27], v[180:181]
	v_pk_mul_f32 v[180:181], v[24:25], v[210:211]
	v_pk_fma_f32 v[24:25], v[214:215], s[38:39], v[28:29] op_sel_hi:[1,0,1]
	v_pk_fma_f32 v[28:29], v[176:177], s[38:39], v[26:27] op_sel_hi:[1,0,1]
	v_pk_fma_f32 v[30:31], v[224:225], s[38:39], v[180:181] op_sel_hi:[1,0,1]
	v_pk_fma_f32 v[168:169], v[212:213], s[38:39], v[174:175] op_sel_hi:[1,0,1]
	v_mov_b32_e32 v22, v24
	v_mov_b32_e32 v23, v30
	v_mov_b32_e32 v26, v25
	v_mov_b32_e32 v27, v31
	v_mov_b32_e32 v174, v20
	v_mov_b32_e32 v175, v28
	v_mov_b32_e32 v176, v21
	v_mov_b32_e32 v177, v29
	v_mov_b32_e32 v180, v168
	v_mov_b32_e32 v181, v167
	v_pk_add_f32 v[22:23], v[22:23], v[26:27]
	v_pk_add_f32 v[26:27], v[174:175], v[176:177]
	s_waitcnt vmcnt(1)
; #define GAS __attribute__((address_space(1)))
; __device__ __forceinline__ unsigned pk2(float lo, float hi) { return f2bf(lo) | (f2bf(hi) << 16); }
; __device__ __forceinline__ unsigned pk4_fp8(float a, float b, float c, float d) { int r = __builtin_amdgcn_cvt_pk_fp8_f32(a, b, 0, false); r = __builtin_amdgcn_cvt_pk_fp8_f32(c, d, r, true); return (unsigned)r; }
; template <int l>
; __device__ __forceinline__ void layer_phases(Frame& F, const XcdBarrier& bar, const int lo, const int hi) {
;     ...
;                     f32x4 (&v)[8] = vv[rq]; float s = 0.f;
; #pragma unroll
;                     for (int j = 0; j < 8; ++j) s += (v[j].x + v[j].y) + (v[j].z + v[j].w);
;                     const float mean = wave_sum(s) * (1.f / D); float s2 = 0.f;
; #pragma unroll
;                     for (int j = 0; j < 8; ++j) { v[j] = v[j] - mean; s2 += (v[j].x * v[j].x + v[j].y * v[j].y) + (v[j].z * v[j].z + v[j].w * v[j].w); }
;     ...
;                     for (int j = 0; j < 8; ++j) { const int k = 4 * lq + 256 * j;
;                         const f32x4 xv = v[j] * rstd * *(const GAS f32x4*)(g1 + k) + *(const GAS f32x4*)(b1 + k);
;                         { v2u xo; xo.x = pk2(xv.x, xv.y); xo.y = pk2(xv.z, xv.w); *(GAS v2u*)(x1 + (size_t)m * D + k) = xo; }
;                         const f32x4 hv = xv * (*(const GAS f32x4*)(mrow + 8192 + k) + 1.0f) + *(const GAS f32x4*)(mrow + 6144 + k);
;                         v2u o; o.x = pk2(hv.x, hv.y); o.y = pk2(hv.z, hv.w);
;                         *(GAS unsigned*)(h2q + (size_t)m * D + k) = pk4_fp8(hv.x, hv.y, hv.z, hv.w);
	v_pk_add_f32 v[0:1], v[154:155], 1.0 op_sel_hi:[1,0]
	s_waitcnt vmcnt(0)
	v_pk_fma_f32 v[0:1], v[206:207], v[0:1], v[190:191]
	v_pk_add_f32 v[2:3], v[156:157], 1.0 op_sel_hi:[1,0]
	v_cvt_pk_fp8_f32 v205, v0, v1
	v_pk_fma_f32 v[2:3], v[208:209], v[2:3], v[192:193]
	v_pk_fma_f32 v[156:157], v[232:233], s[38:39], v[12:13] op_sel_hi:[1,0,1]
	v_pk_fma_f32 v[12:13], v[172:173], s[38:39], v[10:11] op_sel_hi:[1,0,1]
	v_cvt_pk_fp8_f32 v205, v2, v3 op_sel:[0,0,1]
	v_pk_fma_f32 v[154:155], v[178:179], s[38:39], v[14:15] op_sel_hi:[1,0,1]
	v_pk_mov_b32 v[178:179], v[168:169], v[166:167] op_sel:[1,0]
	v_pk_add_f32 v[22:23], v[22:23], v[26:27]
	global_store_dword v[158:159], v205, off offset:1536
	global_load_dwordx4 v[16:19], v[38:39], off offset:3072
	global_load_dwordx4 v[170:173], v[40:41], off offset:3072
	v_pk_add_f32 v[174:175], v[178:179], v[180:181]
	v_add_f32_e32 v22, 0, v22
	v_pk_add_f32 v[26:27], v[174:175], v[174:175] op_sel:[0,1] op_sel_hi:[1,0]
	v_pk_fma_f32 v[14:15], v[236:237], s[38:39], v[8:9] op_sel_hi:[1,0,1]
	v_pk_fma_f32 v[8:9], v[242:243], s[38:39], v[6:7] op_sel_hi:[1,0,1]
	v_pk_fma_f32 v[10:11], v[240:241], s[38:39], v[4:5] op_sel_hi:[1,0,1]
	v_pk_fma_f32 v[4:5], v[246:247], s[38:39], v[184:185] op_sel_hi:[1,0,1]
	v_pk_fma_f32 v[6:7], v[244:245], s[38:39], v[182:183] op_sel_hi:[1,0,1]
	v_add_f32_e32 v182, v164, v165
	v_add_f32_e32 v184, v162, v163
	v_mov_b32_e32 v187, v156
	v_mov_b32_e32 v183, v154
	v_mov_b32_e32 v185, v155
	v_mov_b32_e32 v27, v157
	v_add_f32_e32 v186, v22, v23
	v_pk_mov_b32 v[188:189], v[14:15], v[12:13] op_sel:[1,0]
	v_mov_b32_e32 v190, v14
	v_mov_b32_e32 v191, v13
	v_pk_add_f32 v[176:177], v[182:183], v[184:185]
	v_pk_add_f32 v[22:23], v[186:187], v[26:27]
	v_pk_add_f32 v[178:179], v[188:189], v[190:191]
	v_pk_add_f32 v[22:23], v[22:23], v[176:177]
	v_pk_add_f32 v[174:175], v[178:179], v[178:179] op_sel:[0,1] op_sel_hi:[1,0]
	v_pk_add_f32 v[22:23], v[22:23], v[22:23] op_sel:[0,1] op_sel_hi:[1,0]
	v_add_f32_e32 v192, v10, v11
	v_add_f32_e32 v206, v8, v9
	v_mov_b32_e32 v193, v4
	v_mov_b32_e32 v207, v5
	v_mov_b32_e32 v175, v7
	v_mov_b32_e32 v23, v6
	v_pk_add_f32 v[180:181], v[192:193], v[206:207]
	v_pk_add_f32 v[22:23], v[22:23], v[174:175]
	v_pk_mul_f32 v[26:27], v[150:151], v[60:61] op_sel_hi:[1,0]
	v_pk_add_f32 v[22:23], v[22:23], v[180:181]
	v_mov_b32_e32 v189, 0
	v_add_f32_e32 v22, v22, v23
	ds_bpermute_b32 v23, v53, v22
	s_waitcnt lgkmcnt(0)
	v_add_f32_e32 v22, v22, v23
	ds_bpermute_b32 v23, v194, v22
	s_waitcnt lgkmcnt(0)
	v_add_f32_e32 v22, v22, v23
	ds_bpermute_b32 v23, v195, v22
	s_waitcnt lgkmcnt(0)
	v_add_f32_e32 v22, v22, v23
	ds_bpermute_b32 v23, v196, v22
	s_waitcnt lgkmcnt(0)
	v_add_f32_e32 v22, v22, v23
	ds_bpermute_b32 v23, v197, v22
	s_waitcnt lgkmcnt(0)
	v_add_f32_e32 v174, v22, v23
	v_pk_mul_f32 v[22:23], v[152:153], v[60:61] op_sel_hi:[1,0]
	ds_bpermute_b32 v60, v198, v174
	s_waitcnt lgkmcnt(0)
	v_add_f32_e32 v60, v174, v60
	v_fmamk_f32 v15, v60, 0xba000000, v15
	v_fmac_f32_e32 v14, 0xba000000, v60
	v_fmamk_f32 v13, v60, 0xba000000, v13
	v_fmac_f32_e32 v12, 0xba000000, v60
	v_fmac_f32_e32 v10, 0xba000000, v60
	v_fmac_f32_e32 v8, 0xba000000, v60
	s_waitcnt vmcnt(0)
	v_pk_fma_f32 v[26:27], v[26:27], v[18:19], v[172:173]
	v_pk_fma_f32 v[22:23], v[22:23], v[16:17], v[170:171]
	v_bfe_u32 v18, v26, 16, 1
	v_bfe_u32 v16, v22, 16, 1
	v_bfe_u32 v17, v23, 16, 1
	v_bfe_u32 v19, v27, 16, 1
	v_add3_u32 v16, v22, v16, s86
	v_add3_u32 v18, v26, v18, s86
	v_add3_u32 v17, v23, v17, s86
	v_add3_u32 v19, v27, v19, s86
	v_lshrrev_b32_e32 v16, 16, v16
	v_lshrrev_b32_e32 v18, 16, v18
	v_and_or_b32 v16, v17, s82, v16
	v_and_or_b32 v17, v19, s82, v18
	global_store_dwordx2 v[160:161], v[16:17], off offset:3584
	global_load_dwordx4 v[16:19], v[32:33], off offset:3072
	s_nop 0
	global_load_dwordx4 v[150:153], v[34:35], off offset:3072
	v_fmamk_f32 v11, v60, 0xba000000, v11
	v_fmamk_f32 v9, v60, 0xba000000, v9
	v_pk_mul_f32 v[182:183], v[12:13], v[12:13]
	v_pk_mul_f32 v[184:185], v[14:15], v[14:15]
	v_mul_f32_e32 v186, v10, v10
	v_mul_f32_e32 v188, v8, v8
	v_pk_mov_b32 v[192:193], v[184:185], v[182:183] op_sel:[1,0]
	v_mov_b32_e32 v185, v183
	v_pk_fma_f32 v[182:183], v[10:11], v[10:11], v[186:187] op_sel_hi:[1,1,0]
	v_pk_fma_f32 v[186:187], v[8:9], v[8:9], v[188:189] op_sel_hi:[1,1,0]
	v_fmamk_f32 v21, v60, 0xba000000, v21
	v_fmamk_f32 v25, v60, 0xba000000, v25
	v_fmamk_f32 v29, v60, 0xba000000, v29
	v_fmamk_f32 v31, v60, 0xba000000, v31
	v_fmac_f32_e32 v20, 0xba000000, v60
	v_fmac_f32_e32 v24, 0xba000000, v60
	v_fmac_f32_e32 v28, 0xba000000, v60
	v_fmac_f32_e32 v30, 0xba000000, v60
	v_fmamk_f32 v169, v60, 0xba000000, v169
	v_fmac_f32_e32 v168, 0xba000000, v60
	v_fmamk_f32 v167, v60, 0xba000000, v167
	v_fmac_f32_e32 v166, 0xba000000, v60
	v_mov_b32_e32 v170, v25
	v_mov_b32_e32 v171, v31
	v_mov_b32_e32 v174, v21
	v_mov_b32_e32 v175, v29
	v_mov_b32_e32 v160, v24
	v_mov_b32_e32 v161, v30
	v_mov_b32_e32 v172, v20
	v_mov_b32_e32 v173, v28
	v_pk_mul_f32 v[176:177], v[166:167], v[166:167]
	v_pk_mul_f32 v[178:179], v[168:169], v[168:169]
	v_pk_mul_f32 v[170:171], v[170:171], v[170:171]
	v_pk_mul_f32 v[174:175], v[174:175], v[174:175]
	v_pk_mov_b32 v[190:191], v[178:179], v[176:177] op_sel:[1,0]
	v_mov_b32_e32 v179, v177
	v_pk_fma_f32 v[160:161], v[160:161], v[160:161], v[170:171]
	v_pk_fma_f32 v[170:171], v[172:173], v[172:173], v[174:175]
	v_pk_add_f32 v[172:173], v[190:191], v[178:179]
	v_pk_add_f32 v[160:161], v[160:161], v[170:171]
	v_fmamk_f32 v155, v60, 0xba000000, v155
	v_fmac_f32_e32 v154, 0xba000000, v60
	v_pk_add_f32 v[170:171], v[172:173], v[172:173] op_sel_hi:[0,1]
	v_pk_add_f32 v[160:161], v[160:161], v[160:161] op_sel_hi:[0,1]
	v_mul_f32_e32 v170, v154, v154
	v_mul_f32_e32 v160, v155, v155
	v_fmac_f32_e32 v164, 0xba000000, v60
	v_fmac_f32_e32 v162, 0xba000000, v60
	v_fmamk_f32 v165, v60, 0xba000000, v165
	v_fmamk_f32 v163, v60, 0xba000000, v163
	v_fmamk_f32 v157, v60, 0xba000000, v157
	v_fmac_f32_e32 v156, 0xba000000, v60
	v_fmamk_f32 v5, v60, 0xba000000, v5
	v_fmac_f32_e32 v4, 0xba000000, v60
	v_fmamk_f32 v7, v60, 0xba000000, v7
	v_fmac_f32_e32 v6, 0xba000000, v60
	v_mul_f32_e32 v60, v164, v164
	v_mul_f32_e32 v180, v162, v162
	v_pk_fma_f32 v[176:177], v[164:165], v[164:165], v[60:61] op_sel_hi:[1,1,0]
	v_pk_fma_f32 v[180:181], v[162:163], v[162:163], v[180:181] op_sel_hi:[1,1,0]
	v_mul_f32_e32 v176, v156, v156
	v_mul_f32_e32 v180, v157, v157
	v_pk_add_f32 v[172:173], v[176:177], v[180:181]
	v_pk_add_f32 v[174:175], v[192:193], v[184:185]
	v_mul_f32_e32 v182, v6, v6
	v_pk_add_f32 v[174:175], v[174:175], v[174:175] op_sel_hi:[0,1]
	v_mul_f32_e32 v186, v7, v7
	v_mul_f32_e32 v174, v4, v4
	v_pk_add_f32 v[176:177], v[182:183], v[186:187]
	s_waitcnt vmcnt(1)
; #define GAS __attribute__((address_space(1)))
; __device__ __forceinline__ unsigned pk2(float lo, float hi) { return f2bf(lo) | (f2bf(hi) << 16); }
; __device__ __forceinline__ unsigned pk4_fp8(float a, float b, float c, float d) { int r = __builtin_amdgcn_cvt_pk_fp8_f32(a, b, 0, false); r = __builtin_amdgcn_cvt_pk_fp8_f32(c, d, r, true); return (unsigned)r; }
; template <int l>
; __device__ __forceinline__ void layer_phases(Frame& F, const XcdBarrier& bar, const int lo, const int hi) {
;     ...
;                     const float mean = wave_sum(s) * (1.f / D); float s2 = 0.f;
; #pragma unroll
;                     for (int j = 0; j < 8; ++j) { v[j] = v[j] - mean; s2 += (v[j].x * v[j].x + v[j].y * v[j].y) + (v[j].z * v[j].z + v[j].w * v[j].w); }
;                     const float rstd = 1.f / sqrtf(wave_sum(s2) * (1.f / D) + LN_EPS);
; #pragma unroll
;                     for (int j = 0; j < 8; ++j) { const int k = 4 * lq + 256 * j;
;                         const f32x4 xv = v[j] * rstd * *(const GAS f32x4*)(g1 + k) + *(const GAS f32x4*)(b1 + k);
;                         { v2u xo; xo.x = pk2(xv.x, xv.y); xo.y = pk2(xv.z, xv.w); *(GAS v2u*)(x1 + (size_t)m * D + k) = xo; }
;                         const f32x4 hv = xv * (*(const GAS f32x4*)(mrow + 8192 + k) + 1.0f) + *(const GAS f32x4*)(mrow + 6144 + k);
;                         v2u o; o.x = pk2(hv.x, hv.y); o.y = pk2(hv.z, hv.w);
;                         *(GAS unsigned*)(h2q + (size_t)m * D + k) = pk4_fp8(hv.x, hv.y, hv.z, hv.w);
	v_pk_add_f32 v[16:17], v[16:17], 1.0 op_sel_hi:[1,0]
	s_waitcnt vmcnt(0)
	v_pk_fma_f32 v[16:17], v[22:23], v[16:17], v[150:151]
	v_pk_add_f32 v[18:19], v[18:19], 1.0 op_sel_hi:[1,0]
	v_cvt_pk_fp8_f32 v189, v16, v17
	v_pk_fma_f32 v[18:19], v[26:27], v[18:19], v[152:153]
	v_pk_add_f32 v[22:23], v[170:171], v[160:161]
	v_cvt_pk_fp8_f32 v189, v18, v19 op_sel:[0,0,1]
	v_pk_add_f32 v[22:23], v[172:173], v[22:23]
	global_store_dword v[158:159], v189, off offset:1792
	global_load_dwordx4 v[150:153], v[72:73], off
	s_nop 0
	global_load_dwordx4 v[158:161], v[74:75], off
	v_pk_add_f32 v[22:23], v[22:23], v[22:23] op_sel_hi:[0,1]
	v_mul_f32_e32 v22, v5, v5
	v_pk_add_f32 v[22:23], v[174:175], v[22:23]
	s_nop 0
	v_pk_add_f32 v[22:23], v[176:177], v[22:23]
	s_nop 0
	v_add_f32_e32 v22, v22, v23
	ds_bpermute_b32 v23, v53, v22
	s_waitcnt lgkmcnt(0)
	v_add_f32_e32 v22, v22, v23
	ds_bpermute_b32 v23, v194, v22
	s_waitcnt lgkmcnt(0)
	v_add_f32_e32 v22, v22, v23
	ds_bpermute_b32 v23, v195, v22
	s_waitcnt lgkmcnt(0)
	v_add_f32_e32 v22, v22, v23
	ds_bpermute_b32 v23, v196, v22
	s_waitcnt lgkmcnt(0)
	v_add_f32_e32 v22, v22, v23
	ds_bpermute_b32 v23, v197, v22
	s_waitcnt lgkmcnt(0)
	v_add_f32_e32 v22, v22, v23
	ds_bpermute_b32 v23, v198, v22
	s_waitcnt lgkmcnt(0)
	v_add_f32_e32 v22, v22, v23
	v_fmamk_f32 v22, v22, 0x3a000000, v200
	v_mul_f32_e32 v23, 0x4f800000, v22
	v_cmp_gt_f32_e32 vcc, s85, v22
	s_nop 1
	v_cndmask_b32_e32 v22, v22, v23, vcc
	v_sqrt_f32_e32 v23, v22
	s_nop 0
	v_add_u32_e32 v26, -1, v23
	v_add_u32_e32 v27, 1, v23
	v_fma_f32 v60, -v26, v23, v22
	v_fma_f32 v170, -v27, v23, v22
	v_cmp_ge_f32_e64 s[14:15], 0, v60
	s_nop 1
	v_cndmask_b32_e64 v23, v23, v26, s[14:15]
	v_cmp_lt_f32_e64 s[14:15], 0, v170
	s_nop 1
	v_cndmask_b32_e64 v23, v23, v27, s[14:15]
	v_mul_f32_e32 v26, 0x37800000, v23
	v_cndmask_b32_e32 v23, v23, v26, vcc
	v_cmp_class_f32_e32 vcc, v22, v201
	s_nop 1
	v_cndmask_b32_e32 v26, v23, v22, vcc
	v_div_scale_f32 v27, s[14:15], v26, v26, 1.0
	v_rcp_f32_e32 v60, v27
	v_lshl_add_u64 v[22:23], s[0:1], 0, v[88:89]
	v_div_scale_f32 v88, vcc, 1.0, v26, 1.0
	v_fma_f32 v89, -v27, v60, 1.0
	v_fmac_f32_e32 v60, v89, v60
	v_mul_f32_e32 v89, v88, v60
	v_fma_f32 v170, -v27, v89, v88
	v_fmac_f32_e32 v89, v170, v60
	v_fma_f32 v27, -v27, v89, v88
	v_div_fmas_f32 v27, v27, v60, v89
	v_div_fixup_f32 v88, v27, v26, 1.0
	v_pk_mul_f32 v[24:25], v[24:25], v[88:89] op_sel_hi:[1,0]
	v_pk_mul_f32 v[20:21], v[20:21], v[88:89] op_sel_hi:[1,0]
	s_waitcnt vmcnt(0)
	v_pk_fma_f32 v[158:159], v[150:151], v[24:25], v[158:159]
	v_pk_fma_f32 v[20:21], v[152:153], v[20:21], v[160:161]
	v_bfe_u32 v24, v158, 16, 1
	v_bfe_u32 v26, v20, 16, 1
	v_bfe_u32 v25, v159, 16, 1
	v_bfe_u32 v27, v21, 16, 1
	v_add3_u32 v24, v158, v24, s86
	v_add3_u32 v26, v20, v26, s86
	v_add3_u32 v25, v159, v25, s86
	v_add3_u32 v27, v21, v27, s86
	v_lshrrev_b32_e32 v24, 16, v24
	v_lshrrev_b32_e32 v26, 16, v26
	v_and_or_b32 v24, v25, s82, v24
	v_and_or_b32 v25, v27, s82, v26
	global_store_dwordx2 v[22:23], v[24:25], off
	global_load_dwordx4 v[24:27], v[32:33], off offset:-4096
	s_nop 0
	global_load_dwordx4 v[150:153], v[34:35], off offset:-4096
	v_mov_b32_e32 v60, 0
	s_add_u32 s0, s48, s16
	s_addc_u32 s1, s49, s17
	v_pk_mul_f32 v[30:31], v[30:31], v[88:89] op_sel_hi:[1,0]
	v_pk_mul_f32 v[28:29], v[28:29], v[88:89] op_sel_hi:[1,0]
	v_pk_mul_f32 v[166:167], v[166:167], v[88:89] op_sel_hi:[1,0]
	s_mov_b32 s14, 0x8000
	s_waitcnt vmcnt(1)
	v_pk_add_f32 v[24:25], v[24:25], 1.0 op_sel_hi:[1,0]
	s_waitcnt vmcnt(0)
	v_pk_fma_f32 v[24:25], v[24:25], v[158:159], v[150:151]
	v_pk_add_f32 v[26:27], v[26:27], 1.0 op_sel_hi:[1,0]
	v_cvt_pk_fp8_f32 v60, v24, v25
	v_pk_fma_f32 v[26:27], v[26:27], v[20:21], v[152:153]
	v_lshl_add_u64 v[20:21], s[0:1], 0, v[36:37]
	v_readlane_b32 s0, v248, 24
	v_cvt_pk_fp8_f32 v60, v26, v27 op_sel:[0,0,1]
	global_store_dword v[20:21], v60, off
	global_load_dwordx4 v[150:153], v[72:73], off offset:1024
	global_load_dwordx4 v[158:161], v[74:75], off offset:1024
	v_mov_b32_e32 v60, 0
	s_waitcnt vmcnt(0)
	v_pk_fma_f32 v[36:37], v[152:153], v[28:29], v[160:161]
	v_pk_fma_f32 v[158:159], v[150:151], v[30:31], v[158:159]
	v_bfe_u32 v30, v36, 16, 1
	v_bfe_u32 v28, v158, 16, 1
	v_bfe_u32 v29, v159, 16, 1
	v_bfe_u32 v31, v37, 16, 1
	v_add3_u32 v28, v158, v28, s86
	v_add3_u32 v30, v36, v30, s86
	v_add3_u32 v29, v159, v29, s86
	v_add3_u32 v31, v37, v31, s86
	v_lshrrev_b32_e32 v28, 16, v28
	v_lshrrev_b32_e32 v30, 16, v30
	v_and_or_b32 v28, v29, s82, v28
	v_and_or_b32 v29, v31, s82, v30
	global_store_dwordx2 v[22:23], v[28:29], off offset:512
	global_load_dwordx4 v[28:31], v[82:83], off offset:1024
	s_nop 0
	global_load_dwordx4 v[150:153], v[80:81], off offset:1024
	s_waitcnt vmcnt(1)
	v_pk_add_f32 v[28:29], v[28:29], 1.0 op_sel_hi:[1,0]
	s_waitcnt vmcnt(0)
	v_pk_fma_f32 v[28:29], v[28:29], v[158:159], v[150:151]
	v_pk_add_f32 v[30:31], v[30:31], 1.0 op_sel_hi:[1,0]
	v_cvt_pk_fp8_f32 v60, v28, v29
	v_pk_fma_f32 v[30:31], v[30:31], v[36:37], v[152:153]
	v_pk_mul_f32 v[36:37], v[168:169], v[88:89] op_sel_hi:[1,0]
	v_cvt_pk_fp8_f32 v60, v30, v31 op_sel:[0,0,1]
	global_store_dword v[20:21], v60, off offset:256
	global_load_dwordx4 v[150:153], v[72:73], off offset:2048
	global_load_dwordx4 v[158:161], v[74:75], off offset:2048
	s_waitcnt vmcnt(0)
; #define GAS __attribute__((address_space(1)))
; #define LAS __attribute__((address_space(3)))
; __device__ __forceinline__ unsigned pk2(float lo, float hi) { return f2bf(lo) | (f2bf(hi) << 16); }
; __device__ __forceinline__ unsigned pk4_fp8(float a, float b, float c, float d) { int r = __builtin_amdgcn_cvt_pk_fp8_f32(a, b, 0, false); r = __builtin_amdgcn_cvt_pk_fp8_f32(c, d, r, true); return (unsigned)r; }
; template <int l>
; __device__ __forceinline__ void layer_phases(Frame& F, const XcdBarrier& bar, const int lo, const int hi) {
;     ...
;                     for (int j = 0; j < 8; ++j) { const int k = 4 * lq + 256 * j;
;                         const f32x4 xv = v[j] * rstd * *(const GAS f32x4*)(g1 + k) + *(const GAS f32x4*)(b1 + k);
;                         { v2u xo; xo.x = pk2(xv.x, xv.y); xo.y = pk2(xv.z, xv.w); *(GAS v2u*)(x1 + (size_t)m * D + k) = xo; }
;                         const f32x4 hv = xv * (*(const GAS f32x4*)(mrow + 8192 + k) + 1.0f) + *(const GAS f32x4*)(mrow + 6144 + k);
;                         v2u o; o.x = pk2(hv.x, hv.y); o.y = pk2(hv.z, hv.w);
;                         *(GAS unsigned*)(h2q + (size_t)m * D + k) = pk4_fp8(hv.x, hv.y, hv.z, hv.w);
;                         const int chunk = (lq >> 1) + 32 * j;
;                         *(LAS v2u*)(h2s + rloc * 4096 + ((chunk ^ (rloc & 15)) << 4) + (lq & 1) * 8) = o; }
	v_pk_fma_f32 v[166:167], v[152:153], v[166:167], v[160:161]
	v_pk_fma_f32 v[36:37], v[150:151], v[36:37], v[158:159]
	v_bfe_u32 v150, v166, 16, 1
	v_bfe_u32 v60, v36, 16, 1
	v_bfe_u32 v89, v37, 16, 1
	v_bfe_u32 v151, v167, 16, 1
	v_add3_u32 v60, v36, v60, s86
	v_add3_u32 v150, v166, v150, s86
	v_add3_u32 v89, v37, v89, s86
	v_add3_u32 v151, v167, v151, s86
	v_lshrrev_b32_e32 v60, 16, v60
	v_lshrrev_b32_e32 v152, 16, v150
	v_and_or_b32 v150, v89, s82, v60
	v_and_or_b32 v151, v151, s82, v152
	global_store_dwordx2 v[22:23], v[150:151], off offset:1024
	global_load_dwordx4 v[150:153], v[82:83], off offset:2048
	s_nop 0
	global_load_dwordx4 v[158:161], v[80:81], off offset:2048
	v_mov_b32_e32 v60, 0
	v_pk_mul_f32 v[162:163], v[162:163], v[88:89] op_sel_hi:[1,0]
	s_waitcnt vmcnt(1)
	v_pk_add_f32 v[150:151], v[150:151], 1.0 op_sel_hi:[1,0]
	s_waitcnt vmcnt(0)
	v_pk_fma_f32 v[36:37], v[150:151], v[36:37], v[158:159]
	v_pk_add_f32 v[150:151], v[152:153], 1.0 op_sel_hi:[1,0]
	v_cvt_pk_fp8_f32 v60, v36, v37
	v_pk_fma_f32 v[150:151], v[150:151], v[166:167], v[160:161]
	v_pk_mul_f32 v[152:153], v[164:165], v[88:89] op_sel_hi:[1,0]
	v_lshrrev_b32_e32 v167, 1, v204
	v_cvt_pk_fp8_f32 v60, v150, v151 op_sel:[0,0,1]
	v_add_u32_e32 v170, 32, v167
	v_add_u32_e32 v171, 64, v167
	v_add_u32_e32 v172, 0x60, v167
	global_store_dword v[20:21], v60, off offset:512
	global_load_dwordx4 v[158:161], v[72:73], off offset:3072
	s_nop 0
	global_load_dwordx4 v[72:75], v[74:75], off offset:3072
	v_add_u32_e32 v173, 0x80, v167
	v_add_u32_e32 v174, 0xa0, v167
	v_add_u32_e32 v175, 0xc0, v167
	v_xor_b32_e32 v169, s54, v167
	v_xor_b32_e32 v176, s64, v167
	v_xor_b32_e32 v177, s66, v167
	v_xor_b32_e32 v178, s54, v170
	v_xor_b32_e32 v179, s54, v171
	v_xor_b32_e32 v180, s54, v172
	v_xor_b32_e32 v181, s54, v173
	v_xor_b32_e32 v182, s54, v174
	v_xor_b32_e32 v183, s54, v175
	v_xor_b32_e32 v185, s64, v170
	v_xor_b32_e32 v186, s64, v171
	v_xor_b32_e32 v187, s64, v172
	v_xor_b32_e32 v188, s64, v173
	v_xor_b32_e32 v189, s64, v174
	v_xor_b32_e32 v190, s64, v175
	v_xor_b32_e32 v192, s66, v170
	v_xor_b32_e32 v193, s66, v171
	v_xor_b32_e32 v205, s66, v172
	v_xor_b32_e32 v206, s66, v173
	v_xor_b32_e32 v207, s66, v174
	v_xor_b32_e32 v208, s66, v175
	v_xor_b32_e32 v170, s68, v170
	v_xor_b32_e32 v171, s68, v171
	v_xor_b32_e32 v172, s68, v172
	v_xor_b32_e32 v173, s68, v173
	v_xor_b32_e32 v174, s68, v174
	v_xor_b32_e32 v175, s68, v175
	v_mov_b32_e32 v166, 0
	s_waitcnt vmcnt(0)
	v_pk_fma_f32 v[162:163], v[162:163], v[160:161], v[74:75]
	v_pk_fma_f32 v[72:73], v[152:153], v[158:159], v[72:73]
	v_bfe_u32 v75, v162, 16, 1
	v_bfe_u32 v60, v72, 16, 1
	v_bfe_u32 v74, v73, 16, 1
	v_bfe_u32 v89, v163, 16, 1
	v_add3_u32 v60, v72, v60, s86
	v_add3_u32 v75, v162, v75, s86
	v_add3_u32 v74, v73, v74, s86
	v_add3_u32 v89, v163, v89, s86
	v_lshrrev_b32_e32 v60, 16, v60
	v_lshrrev_b32_e32 v75, 16, v75
	v_and_or_b32 v74, v74, s82, v60
	v_and_or_b32 v75, v89, s82, v75
	global_store_dwordx2 v[22:23], v[74:75], off offset:1536
	global_load_dwordx4 v[158:161], v[82:83], off offset:3072
	s_nop 0
	global_load_dwordx4 v[80:83], v[80:81], off offset:3072
	v_mov_b32_e32 v60, 0
	s_waitcnt vmcnt(1)
	v_pk_add_f32 v[74:75], v[158:159], 1.0 op_sel_hi:[1,0]
	s_waitcnt vmcnt(0)
	v_pk_fma_f32 v[74:75], v[72:73], v[74:75], v[80:81]
	v_pk_add_f32 v[72:73], v[160:161], 1.0 op_sel_hi:[1,0]
	v_cvt_pk_fp8_f32 v60, v74, v75
	v_pk_fma_f32 v[80:81], v[162:163], v[72:73], v[82:83]
	v_pk_mul_f32 v[72:73], v[156:157], v[88:89] op_sel_hi:[1,0]
	v_pk_mul_f32 v[82:83], v[154:155], v[88:89] op_sel_hi:[1,0]
	v_cvt_pk_fp8_f32 v60, v80, v81 op_sel:[0,0,1]
	v_mov_b32_e32 v155, 0
	v_ashrrev_i32_e32 v154, 5, v204
	global_store_dword v[20:21], v60, off offset:768
	global_load_dwordx4 v[158:161], v[38:39], off
	global_load_dwordx4 v[162:165], v[40:41], off
	s_waitcnt vmcnt(0)
	v_pk_fma_f32 v[152:153], v[82:83], v[160:161], v[164:165]
	v_pk_fma_f32 v[72:73], v[72:73], v[158:159], v[162:163]
	v_bfe_u32 v83, v152, 16, 1
	v_bfe_u32 v60, v72, 16, 1
	v_bfe_u32 v82, v73, 16, 1
	v_bfe_u32 v89, v153, 16, 1
	v_add3_u32 v60, v72, v60, s86
	v_add3_u32 v83, v152, v83, s86
	v_add3_u32 v82, v73, v82, s86
	v_add3_u32 v89, v153, v89, s86
	v_lshrrev_b32_e32 v60, 16, v60
	v_lshrrev_b32_e32 v83, 16, v83
	v_and_or_b32 v82, v82, s82, v60
	v_and_or_b32 v83, v89, s82, v83
	global_store_dwordx2 v[22:23], v[82:83], off offset:2048
	global_load_dwordx4 v[156:159], v[32:33], off
	global_load_dwordx4 v[160:163], v[34:35], off
	v_lshlrev_b32_e32 v82, 3, v204
	v_and_b32_e32 v168, 8, v82
	v_mov_b32_e32 v164, 0
	v_add_u32_e32 v168, 0, v168
	v_add_u32_e32 v210, s0, v168
	v_readlane_b32 s0, v248, 25
	v_and_b32_e32 v89, 31, v204
	v_lshl_add_u32 v169, v169, 4, v210
	v_add_u32_e32 v211, s0, v168
	v_readlane_b32 s0, v248, 26
	v_lshl_add_u32 v178, v178, 4, v210
	v_lshl_add_u32 v179, v179, 4, v210
	v_add_u32_e32 v212, s0, v168
	v_readlane_b32 s0, v248, 27
	v_lshl_add_u32 v180, v180, 4, v210
	v_lshl_add_u32 v181, v181, 4, v210
	v_add_u32_e32 v168, s0, v168
	v_lshl_add_u32 v182, v182, 4, v210
	v_lshl_add_u32 v183, v183, 4, v210
	v_lshl_add_u32 v176, v176, 4, v211
	v_lshl_add_u32 v185, v185, 4, v211
	v_lshl_add_u32 v186, v186, 4, v211
	v_lshl_add_u32 v187, v187, 4, v211
	v_lshl_add_u32 v188, v188, 4, v211
	v_lshl_add_u32 v189, v189, 4, v211
	v_lshl_add_u32 v190, v190, 4, v211
	v_lshl_add_u32 v170, v170, 4, v168
	v_lshl_add_u32 v171, v171, 4, v168
	v_lshl_add_u32 v172, v172, 4, v168
	v_lshl_add_u32 v173, v173, 4, v168
	v_lshl_add_u32 v174, v174, 4, v168
	v_lshl_add_u32 v175, v175, 4, v168
	v_pk_mul_f32 v[14:15], v[14:15], v[88:89] op_sel_hi:[1,0]
	v_pk_mul_f32 v[12:13], v[12:13], v[88:89] op_sel_hi:[1,0]
	v_lshl_add_u32 v177, v177, 4, v212
	v_lshl_add_u32 v192, v192, 4, v212
	v_lshl_add_u32 v193, v193, 4, v212
	v_lshl_add_u32 v205, v205, 4, v212
	v_lshl_add_u32 v206, v206, 4, v212
	v_lshl_add_u32 v207, v207, 4, v212
	v_lshl_add_u32 v208, v208, 4, v212
	v_mov_b32_e32 v165, 0
	v_pk_mul_f32 v[10:11], v[10:11], v[88:89] op_sel_hi:[1,0]
	v_pk_mul_f32 v[8:9], v[8:9], v[88:89] op_sel_hi:[1,0]
	v_lshlrev_b32_e32 v60, 4, v204
	s_movk_i32 s0, 0x2000
	s_waitcnt vmcnt(1)
; #define GAS __attribute__((address_space(1)))
; #define LAS __attribute__((address_space(3)))
; __device__ __forceinline__ unsigned pk2(float lo, float hi) { return f2bf(lo) | (f2bf(hi) << 16); }
; __device__ __forceinline__ unsigned pk4_fp8(float a, float b, float c, float d) { int r = __builtin_amdgcn_cvt_pk_fp8_f32(a, b, 0, false); r = __builtin_amdgcn_cvt_pk_fp8_f32(c, d, r, true); return (unsigned)r; }
; template <int l>
; __device__ __forceinline__ void layer_phases(Frame& F, const XcdBarrier& bar, const int lo, const int hi) {
;     ...
;                     for (int j = 0; j < 8; ++j) { const int k = 4 * lq + 256 * j;
;                         const f32x4 xv = v[j] * rstd * *(const GAS f32x4*)(g1 + k) + *(const GAS f32x4*)(b1 + k);
;                         { v2u xo; xo.x = pk2(xv.x, xv.y); xo.y = pk2(xv.z, xv.w); *(GAS v2u*)(x1 + (size_t)m * D + k) = xo; }
;                         const f32x4 hv = xv * (*(const GAS f32x4*)(mrow + 8192 + k) + 1.0f) + *(const GAS f32x4*)(mrow + 6144 + k);
;                         v2u o; o.x = pk2(hv.x, hv.y); o.y = pk2(hv.z, hv.w);
;                         *(GAS unsigned*)(h2q + (size_t)m * D + k) = pk4_fp8(hv.x, hv.y, hv.z, hv.w);
;                         const int chunk = (lq >> 1) + 32 * j;
;                         *(LAS v2u*)(h2s + rloc * 4096 + ((chunk ^ (rloc & 15)) << 4) + (lq & 1) * 8) = o; }
	v_pk_add_f32 v[82:83], v[156:157], 1.0 op_sel_hi:[1,0]
	s_waitcnt vmcnt(0)
	v_pk_fma_f32 v[82:83], v[72:73], v[82:83], v[160:161]
	v_pk_add_f32 v[72:73], v[158:159], 1.0 op_sel_hi:[1,0]
	v_cvt_pk_fp8_f32 v164, v82, v83
	v_pk_fma_f32 v[152:153], v[152:153], v[72:73], v[162:163]
	v_lshl_add_u64 v[72:73], s[36:37], 0, v[60:61]
	v_cvt_pk_fp8_f32 v164, v152, v153 op_sel:[0,0,1]
	global_store_dword v[20:21], v164, off offset:1024
	global_load_dwordx4 v[156:159], v[38:39], off offset:1024
	global_load_dwordx4 v[160:163], v[40:41], off offset:1024
	v_add_u32_e32 v164, 0xe0, v167
	v_xor_b32_e32 v167, s68, v167
	v_xor_b32_e32 v184, s54, v164
	v_xor_b32_e32 v191, s64, v164
	v_xor_b32_e32 v209, s66, v164
	v_xor_b32_e32 v164, s68, v164
	v_lshl_add_u32 v184, v184, 4, v210
	v_lshl_add_u32 v191, v191, 4, v211
	v_lshl_add_u32 v167, v167, 4, v168
	v_lshl_add_u32 v164, v164, 4, v168
	v_and_b32_sdwa v168, v44, v203 dst_sel:DWORD dst_unused:UNUSED_PAD src0_sel:WORD_1 src1_sel:DWORD
	v_and_b32_sdwa v210, v42, v203 dst_sel:DWORD dst_unused:UNUSED_PAD src0_sel:WORD_1 src1_sel:DWORD
	v_and_b32_sdwa v211, v45, v203 dst_sel:DWORD dst_unused:UNUSED_PAD src0_sel:WORD_1 src1_sel:DWORD
	v_add3_u32 v42, v42, v210, s86
	v_add3_u32 v168, v44, v168, s86
	v_add3_u32 v210, v45, v211, s86
	v_lshl_add_u32 v209, v209, 4, v212
	v_and_b32_sdwa v212, v43, v203 dst_sel:DWORD dst_unused:UNUSED_PAD src0_sel:WORD_1 src1_sel:DWORD
	v_add3_u32 v43, v43, v212, s86
	s_waitcnt vmcnt(0)
	v_pk_fma_f32 v[44:45], v[12:13], v[158:159], v[162:163]
	v_pk_fma_f32 v[160:161], v[14:15], v[156:157], v[160:161]
	v_bfe_u32 v14, v44, 16, 1
	v_bfe_u32 v12, v160, 16, 1
	v_bfe_u32 v13, v161, 16, 1
	v_bfe_u32 v15, v45, 16, 1
	v_add3_u32 v12, v160, v12, s86
	v_add3_u32 v14, v44, v14, s86
	v_add3_u32 v13, v161, v13, s86
	v_add3_u32 v15, v45, v15, s86
	v_lshrrev_b32_e32 v12, 16, v12
	v_lshrrev_b32_e32 v14, 16, v14
	v_and_or_b32 v12, v13, s82, v12
	v_and_or_b32 v13, v15, s82, v14
	global_store_dwordx2 v[22:23], v[12:13], off offset:2560
	global_load_dwordx4 v[12:15], v[32:33], off offset:1024
	s_nop 0
	global_load_dwordx4 v[156:159], v[34:35], off offset:1024
	v_and_b32_e32 v162, 0xffff0000, v210
	v_and_b32_e32 v163, 0xffff0000, v43
	v_or_b32_sdwa v43, v162, v168 dst_sel:DWORD dst_unused:UNUSED_PAD src0_sel:DWORD src1_sel:WORD_1
	v_or_b32_sdwa v42, v163, v42 dst_sel:DWORD dst_unused:UNUSED_PAD src0_sel:DWORD src1_sel:WORD_1
	ds_write_b64 v169, v[42:43]
	v_and_b32_sdwa v43, v46, v203 dst_sel:DWORD dst_unused:UNUSED_PAD src0_sel:WORD_1 src1_sel:DWORD
	v_and_b32_sdwa v162, v49, v203 dst_sel:DWORD dst_unused:UNUSED_PAD src0_sel:WORD_1 src1_sel:DWORD
	v_and_b32_sdwa v163, v47, v203 dst_sel:DWORD dst_unused:UNUSED_PAD src0_sel:WORD_1 src1_sel:DWORD
	v_and_b32_sdwa v42, v48, v203 dst_sel:DWORD dst_unused:UNUSED_PAD src0_sel:WORD_1 src1_sel:DWORD
	v_add3_u32 v46, v46, v43, s86
	v_add3_u32 v43, v49, v162, s86
	v_add3_u32 v47, v47, v163, s86
	v_add3_u32 v42, v48, v42, s86
	v_and_b32_e32 v43, 0xffff0000, v43
	v_and_b32_e32 v47, 0xffff0000, v47
	v_or_b32_sdwa v43, v43, v42 dst_sel:DWORD dst_unused:UNUSED_PAD src0_sel:DWORD src1_sel:WORD_1
	v_or_b32_sdwa v42, v47, v46 dst_sel:DWORD dst_unused:UNUSED_PAD src0_sel:DWORD src1_sel:WORD_1
	ds_write_b64 v178, v[42:43]
	v_and_b32_sdwa v43, v50, v203 dst_sel:DWORD dst_unused:UNUSED_PAD src0_sel:WORD_1 src1_sel:DWORD
	v_and_b32_sdwa v46, v63, v203 dst_sel:DWORD dst_unused:UNUSED_PAD src0_sel:WORD_1 src1_sel:DWORD
	v_and_b32_sdwa v47, v51, v203 dst_sel:DWORD dst_unused:UNUSED_PAD src0_sel:WORD_1 src1_sel:DWORD
	v_and_b32_sdwa v42, v62, v203 dst_sel:DWORD dst_unused:UNUSED_PAD src0_sel:WORD_1 src1_sel:DWORD
	v_add3_u32 v48, v50, v43, s86
	v_add3_u32 v43, v63, v46, s86
	v_add3_u32 v46, v51, v47, s86
	v_add3_u32 v42, v62, v42, s86
	v_and_b32_e32 v43, 0xffff0000, v43
	v_and_b32_e32 v46, 0xffff0000, v46
	v_or_b32_sdwa v43, v43, v42 dst_sel:DWORD dst_unused:UNUSED_PAD src0_sel:DWORD src1_sel:WORD_1
	v_or_b32_sdwa v42, v46, v48 dst_sel:DWORD dst_unused:UNUSED_PAD src0_sel:DWORD src1_sel:WORD_1
	ds_write_b64 v179, v[42:43]
	v_and_b32_sdwa v43, v64, v203 dst_sel:DWORD dst_unused:UNUSED_PAD src0_sel:WORD_1 src1_sel:DWORD
	v_and_b32_sdwa v46, v67, v203 dst_sel:DWORD dst_unused:UNUSED_PAD src0_sel:WORD_1 src1_sel:DWORD
	v_and_b32_sdwa v47, v65, v203 dst_sel:DWORD dst_unused:UNUSED_PAD src0_sel:WORD_1 src1_sel:DWORD
	v_and_b32_sdwa v42, v66, v203 dst_sel:DWORD dst_unused:UNUSED_PAD src0_sel:WORD_1 src1_sel:DWORD
	v_add3_u32 v48, v64, v43, s86
	v_add3_u32 v43, v67, v46, s86
	v_add3_u32 v46, v65, v47, s86
	v_add3_u32 v42, v66, v42, s86
	v_and_b32_e32 v43, 0xffff0000, v43
	v_and_b32_e32 v46, 0xffff0000, v46
	v_or_b32_sdwa v43, v43, v42 dst_sel:DWORD dst_unused:UNUSED_PAD src0_sel:DWORD src1_sel:WORD_1
	v_or_b32_sdwa v42, v46, v48 dst_sel:DWORD dst_unused:UNUSED_PAD src0_sel:DWORD src1_sel:WORD_1
	ds_write_b64 v180, v[42:43]
	v_and_b32_sdwa v43, v68, v203 dst_sel:DWORD dst_unused:UNUSED_PAD src0_sel:WORD_1 src1_sel:DWORD
	v_and_b32_sdwa v46, v71, v203 dst_sel:DWORD dst_unused:UNUSED_PAD src0_sel:WORD_1 src1_sel:DWORD
	v_and_b32_sdwa v47, v69, v203 dst_sel:DWORD dst_unused:UNUSED_PAD src0_sel:WORD_1 src1_sel:DWORD
	v_and_b32_sdwa v42, v70, v203 dst_sel:DWORD dst_unused:UNUSED_PAD src0_sel:WORD_1 src1_sel:DWORD
	v_add3_u32 v48, v68, v43, s86
	v_add3_u32 v43, v71, v46, s86
	v_add3_u32 v46, v69, v47, s86
	v_add3_u32 v42, v70, v42, s86
	v_and_b32_e32 v43, 0xffff0000, v43
	v_and_b32_e32 v46, 0xffff0000, v46
	v_or_b32_sdwa v43, v43, v42 dst_sel:DWORD dst_unused:UNUSED_PAD src0_sel:DWORD src1_sel:WORD_1
	v_or_b32_sdwa v42, v46, v48 dst_sel:DWORD dst_unused:UNUSED_PAD src0_sel:DWORD src1_sel:WORD_1
	ds_write_b64 v181, v[42:43]
	v_and_b32_sdwa v43, v76, v203 dst_sel:DWORD dst_unused:UNUSED_PAD src0_sel:WORD_1 src1_sel:DWORD
	v_and_b32_sdwa v46, v79, v203 dst_sel:DWORD dst_unused:UNUSED_PAD src0_sel:WORD_1 src1_sel:DWORD
	v_and_b32_sdwa v47, v77, v203 dst_sel:DWORD dst_unused:UNUSED_PAD src0_sel:WORD_1 src1_sel:DWORD
	v_and_b32_sdwa v42, v78, v203 dst_sel:DWORD dst_unused:UNUSED_PAD src0_sel:WORD_1 src1_sel:DWORD
	v_add3_u32 v48, v76, v43, s86
	v_add3_u32 v43, v79, v46, s86
	v_add3_u32 v46, v77, v47, s86
	v_add3_u32 v42, v78, v42, s86
	v_and_b32_e32 v43, 0xffff0000, v43
	v_and_b32_e32 v46, 0xffff0000, v46
	v_or_b32_sdwa v43, v43, v42 dst_sel:DWORD dst_unused:UNUSED_PAD src0_sel:DWORD src1_sel:WORD_1
	v_or_b32_sdwa v42, v46, v48 dst_sel:DWORD dst_unused:UNUSED_PAD src0_sel:DWORD src1_sel:WORD_1
	ds_write_b64 v182, v[42:43]
	v_and_b32_sdwa v43, v84, v203 dst_sel:DWORD dst_unused:UNUSED_PAD src0_sel:WORD_1 src1_sel:DWORD
	v_and_b32_sdwa v46, v87, v203 dst_sel:DWORD dst_unused:UNUSED_PAD src0_sel:WORD_1 src1_sel:DWORD
	v_and_b32_sdwa v42, v86, v203 dst_sel:DWORD dst_unused:UNUSED_PAD src0_sel:WORD_1 src1_sel:DWORD
	v_and_b32_sdwa v47, v85, v203 dst_sel:DWORD dst_unused:UNUSED_PAD src0_sel:WORD_1 src1_sel:DWORD
	v_add3_u32 v50, v84, v43, s86
	v_add3_u32 v43, v87, v46, s86
	v_add3_u32 v42, v86, v42, s86
	v_add3_u32 v46, v85, v47, s86
	s_waitcnt vmcnt(1)
; #define GAS __attribute__((address_space(1)))
; #define LAS __attribute__((address_space(3)))
; __device__ __forceinline__ unsigned pk2(float lo, float hi) { return f2bf(lo) | (f2bf(hi) << 16); }
; __device__ __forceinline__ unsigned pk4_fp8(float a, float b, float c, float d) { int r = __builtin_amdgcn_cvt_pk_fp8_f32(a, b, 0, false); r = __builtin_amdgcn_cvt_pk_fp8_f32(c, d, r, true); return (unsigned)r; }
; template <int l>
; __device__ __forceinline__ void layer_phases(Frame& F, const XcdBarrier& bar, const int lo, const int hi) {
;     ...
;                     for (int j = 0; j < 8; ++j) { const int k = 4 * lq + 256 * j;
;                         const f32x4 xv = v[j] * rstd * *(const GAS f32x4*)(g1 + k) + *(const GAS f32x4*)(b1 + k);
;                         { v2u xo; xo.x = pk2(xv.x, xv.y); xo.y = pk2(xv.z, xv.w); *(GAS v2u*)(x1 + (size_t)m * D + k) = xo; }
;                         const f32x4 hv = xv * (*(const GAS f32x4*)(mrow + 8192 + k) + 1.0f) + *(const GAS f32x4*)(mrow + 6144 + k);
;                         v2u o; o.x = pk2(hv.x, hv.y); o.y = pk2(hv.z, hv.w);
;                         *(GAS unsigned*)(h2q + (size_t)m * D + k) = pk4_fp8(hv.x, hv.y, hv.z, hv.w);
;                         const int chunk = (lq >> 1) + 32 * j;
;                         *(LAS v2u*)(h2s + rloc * 4096 + ((chunk ^ (rloc & 15)) << 4) + (lq & 1) * 8) = o; }
	v_pk_add_f32 v[12:13], v[12:13], 1.0 op_sel_hi:[1,0]
	v_pk_add_f32 v[14:15], v[14:15], 1.0 op_sel_hi:[1,0]
	s_waitcnt vmcnt(0)
	v_pk_fma_f32 v[12:13], v[160:161], v[12:13], v[156:157]
	v_pk_fma_f32 v[14:15], v[44:45], v[14:15], v[158:159]
	v_cvt_pk_fp8_f32 v165, v12, v13
	v_and_b32_e32 v43, 0xffff0000, v43
	v_and_b32_e32 v62, 0xffff0000, v46
	v_or_b32_sdwa v51, v43, v42 dst_sel:DWORD dst_unused:UNUSED_PAD src0_sel:DWORD src1_sel:WORD_1
	v_cvt_pk_fp8_f32 v165, v14, v15 op_sel:[0,0,1]
	v_or_b32_sdwa v50, v62, v50 dst_sel:DWORD dst_unused:UNUSED_PAD src0_sel:DWORD src1_sel:WORD_1
	v_and_b32_sdwa v62, v93, v203 dst_sel:DWORD dst_unused:UNUSED_PAD src0_sel:WORD_1 src1_sel:DWORD
	v_and_b32_sdwa v63, v91, v203 dst_sel:DWORD dst_unused:UNUSED_PAD src0_sel:WORD_1 src1_sel:DWORD
	global_store_dword v[20:21], v165, off offset:1280
	global_load_dwordx4 v[42:45], v[38:39], off offset:2048
	global_load_dwordx4 v[46:49], v[40:41], off offset:2048
	ds_write_b64 v183, v[50:51]
	v_and_b32_sdwa v51, v90, v203 dst_sel:DWORD dst_unused:UNUSED_PAD src0_sel:WORD_1 src1_sel:DWORD
	v_and_b32_sdwa v50, v92, v203 dst_sel:DWORD dst_unused:UNUSED_PAD src0_sel:WORD_1 src1_sel:DWORD
	v_add3_u32 v64, v90, v51, s86
	v_add3_u32 v51, v93, v62, s86
	v_add3_u32 v62, v91, v63, s86
	v_add3_u32 v50, v92, v50, s86
	v_and_b32_e32 v51, 0xffff0000, v51
	v_and_b32_e32 v62, 0xffff0000, v62
	v_or_b32_sdwa v51, v51, v50 dst_sel:DWORD dst_unused:UNUSED_PAD src0_sel:DWORD src1_sel:WORD_1
	v_or_b32_sdwa v50, v62, v64 dst_sel:DWORD dst_unused:UNUSED_PAD src0_sel:DWORD src1_sel:WORD_1
	ds_write_b64 v184, v[50:51]
	v_and_b32_sdwa v51, v94, v203 dst_sel:DWORD dst_unused:UNUSED_PAD src0_sel:WORD_1 src1_sel:DWORD
	v_and_b32_sdwa v62, v97, v203 dst_sel:DWORD dst_unused:UNUSED_PAD src0_sel:WORD_1 src1_sel:DWORD
	v_and_b32_sdwa v63, v95, v203 dst_sel:DWORD dst_unused:UNUSED_PAD src0_sel:WORD_1 src1_sel:DWORD
	v_and_b32_sdwa v50, v96, v203 dst_sel:DWORD dst_unused:UNUSED_PAD src0_sel:WORD_1 src1_sel:DWORD
	v_add3_u32 v64, v94, v51, s86
	v_add3_u32 v51, v97, v62, s86
	v_add3_u32 v62, v95, v63, s86
	v_add3_u32 v50, v96, v50, s86
	v_and_b32_e32 v51, 0xffff0000, v51
	v_and_b32_e32 v62, 0xffff0000, v62
	v_or_b32_sdwa v51, v51, v50 dst_sel:DWORD dst_unused:UNUSED_PAD src0_sel:DWORD src1_sel:WORD_1
	v_or_b32_sdwa v50, v62, v64 dst_sel:DWORD dst_unused:UNUSED_PAD src0_sel:DWORD src1_sel:WORD_1
	ds_write_b64 v176, v[50:51]
	v_and_b32_sdwa v51, v98, v203 dst_sel:DWORD dst_unused:UNUSED_PAD src0_sel:WORD_1 src1_sel:DWORD
	v_and_b32_sdwa v62, v101, v203 dst_sel:DWORD dst_unused:UNUSED_PAD src0_sel:WORD_1 src1_sel:DWORD
	v_and_b32_sdwa v63, v99, v203 dst_sel:DWORD dst_unused:UNUSED_PAD src0_sel:WORD_1 src1_sel:DWORD
	v_and_b32_sdwa v50, v100, v203 dst_sel:DWORD dst_unused:UNUSED_PAD src0_sel:WORD_1 src1_sel:DWORD
	v_add3_u32 v64, v98, v51, s86
	v_add3_u32 v51, v101, v62, s86
	v_add3_u32 v62, v99, v63, s86
	v_add3_u32 v50, v100, v50, s86
	v_and_b32_e32 v51, 0xffff0000, v51
	v_and_b32_e32 v62, 0xffff0000, v62
	v_or_b32_sdwa v51, v51, v50 dst_sel:DWORD dst_unused:UNUSED_PAD src0_sel:DWORD src1_sel:WORD_1
	v_or_b32_sdwa v50, v62, v64 dst_sel:DWORD dst_unused:UNUSED_PAD src0_sel:DWORD src1_sel:WORD_1
	ds_write_b64 v185, v[50:51]
	v_and_b32_sdwa v51, v102, v203 dst_sel:DWORD dst_unused:UNUSED_PAD src0_sel:WORD_1 src1_sel:DWORD
	v_and_b32_sdwa v62, v105, v203 dst_sel:DWORD dst_unused:UNUSED_PAD src0_sel:WORD_1 src1_sel:DWORD
	v_and_b32_sdwa v63, v103, v203 dst_sel:DWORD dst_unused:UNUSED_PAD src0_sel:WORD_1 src1_sel:DWORD
	v_and_b32_sdwa v50, v104, v203 dst_sel:DWORD dst_unused:UNUSED_PAD src0_sel:WORD_1 src1_sel:DWORD
	v_add3_u32 v64, v102, v51, s86
	v_add3_u32 v51, v105, v62, s86
	v_add3_u32 v62, v103, v63, s86
	v_add3_u32 v50, v104, v50, s86
	v_and_b32_e32 v51, 0xffff0000, v51
	v_and_b32_e32 v62, 0xffff0000, v62
	v_or_b32_sdwa v51, v51, v50 dst_sel:DWORD dst_unused:UNUSED_PAD src0_sel:DWORD src1_sel:WORD_1
	v_or_b32_sdwa v50, v62, v64 dst_sel:DWORD dst_unused:UNUSED_PAD src0_sel:DWORD src1_sel:WORD_1
	ds_write_b64 v186, v[50:51]
	v_and_b32_sdwa v51, v106, v203 dst_sel:DWORD dst_unused:UNUSED_PAD src0_sel:WORD_1 src1_sel:DWORD
	v_and_b32_sdwa v62, v109, v203 dst_sel:DWORD dst_unused:UNUSED_PAD src0_sel:WORD_1 src1_sel:DWORD
	v_and_b32_sdwa v63, v107, v203 dst_sel:DWORD dst_unused:UNUSED_PAD src0_sel:WORD_1 src1_sel:DWORD
	v_and_b32_sdwa v50, v108, v203 dst_sel:DWORD dst_unused:UNUSED_PAD src0_sel:WORD_1 src1_sel:DWORD
	v_add3_u32 v64, v106, v51, s86
	v_add3_u32 v51, v109, v62, s86
	v_add3_u32 v62, v107, v63, s86
	v_add3_u32 v50, v108, v50, s86
	v_and_b32_e32 v51, 0xffff0000, v51
	v_and_b32_e32 v62, 0xffff0000, v62
	v_or_b32_sdwa v51, v51, v50 dst_sel:DWORD dst_unused:UNUSED_PAD src0_sel:DWORD src1_sel:WORD_1
	v_or_b32_sdwa v50, v62, v64 dst_sel:DWORD dst_unused:UNUSED_PAD src0_sel:DWORD src1_sel:WORD_1
	ds_write_b64 v187, v[50:51]
	v_and_b32_sdwa v51, v110, v203 dst_sel:DWORD dst_unused:UNUSED_PAD src0_sel:WORD_1 src1_sel:DWORD
	v_and_b32_sdwa v62, v113, v203 dst_sel:DWORD dst_unused:UNUSED_PAD src0_sel:WORD_1 src1_sel:DWORD
	v_and_b32_sdwa v63, v111, v203 dst_sel:DWORD dst_unused:UNUSED_PAD src0_sel:WORD_1 src1_sel:DWORD
	v_and_b32_sdwa v50, v112, v203 dst_sel:DWORD dst_unused:UNUSED_PAD src0_sel:WORD_1 src1_sel:DWORD
	v_add3_u32 v64, v110, v51, s86
	v_add3_u32 v51, v113, v62, s86
	v_add3_u32 v62, v111, v63, s86
	v_add3_u32 v50, v112, v50, s86
	v_and_b32_e32 v51, 0xffff0000, v51
	v_and_b32_e32 v62, 0xffff0000, v62
	v_or_b32_sdwa v51, v51, v50 dst_sel:DWORD dst_unused:UNUSED_PAD src0_sel:DWORD src1_sel:WORD_1
	v_or_b32_sdwa v50, v62, v64 dst_sel:DWORD dst_unused:UNUSED_PAD src0_sel:DWORD src1_sel:WORD_1
	v_and_b32_sdwa v62, v117, v203 dst_sel:DWORD dst_unused:UNUSED_PAD src0_sel:WORD_1 src1_sel:DWORD
	v_and_b32_sdwa v63, v115, v203 dst_sel:DWORD dst_unused:UNUSED_PAD src0_sel:WORD_1 src1_sel:DWORD
	s_waitcnt vmcnt(0)
; #define GAS __attribute__((address_space(1)))
; #define LAS __attribute__((address_space(3)))
; __device__ __forceinline__ unsigned pk2(float lo, float hi) { return f2bf(lo) | (f2bf(hi) << 16); }
; __device__ __forceinline__ unsigned pk4_fp8(float a, float b, float c, float d) { int r = __builtin_amdgcn_cvt_pk_fp8_f32(a, b, 0, false); r = __builtin_amdgcn_cvt_pk_fp8_f32(c, d, r, true); return (unsigned)r; }
; template <int l>
; __device__ __forceinline__ void layer_phases(Frame& F, const XcdBarrier& bar, const int lo, const int hi) {
;     ...
;                     for (int j = 0; j < 8; ++j) { const int k = 4 * lq + 256 * j;
;                         const f32x4 xv = v[j] * rstd * *(const GAS f32x4*)(g1 + k) + *(const GAS f32x4*)(b1 + k);
;                         { v2u xo; xo.x = pk2(xv.x, xv.y); xo.y = pk2(xv.z, xv.w); *(GAS v2u*)(x1 + (size_t)m * D + k) = xo; }
;                         const f32x4 hv = xv * (*(const GAS f32x4*)(mrow + 8192 + k) + 1.0f) + *(const GAS f32x4*)(mrow + 6144 + k);
;                         v2u o; o.x = pk2(hv.x, hv.y); o.y = pk2(hv.z, hv.w);
;                         *(GAS unsigned*)(h2q + (size_t)m * D + k) = pk4_fp8(hv.x, hv.y, hv.z, hv.w);
;                         const int chunk = (lq >> 1) + 32 * j;
;                         *(LAS v2u*)(h2s + rloc * 4096 + ((chunk ^ (rloc & 15)) << 4) + (lq & 1) * 8) = o; }
	v_pk_fma_f32 v[48:49], v[8:9], v[44:45], v[48:49]
	v_pk_fma_f32 v[46:47], v[10:11], v[42:43], v[46:47]
	v_bfe_u32 v10, v48, 16, 1
	v_bfe_u32 v8, v46, 16, 1
	v_bfe_u32 v9, v47, 16, 1
	v_bfe_u32 v11, v49, 16, 1
	v_add3_u32 v8, v46, v8, s86
	v_add3_u32 v10, v48, v10, s86
	v_add3_u32 v9, v47, v9, s86
	v_add3_u32 v11, v49, v11, s86
	v_lshrrev_b32_e32 v8, 16, v8
	v_lshrrev_b32_e32 v10, 16, v10
	v_and_or_b32 v8, v9, s82, v8
	v_and_or_b32 v9, v11, s82, v10
	global_store_dwordx2 v[22:23], v[8:9], off offset:3072
	global_load_dwordx4 v[8:11], v[32:33], off offset:2048
	s_nop 0
	global_load_dwordx4 v[42:45], v[34:35], off offset:2048
	ds_write_b64 v188, v[50:51]
	v_and_b32_sdwa v51, v114, v203 dst_sel:DWORD dst_unused:UNUSED_PAD src0_sel:WORD_1 src1_sel:DWORD
	v_and_b32_sdwa v50, v116, v203 dst_sel:DWORD dst_unused:UNUSED_PAD src0_sel:WORD_1 src1_sel:DWORD
	v_add3_u32 v64, v114, v51, s86
	v_add3_u32 v51, v117, v62, s86
	v_add3_u32 v62, v115, v63, s86
	v_add3_u32 v50, v116, v50, s86
	v_and_b32_e32 v51, 0xffff0000, v51
	v_and_b32_e32 v62, 0xffff0000, v62
	v_or_b32_sdwa v51, v51, v50 dst_sel:DWORD dst_unused:UNUSED_PAD src0_sel:DWORD src1_sel:WORD_1
	v_or_b32_sdwa v50, v62, v64 dst_sel:DWORD dst_unused:UNUSED_PAD src0_sel:DWORD src1_sel:WORD_1
	ds_write_b64 v189, v[50:51]
	v_and_b32_sdwa v51, v118, v203 dst_sel:DWORD dst_unused:UNUSED_PAD src0_sel:WORD_1 src1_sel:DWORD
	v_and_b32_sdwa v62, v121, v203 dst_sel:DWORD dst_unused:UNUSED_PAD src0_sel:WORD_1 src1_sel:DWORD
	v_and_b32_sdwa v63, v119, v203 dst_sel:DWORD dst_unused:UNUSED_PAD src0_sel:WORD_1 src1_sel:DWORD
	v_and_b32_sdwa v50, v120, v203 dst_sel:DWORD dst_unused:UNUSED_PAD src0_sel:WORD_1 src1_sel:DWORD
	v_add3_u32 v64, v118, v51, s86
	v_add3_u32 v51, v121, v62, s86
	v_add3_u32 v62, v119, v63, s86
	v_add3_u32 v50, v120, v50, s86
	v_and_b32_e32 v51, 0xffff0000, v51
	v_and_b32_e32 v62, 0xffff0000, v62
	v_or_b32_sdwa v51, v51, v50 dst_sel:DWORD dst_unused:UNUSED_PAD src0_sel:DWORD src1_sel:WORD_1
	v_or_b32_sdwa v50, v62, v64 dst_sel:DWORD dst_unused:UNUSED_PAD src0_sel:DWORD src1_sel:WORD_1
	ds_write_b64 v190, v[50:51]
	v_and_b32_sdwa v51, v122, v203 dst_sel:DWORD dst_unused:UNUSED_PAD src0_sel:WORD_1 src1_sel:DWORD
	v_and_b32_sdwa v62, v125, v203 dst_sel:DWORD dst_unused:UNUSED_PAD src0_sel:WORD_1 src1_sel:DWORD
	v_and_b32_sdwa v63, v123, v203 dst_sel:DWORD dst_unused:UNUSED_PAD src0_sel:WORD_1 src1_sel:DWORD
	v_and_b32_sdwa v50, v124, v203 dst_sel:DWORD dst_unused:UNUSED_PAD src0_sel:WORD_1 src1_sel:DWORD
	v_add3_u32 v64, v122, v51, s86
	v_add3_u32 v51, v125, v62, s86
	v_add3_u32 v62, v123, v63, s86
	v_add3_u32 v50, v124, v50, s86
	v_and_b32_e32 v51, 0xffff0000, v51
	v_and_b32_e32 v62, 0xffff0000, v62
	v_or_b32_sdwa v51, v51, v50 dst_sel:DWORD dst_unused:UNUSED_PAD src0_sel:DWORD src1_sel:WORD_1
	v_or_b32_sdwa v50, v62, v64 dst_sel:DWORD dst_unused:UNUSED_PAD src0_sel:DWORD src1_sel:WORD_1
	ds_write_b64 v191, v[50:51]
	v_pk_mul_f32 v[50:51], v[6:7], v[88:89] op_sel_hi:[1,0]
	v_pk_mul_f32 v[62:63], v[4:5], v[88:89] op_sel_hi:[1,0]
	v_and_b32_sdwa v5, v126, v203 dst_sel:DWORD dst_unused:UNUSED_PAD src0_sel:WORD_1 src1_sel:DWORD
	v_and_b32_sdwa v6, v129, v203 dst_sel:DWORD dst_unused:UNUSED_PAD src0_sel:WORD_1 src1_sel:DWORD
	v_and_b32_sdwa v7, v127, v203 dst_sel:DWORD dst_unused:UNUSED_PAD src0_sel:WORD_1 src1_sel:DWORD
	v_and_b32_sdwa v4, v128, v203 dst_sel:DWORD dst_unused:UNUSED_PAD src0_sel:WORD_1 src1_sel:DWORD
	v_add3_u32 v64, v126, v5, s86
	v_add3_u32 v5, v129, v6, s86
	v_add3_u32 v6, v127, v7, s86
	v_add3_u32 v4, v128, v4, s86
	v_and_b32_e32 v5, 0xffff0000, v5
	v_and_b32_e32 v6, 0xffff0000, v6
	v_or_b32_sdwa v5, v5, v4 dst_sel:DWORD dst_unused:UNUSED_PAD src0_sel:DWORD src1_sel:WORD_1
	v_or_b32_sdwa v4, v6, v64 dst_sel:DWORD dst_unused:UNUSED_PAD src0_sel:DWORD src1_sel:WORD_1
	ds_write_b64 v177, v[4:5]
	v_and_b32_sdwa v5, v130, v203 dst_sel:DWORD dst_unused:UNUSED_PAD src0_sel:WORD_1 src1_sel:DWORD
	v_and_b32_sdwa v6, v133, v203 dst_sel:DWORD dst_unused:UNUSED_PAD src0_sel:WORD_1 src1_sel:DWORD
	v_and_b32_sdwa v7, v131, v203 dst_sel:DWORD dst_unused:UNUSED_PAD src0_sel:WORD_1 src1_sel:DWORD
	v_and_b32_sdwa v4, v132, v203 dst_sel:DWORD dst_unused:UNUSED_PAD src0_sel:WORD_1 src1_sel:DWORD
	v_add3_u32 v64, v130, v5, s86
	v_add3_u32 v5, v133, v6, s86
	v_add3_u32 v6, v131, v7, s86
	v_add3_u32 v4, v132, v4, s86
	v_and_b32_e32 v5, 0xffff0000, v5
	v_and_b32_e32 v6, 0xffff0000, v6
	v_or_b32_sdwa v5, v5, v4 dst_sel:DWORD dst_unused:UNUSED_PAD src0_sel:DWORD src1_sel:WORD_1
	v_or_b32_sdwa v4, v6, v64 dst_sel:DWORD dst_unused:UNUSED_PAD src0_sel:DWORD src1_sel:WORD_1
	ds_write_b64 v192, v[4:5]
	v_and_b32_sdwa v4, v136, v203 dst_sel:DWORD dst_unused:UNUSED_PAD src0_sel:WORD_1 src1_sel:DWORD
	v_and_b32_sdwa v5, v134, v203 dst_sel:DWORD dst_unused:UNUSED_PAD src0_sel:WORD_1 src1_sel:DWORD
	v_add3_u32 v64, v134, v5, s86
	v_add3_u32 v65, v136, v4, s86
	v_and_b32_sdwa v6, v137, v203 dst_sel:DWORD dst_unused:UNUSED_PAD src0_sel:WORD_1 src1_sel:DWORD
	v_and_b32_sdwa v7, v135, v203 dst_sel:DWORD dst_unused:UNUSED_PAD src0_sel:WORD_1 src1_sel:DWORD
	v_add3_u32 v6, v137, v6, s86
	v_add3_u32 v7, v135, v7, s86
	v_and_b32_e32 v6, 0xffff0000, v6
	s_waitcnt vmcnt(1)
	v_pk_add_f32 v[4:5], v[8:9], 1.0 op_sel_hi:[1,0]
	s_waitcnt vmcnt(0)
; #define GAS __attribute__((address_space(1)))
; #define LAS __attribute__((address_space(3)))
; __device__ __forceinline__ unsigned pk2(float lo, float hi) { return f2bf(lo) | (f2bf(hi) << 16); }
; __device__ __forceinline__ unsigned pk4_fp8(float a, float b, float c, float d) { int r = __builtin_amdgcn_cvt_pk_fp8_f32(a, b, 0, false); r = __builtin_amdgcn_cvt_pk_fp8_f32(c, d, r, true); return (unsigned)r; }
; template <int l>
; __device__ __forceinline__ void layer_phases(Frame& F, const XcdBarrier& bar, const int lo, const int hi) {
;     ...
;                     for (int j = 0; j < 8; ++j) { const int k = 4 * lq + 256 * j;
;                         const f32x4 xv = v[j] * rstd * *(const GAS f32x4*)(g1 + k) + *(const GAS f32x4*)(b1 + k);
;                         { v2u xo; xo.x = pk2(xv.x, xv.y); xo.y = pk2(xv.z, xv.w); *(GAS v2u*)(x1 + (size_t)m * D + k) = xo; }
;                         const f32x4 hv = xv * (*(const GAS f32x4*)(mrow + 8192 + k) + 1.0f) + *(const GAS f32x4*)(mrow + 6144 + k);
;                         v2u o; o.x = pk2(hv.x, hv.y); o.y = pk2(hv.z, hv.w);
;                         *(GAS unsigned*)(h2q + (size_t)m * D + k) = pk4_fp8(hv.x, hv.y, hv.z, hv.w);
;                         const int chunk = (lq >> 1) + 32 * j;
;                         *(LAS v2u*)(h2s + rloc * 4096 + ((chunk ^ (rloc & 15)) << 4) + (lq & 1) * 8) = o; }
	v_pk_fma_f32 v[42:43], v[46:47], v[4:5], v[42:43]
	v_pk_add_f32 v[4:5], v[10:11], 1.0 op_sel_hi:[1,0]
	v_cvt_pk_fp8_f32 v166, v42, v43
	v_pk_fma_f32 v[44:45], v[48:49], v[4:5], v[44:45]
	v_and_b32_e32 v4, 0xffff0000, v7
	v_or_b32_sdwa v47, v6, v65 dst_sel:DWORD dst_unused:UNUSED_PAD src0_sel:DWORD src1_sel:WORD_1
	v_cvt_pk_fp8_f32 v166, v44, v45 op_sel:[0,0,1]
	v_or_b32_sdwa v46, v4, v64 dst_sel:DWORD dst_unused:UNUSED_PAD src0_sel:DWORD src1_sel:WORD_1
	global_store_dword v[20:21], v166, off offset:1536
	global_load_dwordx4 v[4:7], v[38:39], off offset:3072
	global_load_dwordx4 v[8:11], v[40:41], off offset:3072
	v_and_b32_sdwa v39, v138, v203 dst_sel:DWORD dst_unused:UNUSED_PAD src0_sel:WORD_1 src1_sel:DWORD
	v_and_b32_sdwa v40, v141, v203 dst_sel:DWORD dst_unused:UNUSED_PAD src0_sel:WORD_1 src1_sel:DWORD
	v_and_b32_sdwa v41, v139, v203 dst_sel:DWORD dst_unused:UNUSED_PAD src0_sel:WORD_1 src1_sel:DWORD
	ds_write_b64 v193, v[46:47]
	v_and_b32_sdwa v38, v140, v203 dst_sel:DWORD dst_unused:UNUSED_PAD src0_sel:WORD_1 src1_sel:DWORD
	v_add3_u32 v46, v138, v39, s86
	v_add3_u32 v39, v141, v40, s86
	v_add3_u32 v40, v139, v41, s86
	v_add3_u32 v38, v140, v38, s86
	v_and_b32_e32 v39, 0xffff0000, v39
	v_and_b32_e32 v40, 0xffff0000, v40
	v_or_b32_sdwa v39, v39, v38 dst_sel:DWORD dst_unused:UNUSED_PAD src0_sel:DWORD src1_sel:WORD_1
	v_or_b32_sdwa v38, v40, v46 dst_sel:DWORD dst_unused:UNUSED_PAD src0_sel:DWORD src1_sel:WORD_1
	ds_write_b64 v205, v[38:39]
	v_and_b32_sdwa v39, v142, v203 dst_sel:DWORD dst_unused:UNUSED_PAD src0_sel:WORD_1 src1_sel:DWORD
	v_and_b32_sdwa v40, v145, v203 dst_sel:DWORD dst_unused:UNUSED_PAD src0_sel:WORD_1 src1_sel:DWORD
	v_and_b32_sdwa v41, v143, v203 dst_sel:DWORD dst_unused:UNUSED_PAD src0_sel:WORD_1 src1_sel:DWORD
	v_and_b32_sdwa v38, v144, v203 dst_sel:DWORD dst_unused:UNUSED_PAD src0_sel:WORD_1 src1_sel:DWORD
	v_add3_u32 v46, v142, v39, s86
	v_add3_u32 v39, v145, v40, s86
	v_add3_u32 v40, v143, v41, s86
	v_add3_u32 v38, v144, v38, s86
	v_and_b32_e32 v39, 0xffff0000, v39
	v_and_b32_e32 v40, 0xffff0000, v40
	v_or_b32_sdwa v39, v39, v38 dst_sel:DWORD dst_unused:UNUSED_PAD src0_sel:DWORD src1_sel:WORD_1
	v_or_b32_sdwa v38, v40, v46 dst_sel:DWORD dst_unused:UNUSED_PAD src0_sel:DWORD src1_sel:WORD_1
	ds_write_b64 v206, v[38:39]
	v_and_b32_sdwa v39, v146, v203 dst_sel:DWORD dst_unused:UNUSED_PAD src0_sel:WORD_1 src1_sel:DWORD
	v_and_b32_sdwa v40, v149, v203 dst_sel:DWORD dst_unused:UNUSED_PAD src0_sel:WORD_1 src1_sel:DWORD
	v_and_b32_sdwa v41, v147, v203 dst_sel:DWORD dst_unused:UNUSED_PAD src0_sel:WORD_1 src1_sel:DWORD
	v_and_b32_sdwa v38, v148, v203 dst_sel:DWORD dst_unused:UNUSED_PAD src0_sel:WORD_1 src1_sel:DWORD
	v_add3_u32 v46, v146, v39, s86
	v_add3_u32 v39, v149, v40, s86
	v_add3_u32 v40, v147, v41, s86
	v_add3_u32 v38, v148, v38, s86
	v_and_b32_e32 v39, 0xffff0000, v39
	v_and_b32_e32 v40, 0xffff0000, v40
	v_or_b32_sdwa v39, v39, v38 dst_sel:DWORD dst_unused:UNUSED_PAD src0_sel:DWORD src1_sel:WORD_1
	v_or_b32_sdwa v38, v40, v46 dst_sel:DWORD dst_unused:UNUSED_PAD src0_sel:DWORD src1_sel:WORD_1
	v_and_b32_sdwa v40, v3, v203 dst_sel:DWORD dst_unused:UNUSED_PAD src0_sel:WORD_1 src1_sel:DWORD
	v_and_b32_sdwa v41, v1, v203 dst_sel:DWORD dst_unused:UNUSED_PAD src0_sel:WORD_1 src1_sel:DWORD
	ds_write_b64 v207, v[38:39]
	v_and_b32_sdwa v38, v2, v203 dst_sel:DWORD dst_unused:UNUSED_PAD src0_sel:WORD_1 src1_sel:DWORD
	v_and_b32_sdwa v39, v0, v203 dst_sel:DWORD dst_unused:UNUSED_PAD src0_sel:WORD_1 src1_sel:DWORD
	v_add3_u32 v3, v3, v40, s86
	v_add3_u32 v1, v1, v41, s86
	v_add3_u32 v0, v0, v39, s86
	v_add3_u32 v2, v2, v38, s86
	v_and_b32_e32 v3, 0xffff0000, v3
	v_and_b32_e32 v38, 0xffff0000, v1
	v_or_b32_sdwa v1, v3, v2 dst_sel:DWORD dst_unused:UNUSED_PAD src0_sel:DWORD src1_sel:WORD_1
	v_or_b32_sdwa v0, v38, v0 dst_sel:DWORD dst_unused:UNUSED_PAD src0_sel:DWORD src1_sel:WORD_1
	ds_write_b64 v208, v[0:1]
	v_and_b32_sdwa v1, v16, v203 dst_sel:DWORD dst_unused:UNUSED_PAD src0_sel:WORD_1 src1_sel:DWORD
	v_and_b32_sdwa v2, v19, v203 dst_sel:DWORD dst_unused:UNUSED_PAD src0_sel:WORD_1 src1_sel:DWORD
	v_and_b32_sdwa v3, v17, v203 dst_sel:DWORD dst_unused:UNUSED_PAD src0_sel:WORD_1 src1_sel:DWORD
	v_and_b32_sdwa v0, v18, v203 dst_sel:DWORD dst_unused:UNUSED_PAD src0_sel:WORD_1 src1_sel:DWORD
	v_add3_u32 v16, v16, v1, s86
	v_add3_u32 v1, v19, v2, s86
	v_add3_u32 v2, v17, v3, s86
	v_add3_u32 v0, v18, v0, s86
	v_and_b32_e32 v1, 0xffff0000, v1
	v_and_b32_e32 v2, 0xffff0000, v2
	v_or_b32_sdwa v1, v1, v0 dst_sel:DWORD dst_unused:UNUSED_PAD src0_sel:DWORD src1_sel:WORD_1
	v_or_b32_sdwa v0, v2, v16 dst_sel:DWORD dst_unused:UNUSED_PAD src0_sel:DWORD src1_sel:WORD_1
	ds_write_b64 v209, v[0:1]
	v_and_b32_sdwa v1, v24, v203 dst_sel:DWORD dst_unused:UNUSED_PAD src0_sel:WORD_1 src1_sel:DWORD
	v_and_b32_sdwa v2, v27, v203 dst_sel:DWORD dst_unused:UNUSED_PAD src0_sel:WORD_1 src1_sel:DWORD
	v_and_b32_sdwa v3, v25, v203 dst_sel:DWORD dst_unused:UNUSED_PAD src0_sel:WORD_1 src1_sel:DWORD
	v_and_b32_sdwa v0, v26, v203 dst_sel:DWORD dst_unused:UNUSED_PAD src0_sel:WORD_1 src1_sel:DWORD
	v_add3_u32 v16, v24, v1, s86
	v_add3_u32 v1, v27, v2, s86
	v_add3_u32 v2, v25, v3, s86
	v_add3_u32 v0, v26, v0, s86
	v_and_b32_e32 v1, 0xffff0000, v1
	v_and_b32_e32 v2, 0xffff0000, v2
	v_or_b32_sdwa v1, v1, v0 dst_sel:DWORD dst_unused:UNUSED_PAD src0_sel:DWORD src1_sel:WORD_1
	v_or_b32_sdwa v0, v2, v16 dst_sel:DWORD dst_unused:UNUSED_PAD src0_sel:DWORD src1_sel:WORD_1
	ds_write_b64 v167, v[0:1]
	s_waitcnt vmcnt(0)
; #define GAS __attribute__((address_space(1)))
; #define LAS __attribute__((address_space(3)))
; __device__ __forceinline__ unsigned pk2(float lo, float hi) { return f2bf(lo) | (f2bf(hi) << 16); }
; __device__ __forceinline__ unsigned pk4_fp8(float a, float b, float c, float d) { int r = __builtin_amdgcn_cvt_pk_fp8_f32(a, b, 0, false); r = __builtin_amdgcn_cvt_pk_fp8_f32(c, d, r, true); return (unsigned)r; }
; template <int l>
; __device__ __forceinline__ void layer_phases(Frame& F, const XcdBarrier& bar, const int lo, const int hi) {
;     ...
;                     for (int j = 0; j < 8; ++j) { const int k = 4 * lq + 256 * j;
;                         const f32x4 xv = v[j] * rstd * *(const GAS f32x4*)(g1 + k) + *(const GAS f32x4*)(b1 + k);
;                         { v2u xo; xo.x = pk2(xv.x, xv.y); xo.y = pk2(xv.z, xv.w); *(GAS v2u*)(x1 + (size_t)m * D + k) = xo; }
;                         const f32x4 hv = xv * (*(const GAS f32x4*)(mrow + 8192 + k) + 1.0f) + *(const GAS f32x4*)(mrow + 6144 + k);
;                         v2u o; o.x = pk2(hv.x, hv.y); o.y = pk2(hv.z, hv.w);
;                         *(GAS unsigned*)(h2q + (size_t)m * D + k) = pk4_fp8(hv.x, hv.y, hv.z, hv.w);
;                         const int chunk = (lq >> 1) + 32 * j;
;                         *(LAS v2u*)(h2s + rloc * 4096 + ((chunk ^ (rloc & 15)) << 4) + (lq & 1) * 8) = o; }
	v_pk_fma_f32 v[10:11], v[62:63], v[6:7], v[10:11]
	v_pk_fma_f32 v[8:9], v[50:51], v[4:5], v[8:9]
	v_bfe_u32 v2, v10, 16, 1
	v_bfe_u32 v0, v8, 16, 1
	v_bfe_u32 v1, v9, 16, 1
	v_bfe_u32 v3, v11, 16, 1
	v_add3_u32 v0, v8, v0, s86
	v_add3_u32 v2, v10, v2, s86
	v_add3_u32 v1, v9, v1, s86
	v_add3_u32 v3, v11, v3, s86
	v_lshrrev_b32_e32 v0, 16, v0
	v_lshrrev_b32_e32 v2, 16, v2
	v_and_or_b32 v0, v1, s82, v0
	v_and_or_b32 v1, v3, s82, v2
	global_store_dwordx2 v[22:23], v[0:1], off offset:3584
	global_load_dwordx4 v[0:3], v[32:33], off offset:3072
	v_and_b32_sdwa v17, v28, v203 dst_sel:DWORD dst_unused:UNUSED_PAD src0_sel:WORD_1 src1_sel:DWORD
	global_load_dwordx4 v[4:7], v[34:35], off offset:3072
	v_and_b32_sdwa v18, v31, v203 dst_sel:DWORD dst_unused:UNUSED_PAD src0_sel:WORD_1 src1_sel:DWORD
	v_and_b32_sdwa v19, v29, v203 dst_sel:DWORD dst_unused:UNUSED_PAD src0_sel:WORD_1 src1_sel:DWORD
	v_and_b32_sdwa v16, v30, v203 dst_sel:DWORD dst_unused:UNUSED_PAD src0_sel:WORD_1 src1_sel:DWORD
	v_add3_u32 v22, v28, v17, s86
	v_add3_u32 v17, v31, v18, s86
	v_add3_u32 v18, v29, v19, s86
	v_add3_u32 v16, v30, v16, s86
	v_and_b32_e32 v17, 0xffff0000, v17
	v_and_b32_e32 v18, 0xffff0000, v18
	v_or_b32_sdwa v17, v17, v16 dst_sel:DWORD dst_unused:UNUSED_PAD src0_sel:DWORD src1_sel:WORD_1
	v_or_b32_sdwa v16, v18, v22 dst_sel:DWORD dst_unused:UNUSED_PAD src0_sel:DWORD src1_sel:WORD_1
	ds_write_b64 v170, v[16:17]
	v_and_b32_sdwa v17, v36, v203 dst_sel:DWORD dst_unused:UNUSED_PAD src0_sel:WORD_1 src1_sel:DWORD
	v_and_b32_sdwa v18, v151, v203 dst_sel:DWORD dst_unused:UNUSED_PAD src0_sel:WORD_1 src1_sel:DWORD
	v_and_b32_sdwa v19, v37, v203 dst_sel:DWORD dst_unused:UNUSED_PAD src0_sel:WORD_1 src1_sel:DWORD
	v_and_b32_sdwa v16, v150, v203 dst_sel:DWORD dst_unused:UNUSED_PAD src0_sel:WORD_1 src1_sel:DWORD
	v_add3_u32 v22, v36, v17, s86
	v_add3_u32 v17, v151, v18, s86
	v_add3_u32 v18, v37, v19, s86
	v_add3_u32 v16, v150, v16, s86
	v_and_b32_e32 v17, 0xffff0000, v17
	v_and_b32_e32 v18, 0xffff0000, v18
	v_or_b32_sdwa v17, v17, v16 dst_sel:DWORD dst_unused:UNUSED_PAD src0_sel:DWORD src1_sel:WORD_1
	v_or_b32_sdwa v16, v18, v22 dst_sel:DWORD dst_unused:UNUSED_PAD src0_sel:DWORD src1_sel:WORD_1
	ds_write_b64 v171, v[16:17]
	v_and_b32_sdwa v17, v74, v203 dst_sel:DWORD dst_unused:UNUSED_PAD src0_sel:WORD_1 src1_sel:DWORD
	v_and_b32_sdwa v18, v81, v203 dst_sel:DWORD dst_unused:UNUSED_PAD src0_sel:WORD_1 src1_sel:DWORD
	v_and_b32_sdwa v19, v75, v203 dst_sel:DWORD dst_unused:UNUSED_PAD src0_sel:WORD_1 src1_sel:DWORD
	v_and_b32_sdwa v16, v80, v203 dst_sel:DWORD dst_unused:UNUSED_PAD src0_sel:WORD_1 src1_sel:DWORD
	v_add3_u32 v22, v74, v17, s86
	v_add3_u32 v17, v81, v18, s86
	v_add3_u32 v18, v75, v19, s86
	v_add3_u32 v16, v80, v16, s86
	v_and_b32_e32 v17, 0xffff0000, v17
	v_and_b32_e32 v18, 0xffff0000, v18
	v_or_b32_sdwa v17, v17, v16 dst_sel:DWORD dst_unused:UNUSED_PAD src0_sel:DWORD src1_sel:WORD_1
	v_or_b32_sdwa v16, v18, v22 dst_sel:DWORD dst_unused:UNUSED_PAD src0_sel:DWORD src1_sel:WORD_1
	ds_write_b64 v172, v[16:17]
	v_and_b32_sdwa v17, v82, v203 dst_sel:DWORD dst_unused:UNUSED_PAD src0_sel:WORD_1 src1_sel:DWORD
	v_and_b32_sdwa v18, v153, v203 dst_sel:DWORD dst_unused:UNUSED_PAD src0_sel:WORD_1 src1_sel:DWORD
	v_and_b32_sdwa v19, v83, v203 dst_sel:DWORD dst_unused:UNUSED_PAD src0_sel:WORD_1 src1_sel:DWORD
	v_and_b32_sdwa v16, v152, v203 dst_sel:DWORD dst_unused:UNUSED_PAD src0_sel:WORD_1 src1_sel:DWORD
	v_add3_u32 v22, v82, v17, s86
	v_add3_u32 v17, v153, v18, s86
	v_add3_u32 v18, v83, v19, s86
	v_add3_u32 v16, v152, v16, s86
	v_and_b32_e32 v17, 0xffff0000, v17
	v_and_b32_e32 v18, 0xffff0000, v18
	v_or_b32_sdwa v17, v17, v16 dst_sel:DWORD dst_unused:UNUSED_PAD src0_sel:DWORD src1_sel:WORD_1
	v_or_b32_sdwa v16, v18, v22 dst_sel:DWORD dst_unused:UNUSED_PAD src0_sel:DWORD src1_sel:WORD_1
	v_and_b32_sdwa v18, v15, v203 dst_sel:DWORD dst_unused:UNUSED_PAD src0_sel:WORD_1 src1_sel:DWORD
	v_and_b32_sdwa v19, v13, v203 dst_sel:DWORD dst_unused:UNUSED_PAD src0_sel:WORD_1 src1_sel:DWORD
	ds_write_b64 v173, v[16:17]
	v_and_b32_sdwa v16, v14, v203 dst_sel:DWORD dst_unused:UNUSED_PAD src0_sel:WORD_1 src1_sel:DWORD
	v_and_b32_sdwa v17, v12, v203 dst_sel:DWORD dst_unused:UNUSED_PAD src0_sel:WORD_1 src1_sel:DWORD
	v_add3_u32 v15, v15, v18, s86
	v_add3_u32 v13, v13, v19, s86
	v_add3_u32 v12, v12, v17, s86
	v_add3_u32 v14, v14, v16, s86
	v_and_b32_e32 v15, 0xffff0000, v15
	v_and_b32_e32 v16, 0xffff0000, v13
	v_or_b32_sdwa v13, v15, v14 dst_sel:DWORD dst_unused:UNUSED_PAD src0_sel:DWORD src1_sel:WORD_1
	v_or_b32_sdwa v12, v16, v12 dst_sel:DWORD dst_unused:UNUSED_PAD src0_sel:DWORD src1_sel:WORD_1
	ds_write_b64 v174, v[12:13]
	v_and_b32_sdwa v13, v42, v203 dst_sel:DWORD dst_unused:UNUSED_PAD src0_sel:WORD_1 src1_sel:DWORD
	v_and_b32_sdwa v14, v45, v203 dst_sel:DWORD dst_unused:UNUSED_PAD src0_sel:WORD_1 src1_sel:DWORD
	v_and_b32_sdwa v15, v43, v203 dst_sel:DWORD dst_unused:UNUSED_PAD src0_sel:WORD_1 src1_sel:DWORD
	v_and_b32_sdwa v12, v44, v203 dst_sel:DWORD dst_unused:UNUSED_PAD src0_sel:WORD_1 src1_sel:DWORD
	v_add3_u32 v16, v42, v13, s86
	v_add3_u32 v13, v45, v14, s86
	v_add3_u32 v14, v43, v15, s86
	v_add3_u32 v12, v44, v12, s86
	v_and_b32_e32 v13, 0xffff0000, v13
	v_and_b32_e32 v14, 0xffff0000, v14
	v_or_b32_sdwa v13, v13, v12 dst_sel:DWORD dst_unused:UNUSED_PAD src0_sel:DWORD src1_sel:WORD_1
	v_or_b32_sdwa v12, v14, v16 dst_sel:DWORD dst_unused:UNUSED_PAD src0_sel:DWORD src1_sel:WORD_1
	ds_write_b64 v175, v[12:13]
	s_waitcnt vmcnt(1)
	v_pk_add_f32 v[0:1], v[0:1], 1.0 op_sel_hi:[1,0]
	v_pk_add_f32 v[2:3], v[2:3], 1.0 op_sel_hi:[1,0]
	s_waitcnt vmcnt(0)
; #define LAS __attribute__((address_space(3)))
; #define P5_LDB(dst, q0) do { _Pragma("unroll") for (int q_ = 0; q_ < 4; ++q_) _Pragma("unroll") for (int c_ = 0; c_ < 4; ++c_) dst[q_][c_] = *(const GAS bf16x8*)(wbase + (size_t)((q0) + q_) * 4096 + c_ * 1024); } while (0)
; template <int l>
; __device__ __forceinline__ void layer_phases(Frame& F, const XcdBarrier& bar, const int lo, const int hi) {
;     ...
;                         *(LAS v2u*)(h2s + rloc * 4096 + ((chunk ^ (rloc & 15)) << 4) + (lq & 1) * 8) = o; }
;     ...
;                 bf16x8 bqa[4][4], bqb[4][4];
;                 const unsigned lo_ = lq * 16;
;                 const unsigned char* wbase = wrf + (size_t)(16 * F.wave) * 4096 + lo_;
;     ...
;                 asm volatile("" ::: "memory");
;                 P5_LDB(bqa, 0); P5_LDB(bqb, 4);
;                 __syncthreads();
;                 att::f32x16 acc0 = att::f32x16{}, acc1 = att::f32x16{};
;                 P5_MMA(bqa, 0); asm volatile("" ::: "memory"); P5_LDB(bqa, 8);
;                 P5_MMA(bqb, 4); asm volatile("" ::: "memory"); P5_LDB(bqb, 12);
;                 P5_MMA(bqa, 8); P5_MMA(bqb, 12);
	v_pk_fma_f32 v[0:1], v[8:9], v[0:1], v[4:5]
	v_pk_fma_f32 v[2:3], v[10:11], v[2:3], v[6:7]
	v_cvt_pk_fp8_f32 v155, v0, v1
	v_and_b32_sdwa v5, v0, v203 dst_sel:DWORD dst_unused:UNUSED_PAD src0_sel:WORD_1 src1_sel:DWORD
	v_and_b32_sdwa v6, v3, v203 dst_sel:DWORD dst_unused:UNUSED_PAD src0_sel:WORD_1 src1_sel:DWORD
	v_and_b32_sdwa v7, v1, v203 dst_sel:DWORD dst_unused:UNUSED_PAD src0_sel:WORD_1 src1_sel:DWORD
	v_cvt_pk_fp8_f32 v155, v2, v3 op_sel:[0,0,1]
	v_and_b32_sdwa v4, v2, v203 dst_sel:DWORD dst_unused:UNUSED_PAD src0_sel:WORD_1 src1_sel:DWORD
	v_add3_u32 v0, v0, v5, s86
	v_add3_u32 v5, v3, v6, s86
	v_add3_u32 v1, v1, v7, s86
	v_add3_u32 v4, v2, v4, s86
	v_and_b32_e32 v5, 0xffff0000, v5
	v_and_b32_e32 v6, 0xffff0000, v1
	v_or_b32_sdwa v1, v5, v4 dst_sel:DWORD dst_unused:UNUSED_PAD src0_sel:DWORD src1_sel:WORD_1
	v_or_b32_sdwa v0, v6, v0 dst_sel:DWORD dst_unused:UNUSED_PAD src0_sel:DWORD src1_sel:WORD_1
	ds_write_b64 v164, v[0:1]
	global_store_dword v[20:21], v155, off offset:1792
	global_load_dwordx4 v[0:3], v60, s[36:37]
	global_load_dwordx4 v[36:39], v60, s[36:37] offset:1024
	global_load_dwordx4 v[16:19], v60, s[36:37] offset:2048
	global_load_dwordx4 v[32:35], v60, s[36:37] offset:3072
	v_add_co_u32_e32 v4, vcc, s87, v72
	v_add_u32_e32 v63, s69, v154
	s_nop 0
	v_addc_co_u32_e32 v5, vcc, 0, v73, vcc
	v_add_co_u32_e32 v8, vcc, s0, v72
	s_movk_i32 s0, 0x3000
	s_nop 0
	v_addc_co_u32_e32 v9, vcc, 0, v73, vcc
	global_load_dwordx4 v[40:43], v[8:9], off offset:-4096
	global_load_dwordx4 v[64:67], v[4:5], off offset:1024
	global_load_dwordx4 v[68:71], v[4:5], off offset:2048
	v_add_co_u32_e32 v12, vcc, s0, v72
	s_movk_i32 s0, 0x6000
	s_nop 0
	v_addc_co_u32_e32 v13, vcc, 0, v73, vcc
	v_add_co_u32_e32 v10, vcc, s83, v72
	v_lshl_add_u32 v62, v89, 12, 0
	s_nop 0
	v_addc_co_u32_e32 v11, vcc, 0, v73, vcc
	v_add_co_u32_e32 v6, vcc, s24, v72
	v_bitop3_b32 v22, v63, v204, 15 bitop3:0x78
	s_nop 0
	v_addc_co_u32_e32 v7, vcc, 0, v73, vcc
	v_add_co_u32_e32 v20, vcc, s0, v72
	v_lshl_add_u32 v22, v22, 4, v62
	s_nop 0
	v_addc_co_u32_e32 v21, vcc, 0, v73, vcc
	v_add_co_u32_e32 v14, vcc, s26, v72
	v_readlane_b32 s0, v248, 30
	s_nop 0
	v_addc_co_u32_e32 v15, vcc, 0, v73, vcc
	v_add_co_u32_e32 v86, vcc, s14, v72
	s_nop 1
	v_addc_co_u32_e32 v87, vcc, 0, v73, vcc
	global_load_dwordx4 v[74:77], v[8:9], off
	global_load_dwordx4 v[78:81], v[8:9], off offset:1024
	global_load_dwordx4 v[82:85], v[8:9], off offset:2048
	global_load_dwordx4 v[90:93], v[8:9], off offset:3072
	global_load_dwordx4 v[94:97], v[10:11], off offset:-4096
	global_load_dwordx4 v[98:101], v[4:5], off offset:3072
	global_load_dwordx4 v[102:105], v[12:13], off offset:1024
	global_load_dwordx4 v[106:109], v[12:13], off offset:2048
	global_load_dwordx4 v[110:113], v[12:13], off offset:3072
	global_load_dwordx4 v[114:117], v[10:11], off
	global_load_dwordx4 v[118:121], v[10:11], off offset:1024
	global_load_dwordx4 v[122:125], v[10:11], off offset:2048
	global_load_dwordx4 v[126:129], v[10:11], off offset:3072
	global_load_dwordx4 v[130:133], v[6:7], off offset:1024
	global_load_dwordx4 v[134:137], v[6:7], off offset:2048
	global_load_dwordx4 v[138:141], v[20:21], off offset:-4096
	global_load_dwordx4 v[142:145], v[20:21], off
	global_load_dwordx4 v[146:149], v[20:21], off offset:1024
	global_load_dwordx4 v[150:153], v[20:21], off offset:2048
	global_load_dwordx4 v[156:159], v[20:21], off offset:3072
	global_load_dwordx4 v[160:163], v[86:87], off offset:-4096
	global_load_dwordx4 v[164:167], v[6:7], off offset:3072
	global_load_dwordx4 v[48:51], v[14:15], off offset:1024
	global_load_dwordx4 v[168:171], v[14:15], off offset:2048
	global_load_dwordx4 v[44:47], v[14:15], off offset:3072
	s_waitcnt lgkmcnt(0)
	s_barrier
	ds_read_b128 v[172:175], v22
	v_add_u32_e32 v4, 2, v63
	v_bitop3_b32 v4, v4, v204, 15 bitop3:0x78
	v_lshl_add_u32 v4, v4, 4, v62
	ds_read_b128 v[176:179], v4
	s_waitcnt vmcnt(31) lgkmcnt(1)
	v_mfma_f32_32x32x16_bf16 v[0:15], v[172:175], v[0:3], 0
	s_waitcnt vmcnt(29)
	v_mfma_f32_32x32x16_bf16 v[16:31], v[172:175], v[16:19], 0
	v_mfma_f32_32x32x16_bf16 v[0:15], v[172:175], v[36:39], v[0:15]
	v_add_u32_e32 v36, 6, v63
	v_bitop3_b32 v36, v36, v204, 15 bitop3:0x78
	v_lshl_add_u32 v36, v36, 4, v62
	ds_read_b128 v[36:39], v36
	s_waitcnt vmcnt(28)
	v_mfma_f32_32x32x16_bf16 v[16:31], v[172:175], v[32:35], v[16:31]
	v_add_u32_e32 v32, 4, v63
	v_bitop3_b32 v32, v32, v204, 15 bitop3:0x78
	v_lshl_add_u32 v32, v32, 4, v62
	ds_read_b128 v[32:35], v32
	s_waitcnt vmcnt(27) lgkmcnt(2)
	v_mfma_f32_32x32x16_bf16 v[0:15], v[176:179], v[40:43], v[0:15]
	v_add_u32_e32 v40, s0, v154
	s_mov_b32 s0, 0xa000
	s_waitcnt vmcnt(25)
	v_mfma_f32_32x32x16_bf16 v[16:31], v[176:179], v[68:71], v[16:31]
	v_mfma_f32_32x32x16_bf16 v[0:15], v[176:179], v[64:67], v[0:15]
	global_load_dwordx4 v[64:67], v[86:87], off offset:2048
	s_waitcnt vmcnt(20)
	v_mfma_f32_32x32x16_bf16 v[16:31], v[176:179], v[98:101], v[16:31]
	s_waitcnt lgkmcnt(0)
	v_mfma_f32_32x32x16_bf16 v[0:15], v[32:35], v[74:77], v[0:15]
	v_mfma_f32_32x32x16_bf16 v[16:31], v[32:35], v[82:85], v[16:31]
	v_mfma_f32_32x32x16_bf16 v[0:15], v[32:35], v[78:81], v[0:15]
	v_mfma_f32_32x32x16_bf16 v[16:31], v[32:35], v[90:93], v[16:31]
	v_bitop3_b32 v32, v40, v204, 15 bitop3:0x78
	v_lshl_add_u32 v32, v32, 4, v62
	ds_read_b128 v[32:35], v32
	v_mfma_f32_32x32x16_bf16 v[0:15], v[36:39], v[94:97], v[0:15]
	s_waitcnt vmcnt(18)
	v_mfma_f32_32x32x16_bf16 v[16:31], v[36:39], v[106:109], v[16:31]
	v_mfma_f32_32x32x16_bf16 v[0:15], v[36:39], v[102:105], v[0:15]
	s_waitcnt vmcnt(17)
; #define P5_LDB(dst, q0) do { _Pragma("unroll") for (int q_ = 0; q_ < 4; ++q_) _Pragma("unroll") for (int c_ = 0; c_ < 4; ++c_) dst[q_][c_] = *(const GAS bf16x8*)(wbase + (size_t)((q0) + q_) * 4096 + c_ * 1024); } while (0)
; template <int l>
; __device__ __forceinline__ void layer_phases(Frame& F, const XcdBarrier& bar, const int lo, const int hi) {
;     ...
;                 bf16x8 bqa[4][4], bqb[4][4];
;                 const unsigned lo_ = lq * 16;
;                 const unsigned char* wbase = wrf + (size_t)(16 * F.wave) * 4096 + lo_;
;     ...
;                 asm volatile("" ::: "memory");
;                 P5_LDB(bqa, 0); P5_LDB(bqb, 4);
;                 __syncthreads();
;                 att::f32x16 acc0 = att::f32x16{}, acc1 = att::f32x16{};
;                 P5_MMA(bqa, 0); asm volatile("" ::: "memory"); P5_LDB(bqa, 8);
;                 P5_MMA(bqb, 4); asm volatile("" ::: "memory"); P5_LDB(bqb, 12);
;                 P5_MMA(bqa, 8); P5_MMA(bqb, 12);
	v_mfma_f32_32x32x16_bf16 v[16:31], v[36:39], v[110:113], v[16:31]
	v_add_u32_e32 v36, 2, v40
	v_bitop3_b32 v36, v36, v204, 15 bitop3:0x78
	v_lshl_add_u32 v36, v36, 4, v62
	ds_read_b128 v[36:39], v36
	s_waitcnt vmcnt(16) lgkmcnt(1)
	v_mfma_f32_32x32x16_bf16 v[0:15], v[32:35], v[114:117], v[0:15]
	s_waitcnt vmcnt(14)
	v_mfma_f32_32x32x16_bf16 v[16:31], v[32:35], v[122:125], v[16:31]
	v_mfma_f32_32x32x16_bf16 v[0:15], v[32:35], v[118:121], v[0:15]
	s_waitcnt vmcnt(13)
	v_mfma_f32_32x32x16_bf16 v[16:31], v[32:35], v[126:129], v[16:31]
	v_add_u32_e32 v32, 4, v40
	v_bitop3_b32 v32, v32, v204, 15 bitop3:0x78
	v_lshl_add_u32 v32, v32, 4, v62
	ds_read_b128 v[32:35], v32
	v_add_u32_e32 v40, 6, v40
	v_bitop3_b32 v40, v40, v204, 15 bitop3:0x78
	v_lshl_add_u32 v40, v40, 4, v62
	s_waitcnt vmcnt(10) lgkmcnt(1)
	v_mfma_f32_32x32x16_bf16 v[0:15], v[36:39], v[138:141], v[0:15]
	ds_read_b128 v[40:43], v40
	v_mfma_f32_32x32x16_bf16 v[16:31], v[36:39], v[134:137], v[16:31]
	v_mfma_f32_32x32x16_bf16 v[0:15], v[36:39], v[130:133], v[0:15]
	s_waitcnt vmcnt(4)
	v_mfma_f32_32x32x16_bf16 v[16:31], v[36:39], v[164:167], v[16:31]
	global_load_dwordx4 v[36:39], v[86:87], off
	global_load_dwordx4 v[68:71], v[86:87], off offset:1024
	global_load_dwordx4 v[74:77], v[86:87], off offset:3072
	v_add_co_u32_e32 v86, vcc, s0, v72
	v_readlane_b32 s0, v248, 28
	s_nop 0
	v_addc_co_u32_e32 v87, vcc, 0, v73, vcc
	s_waitcnt lgkmcnt(1)
	v_mfma_f32_32x32x16_bf16 v[0:15], v[32:35], v[142:145], v[0:15]
	v_add_co_u32_e32 v90, vcc, s25, v72
	global_load_dwordx4 v[78:81], v[86:87], off offset:-4096
	global_load_dwordx4 v[94:97], v[86:87], off
	v_addc_co_u32_e32 v91, vcc, 0, v73, vcc
	global_load_dwordx4 v[82:85], v[90:91], off offset:1024
	v_mfma_f32_32x32x16_bf16 v[16:31], v[32:35], v[150:153], v[16:31]
	v_add_u32_e32 v60, s0, v154
	s_mov_b32 s0, 0xb000
	v_add_co_u32_e32 v118, vcc, s0, v72
	s_mov_b32 s0, 0xc000
	s_nop 0
	v_addc_co_u32_e32 v119, vcc, 0, v73, vcc
	v_mfma_f32_32x32x16_bf16 v[0:15], v[32:35], v[146:149], v[0:15]
	v_add_co_u32_e32 v122, vcc, s0, v72
	v_bitop3_b32 v63, v60, v204, 15 bitop3:0x78
	s_nop 0
	v_addc_co_u32_e32 v123, vcc, 0, v73, vcc
	v_lshl_add_u32 v63, v63, 4, v62
	v_readlane_b32 s0, v248, 29
	v_mfma_f32_32x32x16_bf16 v[16:31], v[32:35], v[156:159], v[16:31]
	global_load_dwordx4 v[32:35], v[90:91], off offset:2048
	s_nop 0
	global_load_dwordx4 v[90:93], v[90:91], off offset:3072
	s_waitcnt lgkmcnt(0)
	v_mfma_f32_32x32x16_bf16 v[0:15], v[40:43], v[160:163], v[0:15]
	s_waitcnt vmcnt(11)
	v_mfma_f32_32x32x16_bf16 v[0:15], v[40:43], v[48:51], v[0:15]
	global_load_dwordx4 v[48:51], v[86:87], off offset:1024
	global_load_dwordx4 v[98:101], v[86:87], off offset:2048
	global_load_dwordx4 v[102:105], v[86:87], off offset:3072
	global_load_dwordx4 v[106:109], v[122:123], off offset:-4096
	global_load_dwordx4 v[110:113], v[118:119], off offset:1024
	global_load_dwordx4 v[114:117], v[118:119], off offset:2048
	s_nop 0
	global_load_dwordx4 v[118:121], v[118:119], off offset:3072
	s_waitcnt vmcnt(17)
	v_mfma_f32_32x32x16_bf16 v[16:31], v[40:43], v[168:171], v[16:31]
	s_waitcnt vmcnt(16)
	v_mfma_f32_32x32x16_bf16 v[16:31], v[40:43], v[44:47], v[16:31]
	ds_read_b128 v[40:43], v63
	v_add_u32_e32 v44, 2, v60
	v_bitop3_b32 v44, v44, v204, 15 bitop3:0x78
	v_lshl_add_u32 v44, v44, 4, v62
	ds_read_b128 v[44:47], v44
	s_waitcnt vmcnt(14) lgkmcnt(1)
	v_mfma_f32_32x32x16_bf16 v[0:15], v[40:43], v[36:39], v[0:15]
	v_add_u32_e32 v36, 6, v60
	v_bitop3_b32 v36, v36, v204, 15 bitop3:0x78
	v_lshl_add_u32 v36, v36, 4, v62
	ds_read_b128 v[36:39], v36
	v_mfma_f32_32x32x16_bf16 v[16:31], v[40:43], v[64:67], v[16:31]
	s_waitcnt vmcnt(13)
	v_mfma_f32_32x32x16_bf16 v[0:15], v[40:43], v[68:71], v[0:15]
	s_waitcnt vmcnt(12)
	v_mfma_f32_32x32x16_bf16 v[16:31], v[40:43], v[74:77], v[16:31]
	global_load_dwordx4 v[40:43], v[122:123], off offset:2048
	s_waitcnt vmcnt(12) lgkmcnt(1)
	v_mfma_f32_32x32x16_bf16 v[0:15], v[44:47], v[78:81], v[0:15]
	s_waitcnt vmcnt(9)
	v_mfma_f32_32x32x16_bf16 v[16:31], v[44:47], v[32:35], v[16:31]
	v_add_u32_e32 v32, 4, v60
	v_bitop3_b32 v32, v32, v204, 15 bitop3:0x78
	v_lshl_add_u32 v32, v32, 4, v62
	ds_read_b128 v[32:35], v32
	v_add_u32_e32 v60, s0, v154
	s_mov_b32 s0, 0xe000
	v_add_co_u32_e32 v64, vcc, s0, v72
	v_mfma_f32_32x32x16_bf16 v[0:15], v[44:47], v[82:85], v[0:15]
	s_nop 0
	v_addc_co_u32_e32 v65, vcc, 0, v73, vcc
	s_mov_b32 s0, 0xd000
	v_add_co_u32_e32 v66, vcc, s0, v72
	s_mov_b32 s0, 0xf000
	s_nop 0
	v_addc_co_u32_e32 v67, vcc, 0, v73, vcc
	s_waitcnt vmcnt(8)
	v_mfma_f32_32x32x16_bf16 v[16:31], v[44:47], v[90:93], v[16:31]
	v_bitop3_b32 v44, v60, v204, 15 bitop3:0x78
	v_lshl_add_u32 v44, v44, 4, v62
	ds_read_b128 v[44:47], v44
	s_waitcnt lgkmcnt(1)
	v_mfma_f32_32x32x16_bf16 v[0:15], v[32:35], v[94:97], v[0:15]
	s_waitcnt vmcnt(6)
	v_mfma_f32_32x32x16_bf16 v[16:31], v[32:35], v[98:101], v[16:31]
	v_mfma_f32_32x32x16_bf16 v[0:15], v[32:35], v[48:51], v[0:15]
	v_add_u32_e32 v48, 2, v60
	v_bitop3_b32 v48, v48, v204, 15 bitop3:0x78
	v_lshl_add_u32 v48, v48, 4, v62
	ds_read_b128 v[48:51], v48
	s_waitcnt vmcnt(5)
	v_mfma_f32_32x32x16_bf16 v[16:31], v[32:35], v[102:105], v[16:31]
	global_load_dwordx4 v[32:35], v[122:123], off
	s_waitcnt vmcnt(5)
	v_mfma_f32_32x32x16_bf16 v[0:15], v[36:39], v[106:109], v[0:15]
	s_waitcnt vmcnt(3)
	v_mfma_f32_32x32x16_bf16 v[16:31], v[36:39], v[114:117], v[16:31]
	v_mfma_f32_32x32x16_bf16 v[0:15], v[36:39], v[110:113], v[0:15]
	s_waitcnt vmcnt(2)
	v_mfma_f32_32x32x16_bf16 v[16:31], v[36:39], v[118:121], v[16:31]
	global_load_dwordx4 v[36:39], v[122:123], off offset:1024
	s_waitcnt vmcnt(1) lgkmcnt(1)
; __device__ __forceinline__ int crow(int r, int hi) { return (r & 3) + 8 * (r >> 2) + 4 * hi; }
; #define P5_LDB(dst, q0) do { _Pragma("unroll") for (int q_ = 0; q_ < 4; ++q_) _Pragma("unroll") for (int c_ = 0; c_ < 4; ++c_) dst[q_][c_] = *(const GAS bf16x8*)(wbase + (size_t)((q0) + q_) * 4096 + c_ * 1024); } while (0)
; template <int l>
; __device__ __forceinline__ void layer_phases(Frame& F, const XcdBarrier& bar, const int lo, const int hi) {
;     ...
;                 P5_MMA(bqa, 0); asm volatile("" ::: "memory"); P5_LDB(bqa, 8);
;                 P5_MMA(bqb, 4); asm volatile("" ::: "memory"); P5_LDB(bqb, 12);
;                 P5_MMA(bqa, 8); P5_MMA(bqb, 12);
;     ...
;                 __syncthreads();
; #pragma unroll
;                 for (int r = 0; r < 16; ++r) { const int row = att::crow(r, hi5); part[(F.wave * 32 + row) * 64 + r32] = acc0[r]; part[(F.wave * 32 + row) * 64 + 32 + r32] = acc1[r]; }
;                 __syncthreads();
;                 float score[4]; unsigned key[4]; int ek[4][6]; float sk[4][6];
; #pragma unroll
;                 for (int rr = 0; rr < 4; ++rr) { const int rloc = 4 * F.wave + rr; float lg = 0.f;
; #pragma unroll
;                     for (int w = 0; w < 8; ++w) lg += part[(w * 32 + rloc) * 64 + F.lane];
	v_mfma_f32_32x32x16_bf16 v[0:15], v[44:47], v[32:35], v[0:15]
	global_load_dwordx4 v[32:35], v[122:123], off offset:3072
	s_waitcnt vmcnt(1)
	v_mfma_f32_32x32x16_bf16 v[0:15], v[44:47], v[36:39], v[0:15]
	global_load_dwordx4 v[36:39], v[64:65], off offset:-4096
	v_mfma_f32_32x32x16_bf16 v[16:31], v[44:47], v[40:43], v[16:31]
	s_waitcnt vmcnt(1)
	v_mfma_f32_32x32x16_bf16 v[16:31], v[44:47], v[32:35], v[16:31]
	global_load_dwordx4 v[32:35], v[66:67], off offset:2048
	global_load_dwordx4 v[40:43], v[64:65], off
	s_waitcnt vmcnt(2) lgkmcnt(0)
	v_mfma_f32_32x32x16_bf16 v[0:15], v[48:51], v[36:39], v[0:15]
	global_load_dwordx4 v[36:39], v[66:67], off offset:1024
	s_waitcnt vmcnt(2)
	v_mfma_f32_32x32x16_bf16 v[16:31], v[48:51], v[32:35], v[16:31]
	global_load_dwordx4 v[32:35], v[66:67], off offset:3072
	v_add_co_u32_e32 v66, vcc, s0, v72
	v_readlane_b32 s0, v248, 31
	s_nop 0
	v_addc_co_u32_e32 v67, vcc, 0, v73, vcc
	s_waitcnt vmcnt(0)
	v_mfma_f32_32x32x16_bf16 v[16:31], v[48:51], v[32:35], v[16:31]
	global_load_dwordx4 v[32:35], v[64:65], off offset:2048
	v_mfma_f32_32x32x16_bf16 v[0:15], v[48:51], v[36:39], v[0:15]
	v_add_u32_e32 v36, 4, v60
	v_bitop3_b32 v36, v36, v204, 15 bitop3:0x78
	v_lshl_add_u32 v44, v36, 4, v62
	ds_read_b128 v[44:47], v44
	v_add_u32_e32 v48, 6, v60
	v_bitop3_b32 v48, v48, v204, 15 bitop3:0x78
	v_lshl_add_u32 v48, v48, 4, v62
	global_load_dwordx4 v[36:39], v[66:67], off
	ds_read_b128 v[48:51], v48
	s_waitcnt lgkmcnt(1)
	v_mfma_f32_32x32x16_bf16 v[0:15], v[44:47], v[40:43], v[0:15]
	global_load_dwordx4 v[40:43], v[64:65], off offset:1024
	s_waitcnt vmcnt(2)
	v_mfma_f32_32x32x16_bf16 v[16:31], v[44:47], v[32:35], v[16:31]
	global_load_dwordx4 v[32:35], v[64:65], off offset:3072
	s_waitcnt vmcnt(0)
	v_mfma_f32_32x32x16_bf16 v[16:31], v[44:47], v[32:35], v[16:31]
	global_load_dwordx4 v[32:35], v[66:67], off offset:2048
	v_mfma_f32_32x32x16_bf16 v[0:15], v[44:47], v[40:43], v[0:15]
	v_lshlrev_b32_e32 v40, 10, v154
	v_lshlrev_b32_e32 v41, 2, v89
	s_waitcnt lgkmcnt(0)
	v_mfma_f32_32x32x16_bf16 v[0:15], v[48:51], v[36:39], v[0:15]
	global_load_dwordx4 v[36:39], v[66:67], off offset:1024
	s_waitcnt vmcnt(1)
	v_mfma_f32_32x32x16_bf16 v[16:31], v[48:51], v[32:35], v[16:31]
	global_load_dwordx4 v[32:35], v[66:67], off offset:3072
	s_barrier
	s_waitcnt vmcnt(1)
	v_mfma_f32_32x32x16_bf16 v[0:15], v[48:51], v[36:39], v[0:15]
	v_add3_u32 v36, s0, v40, v41
	v_add_u32_e32 v37, 0x800, v36
	v_add_u32_e32 v38, 0x1000, v36
	v_add_u32_e32 v39, 0x1800, v36
	s_waitcnt vmcnt(0)
	v_mfma_f32_32x32x16_bf16 v[16:31], v[48:51], v[32:35], v[16:31]
	s_nop 11
	ds_write2_b32 v36, v0, v16 offset1:32
	ds_write2_b32 v36, v1, v17 offset0:64 offset1:96
	ds_write2_b32 v36, v2, v18 offset0:128 offset1:160
	ds_write2_b32 v36, v3, v19 offset0:192 offset1:224
	ds_write2_b32 v37, v4, v20 offset1:32
	ds_write2_b32 v37, v5, v21 offset0:64 offset1:96
	ds_write2_b32 v37, v6, v22 offset0:128 offset1:160
	ds_write2_b32 v37, v7, v23 offset0:192 offset1:224
	ds_write2_b32 v38, v8, v24 offset1:32
	ds_write2_b32 v38, v9, v25 offset0:64 offset1:96
	ds_write2_b32 v38, v10, v26 offset0:128 offset1:160
	ds_write2_b32 v38, v11, v27 offset0:192 offset1:224
	ds_write2_b32 v39, v12, v28 offset1:32
	ds_write2_b32 v39, v13, v29 offset0:64 offset1:96
	ds_write2_b32 v39, v14, v30 offset0:128 offset1:160
	ds_write2_b32 v39, v15, v31 offset0:192 offset1:224
	s_waitcnt lgkmcnt(0)
	s_barrier
	ds_read2st64_b32 v[0:1], v202 offset1:1
	ds_read2st64_b32 v[2:3], v202 offset0:32 offset1:33
	ds_read2st64_b32 v[4:5], v202 offset0:34 offset1:35
	ds_read2st64_b32 v[6:7], v202 offset0:2 offset1:3
	ds_read2st64_b32 v[8:9], v202 offset0:64 offset1:65
	ds_read2st64_b32 v[10:11], v202 offset0:96 offset1:97
	ds_read2st64_b32 v[12:13], v202 offset0:98 offset1:99
	ds_read2st64_b32 v[14:15], v202 offset0:66 offset1:67
	ds_read2st64_b32 v[16:17], v202 offset0:128 offset1:129
	ds_read2st64_b32 v[18:19], v202 offset0:160 offset1:161
	ds_read2st64_b32 v[20:21], v202 offset0:162 offset1:163
	ds_read2st64_b32 v[22:23], v202 offset0:130 offset1:131
	ds_read2st64_b32 v[24:25], v202 offset0:192 offset1:193
	ds_read2st64_b32 v[26:27], v202 offset0:224 offset1:225
	ds_read2st64_b32 v[28:29], v202 offset0:226 offset1:227
	ds_read2st64_b32 v[30:31], v202 offset0:194 offset1:195
	s_waitcnt lgkmcnt(14)
	v_add_f32_e32 v0, 0, v0
	v_add_f32_e32 v1, 0, v1
	v_add_f32_e32 v0, v0, v2
	v_add_f32_e32 v1, v1, v3
	s_waitcnt lgkmcnt(12)
	v_add_f32_e32 v6, 0, v6
	v_add_f32_e32 v7, 0, v7
	s_waitcnt lgkmcnt(11)
	v_add_f32_e32 v0, v0, v8
	v_add_f32_e32 v1, v1, v9
	v_add_f32_e32 v2, v6, v4
	v_add_f32_e32 v3, v7, v5
	s_waitcnt lgkmcnt(10)
	v_add_f32_e32 v0, v0, v10
	v_add_f32_e32 v1, v1, v11
	s_waitcnt lgkmcnt(8)
	v_add_f32_e32 v2, v2, v14
	v_add_f32_e32 v3, v3, v15
	s_waitcnt lgkmcnt(7)
	v_add_f32_e32 v0, v0, v16
	v_add_f32_e32 v1, v1, v17
	v_add_f32_e32 v2, v2, v12
	v_add_f32_e32 v3, v3, v13
	s_waitcnt lgkmcnt(6)
	v_add_f32_e32 v0, v0, v18
	v_add_f32_e32 v1, v1, v19
	s_waitcnt lgkmcnt(4)
	v_add_f32_e32 v2, v2, v22
	v_add_f32_e32 v3, v3, v23
	s_waitcnt lgkmcnt(3)
	v_add_f32_e32 v0, v0, v24
	v_add_f32_e32 v1, v1, v25
	v_add_f32_e32 v2, v2, v20
	v_add_f32_e32 v3, v3, v21
	s_waitcnt lgkmcnt(2)
	v_add_f32_e32 v0, v0, v26
	v_add_f32_e32 v1, v1, v27
	s_waitcnt lgkmcnt(0)
; template <int l>
; __device__ __forceinline__ void layer_phases(Frame& F, const XcdBarrier& bar, const int lo, const int hi) {
;     ...
;                 for (int rr = 0; rr < 4; ++rr) { const int rloc = 4 * F.wave + rr; float lg = 0.f;
; #pragma unroll
;                     for (int w = 0; w < 8; ++w) lg += part[(w * 32 + rloc) * 64 + F.lane];
;                     score[rr] = 1.0f / (1.0f + __expf(-lg)); const float sel = score[rr] + rb;
;                     unsigned ob = __float_as_uint(sel); ob = (ob & 0x80000000u) ? ~ob : (ob | 0x80000000u);
;                     key[rr] = (ob & ~63u) | (unsigned)(63 - F.lane); }
; #pragma unroll
;                 for (int k = 0; k < 6; ++k) {
;                     unsigned mx[4];
; #pragma unroll
;                     for (int rr = 0; rr < 4; ++rr) mx[rr] = key[rr];
; #pragma unroll
;                     for (int o = 1; o < 64; o <<= 1) {
; #pragma unroll
;                         for (int rr = 0; rr < 4; ++rr) { const unsigned t = __shfl_xor(mx[rr], o); mx[rr] = t > mx[rr] ? t : mx[rr]; } }
; #pragma unroll
;                     for (int rr = 0; rr < 4; ++rr) { const int win = 63 - (int)(__builtin_amdgcn_readfirstlane((int)mx[rr]) & 63);
;                         ek[rr][k] = win; sk[rr][k] = __uint_as_float((unsigned)__builtin_amdgcn_readlane((int)__float_as_uint(score[rr]), win)); if (F.lane == win) key[rr] = 0u; }
	v_add_f32_e32 v2, v2, v30
	v_add_f32_e32 v3, v3, v31
	v_mul_f32_e32 v0, 0xbfb8aa3b, v0
	v_mul_f32_e32 v4, 0xbfb8aa3b, v1
	v_add_f32_e32 v2, v2, v28
	v_add_f32_e32 v3, v3, v29
	v_exp_f32_e32 v1, v0
	v_exp_f32_e32 v0, v4
	v_mul_f32_e32 v2, 0xbfb8aa3b, v2
	v_mul_f32_e32 v5, 0xbfb8aa3b, v3
	v_exp_f32_e32 v3, v2
	v_exp_f32_e32 v2, v5
	v_pk_add_f32 v[0:1], v[0:1], 1.0 op_sel_hi:[1,0]
	v_pk_add_f32 v[2:3], v[2:3], 1.0 op_sel_hi:[1,0]
	v_div_scale_f32 v4, s[0:1], v1, v1, 1.0
	v_div_scale_f32 v6, s[0:1], v0, v0, 1.0
	v_rcp_f32_e32 v12, v4
	v_div_scale_f32 v8, s[0:1], v3, v3, 1.0
	v_rcp_f32_e32 v13, v6
	v_div_scale_f32 v10, s[0:1], v2, v2, 1.0
	v_rcp_f32_e32 v14, v8
	v_rcp_f32_e32 v15, v10
	v_fma_f32 v16, -v4, v12, 1.0
	v_div_scale_f32 v5, vcc, 1.0, v1, 1.0
	v_fma_f32 v17, -v6, v13, 1.0
	v_fmac_f32_e32 v12, v16, v12
	v_div_scale_f32 v7, s[14:15], 1.0, v0, 1.0
	v_fma_f32 v18, -v8, v14, 1.0
	v_fmac_f32_e32 v13, v17, v13
	v_mul_f32_e32 v16, v5, v12
	v_div_scale_f32 v9, s[16:17], 1.0, v3, 1.0
	v_fma_f32 v19, -v10, v15, 1.0
	v_fmac_f32_e32 v14, v18, v14
	v_mul_f32_e32 v17, v7, v13
	v_fma_f32 v20, -v4, v16, v5
	v_div_scale_f32 v11, s[18:19], 1.0, v2, 1.0
	v_fmac_f32_e32 v15, v19, v15
	v_mul_f32_e32 v18, v9, v14
	v_fma_f32 v21, -v6, v17, v7
	v_fmac_f32_e32 v16, v20, v12
	v_mul_f32_e32 v19, v11, v15
	v_fma_f32 v22, -v8, v18, v9
	v_fmac_f32_e32 v17, v21, v13
	v_fma_f32 v4, -v4, v16, v5
	v_fma_f32 v23, -v10, v19, v11
	v_fmac_f32_e32 v18, v22, v14
	v_fma_f32 v5, -v6, v17, v7
	v_div_fmas_f32 v4, v4, v12, v16
	s_mov_b64 vcc, s[14:15]
	v_fmac_f32_e32 v19, v23, v15
	v_fma_f32 v6, -v8, v18, v9
	v_div_fixup_f32 v1, v4, v1, 1.0
	v_div_fmas_f32 v4, v5, v13, v17
	s_mov_b64 vcc, s[16:17]
	v_fma_f32 v7, -v10, v19, v11
	v_div_fixup_f32 v0, v4, v0, 1.0
	v_div_fmas_f32 v6, v6, v14, v18
	s_mov_b64 vcc, s[18:19]
	v_pk_add_f32 v[4:5], v[54:55], v[0:1]
	v_div_fixup_f32 v3, v6, v3, 1.0
	v_div_fmas_f32 v6, v7, v15, v19
	v_not_b32_e32 v7, v5
	v_or_b32_e32 v8, 0x80000000, v5
	v_div_fixup_f32 v2, v6, v2, 1.0
	v_cmp_gt_i32_e32 vcc, 0, v5
	v_not_b32_e32 v9, v4
	v_or_b32_e32 v10, 0x80000000, v4
	v_cndmask_b32_e32 v6, v8, v7, vcc
	v_cmp_gt_i32_e32 vcc, 0, v4
	v_pk_add_f32 v[4:5], v[54:55], v[2:3]
	v_and_or_b32 v6, v6, s90, v199
	v_cndmask_b32_e32 v7, v10, v9, vcc
	v_not_b32_e32 v8, v5
	v_or_b32_e32 v9, 0x80000000, v5
	v_cmp_gt_i32_e32 vcc, 0, v5
	v_and_or_b32 v7, v7, s90, v199
	v_not_b32_e32 v10, v4
	v_or_b32_e32 v11, 0x80000000, v4
	v_cndmask_b32_e32 v5, v9, v8, vcc
	v_cmp_gt_i32_e32 vcc, 0, v4
	ds_bpermute_b32 v8, v53, v6
	ds_bpermute_b32 v9, v53, v7
	v_cndmask_b32_e32 v4, v11, v10, vcc
	v_and_or_b32 v5, v5, s90, v199
	v_and_or_b32 v4, v4, s90, v199
	ds_bpermute_b32 v10, v53, v5
	ds_bpermute_b32 v11, v53, v4
	s_waitcnt lgkmcnt(3)
	v_max_u32_e32 v8, v8, v6
	s_waitcnt lgkmcnt(2)
	v_max_u32_e32 v9, v9, v7
	ds_bpermute_b32 v12, v194, v8
	ds_bpermute_b32 v13, v194, v9
	s_waitcnt lgkmcnt(3)
	v_max_u32_e32 v10, v10, v5
	s_waitcnt lgkmcnt(2)
	v_max_u32_e32 v11, v11, v4
	ds_bpermute_b32 v14, v194, v10
	ds_bpermute_b32 v15, v194, v11
	s_waitcnt lgkmcnt(3)
	v_max_u32_e32 v8, v12, v8
	s_waitcnt lgkmcnt(2)
	v_max_u32_e32 v9, v13, v9
	ds_bpermute_b32 v12, v195, v8
	ds_bpermute_b32 v13, v195, v9
	s_waitcnt lgkmcnt(3)
	v_max_u32_e32 v10, v14, v10
	s_waitcnt lgkmcnt(2)
	v_max_u32_e32 v11, v15, v11
	ds_bpermute_b32 v14, v195, v10
	ds_bpermute_b32 v15, v195, v11
	s_waitcnt lgkmcnt(3)
	v_max_u32_e32 v8, v12, v8
	s_waitcnt lgkmcnt(2)
	v_max_u32_e32 v9, v13, v9
	ds_bpermute_b32 v12, v196, v8
	ds_bpermute_b32 v13, v196, v9
	s_waitcnt lgkmcnt(3)
	v_max_u32_e32 v10, v14, v10
	s_waitcnt lgkmcnt(2)
	v_max_u32_e32 v11, v15, v11
	ds_bpermute_b32 v14, v196, v10
	ds_bpermute_b32 v15, v196, v11
	s_waitcnt lgkmcnt(3)
	v_max_u32_e32 v8, v12, v8
	s_waitcnt lgkmcnt(2)
	v_max_u32_e32 v9, v13, v9
	ds_bpermute_b32 v12, v197, v8
	ds_bpermute_b32 v13, v197, v9
	s_waitcnt lgkmcnt(3)
	v_max_u32_e32 v10, v14, v10
	s_waitcnt lgkmcnt(2)
	v_max_u32_e32 v11, v15, v11
	ds_bpermute_b32 v14, v197, v10
	ds_bpermute_b32 v15, v197, v11
	s_waitcnt lgkmcnt(3)
	v_max_u32_e32 v8, v12, v8
	s_waitcnt lgkmcnt(2)
	v_max_u32_e32 v9, v13, v9
	ds_bpermute_b32 v12, v198, v8
	ds_bpermute_b32 v13, v198, v9
	s_waitcnt lgkmcnt(3)
	v_max_u32_e32 v10, v14, v10
	s_waitcnt lgkmcnt(2)
	v_max_u32_e32 v11, v15, v11
	ds_bpermute_b32 v14, v198, v10
	ds_bpermute_b32 v15, v198, v11
	s_waitcnt lgkmcnt(3)
	v_max_u32_e32 v8, v12, v8
	s_waitcnt lgkmcnt(2)
	v_max_u32_e32 v9, v13, v9
	v_readfirstlane_b32 s0, v8
	v_readfirstlane_b32 s1, v9
	s_waitcnt lgkmcnt(1)
	v_max_u32_e32 v8, v14, v10
	s_andn2_b32 s16, 63, s0
	s_waitcnt lgkmcnt(0)
	v_max_u32_e32 v9, v15, v11
	s_andn2_b32 s92, 63, s1
	v_cmp_ne_u32_e32 vcc, s16, v52
	v_readfirstlane_b32 s0, v8
	v_readfirstlane_b32 s1, v9
	v_cndmask_b32_e32 v6, 0, v6, vcc
	v_cmp_ne_u32_e32 vcc, s92, v52
	s_andn2_b32 s43, 63, s0
	s_andn2_b32 s19, 63, s1
	v_cndmask_b32_e32 v7, 0, v7, vcc
	ds_bpermute_b32 v8, v53, v6
	v_cmp_ne_u32_e32 vcc, s43, v52
	ds_bpermute_b32 v9, v53, v7
	v_readlane_b32 s93, v1, s16
	v_cndmask_b32_e32 v5, 0, v5, vcc
	v_cmp_ne_u32_e32 vcc, s19, v52
	ds_bpermute_b32 v10, v53, v5
	s_waitcnt lgkmcnt(2)
	v_max_u32_e32 v8, v8, v6
	v_cndmask_b32_e32 v4, 0, v4, vcc
	ds_bpermute_b32 v11, v53, v4
	s_waitcnt lgkmcnt(2)
	v_max_u32_e32 v9, v9, v7
	ds_bpermute_b32 v12, v194, v8
	ds_bpermute_b32 v13, v194, v9
	s_waitcnt lgkmcnt(3)
	v_max_u32_e32 v10, v10, v5
	s_waitcnt lgkmcnt(2)
	v_max_u32_e32 v11, v11, v4
	ds_bpermute_b32 v14, v194, v10
	ds_bpermute_b32 v15, v194, v11
	s_waitcnt lgkmcnt(3)
	v_max_u32_e32 v8, v12, v8
	s_waitcnt lgkmcnt(2)
	v_max_u32_e32 v9, v13, v9
	ds_bpermute_b32 v12, v195, v8
	ds_bpermute_b32 v13, v195, v9
	s_waitcnt lgkmcnt(3)
; template <int l>
; __device__ __forceinline__ void layer_phases(Frame& F, const XcdBarrier& bar, const int lo, const int hi) {
;     ...
;                 for (int k = 0; k < 6; ++k) {
;                     unsigned mx[4];
; #pragma unroll
;                     for (int rr = 0; rr < 4; ++rr) mx[rr] = key[rr];
; #pragma unroll
;                     for (int o = 1; o < 64; o <<= 1) {
; #pragma unroll
;                         for (int rr = 0; rr < 4; ++rr) { const unsigned t = __shfl_xor(mx[rr], o); mx[rr] = t > mx[rr] ? t : mx[rr]; } }
; #pragma unroll
;                     for (int rr = 0; rr < 4; ++rr) { const int win = 63 - (int)(__builtin_amdgcn_readfirstlane((int)mx[rr]) & 63);
;                         ek[rr][k] = win; sk[rr][k] = __uint_as_float((unsigned)__builtin_amdgcn_readlane((int)__float_as_uint(score[rr]), win)); if (F.lane == win) key[rr] = 0u; }
	v_max_u32_e32 v10, v14, v10
	s_waitcnt lgkmcnt(2)
	v_max_u32_e32 v11, v15, v11
	ds_bpermute_b32 v14, v195, v10
	ds_bpermute_b32 v15, v195, v11
	s_waitcnt lgkmcnt(3)
	v_max_u32_e32 v8, v12, v8
	s_waitcnt lgkmcnt(2)
	v_max_u32_e32 v9, v13, v9
	ds_bpermute_b32 v12, v196, v8
	ds_bpermute_b32 v13, v196, v9
	s_waitcnt lgkmcnt(3)
	v_max_u32_e32 v10, v14, v10
	s_waitcnt lgkmcnt(2)
	v_max_u32_e32 v11, v15, v11
	ds_bpermute_b32 v14, v196, v10
	ds_bpermute_b32 v15, v196, v11
	s_waitcnt lgkmcnt(3)
	v_max_u32_e32 v8, v12, v8
	s_waitcnt lgkmcnt(2)
	v_max_u32_e32 v9, v13, v9
	ds_bpermute_b32 v12, v197, v8
	ds_bpermute_b32 v13, v197, v9
	s_waitcnt lgkmcnt(3)
	v_max_u32_e32 v10, v14, v10
	s_waitcnt lgkmcnt(2)
	v_max_u32_e32 v11, v15, v11
	ds_bpermute_b32 v14, v197, v10
	ds_bpermute_b32 v15, v197, v11
	s_waitcnt lgkmcnt(3)
	v_max_u32_e32 v8, v12, v8
	s_waitcnt lgkmcnt(2)
	v_max_u32_e32 v9, v13, v9
	ds_bpermute_b32 v12, v198, v8
	ds_bpermute_b32 v13, v198, v9
	s_waitcnt lgkmcnt(3)
	v_max_u32_e32 v10, v14, v10
	s_waitcnt lgkmcnt(2)
	v_max_u32_e32 v11, v15, v11
	ds_bpermute_b32 v14, v198, v10
	ds_bpermute_b32 v15, v198, v11
	s_waitcnt lgkmcnt(3)
	v_max_u32_e32 v8, v12, v8
	s_waitcnt lgkmcnt(2)
	v_max_u32_e32 v9, v13, v9
	v_readfirstlane_b32 s0, v8
	v_readfirstlane_b32 s1, v9
	s_waitcnt lgkmcnt(1)
	v_max_u32_e32 v8, v14, v10
	s_andn2_b32 s17, 63, s0
	s_waitcnt lgkmcnt(0)
	v_max_u32_e32 v9, v15, v11
	s_andn2_b32 s63, 63, s1
	v_cmp_ne_u32_e32 vcc, s17, v52
	v_readfirstlane_b32 s0, v8
	v_readfirstlane_b32 s1, v9
	v_cndmask_b32_e32 v6, 0, v6, vcc
	v_cmp_ne_u32_e32 vcc, s63, v52
	s_andn2_b32 s95, 63, s0
	s_andn2_b32 s47, 63, s1
	v_cndmask_b32_e32 v7, 0, v7, vcc
	ds_bpermute_b32 v8, v53, v6
	v_cmp_ne_u32_e32 vcc, s95, v52
	ds_bpermute_b32 v9, v53, v7
	v_readlane_b32 s45, v0, s92
	v_cndmask_b32_e32 v5, 0, v5, vcc
	v_cmp_ne_u32_e32 vcc, s47, v52
	ds_bpermute_b32 v10, v53, v5
	s_waitcnt lgkmcnt(2)
	v_max_u32_e32 v8, v8, v6
	v_cndmask_b32_e32 v4, 0, v4, vcc
	ds_bpermute_b32 v11, v53, v4
	s_waitcnt lgkmcnt(2)
	v_max_u32_e32 v9, v9, v7
	ds_bpermute_b32 v12, v194, v8
	ds_bpermute_b32 v13, v194, v9
	s_waitcnt lgkmcnt(3)
	v_max_u32_e32 v10, v10, v5
	s_waitcnt lgkmcnt(2)
	v_max_u32_e32 v11, v11, v4
	ds_bpermute_b32 v14, v194, v10
	ds_bpermute_b32 v15, v194, v11
	s_waitcnt lgkmcnt(3)
	v_max_u32_e32 v8, v12, v8
	s_waitcnt lgkmcnt(2)
	v_max_u32_e32 v9, v13, v9
	ds_bpermute_b32 v12, v195, v8
	ds_bpermute_b32 v13, v195, v9
	s_waitcnt lgkmcnt(3)
	v_max_u32_e32 v10, v14, v10
	s_waitcnt lgkmcnt(2)
	v_max_u32_e32 v11, v15, v11
	ds_bpermute_b32 v14, v195, v10
	ds_bpermute_b32 v15, v195, v11
	s_waitcnt lgkmcnt(3)
	v_max_u32_e32 v8, v12, v8
	s_waitcnt lgkmcnt(2)
	v_max_u32_e32 v9, v13, v9
	ds_bpermute_b32 v12, v196, v8
	ds_bpermute_b32 v13, v196, v9
	s_waitcnt lgkmcnt(3)
	v_max_u32_e32 v10, v14, v10
	s_waitcnt lgkmcnt(2)
	v_max_u32_e32 v11, v15, v11
	ds_bpermute_b32 v14, v196, v10
	ds_bpermute_b32 v15, v196, v11
	s_waitcnt lgkmcnt(3)
	v_max_u32_e32 v8, v12, v8
	s_waitcnt lgkmcnt(2)
	v_max_u32_e32 v9, v13, v9
	ds_bpermute_b32 v12, v197, v8
	ds_bpermute_b32 v13, v197, v9
	s_waitcnt lgkmcnt(3)
	v_max_u32_e32 v10, v14, v10
	s_waitcnt lgkmcnt(2)
	v_max_u32_e32 v11, v15, v11
	ds_bpermute_b32 v14, v197, v10
	ds_bpermute_b32 v15, v197, v11
	s_waitcnt lgkmcnt(3)
	v_max_u32_e32 v8, v12, v8
	s_waitcnt lgkmcnt(2)
	v_max_u32_e32 v9, v13, v9
	ds_bpermute_b32 v12, v198, v8
	ds_bpermute_b32 v13, v198, v9
	s_waitcnt lgkmcnt(3)
	v_max_u32_e32 v10, v14, v10
	s_waitcnt lgkmcnt(2)
	v_max_u32_e32 v11, v15, v11
	ds_bpermute_b32 v14, v198, v10
	ds_bpermute_b32 v15, v198, v11
	s_waitcnt lgkmcnt(3)
	v_max_u32_e32 v8, v12, v8
	s_waitcnt lgkmcnt(2)
	v_max_u32_e32 v9, v13, v9
	v_readfirstlane_b32 s0, v8
	v_readfirstlane_b32 s1, v9
	s_waitcnt lgkmcnt(1)
	v_max_u32_e32 v8, v14, v10
	s_andn2_b32 s77, 63, s0
	s_waitcnt lgkmcnt(0)
	v_max_u32_e32 v9, v15, v11
	s_andn2_b32 s79, 63, s1
	v_cmp_ne_u32_e32 vcc, s77, v52
	v_readfirstlane_b32 s0, v8
	v_readfirstlane_b32 s1, v9
	v_cndmask_b32_e32 v6, 0, v6, vcc
	v_cmp_ne_u32_e32 vcc, s79, v52
	s_andn2_b32 s97, 63, s0
	s_andn2_b32 s94, 63, s1
	v_cndmask_b32_e32 v7, 0, v7, vcc
	ds_bpermute_b32 v8, v53, v6
	v_cmp_ne_u32_e32 vcc, s97, v52
	ds_bpermute_b32 v9, v53, v7
	v_readlane_b32 s41, v3, s43
	v_cndmask_b32_e32 v5, 0, v5, vcc
	v_cmp_ne_u32_e32 vcc, s94, v52
	ds_bpermute_b32 v10, v53, v5
	s_waitcnt lgkmcnt(2)
	v_max_u32_e32 v8, v8, v6
	v_cndmask_b32_e32 v4, 0, v4, vcc
	ds_bpermute_b32 v11, v53, v4
	s_waitcnt lgkmcnt(2)
	v_max_u32_e32 v9, v9, v7
	ds_bpermute_b32 v12, v194, v8
	ds_bpermute_b32 v13, v194, v9
	s_waitcnt lgkmcnt(3)
	v_max_u32_e32 v10, v10, v5
	s_waitcnt lgkmcnt(2)
	v_max_u32_e32 v11, v11, v4
	ds_bpermute_b32 v14, v194, v10
	ds_bpermute_b32 v15, v194, v11
	s_waitcnt lgkmcnt(3)
	v_max_u32_e32 v8, v12, v8
	s_waitcnt lgkmcnt(2)
	v_max_u32_e32 v9, v13, v9
	ds_bpermute_b32 v12, v195, v8
	ds_bpermute_b32 v13, v195, v9
	s_waitcnt lgkmcnt(3)
	v_max_u32_e32 v10, v14, v10
	s_waitcnt lgkmcnt(2)
	v_max_u32_e32 v11, v15, v11
	ds_bpermute_b32 v14, v195, v10
	ds_bpermute_b32 v15, v195, v11
	s_waitcnt lgkmcnt(3)
	v_max_u32_e32 v8, v12, v8
	s_waitcnt lgkmcnt(2)
	v_max_u32_e32 v9, v13, v9
	ds_bpermute_b32 v12, v196, v8
	ds_bpermute_b32 v13, v196, v9
	s_waitcnt lgkmcnt(3)
	v_max_u32_e32 v10, v14, v10
	s_waitcnt lgkmcnt(2)
	v_max_u32_e32 v11, v15, v11
	ds_bpermute_b32 v14, v196, v10
	ds_bpermute_b32 v15, v196, v11
	s_waitcnt lgkmcnt(3)
	v_max_u32_e32 v8, v12, v8
	s_waitcnt lgkmcnt(2)
	v_max_u32_e32 v9, v13, v9
	ds_bpermute_b32 v12, v197, v8
	ds_bpermute_b32 v13, v197, v9
	s_waitcnt lgkmcnt(3)
	v_max_u32_e32 v10, v14, v10
	s_waitcnt lgkmcnt(2)
; template <int l>
; __device__ __forceinline__ void layer_phases(Frame& F, const XcdBarrier& bar, const int lo, const int hi) {
;     ...
;                 for (int k = 0; k < 6; ++k) {
;                     unsigned mx[4];
; #pragma unroll
;                     for (int rr = 0; rr < 4; ++rr) mx[rr] = key[rr];
; #pragma unroll
;                     for (int o = 1; o < 64; o <<= 1) {
; #pragma unroll
;                         for (int rr = 0; rr < 4; ++rr) { const unsigned t = __shfl_xor(mx[rr], o); mx[rr] = t > mx[rr] ? t : mx[rr]; } }
; #pragma unroll
;                     for (int rr = 0; rr < 4; ++rr) { const int win = 63 - (int)(__builtin_amdgcn_readfirstlane((int)mx[rr]) & 63);
;                         ek[rr][k] = win; sk[rr][k] = __uint_as_float((unsigned)__builtin_amdgcn_readlane((int)__float_as_uint(score[rr]), win)); if (F.lane == win) key[rr] = 0u; }
;                 }
; #pragma unroll
;                 for (int rr = 0; rr < 4; ++rr) { const int m = m0 + rr;
;                     const float ssum = ((sk[rr][0] + sk[rr][1]) + (sk[rr][2] + sk[rr][3])) + (sk[rr][4] + sk[rr][5]);
;                     if (F.lane < 6 && rep == 0) { int e = ek[rr][0]; float sc = sk[rr][0];
	v_max_u32_e32 v11, v15, v11
	ds_bpermute_b32 v14, v197, v10
	ds_bpermute_b32 v15, v197, v11
	s_waitcnt lgkmcnt(3)
	v_max_u32_e32 v8, v12, v8
	s_waitcnt lgkmcnt(2)
	v_max_u32_e32 v9, v13, v9
	ds_bpermute_b32 v12, v198, v8
	ds_bpermute_b32 v13, v198, v9
	s_waitcnt lgkmcnt(3)
	v_max_u32_e32 v10, v14, v10
	s_waitcnt lgkmcnt(2)
	v_max_u32_e32 v11, v15, v11
	ds_bpermute_b32 v14, v198, v10
	ds_bpermute_b32 v15, v198, v11
	s_waitcnt lgkmcnt(3)
	v_max_u32_e32 v8, v12, v8
	s_waitcnt lgkmcnt(2)
	v_max_u32_e32 v9, v13, v9
	v_readfirstlane_b32 s0, v8
	v_readfirstlane_b32 s1, v9
	s_waitcnt lgkmcnt(1)
	v_max_u32_e32 v8, v14, v10
	s_andn2_b32 s84, 63, s0
	s_waitcnt lgkmcnt(0)
	v_max_u32_e32 v9, v15, v11
	s_andn2_b32 s59, 63, s1
	v_cmp_ne_u32_e32 vcc, s84, v52
	v_readfirstlane_b32 s0, v8
	v_readfirstlane_b32 s1, v9
	v_cndmask_b32_e32 v6, 0, v6, vcc
	v_cmp_ne_u32_e32 vcc, s59, v52
	s_andn2_b32 s78, 63, s0
	s_andn2_b32 s62, 63, s1
	v_cndmask_b32_e32 v7, 0, v7, vcc
	ds_bpermute_b32 v8, v53, v6
	v_cmp_ne_u32_e32 vcc, s78, v52
	ds_bpermute_b32 v9, v53, v7
	v_readlane_b32 s18, v2, s19
	v_cndmask_b32_e32 v5, 0, v5, vcc
	v_cmp_ne_u32_e32 vcc, s62, v52
	ds_bpermute_b32 v10, v53, v5
	s_waitcnt lgkmcnt(2)
	v_max_u32_e32 v8, v8, v6
	v_cndmask_b32_e32 v4, 0, v4, vcc
	ds_bpermute_b32 v11, v53, v4
	s_waitcnt lgkmcnt(2)
	v_max_u32_e32 v9, v9, v7
	ds_bpermute_b32 v12, v194, v8
	ds_bpermute_b32 v13, v194, v9
	s_waitcnt lgkmcnt(3)
	v_max_u32_e32 v10, v10, v5
	s_waitcnt lgkmcnt(2)
	v_max_u32_e32 v11, v11, v4
	ds_bpermute_b32 v14, v194, v10
	ds_bpermute_b32 v15, v194, v11
	s_waitcnt lgkmcnt(3)
	v_max_u32_e32 v8, v12, v8
	s_waitcnt lgkmcnt(2)
	v_max_u32_e32 v9, v13, v9
	ds_bpermute_b32 v12, v195, v8
	ds_bpermute_b32 v13, v195, v9
	s_waitcnt lgkmcnt(3)
	v_max_u32_e32 v10, v14, v10
	s_waitcnt lgkmcnt(2)
	v_max_u32_e32 v11, v15, v11
	ds_bpermute_b32 v14, v195, v10
	ds_bpermute_b32 v15, v195, v11
	s_waitcnt lgkmcnt(3)
	v_max_u32_e32 v8, v12, v8
	s_waitcnt lgkmcnt(2)
	v_max_u32_e32 v9, v13, v9
	ds_bpermute_b32 v12, v196, v8
	ds_bpermute_b32 v13, v196, v9
	s_waitcnt lgkmcnt(3)
	v_max_u32_e32 v10, v14, v10
	s_waitcnt lgkmcnt(2)
	v_max_u32_e32 v11, v15, v11
	ds_bpermute_b32 v14, v196, v10
	ds_bpermute_b32 v15, v196, v11
	s_waitcnt lgkmcnt(3)
	v_max_u32_e32 v8, v12, v8
	s_waitcnt lgkmcnt(2)
	v_max_u32_e32 v9, v13, v9
	ds_bpermute_b32 v12, v197, v8
	ds_bpermute_b32 v13, v197, v9
	s_waitcnt lgkmcnt(3)
	v_max_u32_e32 v10, v14, v10
	s_waitcnt lgkmcnt(2)
	v_max_u32_e32 v11, v15, v11
	ds_bpermute_b32 v14, v197, v10
	ds_bpermute_b32 v15, v197, v11
	s_waitcnt lgkmcnt(3)
	v_max_u32_e32 v8, v12, v8
	s_waitcnt lgkmcnt(2)
	v_max_u32_e32 v9, v13, v9
	ds_bpermute_b32 v12, v198, v8
	ds_bpermute_b32 v13, v198, v9
	s_waitcnt lgkmcnt(3)
	v_max_u32_e32 v10, v14, v10
	s_waitcnt lgkmcnt(2)
	v_max_u32_e32 v11, v15, v11
	ds_bpermute_b32 v14, v198, v10
	ds_bpermute_b32 v15, v198, v11
	s_waitcnt lgkmcnt(3)
	v_max_u32_e32 v8, v12, v8
	s_waitcnt lgkmcnt(2)
	v_max_u32_e32 v9, v13, v9
	v_readfirstlane_b32 s0, v8
	v_readfirstlane_b32 s1, v9
	s_waitcnt lgkmcnt(1)
	v_max_u32_e32 v8, v14, v10
	s_andn2_b32 s89, 63, s0
	s_waitcnt lgkmcnt(0)
	v_max_u32_e32 v9, v15, v11
	s_andn2_b32 s81, 63, s1
	v_cmp_ne_u32_e32 vcc, s89, v52
	v_readfirstlane_b32 s0, v8
	v_readfirstlane_b32 s1, v9
	v_cndmask_b32_e32 v6, 0, v6, vcc
	v_cmp_ne_u32_e32 vcc, s81, v52
	s_andn2_b32 s58, 63, s0
	s_andn2_b32 s61, 63, s1
	v_cndmask_b32_e32 v7, 0, v7, vcc
	v_cmp_ne_u32_e32 vcc, s58, v52
	ds_bpermute_b32 v8, v53, v6
	ds_bpermute_b32 v9, v53, v7
	v_cndmask_b32_e32 v5, 0, v5, vcc
	v_cmp_ne_u32_e32 vcc, s61, v52
	ds_bpermute_b32 v10, v53, v5
	s_waitcnt lgkmcnt(2)
	v_max_u32_e32 v6, v8, v6
	v_cndmask_b32_e32 v4, 0, v4, vcc
	ds_bpermute_b32 v11, v53, v4
	s_waitcnt lgkmcnt(2)
	v_max_u32_e32 v7, v9, v7
	ds_bpermute_b32 v8, v194, v6
	ds_bpermute_b32 v9, v194, v7
	s_waitcnt lgkmcnt(3)
	v_max_u32_e32 v5, v10, v5
	s_waitcnt lgkmcnt(2)
	v_max_u32_e32 v4, v11, v4
	ds_bpermute_b32 v10, v194, v5
	ds_bpermute_b32 v11, v194, v4
	s_waitcnt lgkmcnt(3)
	v_max_u32_e32 v6, v8, v6
	s_waitcnt lgkmcnt(2)
	v_max_u32_e32 v7, v9, v7
	ds_bpermute_b32 v8, v195, v6
	ds_bpermute_b32 v9, v195, v7
	s_waitcnt lgkmcnt(3)
	v_max_u32_e32 v5, v10, v5
	s_waitcnt lgkmcnt(2)
	v_max_u32_e32 v4, v11, v4
	ds_bpermute_b32 v10, v195, v5
	ds_bpermute_b32 v11, v195, v4
	s_waitcnt lgkmcnt(3)
	v_max_u32_e32 v6, v8, v6
	s_waitcnt lgkmcnt(2)
	v_max_u32_e32 v7, v9, v7
	ds_bpermute_b32 v8, v196, v6
	ds_bpermute_b32 v9, v196, v7
	s_waitcnt lgkmcnt(3)
	v_max_u32_e32 v5, v10, v5
	s_waitcnt lgkmcnt(2)
	v_max_u32_e32 v4, v11, v4
	ds_bpermute_b32 v10, v196, v5
	ds_bpermute_b32 v11, v196, v4
	s_waitcnt lgkmcnt(3)
	v_max_u32_e32 v6, v8, v6
	s_waitcnt lgkmcnt(2)
	v_max_u32_e32 v7, v9, v7
	ds_bpermute_b32 v8, v197, v6
	ds_bpermute_b32 v9, v197, v7
	s_waitcnt lgkmcnt(3)
	v_max_u32_e32 v5, v10, v5
	s_waitcnt lgkmcnt(2)
	v_max_u32_e32 v4, v11, v4
	ds_bpermute_b32 v10, v197, v5
	ds_bpermute_b32 v11, v197, v4
	s_waitcnt lgkmcnt(3)
	v_max_u32_e32 v6, v8, v6
	s_waitcnt lgkmcnt(2)
	v_max_u32_e32 v7, v9, v7
	ds_bpermute_b32 v8, v198, v6
	ds_bpermute_b32 v9, v198, v7
	s_waitcnt lgkmcnt(3)
	v_max_u32_e32 v5, v10, v5
	s_waitcnt lgkmcnt(2)
	v_max_u32_e32 v4, v11, v4
	ds_bpermute_b32 v10, v198, v5
	ds_bpermute_b32 v11, v198, v4
	s_waitcnt lgkmcnt(3)
	v_max_u32_e32 v6, v8, v6
	s_waitcnt lgkmcnt(2)
	v_max_u32_e32 v7, v9, v7
	v_readfirstlane_b32 s0, v6
	v_readfirstlane_b32 s1, v7
	s_waitcnt lgkmcnt(1)
	v_max_u32_e32 v5, v10, v5
	s_waitcnt lgkmcnt(0)
	v_max_u32_e32 v4, v11, v4
	s_andn2_b32 vcc_lo, 63, s0
	s_andn2_b32 s88, 63, s1
	v_readfirstlane_b32 s0, v5
	v_readfirstlane_b32 s1, v4
	s_andn2_b32 s80, 63, s0
	s_andn2_b32 s33, 63, s1
	v_readlane_b32 s60, v1, s17
	v_readlane_b32 s96, v0, s63
	v_readlane_b32 s34, v3, s95
	v_readlane_b32 s50, v2, s47
	v_readlane_b32 s73, v1, s77
	v_readlane_b32 s65, v0, s79
	v_readlane_b32 s53, v3, s97
	v_readlane_b32 s51, v2, s94
	v_readlane_b32 s75, v1, s84
	v_readlane_b32 s72, v0, s59
	v_readlane_b32 s67, v3, s78
	v_readlane_b32 s35, v2, s62
	v_readlane_b32 s25, v1, s89
	v_readlane_b32 s1, v0, s81
	v_readlane_b32 s71, v3, s58
	v_readlane_b32 s55, v2, s61
	v_readlane_b32 s26, v1, vcc_lo
	v_readlane_b32 s24, v0, s88
	v_readlane_b32 s0, v3, s80
	v_readlane_b32 s70, v2, s33
	s_mov_b64 s[14:15], exec
	v_readlane_b32 s28, v248, 32
	v_readlane_b32 s29, v248, 33
	s_and_b64 s[28:29], s[14:15], s[28:29]
	s_mov_b64 exec, s[28:29]
	s_cbranch_execz .LBB0_1519
; template <int l>
; __device__ __forceinline__ void layer_phases(Frame& F, const XcdBarrier& bar, const int lo, const int hi) {
;     ...
; #pragma unroll
;                 for (int rr = 0; rr < 4; ++rr) { const int m = m0 + rr;
;                     const float ssum = ((sk[rr][0] + sk[rr][1]) + (sk[rr][2] + sk[rr][3])) + (sk[rr][4] + sk[rr][5]);
;                     if (F.lane < 6 && rep == 0) { int e = ek[rr][0]; float sc = sk[rr][0];
; #pragma unroll
;                         for (int k = 1; k < 6; ++k) if (F.lane == k) { e = ek[rr][k]; sc = sk[rr][k]; }
;                         const unsigned pos = __hip_atomic_fetch_add(F.ctl + CW_CURSOR + (l * 64 + e) * 16, 1u, RLX_AGENT);
;                         if (pos < (unsigned)LISTCAP) { list[(size_t)e * LISTCAP + pos] = m; list2[(size_t)e * LISTCAP + pos] = m * 7 + F.lane; }
;                         tinfo[(size_t)m * 6 + F.lane] = e | (int)(pos << 8); gates[(size_t)m * 6 + F.lane] = sc / ssum * ROUTED_SCALE; }
	v_mov_b32_e32 v40, s16
	v_mov_b32_e32 v48, s17
	v_cndmask_b32_e64 v40, v40, v48, s[4:5]
	v_mov_b32_e32 v48, s77
	v_cndmask_b32_e64 v40, v40, v48, s[6:7]
	v_mov_b32_e32 v48, s84
	v_cndmask_b32_e64 v40, v40, v48, s[8:9]
	v_mov_b32_e32 v48, s89
	v_cndmask_b32_e64 v40, v40, v48, s[10:11]
	v_mov_b32_e32 v48, vcc_lo
	v_cndmask_b32_e64 v40, v40, v48, s[12:13]
	v_lshlrev_b32_e32 v34, 6, v40
	v_add_u32_e32 v34, 0x9000, v34
	global_atomic_add v44, v34, v203, s[56:57] sc0
	v_mov_b32_e32 v41, s92
	v_mov_b32_e32 v48, s63
	v_cndmask_b32_e64 v41, v41, v48, s[4:5]
	v_mov_b32_e32 v48, s79
	v_cndmask_b32_e64 v41, v41, v48, s[6:7]
	v_mov_b32_e32 v48, s59
	v_cndmask_b32_e64 v41, v41, v48, s[8:9]
	v_mov_b32_e32 v48, s81
	v_cndmask_b32_e64 v41, v41, v48, s[10:11]
	v_mov_b32_e32 v48, s88
	v_cndmask_b32_e64 v41, v41, v48, s[12:13]
	v_lshlrev_b32_e32 v34, 6, v41
	v_add_u32_e32 v34, 0x9000, v34
	global_atomic_add v45, v34, v203, s[56:57] sc0
	v_mov_b32_e32 v42, s43
	v_mov_b32_e32 v48, s95
	v_cndmask_b32_e64 v42, v42, v48, s[4:5]
	v_mov_b32_e32 v48, s97
	v_cndmask_b32_e64 v42, v42, v48, s[6:7]
	v_mov_b32_e32 v48, s78
	v_cndmask_b32_e64 v42, v42, v48, s[8:9]
	v_mov_b32_e32 v48, s58
	v_cndmask_b32_e64 v42, v42, v48, s[10:11]
	v_mov_b32_e32 v48, s80
	v_cndmask_b32_e64 v42, v42, v48, s[12:13]
	v_lshlrev_b32_e32 v34, 6, v42
	v_add_u32_e32 v34, 0x9000, v34
	global_atomic_add v46, v34, v203, s[56:57] sc0
	v_mov_b32_e32 v43, s19
	v_mov_b32_e32 v48, s47
	v_cndmask_b32_e64 v43, v43, v48, s[4:5]
	v_mov_b32_e32 v48, s94
	v_cndmask_b32_e64 v43, v43, v48, s[6:7]
	v_mov_b32_e32 v48, s62
	v_cndmask_b32_e64 v43, v43, v48, s[8:9]
	v_mov_b32_e32 v48, s61
	v_cndmask_b32_e64 v43, v43, v48, s[10:11]
	v_mov_b32_e32 v48, s33
	v_cndmask_b32_e64 v43, v43, v48, s[12:13]
	v_lshlrev_b32_e32 v34, 6, v43
	v_add_u32_e32 v34, 0x9000, v34
	global_atomic_add v47, v34, v203, s[56:57] sc0
	s_waitcnt vmcnt(0)
	v_mov_b32_e32 v0, v40
	v_mov_b32_e32 v60, v44
	v_cmp_gt_u32_e32 vcc, s83, v60
	s_and_saveexec_b64 s[16:17], vcc
	s_cbranch_execz .LBB0_1525
	v_lshlrev_b64 v[2:3], 2, v[60:61]
	v_readlane_b32 s28, v248, 13
	v_lshl_or_b32 v2, v0, 16, v2
	v_readlane_b32 s29, v248, 14
	v_mov_b32_e32 v1, s40
	s_nop 0
	v_lshl_add_u64 v[4:5], s[28:29], 0, v[2:3]
	global_store_dword v[4:5], v1, off
	v_mad_u64_u32 v[4:5], s[28:29], s40, 7, v[52:53]
	v_readlane_b32 s28, v248, 15
	v_readlane_b32 s29, v248, 16
	s_nop 1
	v_lshl_add_u64 v[2:3], s[28:29], 0, v[2:3]
	global_store_dword v[2:3], v4, off
.LBB0_1525:
	s_or_b64 exec, exec, s[16:17]
	v_mov_b32_e32 v1, s93
	v_mov_b32_e32 v2, s60
	v_cndmask_b32_e64 v1, v1, v2, s[4:5]
	v_mov_b32_e32 v3, s73
	v_cndmask_b32_e64 v1, v1, v3, s[6:7]
	v_mov_b32_e32 v3, s75
	v_cndmask_b32_e64 v1, v1, v3, s[8:9]
	v_mov_b32_e32 v4, s25
	v_cndmask_b32_e64 v1, v1, v4, s[10:11]
	v_mov_b32_e32 v4, s26
	v_cndmask_b32_e64 v5, v1, v4, s[12:13]
	v_add_f32_e32 v1, s93, v2
	v_add_f32_e32 v2, s73, v3
	v_add_f32_e32 v1, v1, v2
	v_add_f32_e32 v2, s25, v4
	v_add_f32_e32 v2, v1, v2
	v_div_scale_f32 v4, s[16:17], v2, v2, v5
	v_rcp_f32_e32 v6, v4
	v_lshl_or_b32 v3, v60, 8, v0
	v_mad_i64_i32 v[0:1], s[16:17], s40, 24, v[56:57]
	global_store_dword v[0:1], v3, off
	v_fma_f32 v0, -v4, v6, 1.0
	v_fmac_f32_e32 v6, v0, v6
	v_div_scale_f32 v0, vcc, v5, v2, v5
	v_mul_f32_e32 v1, v0, v6
	v_fma_f32 v3, -v4, v1, v0
	v_fmac_f32_e32 v1, v3, v6
	v_fma_f32 v0, -v4, v1, v0
	v_div_fmas_f32 v0, v0, v6, v1
	v_div_fixup_f32 v0, v0, v2, v5
	v_mul_f32_e32 v2, 0x40200000, v0
	v_mad_i64_i32 v[0:1], s[16:17], s40, 24, v[58:59]
	global_store_dword v[0:1], v2, off
	v_mov_b32_e32 v0, v41
	v_mov_b32_e32 v60, v45
	v_cmp_gt_u32_e32 vcc, s83, v60
	s_and_saveexec_b64 s[16:17], vcc
	s_cbranch_execz .LBB0_1527
	v_lshlrev_b64 v[2:3], 2, v[60:61]
	v_readlane_b32 s26, v248, 13
	v_lshl_or_b32 v2, v0, 16, v2
	v_readlane_b32 s27, v248, 14
	v_mov_b32_e32 v1, s42
	s_nop 0
	v_lshl_add_u64 v[4:5], s[26:27], 0, v[2:3]
	global_store_dword v[4:5], v1, off
	v_mad_u64_u32 v[4:5], s[26:27], s42, 7, v[52:53]
	v_readlane_b32 s26, v248, 15
	v_readlane_b32 s27, v248, 16
	s_nop 1
	v_lshl_add_u64 v[2:3], s[26:27], 0, v[2:3]
	global_store_dword v[2:3], v4, off
; template <int l>
; __device__ __forceinline__ void layer_phases(Frame& F, const XcdBarrier& bar, const int lo, const int hi) {
;     ...
; #pragma unroll
;                 for (int rr = 0; rr < 4; ++rr) { const int m = m0 + rr;
;                     const float ssum = ((sk[rr][0] + sk[rr][1]) + (sk[rr][2] + sk[rr][3])) + (sk[rr][4] + sk[rr][5]);
;                     if (F.lane < 6 && rep == 0) { int e = ek[rr][0]; float sc = sk[rr][0];
; #pragma unroll
;                         for (int k = 1; k < 6; ++k) if (F.lane == k) { e = ek[rr][k]; sc = sk[rr][k]; }
;                         const unsigned pos = __hip_atomic_fetch_add(F.ctl + CW_CURSOR + (l * 64 + e) * 16, 1u, RLX_AGENT);
;                         if (pos < (unsigned)LISTCAP) { list[(size_t)e * LISTCAP + pos] = m; list2[(size_t)e * LISTCAP + pos] = m * 7 + F.lane; }
;                         tinfo[(size_t)m * 6 + F.lane] = e | (int)(pos << 8); gates[(size_t)m * 6 + F.lane] = sc / ssum * ROUTED_SCALE; }
;                 }
.LBB0_1527:
	s_or_b64 exec, exec, s[16:17]
	v_mov_b32_e32 v1, s96
	v_mov_b32_e32 v3, s72
	v_add_f32_e32 v2, s45, v1
	v_add_f32_e32 v4, s65, v3
	v_add_f32_e32 v2, v2, v4
	v_mov_b32_e32 v4, s24
	v_add_f32_e32 v5, s1, v4
	v_add_f32_e32 v2, v2, v5
	v_mov_b32_e32 v5, s45
	v_cndmask_b32_e64 v1, v5, v1, s[4:5]
	v_mov_b32_e32 v5, s65
	v_cndmask_b32_e64 v1, v1, v5, s[6:7]
	v_cndmask_b32_e64 v1, v1, v3, s[8:9]
	v_mov_b32_e32 v3, s1
	v_cndmask_b32_e64 v1, v1, v3, s[10:11]
	v_cndmask_b32_e64 v3, v1, v4, s[12:13]
	v_div_scale_f32 v5, s[16:17], v2, v2, v3
	v_rcp_f32_e32 v6, v5
	v_lshl_or_b32 v4, v60, 8, v0
	v_mad_i64_i32 v[0:1], s[16:17], s42, 24, v[56:57]
	global_store_dword v[0:1], v4, off
	v_fma_f32 v0, -v5, v6, 1.0
	v_fmac_f32_e32 v6, v0, v6
	v_div_scale_f32 v0, vcc, v3, v2, v3
	v_mul_f32_e32 v1, v0, v6
	v_fma_f32 v4, -v5, v1, v0
	v_fmac_f32_e32 v1, v4, v6
	v_fma_f32 v0, -v5, v1, v0
	v_div_fmas_f32 v0, v0, v6, v1
	v_div_fixup_f32 v0, v0, v2, v3
	v_mul_f32_e32 v2, 0x40200000, v0
	v_mad_i64_i32 v[0:1], s[16:17], s42, 24, v[58:59]
	global_store_dword v[0:1], v2, off
	v_mov_b32_e32 v0, v42
	v_mov_b32_e32 v60, v46
	v_cmp_gt_u32_e32 vcc, s83, v60
	s_and_saveexec_b64 s[16:17], vcc
	s_cbranch_execz .LBB0_1529
	v_lshlrev_b64 v[2:3], 2, v[60:61]
	v_readlane_b32 s24, v248, 13
	v_lshl_or_b32 v2, v0, 16, v2
	v_readlane_b32 s25, v248, 14
	v_mov_b32_e32 v1, s44
	s_nop 0
	v_lshl_add_u64 v[4:5], s[24:25], 0, v[2:3]
	global_store_dword v[4:5], v1, off
	v_mad_u64_u32 v[4:5], s[24:25], s44, 7, v[52:53]
	v_readlane_b32 s24, v248, 15
	v_readlane_b32 s25, v248, 16
	s_nop 1
	v_lshl_add_u64 v[2:3], s[24:25], 0, v[2:3]
	global_store_dword v[2:3], v4, off
.LBB0_1529:
	s_or_b64 exec, exec, s[16:17]
	v_mov_b32_e32 v1, s34
	v_mov_b32_e32 v3, s67
	v_add_f32_e32 v2, s41, v1
	v_add_f32_e32 v4, s53, v3
	v_add_f32_e32 v2, v2, v4
	v_mov_b32_e32 v4, s0
	v_add_f32_e32 v5, s71, v4
	v_add_f32_e32 v2, v2, v5
	v_mov_b32_e32 v5, s41
	v_cndmask_b32_e64 v1, v5, v1, s[4:5]
	v_mov_b32_e32 v5, s53
	v_cndmask_b32_e64 v1, v1, v5, s[6:7]
	v_cndmask_b32_e64 v1, v1, v3, s[8:9]
	v_mov_b32_e32 v3, s71
	v_cndmask_b32_e64 v1, v1, v3, s[10:11]
	v_cndmask_b32_e64 v3, v1, v4, s[12:13]
	v_div_scale_f32 v5, s[0:1], v2, v2, v3
	v_rcp_f32_e32 v6, v5
	v_lshl_or_b32 v4, v60, 8, v0
	v_mad_i64_i32 v[0:1], s[0:1], s44, 24, v[56:57]
	global_store_dword v[0:1], v4, off
	v_fma_f32 v0, -v5, v6, 1.0
	v_fmac_f32_e32 v6, v0, v6
	v_div_scale_f32 v0, vcc, v3, v2, v3
	v_mul_f32_e32 v1, v0, v6
	v_fma_f32 v4, -v5, v1, v0
	v_fmac_f32_e32 v1, v4, v6
	v_fma_f32 v0, -v5, v1, v0
	v_div_fmas_f32 v0, v0, v6, v1
	v_div_fixup_f32 v0, v0, v2, v3
	v_mul_f32_e32 v2, 0x40200000, v0
	v_mad_i64_i32 v[0:1], s[0:1], s44, 24, v[58:59]
	global_store_dword v[0:1], v2, off
	v_mov_b32_e32 v0, v43
	v_mov_b32_e32 v60, v47
	v_cmp_gt_u32_e32 vcc, s83, v60
	s_and_saveexec_b64 s[16:17], vcc
	s_cbranch_execz .LBB0_1518
	v_lshlrev_b64 v[2:3], 2, v[60:61]
	v_readlane_b32 s0, v248, 13
	v_lshl_or_b32 v2, v0, 16, v2
	v_readlane_b32 s1, v248, 14
	v_mov_b32_e32 v1, s46
	s_nop 0
	v_lshl_add_u64 v[4:5], s[0:1], 0, v[2:3]
	global_store_dword v[4:5], v1, off
	v_mad_u64_u32 v[4:5], s[0:1], s46, 7, v[52:53]
	v_readlane_b32 s0, v248, 15
	v_readlane_b32 s1, v248, 16
	s_nop 1
	v_lshl_add_u64 v[2:3], s[0:1], 0, v[2:3]
	global_store_dword v[2:3], v4, off
	s_branch .LBB0_1518
